# speedup vs baseline: 1.0312x; 1.0096x over previous
.LBB3_7:
	v_add_u32_e32 v182, s33, v161
	v_add_u32_e32 v181, -1, v182
	v_or_b32_e32 v2, v181, v164
	v_add_u32_e32 v180, 0x18400, v171
	v_cmp_gt_u32_e64 s[0:1], 64, v2
	s_mov_b64 s[4:5], -1
	s_and_b64 vcc, exec, s[24:25]
	s_cbranch_vccz .LBB3_45
	s_load_dwordx2 s[4:5], s[22:23], 0x20
	s_waitcnt lgkmcnt(0)
	s_load_dwordx2 s[26:27], s[4:5], 0x0
	s_load_dword s34, s[4:5], 0x8
	v_cmp_lt_u32_e64 s[64:65], 0, v182
	v_cmp_gt_u32_e64 s[66:67], 63, v182
	v_cmp_lt_u32_e64 s[68:69], 0, v162
	v_cmp_gt_u32_e64 s[70:71], 60, v162
	buffer_load_dwordx4 v[186:189], v180, s[16:19], 0 offen
	s_and_b64 s[72:73], s[68:69], s[64:65]
	s_and_b64 s[74:75], s[68:69], s[66:67]
	s_and_b64 s[76:77], s[70:71], s[64:65]
	s_and_b64 s[78:79], s[70:71], s[66:67]
	v_add_u32_e32 v249, 0xfffe7c00, v180
	v_add_u32_e32 v250, 0xfffe8000, v180
	s_mov_b64 exec, s[72:73]
	buffer_load_dwordx4 v[110:113], v249, s[16:19], 0 offen
	buffer_load_dwordx4 v[70:73], v249, s[16:19], 0 offen offset:512
	s_mov_b64 exec, -1
	s_mov_b64 exec, s[68:69]
	buffer_load_dwordx4 v[126:129], v250, s[16:19], 0 offen offset:512
	buffer_load_dwordx4 v[98:101], v250, s[16:19], 0 offen offset:1024
	s_mov_b64 exec, -1
	s_mov_b64 exec, s[74:75]
	buffer_load_dwordx4 v[134:137], v250, s[16:19], 0 offen offset:2048
	buffer_load_dwordx4 v[114:117], v250, s[16:19], 0 offen offset:2560
	s_mov_b64 exec, -1
	v_add_u32_e32 v249, 0xfffffc00, v180
	s_mov_b64 exec, s[64:65]
	buffer_load_dwordx4 v[82:85], v249, s[16:19], 0 offen
	buffer_load_dwordx4 v[42:45], v249, s[16:19], 0 offen offset:512
	s_mov_b64 exec, -1
	buffer_load_dwordx4 v[106:109], v180, s[16:19], 0 offen offset:512
	buffer_load_dwordx4 v[62:65], v180, s[16:19], 0 offen offset:1024
	s_mov_b64 exec, s[66:67]
	buffer_load_dwordx4 v[122:125], v180, s[16:19], 0 offen offset:2048
	buffer_load_dwordx4 v[86:89], v180, s[16:19], 0 offen offset:2560
	s_mov_b64 exec, -1
	v_add_u32_e32 v249, 0x17c00, v180
	v_add_u32_e32 v250, 0x18000, v180
	s_mov_b64 exec, s[64:65]
	buffer_load_dwordx4 v[50:53], v249, s[16:19], 0 offen
	buffer_load_dwordx4 v[22:25], v249, s[16:19], 0 offen offset:512
	s_mov_b64 exec, -1
	buffer_load_dwordx4 v[66:69], v250, s[16:19], 0 offen offset:512
	buffer_load_dwordx4 v[30:33], v250, s[16:19], 0 offen offset:1024
	s_mov_b64 exec, s[66:67]
	buffer_load_dwordx4 v[94:97], v250, s[16:19], 0 offen offset:2048
	buffer_load_dwordx4 v[46:49], v250, s[16:19], 0 offen offset:2560
	s_mov_b64 exec, -1
	v_add_u32_e32 v249, 0x18000, v180
	buffer_load_dwordx4 v[154:157], v249, s[16:19], 0 offen
	v_add_u32_e32 v250, 0x30000, v180
	buffer_load_dwordx4 v[150:153], v250, s[16:19], 0 offen
	v_add_u32_e32 v249, 0x48000, v180
	buffer_load_dwordx4 v[146:149], v249, s[16:19], 0 offen
	v_add_u32_e32 v249, 0x2fc00, v180
	v_add_u32_e32 v250, 0x30000, v180
	v_add_u32_e32 v251, 0x47c00, v180
	v_add_u32_e32 v252, 0x48000, v180
	v_add_u32_e32 v253, 0x5fc00, v180
	v_add_u32_e32 v254, 0x60000, v180
	s_not_b64 exec, s[72:73]
	s_cbranch_execz .Lmyf_B1_0
	v_mov_b32_e32 v110, v172
	v_mov_b32_e32 v111, v174
	v_mov_b32_e32 v112, v176
	v_mov_b32_e32 v113, v178
	v_mov_b32_e32 v70, v173
	v_mov_b32_e32 v71, v175
	v_mov_b32_e32 v72, v177
	v_mov_b32_e32 v73, v179
.Lmyf_B1_0:
	s_not_b64 exec, s[68:69]
	s_cbranch_execz .Lmyf_B1_1
	v_mov_b32_e32 v126, v172
	v_mov_b32_e32 v127, v174
	v_mov_b32_e32 v128, v176
	v_mov_b32_e32 v129, v178
	v_mov_b32_e32 v98, v173
	v_mov_b32_e32 v99, v175
	v_mov_b32_e32 v100, v177
	v_mov_b32_e32 v101, v179
.Lmyf_B1_1:
	s_not_b64 exec, s[74:75]
	s_cbranch_execz .Lmyf_B1_2
	v_mov_b32_e32 v134, v172
	v_mov_b32_e32 v135, v174
	v_mov_b32_e32 v136, v176
	v_mov_b32_e32 v137, v178
	v_mov_b32_e32 v114, v173
	v_mov_b32_e32 v115, v175
	v_mov_b32_e32 v116, v177
	v_mov_b32_e32 v117, v179
.Lmyf_B1_2:
	s_not_b64 exec, s[64:65]
	s_cbranch_execz .Lmyf_B1_3
	v_mov_b32_e32 v82, v172
	v_mov_b32_e32 v83, v174
	v_mov_b32_e32 v84, v176
	v_mov_b32_e32 v85, v178
	v_mov_b32_e32 v42, v173
	v_mov_b32_e32 v43, v175
	v_mov_b32_e32 v44, v177
	v_mov_b32_e32 v45, v179
	v_mov_b32_e32 v50, v172
	v_mov_b32_e32 v51, v174
	v_mov_b32_e32 v52, v176
	v_mov_b32_e32 v53, v178
	v_mov_b32_e32 v22, v173
	v_mov_b32_e32 v23, v175
	v_mov_b32_e32 v24, v177
	v_mov_b32_e32 v25, v179
	v_mov_b32_e32 v18, v172
	v_mov_b32_e32 v19, v174
	v_mov_b32_e32 v20, v176
	v_mov_b32_e32 v21, v178
	v_mov_b32_e32 v6, v173
	v_mov_b32_e32 v7, v175
	v_mov_b32_e32 v8, v177
	v_mov_b32_e32 v9, v179
	v_mov_b32_e32 v74, v172
	v_mov_b32_e32 v75, v174
	v_mov_b32_e32 v76, v176
	v_mov_b32_e32 v77, v178
	v_mov_b32_e32 v26, v173
	v_mov_b32_e32 v27, v175
	v_mov_b32_e32 v28, v177
	v_mov_b32_e32 v29, v179
.Lmyf_B1_3:
	s_not_b64 exec, s[66:67]
	s_cbranch_execz .Lmyf_B1_4
	v_mov_b32_e32 v122, v172
	v_mov_b32_e32 v123, v174
	v_mov_b32_e32 v124, v176
	v_mov_b32_e32 v125, v178
	v_mov_b32_e32 v86, v173
	v_mov_b32_e32 v87, v175
	v_mov_b32_e32 v88, v177
	v_mov_b32_e32 v89, v179
	v_mov_b32_e32 v94, v172
	v_mov_b32_e32 v95, v174
	v_mov_b32_e32 v96, v176
	v_mov_b32_e32 v97, v178
	v_mov_b32_e32 v46, v173
	v_mov_b32_e32 v47, v175
	v_mov_b32_e32 v48, v177
	v_mov_b32_e32 v49, v179
	v_mov_b32_e32 v54, v172
	v_mov_b32_e32 v55, v174
	v_mov_b32_e32 v56, v176
	v_mov_b32_e32 v57, v178
	v_mov_b32_e32 v14, v173
	v_mov_b32_e32 v15, v175
	v_mov_b32_e32 v16, v177
	v_mov_b32_e32 v17, v179
	v_mov_b32_e32 v118, v172
	v_mov_b32_e32 v119, v174
	v_mov_b32_e32 v120, v176
	v_mov_b32_e32 v121, v178
	v_mov_b32_e32 v58, v173
	v_mov_b32_e32 v59, v175
	v_mov_b32_e32 v60, v177
	v_mov_b32_e32 v61, v179
.Lmyf_B1_4:
	s_not_b64 exec, s[76:77]
	s_cbranch_execz .Lmyf_B1_5
	v_mov_b32_e32 v130, v172
	v_mov_b32_e32 v131, v174
	v_mov_b32_e32 v132, v176
	v_mov_b32_e32 v133, v178
	v_mov_b32_e32 v78, v173
	v_mov_b32_e32 v79, v175
	v_mov_b32_e32 v80, v177
	v_mov_b32_e32 v81, v179
.Lmyf_B1_5:
	s_not_b64 exec, s[70:71]
	s_cbranch_execz .Lmyf_B1_6
	v_mov_b32_e32 v138, v172
	v_mov_b32_e32 v139, v174
	v_mov_b32_e32 v140, v176
	v_mov_b32_e32 v141, v178
	v_mov_b32_e32 v90, v173
	v_mov_b32_e32 v91, v175
	v_mov_b32_e32 v92, v177
	v_mov_b32_e32 v93, v179
.Lmyf_B1_6:
	s_not_b64 exec, s[78:79]
	s_cbranch_execz .Lmyf_B1_7
	v_mov_b32_e32 v142, v172
	v_mov_b32_e32 v143, v174
	v_mov_b32_e32 v144, v176
	v_mov_b32_e32 v145, v178
	v_mov_b32_e32 v2, v173
	v_mov_b32_e32 v3, v175
	v_mov_b32_e32 v4, v177
	v_mov_b32_e32 v5, v179
.Lmyf_B1_7:
	s_mov_b64 exec, -1
	s_waitcnt lgkmcnt(0)
	v_cvt_f16_f32_e32 v183, s27
	v_cvt_f16_f32_e32 v185, s26
	v_cvt_f16_f32_e32 v184, s34
	s_mov_b64 s[4:5], 0
	s_waitcnt vmcnt(3)
	v_pk_mul_f16 v193, v185, v189 op_sel_hi:[0,1]
	v_pk_mul_f16 v197, v183, v189 op_sel_hi:[0,1]
	v_pk_mul_f16 v201, v184, v189 op_sel_hi:[0,1]
	v_pk_mul_f16 v190, v185, v186 op_sel_hi:[0,1]
	v_pk_mul_f16 v191, v185, v187 op_sel_hi:[0,1]
	v_pk_mul_f16 v192, v185, v188 op_sel_hi:[0,1]
	v_pk_mul_f16 v194, v183, v186 op_sel_hi:[0,1]
	s_mov_b64 exec, s[64:65]
	buffer_load_dwordx4 v[18:21], v249, s[16:19], 0 offen
	buffer_load_dwordx4 v[6:9], v249, s[16:19], 0 offen offset:512
	s_mov_b64 exec, -1
	v_pk_mul_f16 v195, v183, v187 op_sel_hi:[0,1]
	v_pk_mul_f16 v196, v183, v188 op_sel_hi:[0,1]
	v_pk_mul_f16 v198, v184, v186 op_sel_hi:[0,1]
	v_pk_mul_f16 v199, v184, v187 op_sel_hi:[0,1]
	v_pk_mul_f16 v200, v184, v188 op_sel_hi:[0,1]
	v_pk_fma_f16 v113, v113, v189, v193
	v_pk_fma_f16 v129, v129, v189, v197
	v_pk_fma_f16 v137, v137, v189, v201
	v_pk_fma_f16 v202, v85, v189, v193
	v_pk_fma_f16 v206, v109, v189, v197
	v_pk_fma_f16 v210, v125, v189, v201
	v_pk_fma_f16 v193, v53, v189, v193
	v_pk_fma_f16 v197, v69, v189, v197
	buffer_load_dwordx4 v[34:37], v250, s[16:19], 0 offen offset:512
	buffer_load_dwordx4 v[10:13], v250, s[16:19], 0 offen offset:1024
	v_pk_fma_f16 v189, v97, v189, v201
	v_pk_maximum3_f16 v201, v113, v129, v137
	v_pk_fma_f16 v112, v112, v188, v192
	v_pk_fma_f16 v111, v111, v187, v191
	v_pk_fma_f16 v110, v110, v186, v190
	v_pk_fma_f16 v128, v128, v188, v196
	v_pk_fma_f16 v127, v127, v187, v195
	v_pk_fma_f16 v126, v126, v186, v194
	v_pk_fma_f16 v136, v136, v188, v200
	v_pk_fma_f16 v135, v135, v187, v199
	v_pk_fma_f16 v134, v134, v186, v198
	v_pk_fma_f16 v203, v84, v188, v192
	v_pk_fma_f16 v204, v83, v187, v191
	v_pk_fma_f16 v205, v82, v186, v190
	v_pk_fma_f16 v207, v108, v188, v196
	v_pk_fma_f16 v208, v107, v187, v195
	s_mov_b64 exec, s[66:67]
	buffer_load_dwordx4 v[54:57], v250, s[16:19], 0 offen offset:2048
	buffer_load_dwordx4 v[14:17], v250, s[16:19], 0 offen offset:2560
	s_mov_b64 exec, -1
	v_pk_fma_f16 v209, v106, v186, v194
	v_pk_fma_f16 v211, v124, v188, v200
	v_pk_fma_f16 v212, v123, v187, v199
	v_pk_fma_f16 v213, v122, v186, v198
	v_pk_fma_f16 v192, v52, v188, v192
	v_pk_fma_f16 v191, v51, v187, v191
	v_pk_fma_f16 v190, v50, v186, v190
	v_pk_fma_f16 v196, v68, v188, v196
	v_pk_fma_f16 v195, v67, v187, v195
	v_pk_fma_f16 v194, v66, v186, v194
	v_pk_fma_f16 v188, v96, v188, v200
	v_pk_fma_f16 v187, v95, v187, v199
	v_pk_fma_f16 v186, v94, v186, v198
	v_pk_maximum3_f16 v198, v110, v126, v134
	v_pk_maximum3_f16 v199, v111, v127, v135
	v_pk_maximum3_f16 v200, v112, v128, v136
	v_pk_maximum3_f16 v217, v202, v206, v210
	v_pk_maximum3_f16 v221, v193, v197, v189
	v_pk_maximum3_f16 v214, v205, v209, v213
	v_pk_maximum3_f16 v215, v204, v208, v212
	v_pk_maximum3_f16 v216, v203, v207, v211
	v_pk_maximum3_f16 v218, v190, v194, v186
	v_pk_maximum3_f16 v219, v191, v195, v187
	v_pk_maximum3_f16 v201, v201, v217, v221
	v_pk_maximum3_f16 v220, v192, v196, v188
	v_pk_maximum3_f16 v198, v198, v214, v218
	v_pk_maximum3_f16 v199, v199, v215, v219
	v_pk_maximum3_f16 v200, v200, v216, v220
	v_pk_add_f16 v113, v113, v201 neg_lo:[0,1] neg_hi:[0,1]
	s_mov_b64 exec, s[64:65]
	buffer_load_dwordx4 v[74:77], v251, s[16:19], 0 offen
	buffer_load_dwordx4 v[26:29], v251, s[16:19], 0 offen offset:512
	s_mov_b64 exec, -1
	v_pk_add_f16 v110, v110, v198 neg_lo:[0,1] neg_hi:[0,1]
	v_pk_add_f16 v111, v111, v199 neg_lo:[0,1] neg_hi:[0,1]
	v_pk_add_f16 v112, v112, v200 neg_lo:[0,1] neg_hi:[0,1]
	v_pk_add_f16 v126, v126, v198 neg_lo:[0,1] neg_hi:[0,1]
	v_exp_f16_sdwa v214, v110 dst_sel:WORD_0 dst_unused:UNUSED_PAD src0_sel:WORD_0
	v_exp_f16_sdwa v215, v111 dst_sel:WORD_0 dst_unused:UNUSED_PAD src0_sel:WORD_0
	v_exp_f16_sdwa v216, v112 dst_sel:WORD_0 dst_unused:UNUSED_PAD src0_sel:WORD_0
	v_exp_f16_sdwa v217, v113 dst_sel:WORD_0 dst_unused:UNUSED_PAD src0_sel:WORD_0
	v_exp_f16_sdwa v214, v110 dst_sel:WORD_1 dst_unused:UNUSED_PRESERVE src0_sel:WORD_1
	v_exp_f16_sdwa v215, v111 dst_sel:WORD_1 dst_unused:UNUSED_PRESERVE src0_sel:WORD_1
	v_exp_f16_sdwa v216, v112 dst_sel:WORD_1 dst_unused:UNUSED_PRESERVE src0_sel:WORD_1
	v_exp_f16_sdwa v217, v113 dst_sel:WORD_1 dst_unused:UNUSED_PRESERVE src0_sel:WORD_1
	v_pk_add_f16 v127, v127, v199 neg_lo:[0,1] neg_hi:[0,1]
	v_pk_add_f16 v113, v214, 0
	v_pk_fma_f16 v73, v73, v217, 0
	v_pk_add_f16 v110, v217, 0
	v_pk_add_f16 v111, v216, 0
	v_pk_add_f16 v112, v215, 0
	v_pk_fma_f16 v72, v72, v216, 0
	v_pk_fma_f16 v71, v71, v215, 0
	v_pk_fma_f16 v70, v70, v214, 0
	v_pk_add_f16 v128, v128, v200 neg_lo:[0,1] neg_hi:[0,1]
	buffer_load_dwordx4 v[102:105], v252, s[16:19], 0 offen offset:512
	buffer_load_dwordx4 v[38:41], v252, s[16:19], 0 offen offset:1024
	v_pk_add_f16 v129, v129, v201 neg_lo:[0,1] neg_hi:[0,1]
	v_exp_f16_sdwa v214, v126 dst_sel:WORD_0 dst_unused:UNUSED_PAD src0_sel:WORD_0
	v_exp_f16_sdwa v215, v127 dst_sel:WORD_0 dst_unused:UNUSED_PAD src0_sel:WORD_0
	v_exp_f16_sdwa v216, v128 dst_sel:WORD_0 dst_unused:UNUSED_PAD src0_sel:WORD_0
	v_exp_f16_sdwa v217, v129 dst_sel:WORD_0 dst_unused:UNUSED_PAD src0_sel:WORD_0
	v_exp_f16_sdwa v214, v126 dst_sel:WORD_1 dst_unused:UNUSED_PRESERVE src0_sel:WORD_1
	v_exp_f16_sdwa v215, v127 dst_sel:WORD_1 dst_unused:UNUSED_PRESERVE src0_sel:WORD_1
	v_exp_f16_sdwa v216, v128 dst_sel:WORD_1 dst_unused:UNUSED_PRESERVE src0_sel:WORD_1
	v_exp_f16_sdwa v217, v129 dst_sel:WORD_1 dst_unused:UNUSED_PRESERVE src0_sel:WORD_1
	v_pk_add_f16 v113, v113, v214
	v_pk_fma_f16 v73, v101, v217, v73
	v_pk_add_f16 v101, v137, v201 neg_lo:[0,1] neg_hi:[0,1]
	v_pk_add_f16 v112, v112, v215
	v_pk_add_f16 v111, v111, v216
	v_pk_add_f16 v110, v110, v217
	v_pk_fma_f16 v70, v98, v214, v70
	v_pk_fma_f16 v71, v99, v215, v71
	v_pk_fma_f16 v72, v100, v216, v72
	v_pk_add_f16 v98, v134, v198 neg_lo:[0,1] neg_hi:[0,1]
	v_pk_add_f16 v99, v135, v199 neg_lo:[0,1] neg_hi:[0,1]
	v_pk_add_f16 v100, v136, v200 neg_lo:[0,1] neg_hi:[0,1]
	v_exp_f16_sdwa v126, v98 dst_sel:WORD_0 dst_unused:UNUSED_PAD src0_sel:WORD_0
	v_exp_f16_sdwa v127, v99 dst_sel:WORD_0 dst_unused:UNUSED_PAD src0_sel:WORD_0
	v_exp_f16_sdwa v128, v100 dst_sel:WORD_0 dst_unused:UNUSED_PAD src0_sel:WORD_0
	v_exp_f16_sdwa v129, v101 dst_sel:WORD_0 dst_unused:UNUSED_PAD src0_sel:WORD_0
	v_exp_f16_sdwa v126, v98 dst_sel:WORD_1 dst_unused:UNUSED_PRESERVE src0_sel:WORD_1
	v_exp_f16_sdwa v127, v99 dst_sel:WORD_1 dst_unused:UNUSED_PRESERVE src0_sel:WORD_1
	v_exp_f16_sdwa v128, v100 dst_sel:WORD_1 dst_unused:UNUSED_PRESERVE src0_sel:WORD_1
	v_exp_f16_sdwa v129, v101 dst_sel:WORD_1 dst_unused:UNUSED_PRESERVE src0_sel:WORD_1
	v_pk_add_f16 v101, v113, v126
	v_pk_add_f16 v98, v110, v129
	s_mov_b64 exec, s[66:67]
	buffer_load_dwordx4 v[118:121], v252, s[16:19], 0 offen offset:2048
	buffer_load_dwordx4 v[58:61], v252, s[16:19], 0 offen offset:2560
	s_mov_b64 exec, -1
	v_pk_add_f16 v99, v111, v128
	v_pk_add_f16 v100, v112, v127
	v_pk_fma_f16 v73, v117, v129, v73
	v_pk_fma_f16 v72, v116, v128, v72
	v_pk_fma_f16 v71, v115, v127, v71
	v_pk_fma_f16 v70, v114, v126, v70
	v_pk_add_f16 v110, v205, v198 neg_lo:[0,1] neg_hi:[0,1]
	v_pk_add_f16 v111, v204, v199 neg_lo:[0,1] neg_hi:[0,1]
	v_pk_add_f16 v112, v203, v200 neg_lo:[0,1] neg_hi:[0,1]
	v_pk_add_f16 v113, v202, v201 neg_lo:[0,1] neg_hi:[0,1]
	v_exp_f16_sdwa v114, v110 dst_sel:WORD_0 dst_unused:UNUSED_PAD src0_sel:WORD_0
	v_exp_f16_sdwa v115, v111 dst_sel:WORD_0 dst_unused:UNUSED_PAD src0_sel:WORD_0
	v_exp_f16_sdwa v116, v112 dst_sel:WORD_0 dst_unused:UNUSED_PAD src0_sel:WORD_0
	v_exp_f16_sdwa v117, v113 dst_sel:WORD_0 dst_unused:UNUSED_PAD src0_sel:WORD_0
	v_exp_f16_sdwa v114, v110 dst_sel:WORD_1 dst_unused:UNUSED_PRESERVE src0_sel:WORD_1
	v_exp_f16_sdwa v115, v111 dst_sel:WORD_1 dst_unused:UNUSED_PRESERVE src0_sel:WORD_1
	v_exp_f16_sdwa v116, v112 dst_sel:WORD_1 dst_unused:UNUSED_PRESERVE src0_sel:WORD_1
	v_exp_f16_sdwa v117, v113 dst_sel:WORD_1 dst_unused:UNUSED_PRESERVE src0_sel:WORD_1
	v_pk_add_f16 v110, v209, v198 neg_lo:[0,1] neg_hi:[0,1]
	v_pk_add_f16 v101, v101, v114
	v_pk_add_f16 v100, v100, v115
	v_pk_add_f16 v99, v99, v116
	s_mov_b64 exec, s[76:77]
	buffer_load_dwordx4 v[130:133], v253, s[16:19], 0 offen
	buffer_load_dwordx4 v[78:81], v253, s[16:19], 0 offen offset:512
	s_mov_b64 exec, -1
	v_pk_add_f16 v98, v98, v117
	v_pk_fma_f16 v70, v42, v114, v70
	v_pk_fma_f16 v71, v43, v115, v71
	v_pk_fma_f16 v72, v44, v116, v72
	v_pk_fma_f16 v73, v45, v117, v73
	v_pk_add_f16 v111, v208, v199 neg_lo:[0,1] neg_hi:[0,1]
	v_pk_add_f16 v112, v207, v200 neg_lo:[0,1] neg_hi:[0,1]
	v_pk_add_f16 v113, v206, v201 neg_lo:[0,1] neg_hi:[0,1]
	v_exp_f16_sdwa v114, v110 dst_sel:WORD_0 dst_unused:UNUSED_PAD src0_sel:WORD_0
	v_exp_f16_sdwa v115, v111 dst_sel:WORD_0 dst_unused:UNUSED_PAD src0_sel:WORD_0
	v_exp_f16_sdwa v116, v112 dst_sel:WORD_0 dst_unused:UNUSED_PAD src0_sel:WORD_0
	v_exp_f16_sdwa v117, v113 dst_sel:WORD_0 dst_unused:UNUSED_PAD src0_sel:WORD_0
	v_exp_f16_sdwa v114, v110 dst_sel:WORD_1 dst_unused:UNUSED_PRESERVE src0_sel:WORD_1
	v_exp_f16_sdwa v115, v111 dst_sel:WORD_1 dst_unused:UNUSED_PRESERVE src0_sel:WORD_1
	v_exp_f16_sdwa v116, v112 dst_sel:WORD_1 dst_unused:UNUSED_PRESERVE src0_sel:WORD_1
	v_exp_f16_sdwa v117, v113 dst_sel:WORD_1 dst_unused:UNUSED_PRESERVE src0_sel:WORD_1
	v_pk_add_f16 v110, v213, v198 neg_lo:[0,1] neg_hi:[0,1]
	v_pk_add_f16 v101, v101, v114
	v_pk_add_f16 v98, v98, v117
	v_pk_add_f16 v99, v99, v116
	v_pk_add_f16 v100, v100, v115
	v_pk_fma_f16 v73, v65, v117, v73
	v_pk_fma_f16 v72, v64, v116, v72
	s_mov_b64 exec, s[70:71]
	buffer_load_dwordx4 v[138:141], v254, s[16:19], 0 offen offset:512
	buffer_load_dwordx4 v[90:93], v254, s[16:19], 0 offen offset:1024
	s_mov_b64 exec, -1
	v_pk_fma_f16 v71, v63, v115, v71
	v_pk_fma_f16 v70, v62, v114, v70
	v_pk_add_f16 v111, v212, v199 neg_lo:[0,1] neg_hi:[0,1]
	v_pk_add_f16 v112, v211, v200 neg_lo:[0,1] neg_hi:[0,1]
	v_pk_add_f16 v113, v210, v201 neg_lo:[0,1] neg_hi:[0,1]
	v_exp_f16_sdwa v114, v110 dst_sel:WORD_0 dst_unused:UNUSED_PAD src0_sel:WORD_0
	v_exp_f16_sdwa v115, v111 dst_sel:WORD_0 dst_unused:UNUSED_PAD src0_sel:WORD_0
	v_exp_f16_sdwa v116, v112 dst_sel:WORD_0 dst_unused:UNUSED_PAD src0_sel:WORD_0
	v_exp_f16_sdwa v117, v113 dst_sel:WORD_0 dst_unused:UNUSED_PAD src0_sel:WORD_0
	v_exp_f16_sdwa v114, v110 dst_sel:WORD_1 dst_unused:UNUSED_PRESERVE src0_sel:WORD_1
	v_exp_f16_sdwa v115, v111 dst_sel:WORD_1 dst_unused:UNUSED_PRESERVE src0_sel:WORD_1
	v_exp_f16_sdwa v116, v112 dst_sel:WORD_1 dst_unused:UNUSED_PRESERVE src0_sel:WORD_1
	v_exp_f16_sdwa v117, v113 dst_sel:WORD_1 dst_unused:UNUSED_PRESERVE src0_sel:WORD_1
	v_pk_add_f16 v110, v190, v198 neg_lo:[0,1] neg_hi:[0,1]
	v_pk_add_f16 v101, v101, v114
	v_pk_add_f16 v100, v100, v115
	v_pk_add_f16 v99, v99, v116
	v_pk_add_f16 v98, v98, v117
	v_pk_fma_f16 v70, v86, v114, v70
	v_pk_fma_f16 v71, v87, v115, v71
	v_pk_fma_f16 v72, v88, v116, v72
	v_pk_fma_f16 v73, v89, v117, v73
	s_mov_b64 exec, s[78:79]
	buffer_load_dwordx4 v[142:145], v254, s[16:19], 0 offen offset:2048
	buffer_load_dwordx4 v[2:5], v254, s[16:19], 0 offen offset:2560
	s_mov_b64 exec, -1
	v_pk_add_f16 v111, v191, v199 neg_lo:[0,1] neg_hi:[0,1]
	v_pk_add_f16 v112, v192, v200 neg_lo:[0,1] neg_hi:[0,1]
	v_pk_add_f16 v113, v193, v201 neg_lo:[0,1] neg_hi:[0,1]
	v_exp_f16_sdwa v114, v110 dst_sel:WORD_0 dst_unused:UNUSED_PAD src0_sel:WORD_0
	v_exp_f16_sdwa v115, v111 dst_sel:WORD_0 dst_unused:UNUSED_PAD src0_sel:WORD_0
	v_exp_f16_sdwa v116, v112 dst_sel:WORD_0 dst_unused:UNUSED_PAD src0_sel:WORD_0
	v_exp_f16_sdwa v117, v113 dst_sel:WORD_0 dst_unused:UNUSED_PAD src0_sel:WORD_0
	v_exp_f16_sdwa v114, v110 dst_sel:WORD_1 dst_unused:UNUSED_PRESERVE src0_sel:WORD_1
	v_exp_f16_sdwa v115, v111 dst_sel:WORD_1 dst_unused:UNUSED_PRESERVE src0_sel:WORD_1
	v_exp_f16_sdwa v116, v112 dst_sel:WORD_1 dst_unused:UNUSED_PRESERVE src0_sel:WORD_1
	v_exp_f16_sdwa v117, v113 dst_sel:WORD_1 dst_unused:UNUSED_PRESERVE src0_sel:WORD_1
	v_pk_add_f16 v110, v194, v198 neg_lo:[0,1] neg_hi:[0,1]
	v_pk_add_f16 v101, v101, v114
	v_pk_add_f16 v98, v98, v117
	v_pk_add_f16 v99, v99, v116
	v_pk_add_f16 v100, v100, v115
	v_pk_fma_f16 v73, v25, v117, v73
	v_pk_fma_f16 v72, v24, v116, v72
	v_pk_fma_f16 v71, v23, v115, v71
	v_pk_fma_f16 v70, v22, v114, v70
	v_pk_add_f16 v111, v195, v199 neg_lo:[0,1] neg_hi:[0,1]
	v_pk_add_f16 v112, v196, v200 neg_lo:[0,1] neg_hi:[0,1]
	v_pk_add_f16 v113, v197, v201 neg_lo:[0,1] neg_hi:[0,1]
	v_exp_f16_sdwa v114, v110 dst_sel:WORD_0 dst_unused:UNUSED_PAD src0_sel:WORD_0
	v_exp_f16_sdwa v115, v111 dst_sel:WORD_0 dst_unused:UNUSED_PAD src0_sel:WORD_0
	v_exp_f16_sdwa v116, v112 dst_sel:WORD_0 dst_unused:UNUSED_PAD src0_sel:WORD_0
	v_exp_f16_sdwa v117, v113 dst_sel:WORD_0 dst_unused:UNUSED_PAD src0_sel:WORD_0
	v_exp_f16_sdwa v114, v110 dst_sel:WORD_1 dst_unused:UNUSED_PRESERVE src0_sel:WORD_1
	v_exp_f16_sdwa v115, v111 dst_sel:WORD_1 dst_unused:UNUSED_PRESERVE src0_sel:WORD_1
	v_exp_f16_sdwa v116, v112 dst_sel:WORD_1 dst_unused:UNUSED_PRESERVE src0_sel:WORD_1
	v_exp_f16_sdwa v117, v113 dst_sel:WORD_1 dst_unused:UNUSED_PRESERVE src0_sel:WORD_1
	v_pk_add_f16 v110, v186, v198 neg_lo:[0,1] neg_hi:[0,1]
	v_pk_add_f16 v101, v101, v114
	v_pk_add_f16 v100, v100, v115
	v_pk_add_f16 v99, v99, v116
	v_pk_add_f16 v98, v98, v117
	v_pk_fma_f16 v70, v30, v114, v70
	v_pk_fma_f16 v71, v31, v115, v71
	v_pk_fma_f16 v72, v32, v116, v72
	v_pk_fma_f16 v73, v33, v117, v73
	v_pk_add_f16 v111, v187, v199 neg_lo:[0,1] neg_hi:[0,1]
	v_pk_add_f16 v112, v188, v200 neg_lo:[0,1] neg_hi:[0,1]
	v_pk_add_f16 v113, v189, v201 neg_lo:[0,1] neg_hi:[0,1]
	v_exp_f16_sdwa v114, v110 dst_sel:WORD_0 dst_unused:UNUSED_PAD src0_sel:WORD_0
	v_exp_f16_sdwa v115, v111 dst_sel:WORD_0 dst_unused:UNUSED_PAD src0_sel:WORD_0
	v_exp_f16_sdwa v116, v112 dst_sel:WORD_0 dst_unused:UNUSED_PAD src0_sel:WORD_0
	v_exp_f16_sdwa v117, v113 dst_sel:WORD_0 dst_unused:UNUSED_PAD src0_sel:WORD_0
	v_exp_f16_sdwa v114, v110 dst_sel:WORD_1 dst_unused:UNUSED_PRESERVE src0_sel:WORD_1
	v_exp_f16_sdwa v115, v111 dst_sel:WORD_1 dst_unused:UNUSED_PRESERVE src0_sel:WORD_1
	v_exp_f16_sdwa v116, v112 dst_sel:WORD_1 dst_unused:UNUSED_PRESERVE src0_sel:WORD_1
	v_exp_f16_sdwa v117, v113 dst_sel:WORD_1 dst_unused:UNUSED_PRESERVE src0_sel:WORD_1
	v_pk_add_f16 v101, v101, v114
	v_pk_add_f16 v100, v100, v115
	v_rcp_f16_e32 v110, v101
	v_rcp_f16_sdwa v101, v101 dst_sel:DWORD dst_unused:UNUSED_PAD src0_sel:WORD_1
	v_pk_add_f16 v99, v99, v116
	v_rcp_f16_e32 v111, v100
	v_rcp_f16_sdwa v100, v100 dst_sel:DWORD dst_unused:UNUSED_PAD src0_sel:WORD_1
	v_pk_add_f16 v98, v98, v117
	v_rcp_f16_e32 v112, v99
	v_rcp_f16_sdwa v99, v99 dst_sel:DWORD dst_unused:UNUSED_PAD src0_sel:WORD_1
	v_rcp_f16_e32 v113, v98
	v_rcp_f16_sdwa v98, v98 dst_sel:DWORD dst_unused:UNUSED_PAD src0_sel:WORD_1
	v_pk_fma_f16 v70, v46, v114, v70
	v_pack_b32_f16 v101, v110, v101
	v_pk_fma_f16 v71, v47, v115, v71
	v_pk_mul_f16 v110, v70, v101
	v_pack_b32_f16 v70, v111, v100
	v_pk_fma_f16 v72, v48, v116, v72
	v_pk_mul_f16 v111, v71, v70
	v_pack_b32_f16 v70, v112, v99
	v_pk_fma_f16 v73, v49, v117, v73
	v_pk_mul_f16 v112, v72, v70
	v_pack_b32_f16 v70, v113, v98
	v_pk_mul_f16 v113, v73, v70
	s_waitcnt vmcnt(12)
	v_pk_mul_f16 v73, v185, v157 op_sel_hi:[0,1]
	v_pk_mul_f16 v101, v183, v157 op_sel_hi:[0,1]
	v_pk_mul_f16 v117, v184, v157 op_sel_hi:[0,1]
	v_pk_mul_f16 v70, v185, v154 op_sel_hi:[0,1]
	v_pk_mul_f16 v71, v185, v155 op_sel_hi:[0,1]
	v_pk_mul_f16 v72, v185, v156 op_sel_hi:[0,1]
	v_pk_mul_f16 v98, v183, v154 op_sel_hi:[0,1]
	v_pk_mul_f16 v99, v183, v155 op_sel_hi:[0,1]
	v_pk_mul_f16 v100, v183, v156 op_sel_hi:[0,1]
	v_pk_mul_f16 v114, v184, v154 op_sel_hi:[0,1]
	v_pk_mul_f16 v115, v184, v155 op_sel_hi:[0,1]
	v_pk_mul_f16 v116, v184, v156 op_sel_hi:[0,1]
	v_pk_fma_f16 v85, v85, v157, v73
	v_pk_fma_f16 v109, v109, v157, v101
	v_pk_fma_f16 v125, v125, v157, v117
	v_pk_fma_f16 v126, v53, v157, v73
	v_pk_fma_f16 v134, v69, v157, v101
	v_pk_fma_f16 v186, v97, v157, v117
	v_pk_fma_f16 v73, v21, v157, v73
	v_pk_fma_f16 v101, v37, v157, v101
	v_pk_fma_f16 v117, v57, v157, v117
	v_pk_maximum3_f16 v157, v85, v109, v125
	v_pk_fma_f16 v84, v84, v156, v72
	v_pk_fma_f16 v83, v83, v155, v71
	v_pk_fma_f16 v82, v82, v154, v70
	v_pk_fma_f16 v108, v108, v156, v100
	v_pk_fma_f16 v107, v107, v155, v99
	v_pk_fma_f16 v106, v106, v154, v98
	v_pk_fma_f16 v124, v124, v156, v116
	v_pk_fma_f16 v123, v123, v155, v115
	v_pk_fma_f16 v122, v122, v154, v114
	v_pk_fma_f16 v127, v52, v156, v72
	v_pk_fma_f16 v128, v51, v155, v71
	v_pk_fma_f16 v129, v50, v154, v70
	v_pk_fma_f16 v135, v68, v156, v100
	v_pk_fma_f16 v136, v67, v155, v99
	v_pk_fma_f16 v137, v66, v154, v98
	v_pk_fma_f16 v187, v96, v156, v116
	v_pk_fma_f16 v188, v95, v155, v115
	v_pk_fma_f16 v189, v94, v154, v114
	v_pk_fma_f16 v72, v20, v156, v72
	v_pk_fma_f16 v71, v19, v155, v71
	v_pk_fma_f16 v70, v18, v154, v70
	v_pk_fma_f16 v100, v36, v156, v100
	v_pk_fma_f16 v99, v35, v155, v99
	v_pk_fma_f16 v98, v34, v154, v98
	v_pk_fma_f16 v116, v56, v156, v116
	v_pk_fma_f16 v115, v55, v155, v115
	v_pk_fma_f16 v114, v54, v154, v114
	v_pk_maximum3_f16 v154, v82, v106, v122
	v_pk_maximum3_f16 v155, v83, v107, v123
	v_pk_maximum3_f16 v156, v84, v108, v124
	v_pk_maximum3_f16 v193, v126, v134, v186
	v_pk_maximum3_f16 v197, v73, v101, v117
	v_pk_maximum3_f16 v190, v129, v137, v189
	v_pk_maximum3_f16 v191, v128, v136, v188
	v_pk_maximum3_f16 v192, v127, v135, v187
	v_pk_maximum3_f16 v194, v70, v98, v114
	v_pk_maximum3_f16 v195, v71, v99, v115
	v_pk_maximum3_f16 v157, v157, v193, v197
	v_pk_maximum3_f16 v196, v72, v100, v116
	v_pk_maximum3_f16 v154, v154, v190, v194
	v_pk_maximum3_f16 v155, v155, v191, v195
	v_pk_maximum3_f16 v156, v156, v192, v196
	v_pk_add_f16 v85, v85, v157 neg_lo:[0,1] neg_hi:[0,1]
	v_pk_add_f16 v82, v82, v154 neg_lo:[0,1] neg_hi:[0,1]
	v_pk_add_f16 v83, v83, v155 neg_lo:[0,1] neg_hi:[0,1]
	v_pk_add_f16 v84, v84, v156 neg_lo:[0,1] neg_hi:[0,1]
	v_pk_add_f16 v106, v106, v154 neg_lo:[0,1] neg_hi:[0,1]
	v_exp_f16_sdwa v190, v82 dst_sel:WORD_0 dst_unused:UNUSED_PAD src0_sel:WORD_0
	v_exp_f16_sdwa v191, v83 dst_sel:WORD_0 dst_unused:UNUSED_PAD src0_sel:WORD_0
	v_exp_f16_sdwa v192, v84 dst_sel:WORD_0 dst_unused:UNUSED_PAD src0_sel:WORD_0
	v_exp_f16_sdwa v193, v85 dst_sel:WORD_0 dst_unused:UNUSED_PAD src0_sel:WORD_0
	v_exp_f16_sdwa v190, v82 dst_sel:WORD_1 dst_unused:UNUSED_PRESERVE src0_sel:WORD_1
	v_exp_f16_sdwa v191, v83 dst_sel:WORD_1 dst_unused:UNUSED_PRESERVE src0_sel:WORD_1
	v_exp_f16_sdwa v192, v84 dst_sel:WORD_1 dst_unused:UNUSED_PRESERVE src0_sel:WORD_1
	v_exp_f16_sdwa v193, v85 dst_sel:WORD_1 dst_unused:UNUSED_PRESERVE src0_sel:WORD_1
	v_pk_add_f16 v107, v107, v155 neg_lo:[0,1] neg_hi:[0,1]
	v_pk_add_f16 v85, v190, 0
	v_pk_fma_f16 v45, v45, v193, 0
	v_pk_add_f16 v82, v193, 0
	v_pk_add_f16 v83, v192, 0
	v_pk_add_f16 v84, v191, 0
	v_pk_fma_f16 v44, v44, v192, 0
	v_pk_fma_f16 v43, v43, v191, 0
	v_pk_fma_f16 v42, v42, v190, 0
	v_pk_add_f16 v108, v108, v156 neg_lo:[0,1] neg_hi:[0,1]
	v_pk_add_f16 v109, v109, v157 neg_lo:[0,1] neg_hi:[0,1]
	v_pk_add_f16 v70, v70, v154 neg_lo:[0,1] neg_hi:[0,1]
	v_exp_f16_sdwa v190, v106 dst_sel:WORD_0 dst_unused:UNUSED_PAD src0_sel:WORD_0
	v_exp_f16_sdwa v191, v107 dst_sel:WORD_0 dst_unused:UNUSED_PAD src0_sel:WORD_0
	v_exp_f16_sdwa v192, v108 dst_sel:WORD_0 dst_unused:UNUSED_PAD src0_sel:WORD_0
	v_exp_f16_sdwa v193, v109 dst_sel:WORD_0 dst_unused:UNUSED_PAD src0_sel:WORD_0
	v_exp_f16_sdwa v190, v106 dst_sel:WORD_1 dst_unused:UNUSED_PRESERVE src0_sel:WORD_1
	v_exp_f16_sdwa v191, v107 dst_sel:WORD_1 dst_unused:UNUSED_PRESERVE src0_sel:WORD_1
	v_exp_f16_sdwa v192, v108 dst_sel:WORD_1 dst_unused:UNUSED_PRESERVE src0_sel:WORD_1
	v_exp_f16_sdwa v193, v109 dst_sel:WORD_1 dst_unused:UNUSED_PRESERVE src0_sel:WORD_1
	v_pk_add_f16 v71, v71, v155 neg_lo:[0,1] neg_hi:[0,1]
	v_pk_add_f16 v85, v85, v190
	v_pk_fma_f16 v45, v65, v193, v45
	v_pk_add_f16 v65, v125, v157 neg_lo:[0,1] neg_hi:[0,1]
	v_pk_add_f16 v84, v84, v191
	v_pk_add_f16 v83, v83, v192
	v_pk_add_f16 v82, v82, v193
	v_pk_fma_f16 v42, v62, v190, v42
	v_pk_fma_f16 v43, v63, v191, v43
	v_pk_fma_f16 v44, v64, v192, v44
	v_pk_add_f16 v62, v122, v154 neg_lo:[0,1] neg_hi:[0,1]
	v_pk_add_f16 v63, v123, v155 neg_lo:[0,1] neg_hi:[0,1]
	v_pk_add_f16 v64, v124, v156 neg_lo:[0,1] neg_hi:[0,1]
	v_pk_add_f16 v72, v72, v156 neg_lo:[0,1] neg_hi:[0,1]
	v_exp_f16_sdwa v106, v62 dst_sel:WORD_0 dst_unused:UNUSED_PAD src0_sel:WORD_0
	v_exp_f16_sdwa v107, v63 dst_sel:WORD_0 dst_unused:UNUSED_PAD src0_sel:WORD_0
	v_exp_f16_sdwa v108, v64 dst_sel:WORD_0 dst_unused:UNUSED_PAD src0_sel:WORD_0
	v_exp_f16_sdwa v109, v65 dst_sel:WORD_0 dst_unused:UNUSED_PAD src0_sel:WORD_0
	v_exp_f16_sdwa v106, v62 dst_sel:WORD_1 dst_unused:UNUSED_PRESERVE src0_sel:WORD_1
	v_exp_f16_sdwa v107, v63 dst_sel:WORD_1 dst_unused:UNUSED_PRESERVE src0_sel:WORD_1
	v_exp_f16_sdwa v108, v64 dst_sel:WORD_1 dst_unused:UNUSED_PRESERVE src0_sel:WORD_1
	v_exp_f16_sdwa v109, v65 dst_sel:WORD_1 dst_unused:UNUSED_PRESERVE src0_sel:WORD_1
	v_pk_add_f16 v73, v73, v157 neg_lo:[0,1] neg_hi:[0,1]
	v_pk_add_f16 v65, v85, v106
	v_pk_add_f16 v62, v82, v109
	v_pk_add_f16 v63, v83, v108
	v_pk_add_f16 v64, v84, v107
	v_pk_fma_f16 v45, v89, v109, v45
	v_pk_fma_f16 v44, v88, v108, v44
	v_pk_fma_f16 v43, v87, v107, v43
	v_pk_fma_f16 v42, v86, v106, v42
	v_pk_add_f16 v82, v129, v154 neg_lo:[0,1] neg_hi:[0,1]
	v_pk_add_f16 v83, v128, v155 neg_lo:[0,1] neg_hi:[0,1]
	v_pk_add_f16 v84, v127, v156 neg_lo:[0,1] neg_hi:[0,1]
	v_pk_add_f16 v85, v126, v157 neg_lo:[0,1] neg_hi:[0,1]
	v_exp_f16_sdwa v86, v82 dst_sel:WORD_0 dst_unused:UNUSED_PAD src0_sel:WORD_0
	v_exp_f16_sdwa v87, v83 dst_sel:WORD_0 dst_unused:UNUSED_PAD src0_sel:WORD_0
	v_exp_f16_sdwa v88, v84 dst_sel:WORD_0 dst_unused:UNUSED_PAD src0_sel:WORD_0
	v_exp_f16_sdwa v89, v85 dst_sel:WORD_0 dst_unused:UNUSED_PAD src0_sel:WORD_0
	v_exp_f16_sdwa v86, v82 dst_sel:WORD_1 dst_unused:UNUSED_PRESERVE src0_sel:WORD_1
	v_exp_f16_sdwa v87, v83 dst_sel:WORD_1 dst_unused:UNUSED_PRESERVE src0_sel:WORD_1
	v_exp_f16_sdwa v88, v84 dst_sel:WORD_1 dst_unused:UNUSED_PRESERVE src0_sel:WORD_1
	v_exp_f16_sdwa v89, v85 dst_sel:WORD_1 dst_unused:UNUSED_PRESERVE src0_sel:WORD_1
	v_pk_add_f16 v82, v137, v154 neg_lo:[0,1] neg_hi:[0,1]
	v_pk_add_f16 v65, v65, v86
	v_pk_add_f16 v64, v64, v87
	v_pk_add_f16 v63, v63, v88
	v_pk_add_f16 v62, v62, v89
	v_pk_fma_f16 v42, v22, v86, v42
	v_pk_fma_f16 v43, v23, v87, v43
	v_pk_fma_f16 v44, v24, v88, v44
	v_pk_fma_f16 v45, v25, v89, v45
	v_pk_add_f16 v83, v136, v155 neg_lo:[0,1] neg_hi:[0,1]
	v_pk_add_f16 v84, v135, v156 neg_lo:[0,1] neg_hi:[0,1]
	v_pk_add_f16 v85, v134, v157 neg_lo:[0,1] neg_hi:[0,1]
	v_exp_f16_sdwa v86, v82 dst_sel:WORD_0 dst_unused:UNUSED_PAD src0_sel:WORD_0
	v_exp_f16_sdwa v87, v83 dst_sel:WORD_0 dst_unused:UNUSED_PAD src0_sel:WORD_0
	v_exp_f16_sdwa v88, v84 dst_sel:WORD_0 dst_unused:UNUSED_PAD src0_sel:WORD_0
	v_exp_f16_sdwa v89, v85 dst_sel:WORD_0 dst_unused:UNUSED_PAD src0_sel:WORD_0
	v_exp_f16_sdwa v86, v82 dst_sel:WORD_1 dst_unused:UNUSED_PRESERVE src0_sel:WORD_1
	v_exp_f16_sdwa v87, v83 dst_sel:WORD_1 dst_unused:UNUSED_PRESERVE src0_sel:WORD_1
	v_exp_f16_sdwa v88, v84 dst_sel:WORD_1 dst_unused:UNUSED_PRESERVE src0_sel:WORD_1
	v_exp_f16_sdwa v89, v85 dst_sel:WORD_1 dst_unused:UNUSED_PRESERVE src0_sel:WORD_1
	v_pk_add_f16 v82, v189, v154 neg_lo:[0,1] neg_hi:[0,1]
	v_pk_add_f16 v65, v65, v86
	v_pk_add_f16 v62, v62, v89
	v_pk_add_f16 v63, v63, v88
	v_pk_add_f16 v64, v64, v87
	v_pk_fma_f16 v45, v33, v89, v45
	v_pk_fma_f16 v44, v32, v88, v44
	v_pk_fma_f16 v43, v31, v87, v43
	v_pk_fma_f16 v42, v30, v86, v42
	v_pk_add_f16 v83, v188, v155 neg_lo:[0,1] neg_hi:[0,1]
	v_pk_add_f16 v84, v187, v156 neg_lo:[0,1] neg_hi:[0,1]
	v_pk_add_f16 v85, v186, v157 neg_lo:[0,1] neg_hi:[0,1]
	v_exp_f16_sdwa v86, v82 dst_sel:WORD_0 dst_unused:UNUSED_PAD src0_sel:WORD_0
	v_exp_f16_sdwa v87, v83 dst_sel:WORD_0 dst_unused:UNUSED_PAD src0_sel:WORD_0
	v_exp_f16_sdwa v88, v84 dst_sel:WORD_0 dst_unused:UNUSED_PAD src0_sel:WORD_0
	v_exp_f16_sdwa v89, v85 dst_sel:WORD_0 dst_unused:UNUSED_PAD src0_sel:WORD_0
	v_exp_f16_sdwa v86, v82 dst_sel:WORD_1 dst_unused:UNUSED_PRESERVE src0_sel:WORD_1
	v_exp_f16_sdwa v87, v83 dst_sel:WORD_1 dst_unused:UNUSED_PRESERVE src0_sel:WORD_1
	v_exp_f16_sdwa v88, v84 dst_sel:WORD_1 dst_unused:UNUSED_PRESERVE src0_sel:WORD_1
	v_exp_f16_sdwa v89, v85 dst_sel:WORD_1 dst_unused:UNUSED_PRESERVE src0_sel:WORD_1
	v_exp_f16_sdwa v82, v70 dst_sel:WORD_0 dst_unused:UNUSED_PAD src0_sel:WORD_0
	v_exp_f16_sdwa v83, v71 dst_sel:WORD_0 dst_unused:UNUSED_PAD src0_sel:WORD_0
	v_exp_f16_sdwa v84, v72 dst_sel:WORD_0 dst_unused:UNUSED_PAD src0_sel:WORD_0
	v_exp_f16_sdwa v85, v73 dst_sel:WORD_0 dst_unused:UNUSED_PAD src0_sel:WORD_0
	v_exp_f16_sdwa v82, v70 dst_sel:WORD_1 dst_unused:UNUSED_PRESERVE src0_sel:WORD_1
	v_exp_f16_sdwa v83, v71 dst_sel:WORD_1 dst_unused:UNUSED_PRESERVE src0_sel:WORD_1
	v_exp_f16_sdwa v84, v72 dst_sel:WORD_1 dst_unused:UNUSED_PRESERVE src0_sel:WORD_1
	v_exp_f16_sdwa v85, v73 dst_sel:WORD_1 dst_unused:UNUSED_PRESERVE src0_sel:WORD_1
	v_pk_add_f16 v70, v98, v154 neg_lo:[0,1] neg_hi:[0,1]
	v_pk_add_f16 v65, v65, v86
	v_pk_add_f16 v64, v64, v87
	v_pk_add_f16 v63, v63, v88
	v_pk_add_f16 v62, v62, v89
	v_pk_fma_f16 v42, v46, v86, v42
	v_pk_fma_f16 v43, v47, v87, v43
	v_pk_fma_f16 v44, v48, v88, v44
	v_pk_fma_f16 v45, v49, v89, v45
	v_pk_add_f16 v65, v65, v82
	v_pk_add_f16 v62, v62, v85
	v_pk_add_f16 v63, v63, v84
	v_pk_add_f16 v64, v64, v83
	v_pk_fma_f16 v45, v9, v85, v45
	v_pk_fma_f16 v44, v8, v84, v44
	v_pk_fma_f16 v43, v7, v83, v43
	v_pk_fma_f16 v42, v6, v82, v42
	v_pk_add_f16 v71, v99, v155 neg_lo:[0,1] neg_hi:[0,1]
	v_pk_add_f16 v72, v100, v156 neg_lo:[0,1] neg_hi:[0,1]
	v_pk_add_f16 v73, v101, v157 neg_lo:[0,1] neg_hi:[0,1]
	v_exp_f16_sdwa v82, v70 dst_sel:WORD_0 dst_unused:UNUSED_PAD src0_sel:WORD_0
	v_exp_f16_sdwa v83, v71 dst_sel:WORD_0 dst_unused:UNUSED_PAD src0_sel:WORD_0
	v_exp_f16_sdwa v84, v72 dst_sel:WORD_0 dst_unused:UNUSED_PAD src0_sel:WORD_0
	v_exp_f16_sdwa v85, v73 dst_sel:WORD_0 dst_unused:UNUSED_PAD src0_sel:WORD_0
	v_exp_f16_sdwa v82, v70 dst_sel:WORD_1 dst_unused:UNUSED_PRESERVE src0_sel:WORD_1
	v_exp_f16_sdwa v83, v71 dst_sel:WORD_1 dst_unused:UNUSED_PRESERVE src0_sel:WORD_1
	v_exp_f16_sdwa v84, v72 dst_sel:WORD_1 dst_unused:UNUSED_PRESERVE src0_sel:WORD_1
	v_exp_f16_sdwa v85, v73 dst_sel:WORD_1 dst_unused:UNUSED_PRESERVE src0_sel:WORD_1
	v_pk_add_f16 v70, v114, v154 neg_lo:[0,1] neg_hi:[0,1]
	v_pk_add_f16 v65, v65, v82
	v_pk_add_f16 v64, v64, v83
	v_pk_add_f16 v63, v63, v84
	v_pk_add_f16 v62, v62, v85
	v_pk_fma_f16 v42, v10, v82, v42
	v_pk_fma_f16 v43, v11, v83, v43
	v_pk_fma_f16 v44, v12, v84, v44
	v_pk_fma_f16 v45, v13, v85, v45
	v_pk_add_f16 v71, v115, v155 neg_lo:[0,1] neg_hi:[0,1]
	v_pk_add_f16 v72, v116, v156 neg_lo:[0,1] neg_hi:[0,1]
	v_pk_add_f16 v73, v117, v157 neg_lo:[0,1] neg_hi:[0,1]
	v_exp_f16_sdwa v82, v70 dst_sel:WORD_0 dst_unused:UNUSED_PAD src0_sel:WORD_0
	v_exp_f16_sdwa v83, v71 dst_sel:WORD_0 dst_unused:UNUSED_PAD src0_sel:WORD_0
	v_exp_f16_sdwa v84, v72 dst_sel:WORD_0 dst_unused:UNUSED_PAD src0_sel:WORD_0
	v_exp_f16_sdwa v85, v73 dst_sel:WORD_0 dst_unused:UNUSED_PAD src0_sel:WORD_0
	v_exp_f16_sdwa v82, v70 dst_sel:WORD_1 dst_unused:UNUSED_PRESERVE src0_sel:WORD_1
	v_exp_f16_sdwa v83, v71 dst_sel:WORD_1 dst_unused:UNUSED_PRESERVE src0_sel:WORD_1
	v_exp_f16_sdwa v84, v72 dst_sel:WORD_1 dst_unused:UNUSED_PRESERVE src0_sel:WORD_1
	v_exp_f16_sdwa v85, v73 dst_sel:WORD_1 dst_unused:UNUSED_PRESERVE src0_sel:WORD_1
	v_pk_add_f16 v65, v65, v82
	v_pk_add_f16 v64, v64, v83
	v_rcp_f16_e32 v70, v65
	v_rcp_f16_sdwa v65, v65 dst_sel:DWORD dst_unused:UNUSED_PAD src0_sel:WORD_1
	v_pk_add_f16 v63, v63, v84
	v_rcp_f16_e32 v71, v64
	v_rcp_f16_sdwa v64, v64 dst_sel:DWORD dst_unused:UNUSED_PAD src0_sel:WORD_1
	v_pk_add_f16 v62, v62, v85
	v_rcp_f16_e32 v72, v63
	v_rcp_f16_sdwa v73, v63 dst_sel:DWORD dst_unused:UNUSED_PAD src0_sel:WORD_1
	v_pk_fma_f16 v43, v15, v83, v43
	v_pk_fma_f16 v42, v14, v82, v42
	v_rcp_f16_e32 v82, v62
	v_rcp_f16_sdwa v83, v62 dst_sel:DWORD dst_unused:UNUSED_PAD src0_sel:WORD_1
	v_pack_b32_f16 v62, v70, v65
	v_pk_mul_f16 v62, v42, v62
	v_pack_b32_f16 v42, v71, v64
	v_pk_fma_f16 v44, v16, v84, v44
	v_pk_mul_f16 v63, v43, v42
	v_pack_b32_f16 v42, v72, v73
	v_pk_fma_f16 v45, v17, v85, v45
	v_pk_mul_f16 v64, v44, v42
	v_pack_b32_f16 v42, v82, v83
	v_pk_mul_f16 v65, v45, v42
	s_waitcnt vmcnt(6)
	v_pk_mul_f16 v42, v185, v150 op_sel_hi:[0,1]
	v_pk_mul_f16 v70, v183, v150 op_sel_hi:[0,1]
	v_pk_mul_f16 v82, v184, v150 op_sel_hi:[0,1]
	v_pk_mul_f16 v43, v185, v151 op_sel_hi:[0,1]
	v_pk_mul_f16 v44, v185, v152 op_sel_hi:[0,1]
	v_pk_mul_f16 v45, v185, v153 op_sel_hi:[0,1]
	v_pk_mul_f16 v71, v183, v151 op_sel_hi:[0,1]
	v_pk_mul_f16 v72, v183, v152 op_sel_hi:[0,1]
	v_pk_mul_f16 v73, v183, v153 op_sel_hi:[0,1]
	v_pk_mul_f16 v83, v184, v151 op_sel_hi:[0,1]
	v_pk_mul_f16 v84, v184, v152 op_sel_hi:[0,1]
	v_pk_mul_f16 v85, v184, v153 op_sel_hi:[0,1]
	v_pk_fma_f16 v50, v50, v150, v42
	v_pk_fma_f16 v66, v66, v150, v70
	v_pk_fma_f16 v89, v94, v150, v82
	v_pk_fma_f16 v53, v53, v153, v45
	v_pk_maximum3_f16 v114, v50, v66, v89
	v_pk_fma_f16 v52, v52, v152, v44
	v_pk_fma_f16 v51, v51, v151, v43
	v_pk_fma_f16 v69, v69, v153, v73
	v_pk_fma_f16 v68, v68, v152, v72
	v_pk_fma_f16 v67, v67, v151, v71
	v_pk_fma_f16 v86, v97, v153, v85
	v_pk_fma_f16 v87, v96, v152, v84
	v_pk_fma_f16 v88, v95, v151, v83
	v_pk_fma_f16 v97, v18, v150, v42
	v_pk_fma_f16 v101, v34, v150, v70
	v_pk_fma_f16 v109, v54, v150, v82
	v_pk_fma_f16 v42, v74, v150, v42
	v_pk_fma_f16 v70, v102, v150, v70
	v_pk_fma_f16 v82, v118, v150, v82
	v_pk_maximum3_f16 v115, v51, v67, v88
	v_pk_maximum3_f16 v116, v52, v68, v87
	v_pk_maximum3_f16 v117, v53, v69, v86
	v_pk_maximum3_f16 v122, v97, v101, v109
	v_pk_fma_f16 v94, v21, v153, v45
	v_pk_maximum3_f16 v126, v42, v70, v82
	v_pk_fma_f16 v95, v20, v152, v44
	v_pk_maximum3_f16 v114, v114, v122, v126
	v_pk_fma_f16 v96, v19, v151, v43
	v_pk_fma_f16 v98, v37, v153, v73
	v_pk_fma_f16 v99, v36, v152, v72
	v_pk_fma_f16 v100, v35, v151, v71
	v_pk_fma_f16 v106, v57, v153, v85
	v_pk_fma_f16 v107, v56, v152, v84
	v_pk_fma_f16 v108, v55, v151, v83
	v_pk_fma_f16 v45, v77, v153, v45
	v_pk_fma_f16 v44, v76, v152, v44
	v_pk_fma_f16 v43, v75, v151, v43
	v_pk_fma_f16 v73, v105, v153, v73
	v_pk_fma_f16 v72, v104, v152, v72
	v_pk_fma_f16 v71, v103, v151, v71
	v_pk_fma_f16 v85, v121, v153, v85
	v_pk_fma_f16 v84, v120, v152, v84
	v_pk_fma_f16 v83, v119, v151, v83
	v_pk_maximum3_f16 v123, v96, v100, v108
	v_pk_maximum3_f16 v124, v95, v99, v107
	v_pk_maximum3_f16 v125, v94, v98, v106
	v_pk_maximum3_f16 v128, v44, v72, v84
	v_pk_maximum3_f16 v129, v45, v73, v85
	v_pk_maximum3_f16 v127, v43, v71, v83
	v_pk_maximum3_f16 v115, v115, v123, v127
	v_pk_maximum3_f16 v116, v116, v124, v128
	v_pk_maximum3_f16 v117, v117, v125, v129
	v_pk_add_f16 v50, v50, v114 neg_lo:[0,1] neg_hi:[0,1]
	v_pk_add_f16 v51, v51, v115 neg_lo:[0,1] neg_hi:[0,1]
	v_pk_add_f16 v52, v52, v116 neg_lo:[0,1] neg_hi:[0,1]
	v_pk_add_f16 v53, v53, v117 neg_lo:[0,1] neg_hi:[0,1]
	v_pk_add_f16 v66, v66, v114 neg_lo:[0,1] neg_hi:[0,1]
	v_exp_f16_sdwa v122, v50 dst_sel:WORD_0 dst_unused:UNUSED_PAD src0_sel:WORD_0
	v_exp_f16_sdwa v123, v51 dst_sel:WORD_0 dst_unused:UNUSED_PAD src0_sel:WORD_0
	v_exp_f16_sdwa v124, v52 dst_sel:WORD_0 dst_unused:UNUSED_PAD src0_sel:WORD_0
	v_exp_f16_sdwa v125, v53 dst_sel:WORD_0 dst_unused:UNUSED_PAD src0_sel:WORD_0
	v_exp_f16_sdwa v122, v50 dst_sel:WORD_1 dst_unused:UNUSED_PRESERVE src0_sel:WORD_1
	v_exp_f16_sdwa v123, v51 dst_sel:WORD_1 dst_unused:UNUSED_PRESERVE src0_sel:WORD_1
	v_exp_f16_sdwa v124, v52 dst_sel:WORD_1 dst_unused:UNUSED_PRESERVE src0_sel:WORD_1
	v_exp_f16_sdwa v125, v53 dst_sel:WORD_1 dst_unused:UNUSED_PRESERVE src0_sel:WORD_1
	v_pk_add_f16 v67, v67, v115 neg_lo:[0,1] neg_hi:[0,1]
	v_pk_add_f16 v50, v125, 0
	v_pk_fma_f16 v22, v22, v122, 0
	v_pk_add_f16 v51, v124, 0
	v_pk_add_f16 v52, v123, 0
	v_pk_add_f16 v53, v122, 0
	v_pk_fma_f16 v23, v23, v123, 0
	v_pk_fma_f16 v24, v24, v124, 0
	v_pk_fma_f16 v25, v25, v125, 0
	v_pk_add_f16 v68, v68, v116 neg_lo:[0,1] neg_hi:[0,1]
	v_pk_add_f16 v69, v69, v117 neg_lo:[0,1] neg_hi:[0,1]
	v_pk_add_f16 v42, v42, v114 neg_lo:[0,1] neg_hi:[0,1]
	v_exp_f16_sdwa v122, v66 dst_sel:WORD_0 dst_unused:UNUSED_PAD src0_sel:WORD_0
	v_exp_f16_sdwa v123, v67 dst_sel:WORD_0 dst_unused:UNUSED_PAD src0_sel:WORD_0
	v_exp_f16_sdwa v124, v68 dst_sel:WORD_0 dst_unused:UNUSED_PAD src0_sel:WORD_0
	v_exp_f16_sdwa v125, v69 dst_sel:WORD_0 dst_unused:UNUSED_PAD src0_sel:WORD_0
	v_exp_f16_sdwa v122, v66 dst_sel:WORD_1 dst_unused:UNUSED_PRESERVE src0_sel:WORD_1
	v_exp_f16_sdwa v123, v67 dst_sel:WORD_1 dst_unused:UNUSED_PRESERVE src0_sel:WORD_1
	v_exp_f16_sdwa v124, v68 dst_sel:WORD_1 dst_unused:UNUSED_PRESERVE src0_sel:WORD_1
	v_exp_f16_sdwa v125, v69 dst_sel:WORD_1 dst_unused:UNUSED_PRESERVE src0_sel:WORD_1
	v_pk_add_f16 v43, v43, v115 neg_lo:[0,1] neg_hi:[0,1]
	v_pk_add_f16 v50, v50, v125
	v_pk_fma_f16 v22, v30, v122, v22
	v_pk_add_f16 v30, v89, v114 neg_lo:[0,1] neg_hi:[0,1]
	v_pk_add_f16 v53, v53, v122
	v_pk_add_f16 v52, v52, v123
	v_pk_add_f16 v51, v51, v124
	v_pk_fma_f16 v25, v33, v125, v25
	v_pk_fma_f16 v24, v32, v124, v24
	v_pk_fma_f16 v23, v31, v123, v23
	v_pk_add_f16 v31, v88, v115 neg_lo:[0,1] neg_hi:[0,1]
	v_pk_add_f16 v32, v87, v116 neg_lo:[0,1] neg_hi:[0,1]
	v_pk_add_f16 v33, v86, v117 neg_lo:[0,1] neg_hi:[0,1]
	v_pk_add_f16 v44, v44, v116 neg_lo:[0,1] neg_hi:[0,1]
	v_exp_f16_sdwa v66, v30 dst_sel:WORD_0 dst_unused:UNUSED_PAD src0_sel:WORD_0
	v_exp_f16_sdwa v67, v31 dst_sel:WORD_0 dst_unused:UNUSED_PAD src0_sel:WORD_0
	v_exp_f16_sdwa v68, v32 dst_sel:WORD_0 dst_unused:UNUSED_PAD src0_sel:WORD_0
	v_exp_f16_sdwa v69, v33 dst_sel:WORD_0 dst_unused:UNUSED_PAD src0_sel:WORD_0
	v_exp_f16_sdwa v66, v30 dst_sel:WORD_1 dst_unused:UNUSED_PRESERVE src0_sel:WORD_1
	v_exp_f16_sdwa v67, v31 dst_sel:WORD_1 dst_unused:UNUSED_PRESERVE src0_sel:WORD_1
	v_exp_f16_sdwa v68, v32 dst_sel:WORD_1 dst_unused:UNUSED_PRESERVE src0_sel:WORD_1
	v_exp_f16_sdwa v69, v33 dst_sel:WORD_1 dst_unused:UNUSED_PRESERVE src0_sel:WORD_1
	v_pk_add_f16 v45, v45, v117 neg_lo:[0,1] neg_hi:[0,1]
	v_pk_add_f16 v30, v50, v69
	v_pk_add_f16 v31, v51, v68
	v_pk_add_f16 v32, v52, v67
	v_pk_add_f16 v33, v53, v66
	v_pk_fma_f16 v22, v46, v66, v22
	v_pk_fma_f16 v23, v47, v67, v23
	v_pk_fma_f16 v24, v48, v68, v24
	v_pk_fma_f16 v25, v49, v69, v25
	v_pk_add_f16 v46, v97, v114 neg_lo:[0,1] neg_hi:[0,1]
	v_pk_add_f16 v47, v96, v115 neg_lo:[0,1] neg_hi:[0,1]
	v_pk_add_f16 v48, v95, v116 neg_lo:[0,1] neg_hi:[0,1]
	v_pk_add_f16 v49, v94, v117 neg_lo:[0,1] neg_hi:[0,1]
	v_exp_f16_sdwa v50, v46 dst_sel:WORD_0 dst_unused:UNUSED_PAD src0_sel:WORD_0
	v_exp_f16_sdwa v51, v47 dst_sel:WORD_0 dst_unused:UNUSED_PAD src0_sel:WORD_0
	v_exp_f16_sdwa v52, v48 dst_sel:WORD_0 dst_unused:UNUSED_PAD src0_sel:WORD_0
	v_exp_f16_sdwa v53, v49 dst_sel:WORD_0 dst_unused:UNUSED_PAD src0_sel:WORD_0
	v_exp_f16_sdwa v50, v46 dst_sel:WORD_1 dst_unused:UNUSED_PRESERVE src0_sel:WORD_1
	v_exp_f16_sdwa v51, v47 dst_sel:WORD_1 dst_unused:UNUSED_PRESERVE src0_sel:WORD_1
	v_exp_f16_sdwa v52, v48 dst_sel:WORD_1 dst_unused:UNUSED_PRESERVE src0_sel:WORD_1
	v_exp_f16_sdwa v53, v49 dst_sel:WORD_1 dst_unused:UNUSED_PRESERVE src0_sel:WORD_1
	v_pk_add_f16 v46, v101, v114 neg_lo:[0,1] neg_hi:[0,1]
	v_pk_add_f16 v30, v30, v53
	v_pk_add_f16 v33, v33, v50
	v_pk_add_f16 v32, v32, v51
	v_pk_add_f16 v31, v31, v52
	v_pk_fma_f16 v25, v9, v53, v25
	v_pk_fma_f16 v24, v8, v52, v24
	v_pk_fma_f16 v23, v7, v51, v23
	v_pk_fma_f16 v22, v6, v50, v22
	v_pk_add_f16 v47, v100, v115 neg_lo:[0,1] neg_hi:[0,1]
	v_pk_add_f16 v48, v99, v116 neg_lo:[0,1] neg_hi:[0,1]
	v_pk_add_f16 v49, v98, v117 neg_lo:[0,1] neg_hi:[0,1]
	v_exp_f16_sdwa v50, v46 dst_sel:WORD_0 dst_unused:UNUSED_PAD src0_sel:WORD_0
	v_exp_f16_sdwa v51, v47 dst_sel:WORD_0 dst_unused:UNUSED_PAD src0_sel:WORD_0
	v_exp_f16_sdwa v52, v48 dst_sel:WORD_0 dst_unused:UNUSED_PAD src0_sel:WORD_0
	v_exp_f16_sdwa v53, v49 dst_sel:WORD_0 dst_unused:UNUSED_PAD src0_sel:WORD_0
	v_exp_f16_sdwa v50, v46 dst_sel:WORD_1 dst_unused:UNUSED_PRESERVE src0_sel:WORD_1
	v_exp_f16_sdwa v51, v47 dst_sel:WORD_1 dst_unused:UNUSED_PRESERVE src0_sel:WORD_1
	v_exp_f16_sdwa v52, v48 dst_sel:WORD_1 dst_unused:UNUSED_PRESERVE src0_sel:WORD_1
	v_exp_f16_sdwa v53, v49 dst_sel:WORD_1 dst_unused:UNUSED_PRESERVE src0_sel:WORD_1
	v_pk_add_f16 v46, v109, v114 neg_lo:[0,1] neg_hi:[0,1]
	v_pk_add_f16 v30, v30, v53
	v_pk_add_f16 v31, v31, v52
	v_pk_add_f16 v32, v32, v51
	v_pk_add_f16 v33, v33, v50
	v_pk_fma_f16 v22, v10, v50, v22
	v_pk_fma_f16 v23, v11, v51, v23
	v_pk_fma_f16 v24, v12, v52, v24
	v_pk_fma_f16 v25, v13, v53, v25
	v_pk_add_f16 v47, v108, v115 neg_lo:[0,1] neg_hi:[0,1]
	v_pk_add_f16 v48, v107, v116 neg_lo:[0,1] neg_hi:[0,1]
	v_pk_add_f16 v49, v106, v117 neg_lo:[0,1] neg_hi:[0,1]
	v_exp_f16_sdwa v50, v46 dst_sel:WORD_0 dst_unused:UNUSED_PAD src0_sel:WORD_0
	v_exp_f16_sdwa v51, v47 dst_sel:WORD_0 dst_unused:UNUSED_PAD src0_sel:WORD_0
	v_exp_f16_sdwa v52, v48 dst_sel:WORD_0 dst_unused:UNUSED_PAD src0_sel:WORD_0
	v_exp_f16_sdwa v53, v49 dst_sel:WORD_0 dst_unused:UNUSED_PAD src0_sel:WORD_0
	v_exp_f16_sdwa v50, v46 dst_sel:WORD_1 dst_unused:UNUSED_PRESERVE src0_sel:WORD_1
	v_exp_f16_sdwa v51, v47 dst_sel:WORD_1 dst_unused:UNUSED_PRESERVE src0_sel:WORD_1
	v_exp_f16_sdwa v52, v48 dst_sel:WORD_1 dst_unused:UNUSED_PRESERVE src0_sel:WORD_1
	v_exp_f16_sdwa v53, v49 dst_sel:WORD_1 dst_unused:UNUSED_PRESERVE src0_sel:WORD_1
	v_exp_f16_sdwa v46, v42 dst_sel:WORD_0 dst_unused:UNUSED_PAD src0_sel:WORD_0
	v_exp_f16_sdwa v47, v43 dst_sel:WORD_0 dst_unused:UNUSED_PAD src0_sel:WORD_0
	v_exp_f16_sdwa v48, v44 dst_sel:WORD_0 dst_unused:UNUSED_PAD src0_sel:WORD_0
	v_exp_f16_sdwa v49, v45 dst_sel:WORD_0 dst_unused:UNUSED_PAD src0_sel:WORD_0
	v_exp_f16_sdwa v46, v42 dst_sel:WORD_1 dst_unused:UNUSED_PRESERVE src0_sel:WORD_1
	v_exp_f16_sdwa v47, v43 dst_sel:WORD_1 dst_unused:UNUSED_PRESERVE src0_sel:WORD_1
	v_exp_f16_sdwa v48, v44 dst_sel:WORD_1 dst_unused:UNUSED_PRESERVE src0_sel:WORD_1
	v_exp_f16_sdwa v49, v45 dst_sel:WORD_1 dst_unused:UNUSED_PRESERVE src0_sel:WORD_1
	v_pk_add_f16 v42, v70, v114 neg_lo:[0,1] neg_hi:[0,1]
	v_pk_add_f16 v30, v30, v53
	v_pk_add_f16 v33, v33, v50
	v_pk_add_f16 v32, v32, v51
	v_pk_add_f16 v31, v31, v52
	v_pk_fma_f16 v25, v17, v53, v25
	v_pk_fma_f16 v24, v16, v52, v24
	v_pk_fma_f16 v23, v15, v51, v23
	v_pk_fma_f16 v22, v14, v50, v22
	v_pk_add_f16 v30, v30, v49
	v_pk_add_f16 v31, v31, v48
	v_pk_add_f16 v32, v32, v47
	v_pk_add_f16 v33, v33, v46
	v_pk_fma_f16 v22, v26, v46, v22
	v_pk_fma_f16 v23, v27, v47, v23
	v_pk_fma_f16 v24, v28, v48, v24
	v_pk_fma_f16 v25, v29, v49, v25
	v_pk_add_f16 v43, v71, v115 neg_lo:[0,1] neg_hi:[0,1]
	v_pk_add_f16 v44, v72, v116 neg_lo:[0,1] neg_hi:[0,1]
	v_pk_add_f16 v45, v73, v117 neg_lo:[0,1] neg_hi:[0,1]
	v_exp_f16_sdwa v46, v42 dst_sel:WORD_0 dst_unused:UNUSED_PAD src0_sel:WORD_0
	v_exp_f16_sdwa v47, v43 dst_sel:WORD_0 dst_unused:UNUSED_PAD src0_sel:WORD_0
	v_exp_f16_sdwa v48, v44 dst_sel:WORD_0 dst_unused:UNUSED_PAD src0_sel:WORD_0
	v_exp_f16_sdwa v49, v45 dst_sel:WORD_0 dst_unused:UNUSED_PAD src0_sel:WORD_0
	v_exp_f16_sdwa v46, v42 dst_sel:WORD_1 dst_unused:UNUSED_PRESERVE src0_sel:WORD_1
	v_exp_f16_sdwa v47, v43 dst_sel:WORD_1 dst_unused:UNUSED_PRESERVE src0_sel:WORD_1
	v_exp_f16_sdwa v48, v44 dst_sel:WORD_1 dst_unused:UNUSED_PRESERVE src0_sel:WORD_1
	v_exp_f16_sdwa v49, v45 dst_sel:WORD_1 dst_unused:UNUSED_PRESERVE src0_sel:WORD_1
	v_pk_add_f16 v42, v82, v114 neg_lo:[0,1] neg_hi:[0,1]
	v_pk_add_f16 v30, v30, v49
	v_pk_add_f16 v33, v33, v46
	v_pk_add_f16 v32, v32, v47
	v_pk_add_f16 v31, v31, v48
	v_pk_fma_f16 v25, v41, v49, v25
	v_pk_fma_f16 v24, v40, v48, v24
	v_pk_fma_f16 v23, v39, v47, v23
	v_pk_fma_f16 v22, v38, v46, v22
	v_pk_add_f16 v43, v83, v115 neg_lo:[0,1] neg_hi:[0,1]
	v_pk_add_f16 v44, v84, v116 neg_lo:[0,1] neg_hi:[0,1]
	v_pk_add_f16 v45, v85, v117 neg_lo:[0,1] neg_hi:[0,1]
	v_exp_f16_sdwa v46, v42 dst_sel:WORD_0 dst_unused:UNUSED_PAD src0_sel:WORD_0
	v_exp_f16_sdwa v47, v43 dst_sel:WORD_0 dst_unused:UNUSED_PAD src0_sel:WORD_0
	v_exp_f16_sdwa v48, v44 dst_sel:WORD_0 dst_unused:UNUSED_PAD src0_sel:WORD_0
	v_exp_f16_sdwa v49, v45 dst_sel:WORD_0 dst_unused:UNUSED_PAD src0_sel:WORD_0
	v_exp_f16_sdwa v46, v42 dst_sel:WORD_1 dst_unused:UNUSED_PRESERVE src0_sel:WORD_1
	v_exp_f16_sdwa v47, v43 dst_sel:WORD_1 dst_unused:UNUSED_PRESERVE src0_sel:WORD_1
	v_exp_f16_sdwa v48, v44 dst_sel:WORD_1 dst_unused:UNUSED_PRESERVE src0_sel:WORD_1
	v_exp_f16_sdwa v49, v45 dst_sel:WORD_1 dst_unused:UNUSED_PRESERVE src0_sel:WORD_1
	s_nop 0
	v_pk_add_f16 v30, v30, v49
	v_pk_add_f16 v31, v31, v48
	v_rcp_f16_e32 v44, v30
	v_rcp_f16_sdwa v30, v30 dst_sel:DWORD dst_unused:UNUSED_PAD src0_sel:WORD_1
	v_pk_add_f16 v32, v32, v47
	v_rcp_f16_e32 v45, v31
	v_rcp_f16_sdwa v31, v31 dst_sel:DWORD dst_unused:UNUSED_PAD src0_sel:WORD_1
	v_pk_add_f16 v33, v33, v46
	v_rcp_f16_e32 v43, v32
	v_rcp_f16_sdwa v32, v32 dst_sel:DWORD dst_unused:UNUSED_PAD src0_sel:WORD_1
	v_rcp_f16_e32 v42, v33
	v_rcp_f16_sdwa v33, v33 dst_sel:DWORD dst_unused:UNUSED_PAD src0_sel:WORD_1
	v_pk_fma_f16 v25, v61, v49, v25
	v_pack_b32_f16 v30, v44, v30
	v_pk_fma_f16 v24, v60, v48, v24
	v_pk_mul_f16 v25, v25, v30
	v_pack_b32_f16 v30, v45, v31
	v_pk_fma_f16 v23, v59, v47, v23
	v_pk_mul_f16 v24, v24, v30
	v_pack_b32_f16 v30, v43, v32
	v_pk_fma_f16 v22, v58, v46, v22
	v_pk_mul_f16 v23, v23, v30
	v_pack_b32_f16 v30, v42, v33
	v_pk_mul_f16 v22, v22, v30
	s_waitcnt vmcnt(0)
	v_pk_mul_f16 v30, v185, v146 op_sel_hi:[0,1]
	v_pk_mul_f16 v31, v185, v147 op_sel_hi:[0,1]
	v_pk_mul_f16 v32, v185, v148 op_sel_hi:[0,1]
	v_pk_mul_f16 v33, v185, v149 op_sel_hi:[0,1]
	v_pk_mul_f16 v42, v183, v146 op_sel_hi:[0,1]
	v_pk_mul_f16 v43, v183, v147 op_sel_hi:[0,1]
	v_pk_mul_f16 v44, v183, v148 op_sel_hi:[0,1]
	v_pk_mul_f16 v45, v183, v149 op_sel_hi:[0,1]
	v_pk_mul_f16 v46, v184, v146 op_sel_hi:[0,1]
	v_pk_mul_f16 v47, v184, v147 op_sel_hi:[0,1]
	v_pk_mul_f16 v48, v184, v148 op_sel_hi:[0,1]
	v_pk_mul_f16 v49, v184, v149 op_sel_hi:[0,1]
	v_pk_fma_f16 v21, v21, v149, v33
	v_pk_fma_f16 v20, v20, v148, v32
	v_pk_fma_f16 v19, v19, v147, v31
	v_pk_fma_f16 v18, v18, v146, v30
	v_pk_fma_f16 v37, v37, v149, v45
	v_pk_fma_f16 v36, v36, v148, v44
	v_pk_fma_f16 v35, v35, v147, v43
	v_pk_fma_f16 v34, v34, v146, v42
	v_pk_fma_f16 v50, v57, v149, v49
	v_pk_fma_f16 v51, v56, v148, v48
	v_pk_fma_f16 v52, v55, v147, v47
	v_pk_fma_f16 v53, v54, v146, v46
	v_pk_fma_f16 v54, v77, v149, v33
	v_pk_fma_f16 v55, v76, v148, v32
	v_pk_fma_f16 v56, v75, v147, v31
	v_pk_fma_f16 v57, v74, v146, v30
	v_pk_maximum3_f16 v74, v18, v34, v53
	v_pk_maximum3_f16 v75, v19, v35, v52
	v_pk_maximum3_f16 v76, v20, v36, v51
	v_pk_maximum3_f16 v77, v21, v37, v50
	v_pk_fma_f16 v66, v105, v149, v45
	v_pk_fma_f16 v67, v104, v148, v44
	v_pk_fma_f16 v68, v103, v147, v43
	v_pk_fma_f16 v69, v102, v146, v42
	v_pk_fma_f16 v70, v121, v149, v49
	v_pk_fma_f16 v71, v120, v148, v48
	v_pk_fma_f16 v72, v119, v147, v47
	v_pk_fma_f16 v73, v118, v146, v46
	v_pk_fma_f16 v33, v133, v149, v33
	v_pk_fma_f16 v32, v132, v148, v32
	v_pk_fma_f16 v31, v131, v147, v31
	v_pk_fma_f16 v30, v130, v146, v30
	v_pk_fma_f16 v45, v141, v149, v45
	v_pk_fma_f16 v44, v140, v148, v44
	v_pk_fma_f16 v43, v139, v147, v43
	v_pk_fma_f16 v42, v138, v146, v42
	v_pk_fma_f16 v49, v145, v149, v49
	v_pk_fma_f16 v48, v144, v148, v48
	v_pk_fma_f16 v47, v143, v147, v47
	v_pk_fma_f16 v46, v142, v146, v46
	v_pk_maximum3_f16 v82, v57, v69, v73
	v_pk_maximum3_f16 v83, v56, v68, v72
	v_pk_maximum3_f16 v84, v55, v67, v71
	v_pk_maximum3_f16 v85, v54, v66, v70
	v_pk_maximum3_f16 v87, v31, v43, v47
	v_pk_maximum3_f16 v86, v30, v42, v46
	v_pk_maximum3_f16 v88, v32, v44, v48
	v_pk_maximum3_f16 v89, v33, v45, v49
	v_pk_maximum3_f16 v74, v74, v82, v86
	v_pk_maximum3_f16 v75, v75, v83, v87
	v_pk_maximum3_f16 v76, v76, v84, v88
	v_pk_maximum3_f16 v77, v77, v85, v89
	s_nop 0
	v_pk_add_f16 v18, v18, v74 neg_lo:[0,1] neg_hi:[0,1]
	v_pk_add_f16 v19, v19, v75 neg_lo:[0,1] neg_hi:[0,1]
	v_pk_add_f16 v20, v20, v76 neg_lo:[0,1] neg_hi:[0,1]
	v_pk_add_f16 v21, v21, v77 neg_lo:[0,1] neg_hi:[0,1]
	v_pk_add_f16 v34, v34, v74 neg_lo:[0,1] neg_hi:[0,1]
	v_exp_f16_sdwa v82, v18 dst_sel:WORD_0 dst_unused:UNUSED_PAD src0_sel:WORD_0
	v_exp_f16_sdwa v83, v19 dst_sel:WORD_0 dst_unused:UNUSED_PAD src0_sel:WORD_0
	v_exp_f16_sdwa v84, v20 dst_sel:WORD_0 dst_unused:UNUSED_PAD src0_sel:WORD_0
	v_exp_f16_sdwa v85, v21 dst_sel:WORD_0 dst_unused:UNUSED_PAD src0_sel:WORD_0
	v_exp_f16_sdwa v82, v18 dst_sel:WORD_1 dst_unused:UNUSED_PRESERVE src0_sel:WORD_1
	v_exp_f16_sdwa v83, v19 dst_sel:WORD_1 dst_unused:UNUSED_PRESERVE src0_sel:WORD_1
	v_exp_f16_sdwa v84, v20 dst_sel:WORD_1 dst_unused:UNUSED_PRESERVE src0_sel:WORD_1
	v_exp_f16_sdwa v85, v21 dst_sel:WORD_1 dst_unused:UNUSED_PRESERVE src0_sel:WORD_1
	v_pk_add_f16 v35, v35, v75 neg_lo:[0,1] neg_hi:[0,1]
	v_pk_add_f16 v18, v82, 0
	v_pk_add_f16 v19, v83, 0
	v_pk_add_f16 v20, v84, 0
	v_pk_add_f16 v21, v85, 0
	v_pk_fma_f16 v6, v6, v82, 0
	v_pk_fma_f16 v7, v7, v83, 0
	v_pk_fma_f16 v8, v8, v84, 0
	v_pk_fma_f16 v9, v9, v85, 0
	v_pk_add_f16 v36, v36, v76 neg_lo:[0,1] neg_hi:[0,1]
	v_pk_add_f16 v37, v37, v77 neg_lo:[0,1] neg_hi:[0,1]
	v_exp_f16_sdwa v82, v34 dst_sel:WORD_0 dst_unused:UNUSED_PAD src0_sel:WORD_0
	v_exp_f16_sdwa v83, v35 dst_sel:WORD_0 dst_unused:UNUSED_PAD src0_sel:WORD_0
	v_exp_f16_sdwa v84, v36 dst_sel:WORD_0 dst_unused:UNUSED_PAD src0_sel:WORD_0
	v_exp_f16_sdwa v85, v37 dst_sel:WORD_0 dst_unused:UNUSED_PAD src0_sel:WORD_0
	v_exp_f16_sdwa v82, v34 dst_sel:WORD_1 dst_unused:UNUSED_PRESERVE src0_sel:WORD_1
	v_exp_f16_sdwa v83, v35 dst_sel:WORD_1 dst_unused:UNUSED_PRESERVE src0_sel:WORD_1
	v_exp_f16_sdwa v84, v36 dst_sel:WORD_1 dst_unused:UNUSED_PRESERVE src0_sel:WORD_1
	v_exp_f16_sdwa v85, v37 dst_sel:WORD_1 dst_unused:UNUSED_PRESERVE src0_sel:WORD_1
	s_nop 0
	v_pk_add_f16 v21, v21, v85
	v_pk_add_f16 v20, v20, v84
	v_pk_add_f16 v19, v19, v83
	v_pk_add_f16 v18, v18, v82
	v_pk_fma_f16 v9, v13, v85, v9
	v_pk_fma_f16 v8, v12, v84, v8
	v_pk_fma_f16 v7, v11, v83, v7
	v_pk_fma_f16 v6, v10, v82, v6
	v_pk_add_f16 v10, v53, v74 neg_lo:[0,1] neg_hi:[0,1]
	v_pk_add_f16 v11, v52, v75 neg_lo:[0,1] neg_hi:[0,1]
	v_pk_add_f16 v12, v51, v76 neg_lo:[0,1] neg_hi:[0,1]
	v_pk_add_f16 v13, v50, v77 neg_lo:[0,1] neg_hi:[0,1]
	v_exp_f16_sdwa v34, v10 dst_sel:WORD_0 dst_unused:UNUSED_PAD src0_sel:WORD_0
	v_exp_f16_sdwa v35, v11 dst_sel:WORD_0 dst_unused:UNUSED_PAD src0_sel:WORD_0
	v_exp_f16_sdwa v36, v12 dst_sel:WORD_0 dst_unused:UNUSED_PAD src0_sel:WORD_0
	v_exp_f16_sdwa v37, v13 dst_sel:WORD_0 dst_unused:UNUSED_PAD src0_sel:WORD_0
	v_exp_f16_sdwa v34, v10 dst_sel:WORD_1 dst_unused:UNUSED_PRESERVE src0_sel:WORD_1
	v_exp_f16_sdwa v35, v11 dst_sel:WORD_1 dst_unused:UNUSED_PRESERVE src0_sel:WORD_1
	v_exp_f16_sdwa v36, v12 dst_sel:WORD_1 dst_unused:UNUSED_PRESERVE src0_sel:WORD_1
	v_exp_f16_sdwa v37, v13 dst_sel:WORD_1 dst_unused:UNUSED_PRESERVE src0_sel:WORD_1
	v_pk_add_f16 v10, v18, v34
	v_pk_add_f16 v11, v19, v35
	v_pk_add_f16 v12, v20, v36
	v_pk_add_f16 v13, v21, v37
	v_pk_fma_f16 v6, v14, v34, v6
	v_pk_fma_f16 v7, v15, v35, v7
	v_pk_fma_f16 v8, v16, v36, v8
	v_pk_fma_f16 v9, v17, v37, v9
	v_pk_add_f16 v14, v57, v74 neg_lo:[0,1] neg_hi:[0,1]
	v_pk_add_f16 v15, v56, v75 neg_lo:[0,1] neg_hi:[0,1]
	v_pk_add_f16 v16, v55, v76 neg_lo:[0,1] neg_hi:[0,1]
	v_pk_add_f16 v17, v54, v77 neg_lo:[0,1] neg_hi:[0,1]
	v_exp_f16_sdwa v18, v14 dst_sel:WORD_0 dst_unused:UNUSED_PAD src0_sel:WORD_0
	v_exp_f16_sdwa v19, v15 dst_sel:WORD_0 dst_unused:UNUSED_PAD src0_sel:WORD_0
	v_exp_f16_sdwa v20, v16 dst_sel:WORD_0 dst_unused:UNUSED_PAD src0_sel:WORD_0
	v_exp_f16_sdwa v21, v17 dst_sel:WORD_0 dst_unused:UNUSED_PAD src0_sel:WORD_0
	v_exp_f16_sdwa v18, v14 dst_sel:WORD_1 dst_unused:UNUSED_PRESERVE src0_sel:WORD_1
	v_exp_f16_sdwa v19, v15 dst_sel:WORD_1 dst_unused:UNUSED_PRESERVE src0_sel:WORD_1
	v_exp_f16_sdwa v20, v16 dst_sel:WORD_1 dst_unused:UNUSED_PRESERVE src0_sel:WORD_1
	v_exp_f16_sdwa v21, v17 dst_sel:WORD_1 dst_unused:UNUSED_PRESERVE src0_sel:WORD_1
	v_pk_add_f16 v14, v69, v74 neg_lo:[0,1] neg_hi:[0,1]
	v_pk_add_f16 v13, v13, v21
	v_pk_add_f16 v12, v12, v20
	v_pk_add_f16 v11, v11, v19
	v_pk_add_f16 v10, v10, v18
	v_pk_fma_f16 v9, v29, v21, v9
	v_pk_fma_f16 v8, v28, v20, v8
	v_pk_fma_f16 v7, v27, v19, v7
	v_pk_fma_f16 v6, v26, v18, v6
	v_pk_add_f16 v15, v68, v75 neg_lo:[0,1] neg_hi:[0,1]
	v_pk_add_f16 v16, v67, v76 neg_lo:[0,1] neg_hi:[0,1]
	v_pk_add_f16 v17, v66, v77 neg_lo:[0,1] neg_hi:[0,1]
	v_exp_f16_sdwa v18, v14 dst_sel:WORD_0 dst_unused:UNUSED_PAD src0_sel:WORD_0
	v_exp_f16_sdwa v19, v15 dst_sel:WORD_0 dst_unused:UNUSED_PAD src0_sel:WORD_0
	v_exp_f16_sdwa v20, v16 dst_sel:WORD_0 dst_unused:UNUSED_PAD src0_sel:WORD_0
	v_exp_f16_sdwa v21, v17 dst_sel:WORD_0 dst_unused:UNUSED_PAD src0_sel:WORD_0
	v_exp_f16_sdwa v18, v14 dst_sel:WORD_1 dst_unused:UNUSED_PRESERVE src0_sel:WORD_1
	v_exp_f16_sdwa v19, v15 dst_sel:WORD_1 dst_unused:UNUSED_PRESERVE src0_sel:WORD_1
	v_exp_f16_sdwa v20, v16 dst_sel:WORD_1 dst_unused:UNUSED_PRESERVE src0_sel:WORD_1
	v_exp_f16_sdwa v21, v17 dst_sel:WORD_1 dst_unused:UNUSED_PRESERVE src0_sel:WORD_1
	v_pk_add_f16 v14, v73, v74 neg_lo:[0,1] neg_hi:[0,1]
	v_pk_add_f16 v10, v10, v18
	v_pk_add_f16 v11, v11, v19
	v_pk_add_f16 v12, v12, v20
	v_pk_add_f16 v13, v13, v21
	v_pk_fma_f16 v6, v38, v18, v6
	v_pk_fma_f16 v7, v39, v19, v7
	v_pk_fma_f16 v8, v40, v20, v8
	v_pk_fma_f16 v9, v41, v21, v9
	v_pk_add_f16 v15, v72, v75 neg_lo:[0,1] neg_hi:[0,1]
	v_pk_add_f16 v16, v71, v76 neg_lo:[0,1] neg_hi:[0,1]
	v_pk_add_f16 v17, v70, v77 neg_lo:[0,1] neg_hi:[0,1]
	v_exp_f16_sdwa v18, v14 dst_sel:WORD_0 dst_unused:UNUSED_PAD src0_sel:WORD_0
	v_exp_f16_sdwa v19, v15 dst_sel:WORD_0 dst_unused:UNUSED_PAD src0_sel:WORD_0
	v_exp_f16_sdwa v20, v16 dst_sel:WORD_0 dst_unused:UNUSED_PAD src0_sel:WORD_0
	v_exp_f16_sdwa v21, v17 dst_sel:WORD_0 dst_unused:UNUSED_PAD src0_sel:WORD_0
	v_exp_f16_sdwa v18, v14 dst_sel:WORD_1 dst_unused:UNUSED_PRESERVE src0_sel:WORD_1
	v_exp_f16_sdwa v19, v15 dst_sel:WORD_1 dst_unused:UNUSED_PRESERVE src0_sel:WORD_1
	v_exp_f16_sdwa v20, v16 dst_sel:WORD_1 dst_unused:UNUSED_PRESERVE src0_sel:WORD_1
	v_exp_f16_sdwa v21, v17 dst_sel:WORD_1 dst_unused:UNUSED_PRESERVE src0_sel:WORD_1
	v_pk_add_f16 v14, v30, v74 neg_lo:[0,1] neg_hi:[0,1]
	v_pk_add_f16 v13, v13, v21
	v_pk_add_f16 v12, v12, v20
	v_pk_add_f16 v11, v11, v19
	v_pk_add_f16 v10, v10, v18
	v_pk_fma_f16 v9, v61, v21, v9
	v_pk_fma_f16 v8, v60, v20, v8
	v_pk_fma_f16 v7, v59, v19, v7
	v_pk_fma_f16 v6, v58, v18, v6
	v_pk_add_f16 v15, v31, v75 neg_lo:[0,1] neg_hi:[0,1]
	v_pk_add_f16 v16, v32, v76 neg_lo:[0,1] neg_hi:[0,1]
	v_pk_add_f16 v17, v33, v77 neg_lo:[0,1] neg_hi:[0,1]
	v_exp_f16_sdwa v18, v14 dst_sel:WORD_0 dst_unused:UNUSED_PAD src0_sel:WORD_0
	v_exp_f16_sdwa v19, v15 dst_sel:WORD_0 dst_unused:UNUSED_PAD src0_sel:WORD_0
	v_exp_f16_sdwa v20, v16 dst_sel:WORD_0 dst_unused:UNUSED_PAD src0_sel:WORD_0
	v_exp_f16_sdwa v21, v17 dst_sel:WORD_0 dst_unused:UNUSED_PAD src0_sel:WORD_0
	v_exp_f16_sdwa v18, v14 dst_sel:WORD_1 dst_unused:UNUSED_PRESERVE src0_sel:WORD_1
	v_exp_f16_sdwa v19, v15 dst_sel:WORD_1 dst_unused:UNUSED_PRESERVE src0_sel:WORD_1
	v_exp_f16_sdwa v20, v16 dst_sel:WORD_1 dst_unused:UNUSED_PRESERVE src0_sel:WORD_1
	v_exp_f16_sdwa v21, v17 dst_sel:WORD_1 dst_unused:UNUSED_PRESERVE src0_sel:WORD_1
	v_pk_add_f16 v10, v10, v18
	v_pk_add_f16 v11, v11, v19
	v_pk_add_f16 v12, v12, v20
	v_pk_add_f16 v13, v13, v21
	v_pk_fma_f16 v14, v78, v18, v6
	v_pk_fma_f16 v15, v79, v19, v7
	v_pk_fma_f16 v16, v80, v20, v8
	v_pk_fma_f16 v17, v81, v21, v9
	v_pk_add_f16 v6, v42, v74 neg_lo:[0,1] neg_hi:[0,1]
	v_pk_add_f16 v7, v43, v75 neg_lo:[0,1] neg_hi:[0,1]
	v_pk_add_f16 v8, v44, v76 neg_lo:[0,1] neg_hi:[0,1]
	v_pk_add_f16 v9, v45, v77 neg_lo:[0,1] neg_hi:[0,1]
	v_exp_f16_sdwa v18, v6 dst_sel:WORD_0 dst_unused:UNUSED_PAD src0_sel:WORD_0
	v_exp_f16_sdwa v19, v7 dst_sel:WORD_0 dst_unused:UNUSED_PAD src0_sel:WORD_0
	v_exp_f16_sdwa v20, v8 dst_sel:WORD_0 dst_unused:UNUSED_PAD src0_sel:WORD_0
	v_exp_f16_sdwa v21, v9 dst_sel:WORD_0 dst_unused:UNUSED_PAD src0_sel:WORD_0
	v_exp_f16_sdwa v18, v6 dst_sel:WORD_1 dst_unused:UNUSED_PRESERVE src0_sel:WORD_1
	v_exp_f16_sdwa v19, v7 dst_sel:WORD_1 dst_unused:UNUSED_PRESERVE src0_sel:WORD_1
	v_exp_f16_sdwa v20, v8 dst_sel:WORD_1 dst_unused:UNUSED_PRESERVE src0_sel:WORD_1
	v_exp_f16_sdwa v21, v9 dst_sel:WORD_1 dst_unused:UNUSED_PRESERVE src0_sel:WORD_1
	s_nop 0
	v_pk_add_f16 v9, v13, v21
	v_pk_add_f16 v8, v12, v20
	v_pk_add_f16 v7, v11, v19
	v_pk_add_f16 v6, v10, v18
	v_pk_fma_f16 v13, v93, v21, v17
	v_pk_fma_f16 v12, v92, v20, v16
	v_pk_fma_f16 v11, v91, v19, v15
	v_pk_fma_f16 v10, v90, v18, v14
	v_pk_add_f16 v18, v46, v74 neg_lo:[0,1] neg_hi:[0,1]
	v_pk_add_f16 v19, v47, v75 neg_lo:[0,1] neg_hi:[0,1]
	v_pk_add_f16 v20, v48, v76 neg_lo:[0,1] neg_hi:[0,1]
	v_pk_add_f16 v21, v49, v77 neg_lo:[0,1] neg_hi:[0,1]
	v_exp_f16_sdwa v14, v18 dst_sel:WORD_0 dst_unused:UNUSED_PAD src0_sel:WORD_0
	v_exp_f16_sdwa v17, v19 dst_sel:WORD_0 dst_unused:UNUSED_PAD src0_sel:WORD_0
	v_exp_f16_sdwa v15, v20 dst_sel:WORD_0 dst_unused:UNUSED_PAD src0_sel:WORD_0
	v_exp_f16_sdwa v16, v21 dst_sel:WORD_0 dst_unused:UNUSED_PAD src0_sel:WORD_0
	v_exp_f16_sdwa v14, v18 dst_sel:WORD_1 dst_unused:UNUSED_PRESERVE src0_sel:WORD_1
	v_exp_f16_sdwa v17, v19 dst_sel:WORD_1 dst_unused:UNUSED_PRESERVE src0_sel:WORD_1
	v_exp_f16_sdwa v15, v20 dst_sel:WORD_1 dst_unused:UNUSED_PRESERVE src0_sel:WORD_1
	v_exp_f16_sdwa v16, v21 dst_sel:WORD_1 dst_unused:UNUSED_PRESERVE src0_sel:WORD_1
	s_nop 0
.LBB3_45:
	s_and_b64 vcc, exec, s[4:5]
	s_cbranch_vccz .LBB3_6
	s_load_dwordx2 s[0:1], s[22:23], 0x18
	s_waitcnt lgkmcnt(0)
	s_load_dwordx2 s[6:7], s[0:1], 0x0
	s_load_dword s28, s[0:1], 0x8
	v_cmp_lt_u32_e64 s[64:65], 0, v182
	v_cmp_gt_u32_e64 s[66:67], 63, v182
	v_cmp_lt_u32_e64 s[68:69], 0, v162
	v_cmp_gt_u32_e64 s[70:71], 60, v162
	buffer_load_dwordx4 v[184:187], v180, s[16:19], 0 offen
	s_and_b64 s[72:73], s[68:69], s[64:65]
	s_and_b64 s[74:75], s[68:69], s[66:67]
	s_and_b64 s[76:77], s[70:71], s[64:65]
	s_and_b64 s[78:79], s[70:71], s[66:67]
	v_add_u32_e32 v249, 0xfffe7c00, v180
	v_add_u32_e32 v250, 0xfffe8000, v180
	s_mov_b64 exec, s[72:73]
	buffer_load_dwordx4 v[110:113], v249, s[16:19], 0 offen
	buffer_load_dwordx4 v[78:81], v249, s[16:19], 0 offen offset:512
	s_mov_b64 exec, -1
	s_mov_b64 exec, s[68:69]
	buffer_load_dwordx4 v[126:129], v250, s[16:19], 0 offen offset:512
	buffer_load_dwordx4 v[102:105], v250, s[16:19], 0 offen offset:1024
	s_mov_b64 exec, -1
	s_mov_b64 exec, s[74:75]
	buffer_load_dwordx4 v[138:141], v250, s[16:19], 0 offen offset:2048
	buffer_load_dwordx4 v[118:121], v250, s[16:19], 0 offen offset:2560
	s_mov_b64 exec, -1
	v_add_u32_e32 v249, 0xfffffc00, v180
	s_mov_b64 exec, s[64:65]
	buffer_load_dwordx4 v[86:89], v249, s[16:19], 0 offen
	buffer_load_dwordx4 v[46:49], v249, s[16:19], 0 offen offset:512
	s_mov_b64 exec, -1
	buffer_load_dwordx4 v[106:109], v180, s[16:19], 0 offen offset:512
	buffer_load_dwordx4 v[62:65], v180, s[16:19], 0 offen offset:1024
	s_mov_b64 exec, s[66:67]
	buffer_load_dwordx4 v[122:125], v180, s[16:19], 0 offen offset:2048
	buffer_load_dwordx4 v[82:85], v180, s[16:19], 0 offen offset:2560
	s_mov_b64 exec, -1
	v_add_u32_e32 v249, 0x17c00, v180
	v_add_u32_e32 v250, 0x18000, v180
	s_mov_b64 exec, s[64:65]
	buffer_load_dwordx4 v[50:53], v249, s[16:19], 0 offen
	buffer_load_dwordx4 v[22:25], v249, s[16:19], 0 offen offset:512
	s_mov_b64 exec, -1
	buffer_load_dwordx4 v[66:69], v250, s[16:19], 0 offen offset:512
	buffer_load_dwordx4 v[34:37], v250, s[16:19], 0 offen offset:1024
	s_mov_b64 exec, s[66:67]
	buffer_load_dwordx4 v[94:97], v250, s[16:19], 0 offen offset:2048
	buffer_load_dwordx4 v[42:45], v250, s[16:19], 0 offen offset:2560
	s_mov_b64 exec, -1
	v_add_u32_e32 v249, 0x18000, v180
	buffer_load_dwordx4 v[154:157], v249, s[16:19], 0 offen
	v_add_u32_e32 v250, 0x30000, v180
	buffer_load_dwordx4 v[150:153], v250, s[16:19], 0 offen
	v_add_u32_e32 v249, 0x48000, v180
	buffer_load_dwordx4 v[146:149], v249, s[16:19], 0 offen
	v_add_u32_e32 v249, 0x2fc00, v180
	v_add_u32_e32 v250, 0x30000, v180
	v_add_u32_e32 v251, 0x47c00, v180
	v_add_u32_e32 v252, 0x48000, v180
	v_add_u32_e32 v253, 0x5fc00, v180
	v_add_u32_e32 v254, 0x60000, v180
	s_not_b64 exec, s[72:73]
	s_cbranch_execz .Lmyf_B2_0
	v_mov_b32_e32 v110, v172
	v_mov_b32_e32 v111, v174
	v_mov_b32_e32 v112, v176
	v_mov_b32_e32 v113, v178
	v_mov_b32_e32 v78, v173
	v_mov_b32_e32 v79, v175
	v_mov_b32_e32 v80, v177
	v_mov_b32_e32 v81, v179
.Lmyf_B2_0:
	s_not_b64 exec, s[68:69]
	s_cbranch_execz .Lmyf_B2_1
	v_mov_b32_e32 v126, v172
	v_mov_b32_e32 v127, v174
	v_mov_b32_e32 v128, v176
	v_mov_b32_e32 v129, v178
	v_mov_b32_e32 v102, v173
	v_mov_b32_e32 v103, v175
	v_mov_b32_e32 v104, v177
	v_mov_b32_e32 v105, v179
.Lmyf_B2_1:
	s_not_b64 exec, s[74:75]
	s_cbranch_execz .Lmyf_B2_2
	v_mov_b32_e32 v138, v172
	v_mov_b32_e32 v139, v174
	v_mov_b32_e32 v140, v176
	v_mov_b32_e32 v141, v178
	v_mov_b32_e32 v118, v173
	v_mov_b32_e32 v119, v175
	v_mov_b32_e32 v120, v177
	v_mov_b32_e32 v121, v179
.Lmyf_B2_2:
	s_not_b64 exec, s[64:65]
	s_cbranch_execz .Lmyf_B2_3
	v_mov_b32_e32 v86, v172
	v_mov_b32_e32 v87, v174
	v_mov_b32_e32 v88, v176
	v_mov_b32_e32 v89, v178
	v_mov_b32_e32 v46, v173
	v_mov_b32_e32 v47, v175
	v_mov_b32_e32 v48, v177
	v_mov_b32_e32 v49, v179
	v_mov_b32_e32 v50, v172
	v_mov_b32_e32 v51, v174
	v_mov_b32_e32 v52, v176
	v_mov_b32_e32 v53, v178
	v_mov_b32_e32 v22, v173
	v_mov_b32_e32 v23, v175
	v_mov_b32_e32 v24, v177
	v_mov_b32_e32 v25, v179
	v_mov_b32_e32 v18, v172
	v_mov_b32_e32 v19, v174
	v_mov_b32_e32 v20, v176
	v_mov_b32_e32 v21, v178
	v_mov_b32_e32 v6, v173
	v_mov_b32_e32 v7, v175
	v_mov_b32_e32 v8, v177
	v_mov_b32_e32 v9, v179
	v_mov_b32_e32 v74, v172
	v_mov_b32_e32 v75, v174
	v_mov_b32_e32 v76, v176
	v_mov_b32_e32 v77, v178
	v_mov_b32_e32 v26, v173
	v_mov_b32_e32 v27, v175
	v_mov_b32_e32 v28, v177
	v_mov_b32_e32 v29, v179
.Lmyf_B2_3:
	s_not_b64 exec, s[66:67]
	s_cbranch_execz .Lmyf_B2_4
	v_mov_b32_e32 v122, v172
	v_mov_b32_e32 v123, v174
	v_mov_b32_e32 v124, v176
	v_mov_b32_e32 v125, v178
	v_mov_b32_e32 v82, v173
	v_mov_b32_e32 v83, v175
	v_mov_b32_e32 v84, v177
	v_mov_b32_e32 v85, v179
	v_mov_b32_e32 v94, v172
	v_mov_b32_e32 v95, v174
	v_mov_b32_e32 v96, v176
	v_mov_b32_e32 v97, v178
	v_mov_b32_e32 v42, v173
	v_mov_b32_e32 v43, v175
	v_mov_b32_e32 v44, v177
	v_mov_b32_e32 v45, v179
	v_mov_b32_e32 v54, v172
	v_mov_b32_e32 v55, v174
	v_mov_b32_e32 v56, v176
	v_mov_b32_e32 v57, v178
	v_mov_b32_e32 v14, v173
	v_mov_b32_e32 v15, v175
	v_mov_b32_e32 v16, v177
	v_mov_b32_e32 v17, v179
	v_mov_b32_e32 v114, v172
	v_mov_b32_e32 v115, v174
	v_mov_b32_e32 v116, v176
	v_mov_b32_e32 v117, v178
	v_mov_b32_e32 v58, v173
	v_mov_b32_e32 v59, v175
	v_mov_b32_e32 v60, v177
	v_mov_b32_e32 v61, v179
.Lmyf_B2_4:
	s_not_b64 exec, s[76:77]
	s_cbranch_execz .Lmyf_B2_5
	v_mov_b32_e32 v130, v172
	v_mov_b32_e32 v131, v174
	v_mov_b32_e32 v132, v176
	v_mov_b32_e32 v133, v178
	v_mov_b32_e32 v70, v173
	v_mov_b32_e32 v71, v175
	v_mov_b32_e32 v72, v177
	v_mov_b32_e32 v73, v179
.Lmyf_B2_5:
	s_not_b64 exec, s[70:71]
	s_cbranch_execz .Lmyf_B2_6
	v_mov_b32_e32 v134, v172
	v_mov_b32_e32 v135, v174
	v_mov_b32_e32 v136, v176
	v_mov_b32_e32 v137, v178
	v_mov_b32_e32 v90, v173
	v_mov_b32_e32 v91, v175
	v_mov_b32_e32 v92, v177
	v_mov_b32_e32 v93, v179

.Lmyf_B2_7:
	s_mov_b64 exec, -1
	s_branch .LBB3_5

.LBB4_4:
	global_load_dwordx4 v[2:5], v[170:171], off
	global_load_dwordx4 v[8:11], v[172:173], off
	global_load_dwordx4 v[22:25], v[170:171], off offset:16
	global_load_dwordx4 v[26:29], v[172:173], off offset:16
	s_lshl_b32 s48, s46, 3
	s_add_i32 s48, s48, s44
	v_or_b32_e32 v199, s48, v178
	v_add_u32_e32 v168, v199, v181
	v_add_u32_e32 v201, -1, v199
	v_mul_lo_u32 v6, v168, s47
	v_or_b32_e32 v7, v201, v182
	v_or_b32_e32 v6, v6, v166
	s_mov_b64 s[4:5], -1
	s_and_b64 vcc, exec, s[26:27]
	v_cmp_gt_u32_e64 s[2:3], 64, v7
	v_lshlrev_b32_e32 v200, 1, v6
	s_waitcnt vmcnt(3)
	v_cvt_pk_f16_f32 v6, v2, v3
	s_waitcnt vmcnt(2)
	v_cvt_pk_f16_f32 v2, v8, v9
	v_cvt_pk_f16_f32 v7, v4, v5
	v_cvt_pk_f16_f32 v3, v10, v11
	s_waitcnt vmcnt(1)
	v_cvt_pk_f16_f32 v8, v22, v23
	s_waitcnt vmcnt(0)
	v_cvt_pk_f16_f32 v4, v26, v27
	v_cvt_pk_f16_f32 v9, v24, v25
	v_cvt_pk_f16_f32 v5, v28, v29
	s_cbranch_vccz .LBB4_42
	global_load_dwordx3 v[154:156], v169, s[10:11]
	v_cmp_lt_u32_e64 s[64:65], 0, v199
	v_cmp_gt_u32_e64 s[66:67], 63, v199
	v_cmp_lt_u32_e64 s[68:69], 0, v180
	v_cmp_gt_u32_e64 s[70:71], 60, v180
	buffer_load_dwordx4 v[206:209], v200, s[36:39], 0 offen
	s_and_b64 s[72:73], s[68:69], s[64:65]
	s_and_b64 s[74:75], s[68:69], s[66:67]
	s_and_b64 s[76:77], s[70:71], s[64:65]
	s_and_b64 s[78:79], s[70:71], s[66:67]
	v_add_u32_e32 v245, 0xfffe7c00, v200
	v_add_u32_e32 v246, 0xfffe8000, v200
	s_mov_b64 exec, s[72:73]
	buffer_load_dwordx4 v[122:125], v245, s[36:39], 0 offen
	buffer_load_dwordx4 v[82:85], v245, s[36:39], 0 offen offset:512
	s_mov_b64 exec, -1
	s_mov_b64 exec, s[68:69]
	buffer_load_dwordx4 v[138:141], v246, s[36:39], 0 offen offset:512
	buffer_load_dwordx4 v[106:109], v246, s[36:39], 0 offen offset:1024
	s_mov_b64 exec, -1
	s_mov_b64 exec, s[74:75]
	buffer_load_dwordx4 v[146:149], v246, s[36:39], 0 offen offset:2048
	buffer_load_dwordx4 v[126:129], v246, s[36:39], 0 offen offset:2560
	s_mov_b64 exec, -1
	v_add_u32_e32 v245, 0xfffffc00, v200
	s_mov_b64 exec, s[64:65]
	buffer_load_dwordx4 v[94:97], v245, s[36:39], 0 offen
	buffer_load_dwordx4 v[54:57], v245, s[36:39], 0 offen offset:512
	s_mov_b64 exec, -1
	buffer_load_dwordx4 v[118:121], v200, s[36:39], 0 offen offset:512
	buffer_load_dwordx4 v[74:77], v200, s[36:39], 0 offen offset:1024
	s_mov_b64 exec, s[66:67]
	buffer_load_dwordx4 v[134:137], v200, s[36:39], 0 offen offset:2048
	buffer_load_dwordx4 v[98:101], v200, s[36:39], 0 offen offset:2560
	s_mov_b64 exec, -1
	v_add_u32_e32 v245, 0x17c00, v200
	v_add_u32_e32 v246, 0x18000, v200
	s_mov_b64 exec, s[64:65]
	buffer_load_dwordx4 v[62:65], v245, s[36:39], 0 offen
	buffer_load_dwordx4 v[30:33], v245, s[36:39], 0 offen offset:512
	s_mov_b64 exec, -1
	buffer_load_dwordx4 v[78:81], v246, s[36:39], 0 offen offset:512
	buffer_load_dwordx4 v[42:45], v246, s[36:39], 0 offen offset:1024
	s_mov_b64 exec, s[66:67]
	buffer_load_dwordx4 v[102:105], v246, s[36:39], 0 offen offset:2048
	buffer_load_dwordx4 v[58:61], v246, s[36:39], 0 offen offset:2560
	s_mov_b64 exec, -1
	v_add_u32_e32 v245, 0x18000, v200
	buffer_load_dwordx4 v[162:165], v245, s[36:39], 0 offen
	v_add_u32_e32 v246, 0x30000, v200
	buffer_load_dwordx4 v[158:161], v246, s[36:39], 0 offen
	v_add_u32_e32 v245, 0x2fc00, v200
	v_add_u32_e32 v246, 0x30000, v200
	v_add_u32_e32 v247, 0x47c00, v200
	v_add_u32_e32 v248, 0x48000, v200
	v_add_u32_e32 v249, 0x5fc00, v200
	v_add_u32_e32 v250, 0x60000, v200
	s_not_b64 exec, s[72:73]
	s_cbranch_execz .Lmyf_C1_0
	v_mov_b32_e32 v122, v6
	v_mov_b32_e32 v123, v7
	v_mov_b32_e32 v124, v8
	v_mov_b32_e32 v125, v9
	v_mov_b32_e32 v82, v2
	v_mov_b32_e32 v83, v3
	v_mov_b32_e32 v84, v4
	v_mov_b32_e32 v85, v5
.Lmyf_C1_0:
	s_not_b64 exec, s[68:69]
	s_cbranch_execz .Lmyf_C1_1
	v_mov_b32_e32 v138, v6
	v_mov_b32_e32 v139, v7
	v_mov_b32_e32 v140, v8
	v_mov_b32_e32 v141, v9
	v_mov_b32_e32 v106, v2
	v_mov_b32_e32 v107, v3
	v_mov_b32_e32 v108, v4
	v_mov_b32_e32 v109, v5
.Lmyf_C1_1:
	s_not_b64 exec, s[74:75]
	s_cbranch_execz .Lmyf_C1_2
	v_mov_b32_e32 v146, v6
	v_mov_b32_e32 v147, v7
	v_mov_b32_e32 v148, v8
	v_mov_b32_e32 v149, v9
	v_mov_b32_e32 v126, v2
	v_mov_b32_e32 v127, v3
	v_mov_b32_e32 v128, v4
	v_mov_b32_e32 v129, v5
.Lmyf_C1_2:
	s_not_b64 exec, s[64:65]
	s_cbranch_execz .Lmyf_C1_3
	v_mov_b32_e32 v94, v6
	v_mov_b32_e32 v95, v7
	v_mov_b32_e32 v96, v8
	v_mov_b32_e32 v97, v9
	v_mov_b32_e32 v54, v2
	v_mov_b32_e32 v55, v3
	v_mov_b32_e32 v56, v4
	v_mov_b32_e32 v57, v5
	v_mov_b32_e32 v62, v6
	v_mov_b32_e32 v63, v7
	v_mov_b32_e32 v64, v8
	v_mov_b32_e32 v65, v9
	v_mov_b32_e32 v30, v2
	v_mov_b32_e32 v31, v3
	v_mov_b32_e32 v32, v4
	v_mov_b32_e32 v33, v5
	v_mov_b32_e32 v34, v6
	v_mov_b32_e32 v35, v7
	v_mov_b32_e32 v36, v8
	v_mov_b32_e32 v37, v9
	v_mov_b32_e32 v18, v2
	v_mov_b32_e32 v19, v3
	v_mov_b32_e32 v20, v4
	v_mov_b32_e32 v21, v5
	v_mov_b32_e32 v86, v6
	v_mov_b32_e32 v87, v7
	v_mov_b32_e32 v88, v8
	v_mov_b32_e32 v89, v9
	v_mov_b32_e32 v38, v2
	v_mov_b32_e32 v39, v3
	v_mov_b32_e32 v40, v4
	v_mov_b32_e32 v41, v5
.Lmyf_C1_3:
	s_not_b64 exec, s[66:67]
	s_cbranch_execz .Lmyf_C1_4
	v_mov_b32_e32 v134, v6
	v_mov_b32_e32 v135, v7
	v_mov_b32_e32 v136, v8
	v_mov_b32_e32 v137, v9
	v_mov_b32_e32 v98, v2
	v_mov_b32_e32 v99, v3
	v_mov_b32_e32 v100, v4
	v_mov_b32_e32 v101, v5
	v_mov_b32_e32 v102, v6
	v_mov_b32_e32 v103, v7
	v_mov_b32_e32 v104, v8
	v_mov_b32_e32 v105, v9
	v_mov_b32_e32 v58, v2
	v_mov_b32_e32 v59, v3
	v_mov_b32_e32 v60, v4
	v_mov_b32_e32 v61, v5
	v_mov_b32_e32 v66, v6
	v_mov_b32_e32 v67, v7
	v_mov_b32_e32 v68, v8
	v_mov_b32_e32 v69, v9
	v_mov_b32_e32 v26, v2
	v_mov_b32_e32 v27, v3
	v_mov_b32_e32 v28, v4
	v_mov_b32_e32 v29, v5
	v_mov_b32_e32 v130, v6
	v_mov_b32_e32 v131, v7
	v_mov_b32_e32 v132, v8
	v_mov_b32_e32 v133, v9
	v_mov_b32_e32 v70, v2
	v_mov_b32_e32 v71, v3
	v_mov_b32_e32 v72, v4
	v_mov_b32_e32 v73, v5
.Lmyf_C1_4:
	s_not_b64 exec, s[76:77]
	s_cbranch_execz .Lmyf_C1_5
	v_mov_b32_e32 v142, v6
	v_mov_b32_e32 v143, v7
	v_mov_b32_e32 v144, v8
	v_mov_b32_e32 v145, v9
	v_mov_b32_e32 v90, v2
	v_mov_b32_e32 v91, v3
	v_mov_b32_e32 v92, v4
	v_mov_b32_e32 v93, v5
.Lmyf_C1_5:
	s_not_b64 exec, s[70:71]
	s_cbranch_execz .Lmyf_C1_6
	v_mov_b32_e32 v150, v6
	v_mov_b32_e32 v151, v7
	v_mov_b32_e32 v152, v8
	v_mov_b32_e32 v153, v9
	v_mov_b32_e32 v110, v2
	v_mov_b32_e32 v111, v3
	v_mov_b32_e32 v112, v4
	v_mov_b32_e32 v113, v5
.Lmyf_C1_6:
	s_not_b64 exec, s[78:79]
	s_cbranch_execz .Lmyf_C1_7
	v_mov_b32_e32 v14, v6
	v_mov_b32_e32 v15, v7
	v_mov_b32_e32 v16, v8
	v_mov_b32_e32 v17, v9
	v_mov_b32_e32 v10, v2
	v_mov_b32_e32 v11, v3
	v_mov_b32_e32 v12, v4
	v_mov_b32_e32 v13, v5
.Lmyf_C1_7:
	s_mov_b64 exec, -1
	s_waitcnt vmcnt(21)
	v_cvt_f16_f32_e32 v202, v155
	v_cvt_f16_f32_e32 v204, v154
	v_cvt_f16_f32_e32 v203, v156
	v_add_u32_e32 v251, 0x48000, v200
	buffer_load_dwordx4 v[154:157], v251, s[36:39], 0 offen
	s_mov_b64 s[4:5], 0
	s_waitcnt vmcnt(3)
	v_pk_mul_f16 v212, v204, v209 op_sel_hi:[0,1]
	v_pk_mul_f16 v216, v202, v209 op_sel_hi:[0,1]
	v_pk_mul_f16 v220, v203, v209 op_sel_hi:[0,1]
	v_pk_mul_f16 v205, v204, v206 op_sel_hi:[0,1]
	v_pk_mul_f16 v210, v204, v207 op_sel_hi:[0,1]
	v_pk_mul_f16 v211, v204, v208 op_sel_hi:[0,1]
	v_pk_mul_f16 v213, v202, v206 op_sel_hi:[0,1]
	s_mov_b64 exec, s[64:65]
	buffer_load_dwordx4 v[34:37], v245, s[36:39], 0 offen
	buffer_load_dwordx4 v[18:21], v245, s[36:39], 0 offen offset:512
	s_mov_b64 exec, -1
	v_pk_mul_f16 v214, v202, v207 op_sel_hi:[0,1]
	v_pk_mul_f16 v215, v202, v208 op_sel_hi:[0,1]
	v_pk_mul_f16 v217, v203, v206 op_sel_hi:[0,1]
	v_pk_mul_f16 v218, v203, v207 op_sel_hi:[0,1]
	v_pk_mul_f16 v219, v203, v208 op_sel_hi:[0,1]
	v_pk_fma_f16 v125, v125, v209, v212
	v_pk_fma_f16 v141, v141, v209, v216
	v_pk_fma_f16 v149, v149, v209, v220
	v_pk_fma_f16 v221, v97, v209, v212
	v_pk_fma_f16 v225, v121, v209, v216
	v_pk_fma_f16 v229, v137, v209, v220
	v_pk_fma_f16 v212, v65, v209, v212
	v_pk_fma_f16 v216, v81, v209, v216
	buffer_load_dwordx4 v[46:49], v246, s[36:39], 0 offen offset:512
	buffer_load_dwordx4 v[22:25], v246, s[36:39], 0 offen offset:1024
	v_pk_fma_f16 v209, v105, v209, v220
	v_pk_maximum3_f16 v220, v125, v141, v149
	v_pk_fma_f16 v124, v124, v208, v211
	v_pk_fma_f16 v123, v123, v207, v210
	v_pk_fma_f16 v122, v122, v206, v205
	v_pk_fma_f16 v140, v140, v208, v215
	v_pk_fma_f16 v139, v139, v207, v214
	v_pk_fma_f16 v138, v138, v206, v213
	v_pk_fma_f16 v148, v148, v208, v219
	v_pk_fma_f16 v147, v147, v207, v218
	v_pk_fma_f16 v146, v146, v206, v217
	v_pk_fma_f16 v222, v96, v208, v211
	v_pk_fma_f16 v223, v95, v207, v210
	v_pk_fma_f16 v224, v94, v206, v205
	v_pk_fma_f16 v226, v120, v208, v215
	v_pk_fma_f16 v227, v119, v207, v214
	s_mov_b64 exec, s[66:67]
	buffer_load_dwordx4 v[66:69], v246, s[36:39], 0 offen offset:2048
	buffer_load_dwordx4 v[26:29], v246, s[36:39], 0 offen offset:2560
	s_mov_b64 exec, -1
	v_pk_fma_f16 v228, v118, v206, v213
	v_pk_fma_f16 v230, v136, v208, v219
	v_pk_fma_f16 v231, v135, v207, v218
	v_pk_fma_f16 v232, v134, v206, v217
	v_pk_fma_f16 v211, v64, v208, v211
	v_pk_fma_f16 v210, v63, v207, v210
	v_pk_fma_f16 v205, v62, v206, v205
	v_pk_fma_f16 v215, v80, v208, v215
	v_pk_fma_f16 v214, v79, v207, v214
	v_pk_fma_f16 v213, v78, v206, v213
	v_pk_fma_f16 v208, v104, v208, v219
	v_pk_fma_f16 v207, v103, v207, v218
	v_pk_fma_f16 v206, v102, v206, v217
	v_pk_maximum3_f16 v217, v122, v138, v146
	v_pk_maximum3_f16 v218, v123, v139, v147
	v_pk_maximum3_f16 v219, v124, v140, v148
	v_pk_maximum3_f16 v236, v221, v225, v229
	v_pk_maximum3_f16 v240, v212, v216, v209
	v_pk_maximum3_f16 v233, v224, v228, v232
	v_pk_maximum3_f16 v234, v223, v227, v231
	v_pk_maximum3_f16 v235, v222, v226, v230
	v_pk_maximum3_f16 v237, v205, v213, v206
	v_pk_maximum3_f16 v238, v210, v214, v207
	v_pk_maximum3_f16 v220, v220, v236, v240
	v_pk_maximum3_f16 v239, v211, v215, v208
	v_pk_maximum3_f16 v217, v217, v233, v237
	v_pk_maximum3_f16 v218, v218, v234, v238
	v_pk_maximum3_f16 v219, v219, v235, v239
	v_pk_add_f16 v125, v125, v220 neg_lo:[0,1] neg_hi:[0,1]
	s_mov_b64 exec, s[64:65]
	buffer_load_dwordx4 v[86:89], v247, s[36:39], 0 offen
	buffer_load_dwordx4 v[38:41], v247, s[36:39], 0 offen offset:512
	s_mov_b64 exec, -1
	v_pk_add_f16 v122, v122, v217 neg_lo:[0,1] neg_hi:[0,1]
	v_pk_add_f16 v123, v123, v218 neg_lo:[0,1] neg_hi:[0,1]
	v_pk_add_f16 v124, v124, v219 neg_lo:[0,1] neg_hi:[0,1]
	v_pk_add_f16 v138, v138, v217 neg_lo:[0,1] neg_hi:[0,1]
	v_exp_f16_sdwa v233, v122 dst_sel:WORD_0 dst_unused:UNUSED_PAD src0_sel:WORD_0
	v_exp_f16_sdwa v234, v123 dst_sel:WORD_0 dst_unused:UNUSED_PAD src0_sel:WORD_0
	v_exp_f16_sdwa v235, v124 dst_sel:WORD_0 dst_unused:UNUSED_PAD src0_sel:WORD_0
	v_exp_f16_sdwa v236, v125 dst_sel:WORD_0 dst_unused:UNUSED_PAD src0_sel:WORD_0
	v_exp_f16_sdwa v233, v122 dst_sel:WORD_1 dst_unused:UNUSED_PRESERVE src0_sel:WORD_1
	v_exp_f16_sdwa v234, v123 dst_sel:WORD_1 dst_unused:UNUSED_PRESERVE src0_sel:WORD_1
	v_exp_f16_sdwa v235, v124 dst_sel:WORD_1 dst_unused:UNUSED_PRESERVE src0_sel:WORD_1
	v_exp_f16_sdwa v236, v125 dst_sel:WORD_1 dst_unused:UNUSED_PRESERVE src0_sel:WORD_1
	v_pk_add_f16 v139, v139, v218 neg_lo:[0,1] neg_hi:[0,1]
	v_pk_add_f16 v125, v233, 0
	v_pk_fma_f16 v85, v85, v236, 0
	v_pk_add_f16 v122, v236, 0
	v_pk_add_f16 v123, v235, 0
	v_pk_add_f16 v124, v234, 0
	v_pk_fma_f16 v84, v84, v235, 0
	v_pk_fma_f16 v83, v83, v234, 0
	v_pk_fma_f16 v82, v82, v233, 0
	v_pk_add_f16 v140, v140, v219 neg_lo:[0,1] neg_hi:[0,1]
	buffer_load_dwordx4 v[114:117], v248, s[36:39], 0 offen offset:512
	buffer_load_dwordx4 v[50:53], v248, s[36:39], 0 offen offset:1024
	v_pk_add_f16 v141, v141, v220 neg_lo:[0,1] neg_hi:[0,1]
	v_exp_f16_sdwa v233, v138 dst_sel:WORD_0 dst_unused:UNUSED_PAD src0_sel:WORD_0
	v_exp_f16_sdwa v234, v139 dst_sel:WORD_0 dst_unused:UNUSED_PAD src0_sel:WORD_0
	v_exp_f16_sdwa v235, v140 dst_sel:WORD_0 dst_unused:UNUSED_PAD src0_sel:WORD_0
	v_exp_f16_sdwa v236, v141 dst_sel:WORD_0 dst_unused:UNUSED_PAD src0_sel:WORD_0
	v_exp_f16_sdwa v233, v138 dst_sel:WORD_1 dst_unused:UNUSED_PRESERVE src0_sel:WORD_1
	v_exp_f16_sdwa v234, v139 dst_sel:WORD_1 dst_unused:UNUSED_PRESERVE src0_sel:WORD_1
	v_exp_f16_sdwa v235, v140 dst_sel:WORD_1 dst_unused:UNUSED_PRESERVE src0_sel:WORD_1
	v_exp_f16_sdwa v236, v141 dst_sel:WORD_1 dst_unused:UNUSED_PRESERVE src0_sel:WORD_1
	v_pk_add_f16 v125, v125, v233
	v_pk_fma_f16 v85, v109, v236, v85
	v_pk_add_f16 v109, v149, v220 neg_lo:[0,1] neg_hi:[0,1]
	v_pk_add_f16 v124, v124, v234
	v_pk_add_f16 v123, v123, v235
	v_pk_add_f16 v122, v122, v236
	v_pk_fma_f16 v82, v106, v233, v82
	v_pk_fma_f16 v83, v107, v234, v83
	v_pk_fma_f16 v84, v108, v235, v84
	v_pk_add_f16 v106, v146, v217 neg_lo:[0,1] neg_hi:[0,1]
	v_pk_add_f16 v107, v147, v218 neg_lo:[0,1] neg_hi:[0,1]
	v_pk_add_f16 v108, v148, v219 neg_lo:[0,1] neg_hi:[0,1]
	v_exp_f16_sdwa v138, v106 dst_sel:WORD_0 dst_unused:UNUSED_PAD src0_sel:WORD_0
	v_exp_f16_sdwa v139, v107 dst_sel:WORD_0 dst_unused:UNUSED_PAD src0_sel:WORD_0
	v_exp_f16_sdwa v140, v108 dst_sel:WORD_0 dst_unused:UNUSED_PAD src0_sel:WORD_0
	v_exp_f16_sdwa v141, v109 dst_sel:WORD_0 dst_unused:UNUSED_PAD src0_sel:WORD_0
	v_exp_f16_sdwa v138, v106 dst_sel:WORD_1 dst_unused:UNUSED_PRESERVE src0_sel:WORD_1
	v_exp_f16_sdwa v139, v107 dst_sel:WORD_1 dst_unused:UNUSED_PRESERVE src0_sel:WORD_1
	v_exp_f16_sdwa v140, v108 dst_sel:WORD_1 dst_unused:UNUSED_PRESERVE src0_sel:WORD_1
	v_exp_f16_sdwa v141, v109 dst_sel:WORD_1 dst_unused:UNUSED_PRESERVE src0_sel:WORD_1
	v_pk_add_f16 v109, v125, v138
	v_pk_add_f16 v106, v122, v141
	s_mov_b64 exec, s[66:67]
	buffer_load_dwordx4 v[130:133], v248, s[36:39], 0 offen offset:2048
	buffer_load_dwordx4 v[70:73], v248, s[36:39], 0 offen offset:2560
	s_mov_b64 exec, -1
	v_pk_add_f16 v107, v123, v140
	v_pk_add_f16 v108, v124, v139
	v_pk_fma_f16 v85, v129, v141, v85
	v_pk_fma_f16 v84, v128, v140, v84
	v_pk_fma_f16 v83, v127, v139, v83
	v_pk_fma_f16 v82, v126, v138, v82
	v_pk_add_f16 v122, v224, v217 neg_lo:[0,1] neg_hi:[0,1]
	v_pk_add_f16 v123, v223, v218 neg_lo:[0,1] neg_hi:[0,1]
	v_pk_add_f16 v124, v222, v219 neg_lo:[0,1] neg_hi:[0,1]
	v_pk_add_f16 v125, v221, v220 neg_lo:[0,1] neg_hi:[0,1]
	v_exp_f16_sdwa v126, v122 dst_sel:WORD_0 dst_unused:UNUSED_PAD src0_sel:WORD_0
	v_exp_f16_sdwa v127, v123 dst_sel:WORD_0 dst_unused:UNUSED_PAD src0_sel:WORD_0
	v_exp_f16_sdwa v128, v124 dst_sel:WORD_0 dst_unused:UNUSED_PAD src0_sel:WORD_0
	v_exp_f16_sdwa v129, v125 dst_sel:WORD_0 dst_unused:UNUSED_PAD src0_sel:WORD_0
	v_exp_f16_sdwa v126, v122 dst_sel:WORD_1 dst_unused:UNUSED_PRESERVE src0_sel:WORD_1
	v_exp_f16_sdwa v127, v123 dst_sel:WORD_1 dst_unused:UNUSED_PRESERVE src0_sel:WORD_1
	v_exp_f16_sdwa v128, v124 dst_sel:WORD_1 dst_unused:UNUSED_PRESERVE src0_sel:WORD_1
	v_exp_f16_sdwa v129, v125 dst_sel:WORD_1 dst_unused:UNUSED_PRESERVE src0_sel:WORD_1
	v_pk_add_f16 v122, v228, v217 neg_lo:[0,1] neg_hi:[0,1]
	v_pk_add_f16 v109, v109, v126
	v_pk_add_f16 v108, v108, v127
	v_pk_add_f16 v107, v107, v128
	s_mov_b64 exec, s[76:77]
	buffer_load_dwordx4 v[142:145], v249, s[36:39], 0 offen
	buffer_load_dwordx4 v[90:93], v249, s[36:39], 0 offen offset:512
	s_mov_b64 exec, -1
	v_pk_add_f16 v106, v106, v129
	v_pk_fma_f16 v82, v54, v126, v82
	v_pk_fma_f16 v83, v55, v127, v83
	v_pk_fma_f16 v84, v56, v128, v84
	v_pk_fma_f16 v85, v57, v129, v85
	v_pk_add_f16 v123, v227, v218 neg_lo:[0,1] neg_hi:[0,1]
	v_pk_add_f16 v124, v226, v219 neg_lo:[0,1] neg_hi:[0,1]
	v_pk_add_f16 v125, v225, v220 neg_lo:[0,1] neg_hi:[0,1]
	v_exp_f16_sdwa v126, v122 dst_sel:WORD_0 dst_unused:UNUSED_PAD src0_sel:WORD_0
	v_exp_f16_sdwa v127, v123 dst_sel:WORD_0 dst_unused:UNUSED_PAD src0_sel:WORD_0
	v_exp_f16_sdwa v128, v124 dst_sel:WORD_0 dst_unused:UNUSED_PAD src0_sel:WORD_0
	v_exp_f16_sdwa v129, v125 dst_sel:WORD_0 dst_unused:UNUSED_PAD src0_sel:WORD_0
	v_exp_f16_sdwa v126, v122 dst_sel:WORD_1 dst_unused:UNUSED_PRESERVE src0_sel:WORD_1
	v_exp_f16_sdwa v127, v123 dst_sel:WORD_1 dst_unused:UNUSED_PRESERVE src0_sel:WORD_1
	v_exp_f16_sdwa v128, v124 dst_sel:WORD_1 dst_unused:UNUSED_PRESERVE src0_sel:WORD_1
	v_exp_f16_sdwa v129, v125 dst_sel:WORD_1 dst_unused:UNUSED_PRESERVE src0_sel:WORD_1
	v_pk_add_f16 v122, v232, v217 neg_lo:[0,1] neg_hi:[0,1]
	v_pk_add_f16 v109, v109, v126
	v_pk_add_f16 v106, v106, v129
	v_pk_add_f16 v107, v107, v128
	v_pk_add_f16 v108, v108, v127
	v_pk_fma_f16 v85, v77, v129, v85
	v_pk_fma_f16 v84, v76, v128, v84
	s_mov_b64 exec, s[70:71]
	buffer_load_dwordx4 v[150:153], v250, s[36:39], 0 offen offset:512
	buffer_load_dwordx4 v[110:113], v250, s[36:39], 0 offen offset:1024
	s_mov_b64 exec, -1
	v_pk_fma_f16 v83, v75, v127, v83
	v_pk_fma_f16 v82, v74, v126, v82
	v_pk_add_f16 v123, v231, v218 neg_lo:[0,1] neg_hi:[0,1]
	v_pk_add_f16 v124, v230, v219 neg_lo:[0,1] neg_hi:[0,1]
	v_pk_add_f16 v125, v229, v220 neg_lo:[0,1] neg_hi:[0,1]
	v_exp_f16_sdwa v126, v122 dst_sel:WORD_0 dst_unused:UNUSED_PAD src0_sel:WORD_0
	v_exp_f16_sdwa v127, v123 dst_sel:WORD_0 dst_unused:UNUSED_PAD src0_sel:WORD_0
	v_exp_f16_sdwa v128, v124 dst_sel:WORD_0 dst_unused:UNUSED_PAD src0_sel:WORD_0
	v_exp_f16_sdwa v129, v125 dst_sel:WORD_0 dst_unused:UNUSED_PAD src0_sel:WORD_0
	v_exp_f16_sdwa v126, v122 dst_sel:WORD_1 dst_unused:UNUSED_PRESERVE src0_sel:WORD_1
	v_exp_f16_sdwa v127, v123 dst_sel:WORD_1 dst_unused:UNUSED_PRESERVE src0_sel:WORD_1
	v_exp_f16_sdwa v128, v124 dst_sel:WORD_1 dst_unused:UNUSED_PRESERVE src0_sel:WORD_1
	v_exp_f16_sdwa v129, v125 dst_sel:WORD_1 dst_unused:UNUSED_PRESERVE src0_sel:WORD_1
	v_pk_add_f16 v122, v205, v217 neg_lo:[0,1] neg_hi:[0,1]
	v_pk_add_f16 v109, v109, v126
	v_pk_add_f16 v108, v108, v127
	v_pk_add_f16 v107, v107, v128
	v_pk_add_f16 v106, v106, v129
	v_pk_fma_f16 v82, v98, v126, v82
	v_pk_fma_f16 v83, v99, v127, v83
	v_pk_fma_f16 v84, v100, v128, v84
	v_pk_fma_f16 v85, v101, v129, v85
	s_mov_b64 exec, s[78:79]
	buffer_load_dwordx4 v[14:17], v250, s[36:39], 0 offen offset:2048
	buffer_load_dwordx4 v[10:13], v250, s[36:39], 0 offen offset:2560
	s_mov_b64 exec, -1
	v_pk_add_f16 v123, v210, v218 neg_lo:[0,1] neg_hi:[0,1]
	v_pk_add_f16 v124, v211, v219 neg_lo:[0,1] neg_hi:[0,1]
	v_pk_add_f16 v125, v212, v220 neg_lo:[0,1] neg_hi:[0,1]
	v_exp_f16_sdwa v126, v122 dst_sel:WORD_0 dst_unused:UNUSED_PAD src0_sel:WORD_0
	v_exp_f16_sdwa v127, v123 dst_sel:WORD_0 dst_unused:UNUSED_PAD src0_sel:WORD_0
	v_exp_f16_sdwa v128, v124 dst_sel:WORD_0 dst_unused:UNUSED_PAD src0_sel:WORD_0
	v_exp_f16_sdwa v129, v125 dst_sel:WORD_0 dst_unused:UNUSED_PAD src0_sel:WORD_0
	v_exp_f16_sdwa v126, v122 dst_sel:WORD_1 dst_unused:UNUSED_PRESERVE src0_sel:WORD_1
	v_exp_f16_sdwa v127, v123 dst_sel:WORD_1 dst_unused:UNUSED_PRESERVE src0_sel:WORD_1
	v_exp_f16_sdwa v128, v124 dst_sel:WORD_1 dst_unused:UNUSED_PRESERVE src0_sel:WORD_1
	v_exp_f16_sdwa v129, v125 dst_sel:WORD_1 dst_unused:UNUSED_PRESERVE src0_sel:WORD_1
	v_pk_add_f16 v122, v213, v217 neg_lo:[0,1] neg_hi:[0,1]
	v_pk_add_f16 v109, v109, v126
	v_pk_add_f16 v106, v106, v129
	v_pk_add_f16 v107, v107, v128
	v_pk_add_f16 v108, v108, v127
	v_pk_fma_f16 v85, v33, v129, v85
	v_pk_fma_f16 v84, v32, v128, v84
	v_pk_fma_f16 v83, v31, v127, v83
	v_pk_fma_f16 v82, v30, v126, v82
	v_pk_add_f16 v123, v214, v218 neg_lo:[0,1] neg_hi:[0,1]
	v_pk_add_f16 v124, v215, v219 neg_lo:[0,1] neg_hi:[0,1]
	v_pk_add_f16 v125, v216, v220 neg_lo:[0,1] neg_hi:[0,1]
	v_exp_f16_sdwa v126, v122 dst_sel:WORD_0 dst_unused:UNUSED_PAD src0_sel:WORD_0
	v_exp_f16_sdwa v127, v123 dst_sel:WORD_0 dst_unused:UNUSED_PAD src0_sel:WORD_0
	v_exp_f16_sdwa v128, v124 dst_sel:WORD_0 dst_unused:UNUSED_PAD src0_sel:WORD_0
	v_exp_f16_sdwa v129, v125 dst_sel:WORD_0 dst_unused:UNUSED_PAD src0_sel:WORD_0
	v_exp_f16_sdwa v126, v122 dst_sel:WORD_1 dst_unused:UNUSED_PRESERVE src0_sel:WORD_1
	v_exp_f16_sdwa v127, v123 dst_sel:WORD_1 dst_unused:UNUSED_PRESERVE src0_sel:WORD_1
	v_exp_f16_sdwa v128, v124 dst_sel:WORD_1 dst_unused:UNUSED_PRESERVE src0_sel:WORD_1
	v_exp_f16_sdwa v129, v125 dst_sel:WORD_1 dst_unused:UNUSED_PRESERVE src0_sel:WORD_1
	v_pk_add_f16 v122, v206, v217 neg_lo:[0,1] neg_hi:[0,1]
	v_pk_add_f16 v109, v109, v126
	v_pk_add_f16 v108, v108, v127
	v_pk_add_f16 v107, v107, v128
	v_pk_add_f16 v106, v106, v129
	v_pk_fma_f16 v82, v42, v126, v82
	v_pk_fma_f16 v83, v43, v127, v83
	v_pk_fma_f16 v84, v44, v128, v84
	v_pk_fma_f16 v85, v45, v129, v85
	v_pk_add_f16 v123, v207, v218 neg_lo:[0,1] neg_hi:[0,1]
	v_pk_add_f16 v124, v208, v219 neg_lo:[0,1] neg_hi:[0,1]
	v_pk_add_f16 v125, v209, v220 neg_lo:[0,1] neg_hi:[0,1]
	v_exp_f16_sdwa v126, v122 dst_sel:WORD_0 dst_unused:UNUSED_PAD src0_sel:WORD_0
	v_exp_f16_sdwa v127, v123 dst_sel:WORD_0 dst_unused:UNUSED_PAD src0_sel:WORD_0
	v_exp_f16_sdwa v128, v124 dst_sel:WORD_0 dst_unused:UNUSED_PAD src0_sel:WORD_0
	v_exp_f16_sdwa v129, v125 dst_sel:WORD_0 dst_unused:UNUSED_PAD src0_sel:WORD_0
	v_exp_f16_sdwa v126, v122 dst_sel:WORD_1 dst_unused:UNUSED_PRESERVE src0_sel:WORD_1
	v_exp_f16_sdwa v127, v123 dst_sel:WORD_1 dst_unused:UNUSED_PRESERVE src0_sel:WORD_1
	v_exp_f16_sdwa v128, v124 dst_sel:WORD_1 dst_unused:UNUSED_PRESERVE src0_sel:WORD_1
	v_exp_f16_sdwa v129, v125 dst_sel:WORD_1 dst_unused:UNUSED_PRESERVE src0_sel:WORD_1
	v_pk_add_f16 v109, v109, v126
	v_pk_add_f16 v108, v108, v127
	v_rcp_f16_e32 v122, v109
	v_rcp_f16_sdwa v109, v109 dst_sel:DWORD dst_unused:UNUSED_PAD src0_sel:WORD_1
	v_pk_add_f16 v107, v107, v128
	v_rcp_f16_e32 v123, v108
	v_rcp_f16_sdwa v108, v108 dst_sel:DWORD dst_unused:UNUSED_PAD src0_sel:WORD_1
	v_pk_add_f16 v106, v106, v129
	v_rcp_f16_e32 v124, v107
	v_rcp_f16_sdwa v107, v107 dst_sel:DWORD dst_unused:UNUSED_PAD src0_sel:WORD_1
	v_rcp_f16_e32 v125, v106
	v_rcp_f16_sdwa v106, v106 dst_sel:DWORD dst_unused:UNUSED_PAD src0_sel:WORD_1
	v_pk_fma_f16 v82, v58, v126, v82
	v_pack_b32_f16 v109, v122, v109
	v_pk_fma_f16 v83, v59, v127, v83
	v_pk_mul_f16 v138, v82, v109
	v_pack_b32_f16 v82, v123, v108
	v_pk_fma_f16 v84, v60, v128, v84
	v_pk_mul_f16 v139, v83, v82
	v_pack_b32_f16 v82, v124, v107
	v_pk_fma_f16 v85, v61, v129, v85
	v_pk_mul_f16 v140, v84, v82
	v_pack_b32_f16 v82, v125, v106
	v_pk_mul_f16 v141, v85, v82
	s_waitcnt vmcnt(12)
	v_pk_mul_f16 v85, v204, v165 op_sel_hi:[0,1]
	v_pk_mul_f16 v109, v202, v165 op_sel_hi:[0,1]
	v_pk_mul_f16 v122, v203, v162 op_sel_hi:[0,1]
	v_pk_mul_f16 v125, v203, v165 op_sel_hi:[0,1]
	v_pk_mul_f16 v82, v204, v162 op_sel_hi:[0,1]
	v_pk_mul_f16 v83, v204, v163 op_sel_hi:[0,1]
	v_pk_mul_f16 v84, v204, v164 op_sel_hi:[0,1]
	v_pk_mul_f16 v106, v202, v162 op_sel_hi:[0,1]
	v_pk_mul_f16 v107, v202, v163 op_sel_hi:[0,1]
	v_pk_mul_f16 v108, v202, v164 op_sel_hi:[0,1]
	v_pk_mul_f16 v123, v203, v163 op_sel_hi:[0,1]
	v_pk_mul_f16 v124, v203, v164 op_sel_hi:[0,1]
	v_pk_fma_f16 v97, v97, v165, v85
	v_pk_fma_f16 v121, v121, v165, v109
	v_pk_fma_f16 v126, v137, v165, v125
	v_pk_fma_f16 v129, v134, v162, v122
	v_pk_fma_f16 v134, v65, v165, v85
	v_pk_fma_f16 v146, v81, v165, v109
	v_pk_fma_f16 v205, v105, v165, v125
	v_pk_fma_f16 v85, v37, v165, v85
	v_pk_fma_f16 v109, v49, v165, v109
	v_pk_fma_f16 v125, v69, v165, v125
	v_pk_maximum3_f16 v165, v97, v121, v126
	v_pk_fma_f16 v96, v96, v164, v84
	v_pk_fma_f16 v95, v95, v163, v83
	v_pk_fma_f16 v94, v94, v162, v82
	v_pk_fma_f16 v120, v120, v164, v108
	v_pk_fma_f16 v119, v119, v163, v107
	v_pk_fma_f16 v118, v118, v162, v106
	v_pk_fma_f16 v127, v136, v164, v124
	v_pk_fma_f16 v128, v135, v163, v123
	v_pk_fma_f16 v135, v64, v164, v84
	v_pk_fma_f16 v136, v63, v163, v83
	v_pk_fma_f16 v137, v62, v162, v82
	v_pk_fma_f16 v147, v80, v164, v108
	v_pk_fma_f16 v148, v79, v163, v107
	v_pk_fma_f16 v149, v78, v162, v106
	v_pk_fma_f16 v206, v104, v164, v124
	v_pk_fma_f16 v207, v103, v163, v123
	v_pk_fma_f16 v208, v102, v162, v122
	v_pk_fma_f16 v84, v36, v164, v84
	v_pk_fma_f16 v83, v35, v163, v83
	v_pk_fma_f16 v82, v34, v162, v82
	v_pk_fma_f16 v108, v48, v164, v108
	v_pk_fma_f16 v107, v47, v163, v107
	v_pk_fma_f16 v106, v46, v162, v106
	v_pk_fma_f16 v124, v68, v164, v124
	v_pk_fma_f16 v123, v67, v163, v123
	v_pk_fma_f16 v122, v66, v162, v122
	v_pk_maximum3_f16 v162, v94, v118, v129
	v_pk_maximum3_f16 v163, v95, v119, v128
	v_pk_maximum3_f16 v164, v96, v120, v127
	v_pk_maximum3_f16 v212, v134, v146, v205
	v_pk_maximum3_f16 v216, v85, v109, v125
	v_pk_maximum3_f16 v209, v137, v149, v208
	v_pk_maximum3_f16 v210, v136, v148, v207
	v_pk_maximum3_f16 v211, v135, v147, v206
	v_pk_maximum3_f16 v213, v82, v106, v122
	v_pk_maximum3_f16 v214, v83, v107, v123
	v_pk_maximum3_f16 v165, v165, v212, v216
	v_pk_maximum3_f16 v215, v84, v108, v124
	v_pk_maximum3_f16 v162, v162, v209, v213
	v_pk_maximum3_f16 v163, v163, v210, v214
	v_pk_maximum3_f16 v164, v164, v211, v215
	v_pk_add_f16 v97, v97, v165 neg_lo:[0,1] neg_hi:[0,1]
	v_pk_add_f16 v94, v94, v162 neg_lo:[0,1] neg_hi:[0,1]
	v_pk_add_f16 v95, v95, v163 neg_lo:[0,1] neg_hi:[0,1]
	v_pk_add_f16 v96, v96, v164 neg_lo:[0,1] neg_hi:[0,1]
	v_pk_add_f16 v118, v118, v162 neg_lo:[0,1] neg_hi:[0,1]
	v_exp_f16_sdwa v209, v94 dst_sel:WORD_0 dst_unused:UNUSED_PAD src0_sel:WORD_0
	v_exp_f16_sdwa v210, v95 dst_sel:WORD_0 dst_unused:UNUSED_PAD src0_sel:WORD_0
	v_exp_f16_sdwa v211, v96 dst_sel:WORD_0 dst_unused:UNUSED_PAD src0_sel:WORD_0
	v_exp_f16_sdwa v212, v97 dst_sel:WORD_0 dst_unused:UNUSED_PAD src0_sel:WORD_0
	v_exp_f16_sdwa v209, v94 dst_sel:WORD_1 dst_unused:UNUSED_PRESERVE src0_sel:WORD_1
	v_exp_f16_sdwa v210, v95 dst_sel:WORD_1 dst_unused:UNUSED_PRESERVE src0_sel:WORD_1
	v_exp_f16_sdwa v211, v96 dst_sel:WORD_1 dst_unused:UNUSED_PRESERVE src0_sel:WORD_1
	v_exp_f16_sdwa v212, v97 dst_sel:WORD_1 dst_unused:UNUSED_PRESERVE src0_sel:WORD_1
	v_pk_add_f16 v119, v119, v163 neg_lo:[0,1] neg_hi:[0,1]
	v_pk_add_f16 v97, v209, 0
	v_pk_fma_f16 v57, v57, v212, 0
	v_pk_add_f16 v94, v212, 0
	v_pk_add_f16 v95, v211, 0
	v_pk_add_f16 v96, v210, 0
	v_pk_fma_f16 v56, v56, v211, 0
	v_pk_fma_f16 v55, v55, v210, 0
	v_pk_fma_f16 v54, v54, v209, 0
	v_pk_add_f16 v120, v120, v164 neg_lo:[0,1] neg_hi:[0,1]
	v_pk_add_f16 v121, v121, v165 neg_lo:[0,1] neg_hi:[0,1]
	v_pk_add_f16 v82, v82, v162 neg_lo:[0,1] neg_hi:[0,1]
	v_exp_f16_sdwa v209, v118 dst_sel:WORD_0 dst_unused:UNUSED_PAD src0_sel:WORD_0
	v_exp_f16_sdwa v210, v119 dst_sel:WORD_0 dst_unused:UNUSED_PAD src0_sel:WORD_0
	v_exp_f16_sdwa v211, v120 dst_sel:WORD_0 dst_unused:UNUSED_PAD src0_sel:WORD_0
	v_exp_f16_sdwa v212, v121 dst_sel:WORD_0 dst_unused:UNUSED_PAD src0_sel:WORD_0
	v_exp_f16_sdwa v209, v118 dst_sel:WORD_1 dst_unused:UNUSED_PRESERVE src0_sel:WORD_1
	v_exp_f16_sdwa v210, v119 dst_sel:WORD_1 dst_unused:UNUSED_PRESERVE src0_sel:WORD_1
	v_exp_f16_sdwa v211, v120 dst_sel:WORD_1 dst_unused:UNUSED_PRESERVE src0_sel:WORD_1
	v_exp_f16_sdwa v212, v121 dst_sel:WORD_1 dst_unused:UNUSED_PRESERVE src0_sel:WORD_1
	v_pk_add_f16 v83, v83, v163 neg_lo:[0,1] neg_hi:[0,1]
	v_pk_add_f16 v97, v97, v209
	v_pk_fma_f16 v57, v77, v212, v57
	v_pk_add_f16 v77, v126, v165 neg_lo:[0,1] neg_hi:[0,1]
	v_pk_add_f16 v96, v96, v210
	v_pk_add_f16 v95, v95, v211
	v_pk_add_f16 v94, v94, v212
	v_pk_fma_f16 v54, v74, v209, v54
	v_pk_fma_f16 v55, v75, v210, v55
	v_pk_fma_f16 v56, v76, v211, v56
	v_pk_add_f16 v74, v129, v162 neg_lo:[0,1] neg_hi:[0,1]
	v_pk_add_f16 v75, v128, v163 neg_lo:[0,1] neg_hi:[0,1]
	v_pk_add_f16 v76, v127, v164 neg_lo:[0,1] neg_hi:[0,1]
	v_pk_add_f16 v84, v84, v164 neg_lo:[0,1] neg_hi:[0,1]
	v_exp_f16_sdwa v118, v74 dst_sel:WORD_0 dst_unused:UNUSED_PAD src0_sel:WORD_0
	v_exp_f16_sdwa v119, v75 dst_sel:WORD_0 dst_unused:UNUSED_PAD src0_sel:WORD_0
	v_exp_f16_sdwa v120, v76 dst_sel:WORD_0 dst_unused:UNUSED_PAD src0_sel:WORD_0
	v_exp_f16_sdwa v121, v77 dst_sel:WORD_0 dst_unused:UNUSED_PAD src0_sel:WORD_0
	v_exp_f16_sdwa v118, v74 dst_sel:WORD_1 dst_unused:UNUSED_PRESERVE src0_sel:WORD_1
	v_exp_f16_sdwa v119, v75 dst_sel:WORD_1 dst_unused:UNUSED_PRESERVE src0_sel:WORD_1
	v_exp_f16_sdwa v120, v76 dst_sel:WORD_1 dst_unused:UNUSED_PRESERVE src0_sel:WORD_1
	v_exp_f16_sdwa v121, v77 dst_sel:WORD_1 dst_unused:UNUSED_PRESERVE src0_sel:WORD_1
	v_pk_add_f16 v85, v85, v165 neg_lo:[0,1] neg_hi:[0,1]
	v_pk_add_f16 v77, v97, v118
	v_pk_add_f16 v74, v94, v121
	v_pk_add_f16 v75, v95, v120
	v_pk_add_f16 v76, v96, v119
	v_pk_fma_f16 v57, v101, v121, v57
	v_pk_fma_f16 v56, v100, v120, v56
	v_pk_fma_f16 v55, v99, v119, v55
	v_pk_fma_f16 v54, v98, v118, v54
	v_pk_add_f16 v94, v137, v162 neg_lo:[0,1] neg_hi:[0,1]
	v_pk_add_f16 v95, v136, v163 neg_lo:[0,1] neg_hi:[0,1]
	v_pk_add_f16 v96, v135, v164 neg_lo:[0,1] neg_hi:[0,1]
	v_pk_add_f16 v97, v134, v165 neg_lo:[0,1] neg_hi:[0,1]
	v_exp_f16_sdwa v98, v94 dst_sel:WORD_0 dst_unused:UNUSED_PAD src0_sel:WORD_0
	v_exp_f16_sdwa v99, v95 dst_sel:WORD_0 dst_unused:UNUSED_PAD src0_sel:WORD_0
	v_exp_f16_sdwa v100, v96 dst_sel:WORD_0 dst_unused:UNUSED_PAD src0_sel:WORD_0
	v_exp_f16_sdwa v101, v97 dst_sel:WORD_0 dst_unused:UNUSED_PAD src0_sel:WORD_0
	v_exp_f16_sdwa v98, v94 dst_sel:WORD_1 dst_unused:UNUSED_PRESERVE src0_sel:WORD_1
	v_exp_f16_sdwa v99, v95 dst_sel:WORD_1 dst_unused:UNUSED_PRESERVE src0_sel:WORD_1
	v_exp_f16_sdwa v100, v96 dst_sel:WORD_1 dst_unused:UNUSED_PRESERVE src0_sel:WORD_1
	v_exp_f16_sdwa v101, v97 dst_sel:WORD_1 dst_unused:UNUSED_PRESERVE src0_sel:WORD_1
	v_pk_add_f16 v94, v149, v162 neg_lo:[0,1] neg_hi:[0,1]
	v_pk_add_f16 v77, v77, v98
	v_pk_add_f16 v76, v76, v99
	v_pk_add_f16 v75, v75, v100
	v_pk_add_f16 v74, v74, v101
	v_pk_fma_f16 v54, v30, v98, v54
	v_pk_fma_f16 v55, v31, v99, v55
	v_pk_fma_f16 v56, v32, v100, v56
	v_pk_fma_f16 v57, v33, v101, v57
	v_pk_add_f16 v95, v148, v163 neg_lo:[0,1] neg_hi:[0,1]
	v_pk_add_f16 v96, v147, v164 neg_lo:[0,1] neg_hi:[0,1]
	v_pk_add_f16 v97, v146, v165 neg_lo:[0,1] neg_hi:[0,1]
	v_exp_f16_sdwa v98, v94 dst_sel:WORD_0 dst_unused:UNUSED_PAD src0_sel:WORD_0
	v_exp_f16_sdwa v99, v95 dst_sel:WORD_0 dst_unused:UNUSED_PAD src0_sel:WORD_0
	v_exp_f16_sdwa v100, v96 dst_sel:WORD_0 dst_unused:UNUSED_PAD src0_sel:WORD_0
	v_exp_f16_sdwa v101, v97 dst_sel:WORD_0 dst_unused:UNUSED_PAD src0_sel:WORD_0
	v_exp_f16_sdwa v98, v94 dst_sel:WORD_1 dst_unused:UNUSED_PRESERVE src0_sel:WORD_1
	v_exp_f16_sdwa v99, v95 dst_sel:WORD_1 dst_unused:UNUSED_PRESERVE src0_sel:WORD_1
	v_exp_f16_sdwa v100, v96 dst_sel:WORD_1 dst_unused:UNUSED_PRESERVE src0_sel:WORD_1
	v_exp_f16_sdwa v101, v97 dst_sel:WORD_1 dst_unused:UNUSED_PRESERVE src0_sel:WORD_1
	v_pk_add_f16 v94, v208, v162 neg_lo:[0,1] neg_hi:[0,1]
	v_pk_add_f16 v77, v77, v98
	v_pk_add_f16 v74, v74, v101
	v_pk_add_f16 v75, v75, v100
	v_pk_add_f16 v76, v76, v99
	v_pk_fma_f16 v57, v45, v101, v57
	v_pk_fma_f16 v56, v44, v100, v56
	v_pk_fma_f16 v55, v43, v99, v55
	v_pk_fma_f16 v54, v42, v98, v54
	v_pk_add_f16 v95, v207, v163 neg_lo:[0,1] neg_hi:[0,1]
	v_pk_add_f16 v96, v206, v164 neg_lo:[0,1] neg_hi:[0,1]
	v_pk_add_f16 v97, v205, v165 neg_lo:[0,1] neg_hi:[0,1]
	v_exp_f16_sdwa v98, v94 dst_sel:WORD_0 dst_unused:UNUSED_PAD src0_sel:WORD_0
	v_exp_f16_sdwa v99, v95 dst_sel:WORD_0 dst_unused:UNUSED_PAD src0_sel:WORD_0
	v_exp_f16_sdwa v100, v96 dst_sel:WORD_0 dst_unused:UNUSED_PAD src0_sel:WORD_0
	v_exp_f16_sdwa v101, v97 dst_sel:WORD_0 dst_unused:UNUSED_PAD src0_sel:WORD_0
	v_exp_f16_sdwa v98, v94 dst_sel:WORD_1 dst_unused:UNUSED_PRESERVE src0_sel:WORD_1
	v_exp_f16_sdwa v99, v95 dst_sel:WORD_1 dst_unused:UNUSED_PRESERVE src0_sel:WORD_1
	v_exp_f16_sdwa v100, v96 dst_sel:WORD_1 dst_unused:UNUSED_PRESERVE src0_sel:WORD_1
	v_exp_f16_sdwa v101, v97 dst_sel:WORD_1 dst_unused:UNUSED_PRESERVE src0_sel:WORD_1
	v_exp_f16_sdwa v94, v82 dst_sel:WORD_0 dst_unused:UNUSED_PAD src0_sel:WORD_0
	v_exp_f16_sdwa v95, v83 dst_sel:WORD_0 dst_unused:UNUSED_PAD src0_sel:WORD_0
	v_exp_f16_sdwa v96, v84 dst_sel:WORD_0 dst_unused:UNUSED_PAD src0_sel:WORD_0
	v_exp_f16_sdwa v97, v85 dst_sel:WORD_0 dst_unused:UNUSED_PAD src0_sel:WORD_0
	v_exp_f16_sdwa v94, v82 dst_sel:WORD_1 dst_unused:UNUSED_PRESERVE src0_sel:WORD_1
	v_exp_f16_sdwa v95, v83 dst_sel:WORD_1 dst_unused:UNUSED_PRESERVE src0_sel:WORD_1
	v_exp_f16_sdwa v96, v84 dst_sel:WORD_1 dst_unused:UNUSED_PRESERVE src0_sel:WORD_1
	v_exp_f16_sdwa v97, v85 dst_sel:WORD_1 dst_unused:UNUSED_PRESERVE src0_sel:WORD_1
	v_pk_add_f16 v82, v106, v162 neg_lo:[0,1] neg_hi:[0,1]
	v_pk_add_f16 v77, v77, v98
	v_pk_add_f16 v76, v76, v99
	v_pk_add_f16 v75, v75, v100
	v_pk_add_f16 v74, v74, v101
	v_pk_fma_f16 v54, v58, v98, v54
	v_pk_fma_f16 v55, v59, v99, v55
	v_pk_fma_f16 v56, v60, v100, v56
	v_pk_fma_f16 v57, v61, v101, v57
	v_pk_add_f16 v77, v77, v94
	v_pk_add_f16 v74, v74, v97
	v_pk_add_f16 v75, v75, v96
	v_pk_add_f16 v76, v76, v95
	v_pk_fma_f16 v57, v21, v97, v57
	v_pk_fma_f16 v56, v20, v96, v56
	v_pk_fma_f16 v55, v19, v95, v55
	v_pk_fma_f16 v54, v18, v94, v54
	v_pk_add_f16 v83, v107, v163 neg_lo:[0,1] neg_hi:[0,1]
	v_pk_add_f16 v84, v108, v164 neg_lo:[0,1] neg_hi:[0,1]
	v_pk_add_f16 v85, v109, v165 neg_lo:[0,1] neg_hi:[0,1]
	v_exp_f16_sdwa v94, v82 dst_sel:WORD_0 dst_unused:UNUSED_PAD src0_sel:WORD_0
	v_exp_f16_sdwa v95, v83 dst_sel:WORD_0 dst_unused:UNUSED_PAD src0_sel:WORD_0
	v_exp_f16_sdwa v96, v84 dst_sel:WORD_0 dst_unused:UNUSED_PAD src0_sel:WORD_0
	v_exp_f16_sdwa v97, v85 dst_sel:WORD_0 dst_unused:UNUSED_PAD src0_sel:WORD_0
	v_exp_f16_sdwa v94, v82 dst_sel:WORD_1 dst_unused:UNUSED_PRESERVE src0_sel:WORD_1
	v_exp_f16_sdwa v95, v83 dst_sel:WORD_1 dst_unused:UNUSED_PRESERVE src0_sel:WORD_1
	v_exp_f16_sdwa v96, v84 dst_sel:WORD_1 dst_unused:UNUSED_PRESERVE src0_sel:WORD_1
	v_exp_f16_sdwa v97, v85 dst_sel:WORD_1 dst_unused:UNUSED_PRESERVE src0_sel:WORD_1
	v_pk_add_f16 v82, v122, v162 neg_lo:[0,1] neg_hi:[0,1]
	v_pk_add_f16 v77, v77, v94
	v_pk_add_f16 v76, v76, v95
	v_pk_add_f16 v75, v75, v96
	v_pk_add_f16 v74, v74, v97
	v_pk_fma_f16 v54, v22, v94, v54
	v_pk_fma_f16 v55, v23, v95, v55
	v_pk_fma_f16 v56, v24, v96, v56
	v_pk_fma_f16 v57, v25, v97, v57
	v_pk_add_f16 v83, v123, v163 neg_lo:[0,1] neg_hi:[0,1]
	v_pk_add_f16 v84, v124, v164 neg_lo:[0,1] neg_hi:[0,1]
	v_pk_add_f16 v85, v125, v165 neg_lo:[0,1] neg_hi:[0,1]
	v_exp_f16_sdwa v94, v82 dst_sel:WORD_0 dst_unused:UNUSED_PAD src0_sel:WORD_0
	v_exp_f16_sdwa v95, v83 dst_sel:WORD_0 dst_unused:UNUSED_PAD src0_sel:WORD_0
	v_exp_f16_sdwa v96, v84 dst_sel:WORD_0 dst_unused:UNUSED_PAD src0_sel:WORD_0
	v_exp_f16_sdwa v97, v85 dst_sel:WORD_0 dst_unused:UNUSED_PAD src0_sel:WORD_0
	v_exp_f16_sdwa v94, v82 dst_sel:WORD_1 dst_unused:UNUSED_PRESERVE src0_sel:WORD_1
	v_exp_f16_sdwa v95, v83 dst_sel:WORD_1 dst_unused:UNUSED_PRESERVE src0_sel:WORD_1
	v_exp_f16_sdwa v96, v84 dst_sel:WORD_1 dst_unused:UNUSED_PRESERVE src0_sel:WORD_1
	v_exp_f16_sdwa v97, v85 dst_sel:WORD_1 dst_unused:UNUSED_PRESERVE src0_sel:WORD_1
	v_pk_add_f16 v77, v77, v94
	v_pk_add_f16 v76, v76, v95
	v_rcp_f16_e32 v82, v77
	v_rcp_f16_sdwa v77, v77 dst_sel:DWORD dst_unused:UNUSED_PAD src0_sel:WORD_1
	v_pk_add_f16 v75, v75, v96
	v_rcp_f16_e32 v83, v76
	v_rcp_f16_sdwa v76, v76 dst_sel:DWORD dst_unused:UNUSED_PAD src0_sel:WORD_1
	v_pk_add_f16 v74, v74, v97
	v_rcp_f16_e32 v84, v75
	v_rcp_f16_sdwa v75, v75 dst_sel:DWORD dst_unused:UNUSED_PAD src0_sel:WORD_1
	v_rcp_f16_e32 v85, v74
	v_rcp_f16_sdwa v74, v74 dst_sel:DWORD dst_unused:UNUSED_PAD src0_sel:WORD_1
	v_pk_fma_f16 v54, v26, v94, v54
	v_pack_b32_f16 v77, v82, v77
	v_pk_fma_f16 v55, v27, v95, v55
	v_pk_mul_f16 v77, v54, v77
	v_pack_b32_f16 v54, v83, v76
	v_pk_fma_f16 v56, v28, v96, v56
	v_pk_mul_f16 v76, v55, v54
	v_pack_b32_f16 v54, v84, v75
	v_pk_fma_f16 v57, v29, v97, v57
	v_pk_mul_f16 v75, v56, v54
	v_pack_b32_f16 v54, v85, v74
	v_pk_mul_f16 v74, v57, v54
	s_waitcnt vmcnt(6)
	v_pk_mul_f16 v57, v204, v161 op_sel_hi:[0,1]
	v_pk_mul_f16 v85, v202, v161 op_sel_hi:[0,1]
	v_pk_mul_f16 v97, v203, v161 op_sel_hi:[0,1]
	v_pk_mul_f16 v54, v204, v158 op_sel_hi:[0,1]
	v_pk_mul_f16 v55, v204, v159 op_sel_hi:[0,1]
	v_pk_mul_f16 v56, v204, v160 op_sel_hi:[0,1]
	v_pk_mul_f16 v82, v202, v158 op_sel_hi:[0,1]
	v_pk_mul_f16 v83, v202, v159 op_sel_hi:[0,1]
	v_pk_mul_f16 v84, v202, v160 op_sel_hi:[0,1]
	v_pk_mul_f16 v94, v203, v158 op_sel_hi:[0,1]
	v_pk_mul_f16 v95, v203, v159 op_sel_hi:[0,1]
	v_pk_mul_f16 v96, v203, v160 op_sel_hi:[0,1]
	v_pk_fma_f16 v65, v65, v161, v57
	v_pk_fma_f16 v81, v81, v161, v85
	v_pk_fma_f16 v98, v105, v161, v97
	v_pk_fma_f16 v64, v64, v160, v56
	v_pk_maximum3_f16 v125, v65, v81, v98
	v_pk_fma_f16 v63, v63, v159, v55
	v_pk_fma_f16 v62, v62, v158, v54
	v_pk_fma_f16 v80, v80, v160, v84
	v_pk_fma_f16 v79, v79, v159, v83
	v_pk_fma_f16 v78, v78, v158, v82
	v_pk_fma_f16 v99, v104, v160, v96
	v_pk_fma_f16 v100, v103, v159, v95
	v_pk_fma_f16 v101, v102, v158, v94
	v_pk_fma_f16 v102, v37, v161, v57
	v_pk_fma_f16 v106, v49, v161, v85
	v_pk_fma_f16 v118, v69, v161, v97
	v_pk_fma_f16 v57, v89, v161, v57
	v_pk_fma_f16 v85, v117, v161, v85
	v_pk_fma_f16 v97, v133, v161, v97
	v_pk_maximum3_f16 v122, v62, v78, v101
	v_pk_maximum3_f16 v123, v63, v79, v100
	v_pk_maximum3_f16 v124, v64, v80, v99
	v_pk_maximum3_f16 v129, v102, v106, v118
	v_pk_fma_f16 v103, v36, v160, v56
	v_pk_maximum3_f16 v137, v57, v85, v97
	v_pk_fma_f16 v104, v35, v159, v55
	v_pk_maximum3_f16 v125, v125, v129, v137
	v_pk_fma_f16 v105, v34, v158, v54
	v_pk_fma_f16 v107, v48, v160, v84
	v_pk_fma_f16 v108, v47, v159, v83
	v_pk_fma_f16 v109, v46, v158, v82
	v_pk_fma_f16 v119, v68, v160, v96
	v_pk_fma_f16 v120, v67, v159, v95
	v_pk_fma_f16 v121, v66, v158, v94
	v_pk_fma_f16 v56, v88, v160, v56
	v_pk_fma_f16 v55, v87, v159, v55
	v_pk_fma_f16 v54, v86, v158, v54
	v_pk_fma_f16 v84, v116, v160, v84
	v_pk_fma_f16 v83, v115, v159, v83
	v_pk_fma_f16 v82, v114, v158, v82
	v_pk_fma_f16 v96, v132, v160, v96
	v_pk_fma_f16 v95, v131, v159, v95
	v_pk_fma_f16 v94, v130, v158, v94
	v_pk_maximum3_f16 v126, v105, v109, v121
	v_pk_maximum3_f16 v127, v104, v108, v120
	v_pk_maximum3_f16 v128, v103, v107, v119
	v_pk_maximum3_f16 v135, v55, v83, v95
	v_pk_maximum3_f16 v136, v56, v84, v96
	v_pk_maximum3_f16 v134, v54, v82, v94
	v_pk_maximum3_f16 v122, v122, v126, v134
	v_pk_maximum3_f16 v123, v123, v127, v135
	v_pk_maximum3_f16 v124, v124, v128, v136
	v_pk_add_f16 v65, v65, v125 neg_lo:[0,1] neg_hi:[0,1]
	v_pk_add_f16 v62, v62, v122 neg_lo:[0,1] neg_hi:[0,1]
	v_pk_add_f16 v63, v63, v123 neg_lo:[0,1] neg_hi:[0,1]
	v_pk_add_f16 v64, v64, v124 neg_lo:[0,1] neg_hi:[0,1]
	v_pk_add_f16 v78, v78, v122 neg_lo:[0,1] neg_hi:[0,1]
	v_exp_f16_sdwa v126, v62 dst_sel:WORD_0 dst_unused:UNUSED_PAD src0_sel:WORD_0
	v_exp_f16_sdwa v127, v63 dst_sel:WORD_0 dst_unused:UNUSED_PAD src0_sel:WORD_0
	v_exp_f16_sdwa v128, v64 dst_sel:WORD_0 dst_unused:UNUSED_PAD src0_sel:WORD_0
	v_exp_f16_sdwa v129, v65 dst_sel:WORD_0 dst_unused:UNUSED_PAD src0_sel:WORD_0
	v_exp_f16_sdwa v126, v62 dst_sel:WORD_1 dst_unused:UNUSED_PRESERVE src0_sel:WORD_1
	v_exp_f16_sdwa v127, v63 dst_sel:WORD_1 dst_unused:UNUSED_PRESERVE src0_sel:WORD_1
	v_exp_f16_sdwa v128, v64 dst_sel:WORD_1 dst_unused:UNUSED_PRESERVE src0_sel:WORD_1
	v_exp_f16_sdwa v129, v65 dst_sel:WORD_1 dst_unused:UNUSED_PRESERVE src0_sel:WORD_1
	v_pk_add_f16 v79, v79, v123 neg_lo:[0,1] neg_hi:[0,1]
	v_pk_add_f16 v65, v126, 0
	v_pk_fma_f16 v33, v33, v129, 0
	v_pk_add_f16 v62, v129, 0
	v_pk_add_f16 v63, v128, 0
	v_pk_add_f16 v64, v127, 0
	v_pk_fma_f16 v32, v32, v128, 0
	v_pk_fma_f16 v31, v31, v127, 0
	v_pk_fma_f16 v30, v30, v126, 0
	v_pk_add_f16 v80, v80, v124 neg_lo:[0,1] neg_hi:[0,1]
	v_pk_add_f16 v81, v81, v125 neg_lo:[0,1] neg_hi:[0,1]
	v_pk_add_f16 v54, v54, v122 neg_lo:[0,1] neg_hi:[0,1]
	v_exp_f16_sdwa v126, v78 dst_sel:WORD_0 dst_unused:UNUSED_PAD src0_sel:WORD_0
	v_exp_f16_sdwa v127, v79 dst_sel:WORD_0 dst_unused:UNUSED_PAD src0_sel:WORD_0
	v_exp_f16_sdwa v128, v80 dst_sel:WORD_0 dst_unused:UNUSED_PAD src0_sel:WORD_0
	v_exp_f16_sdwa v129, v81 dst_sel:WORD_0 dst_unused:UNUSED_PAD src0_sel:WORD_0
	v_exp_f16_sdwa v126, v78 dst_sel:WORD_1 dst_unused:UNUSED_PRESERVE src0_sel:WORD_1
	v_exp_f16_sdwa v127, v79 dst_sel:WORD_1 dst_unused:UNUSED_PRESERVE src0_sel:WORD_1
	v_exp_f16_sdwa v128, v80 dst_sel:WORD_1 dst_unused:UNUSED_PRESERVE src0_sel:WORD_1
	v_exp_f16_sdwa v129, v81 dst_sel:WORD_1 dst_unused:UNUSED_PRESERVE src0_sel:WORD_1
	v_pk_add_f16 v55, v55, v123 neg_lo:[0,1] neg_hi:[0,1]
	v_pk_add_f16 v65, v65, v126
	v_pk_fma_f16 v33, v45, v129, v33
	v_pk_add_f16 v45, v98, v125 neg_lo:[0,1] neg_hi:[0,1]
	v_pk_add_f16 v64, v64, v127
	v_pk_add_f16 v63, v63, v128
	v_pk_add_f16 v62, v62, v129
	v_pk_fma_f16 v30, v42, v126, v30
	v_pk_fma_f16 v31, v43, v127, v31
	v_pk_fma_f16 v32, v44, v128, v32
	v_pk_add_f16 v42, v101, v122 neg_lo:[0,1] neg_hi:[0,1]
	v_pk_add_f16 v43, v100, v123 neg_lo:[0,1] neg_hi:[0,1]
	v_pk_add_f16 v44, v99, v124 neg_lo:[0,1] neg_hi:[0,1]
	v_pk_add_f16 v56, v56, v124 neg_lo:[0,1] neg_hi:[0,1]
	v_exp_f16_sdwa v78, v42 dst_sel:WORD_0 dst_unused:UNUSED_PAD src0_sel:WORD_0
	v_exp_f16_sdwa v79, v43 dst_sel:WORD_0 dst_unused:UNUSED_PAD src0_sel:WORD_0
	v_exp_f16_sdwa v80, v44 dst_sel:WORD_0 dst_unused:UNUSED_PAD src0_sel:WORD_0
	v_exp_f16_sdwa v81, v45 dst_sel:WORD_0 dst_unused:UNUSED_PAD src0_sel:WORD_0
	v_exp_f16_sdwa v78, v42 dst_sel:WORD_1 dst_unused:UNUSED_PRESERVE src0_sel:WORD_1
	v_exp_f16_sdwa v79, v43 dst_sel:WORD_1 dst_unused:UNUSED_PRESERVE src0_sel:WORD_1
	v_exp_f16_sdwa v80, v44 dst_sel:WORD_1 dst_unused:UNUSED_PRESERVE src0_sel:WORD_1
	v_exp_f16_sdwa v81, v45 dst_sel:WORD_1 dst_unused:UNUSED_PRESERVE src0_sel:WORD_1
	v_pk_add_f16 v57, v57, v125 neg_lo:[0,1] neg_hi:[0,1]
	v_pk_add_f16 v45, v65, v78
	v_pk_add_f16 v42, v62, v81
	v_pk_add_f16 v43, v63, v80
	v_pk_add_f16 v44, v64, v79
	v_pk_fma_f16 v33, v61, v81, v33
	v_pk_fma_f16 v32, v60, v80, v32
	v_pk_fma_f16 v31, v59, v79, v31
	v_pk_fma_f16 v30, v58, v78, v30
	v_pk_add_f16 v58, v105, v122 neg_lo:[0,1] neg_hi:[0,1]
	v_pk_add_f16 v59, v104, v123 neg_lo:[0,1] neg_hi:[0,1]
	v_pk_add_f16 v60, v103, v124 neg_lo:[0,1] neg_hi:[0,1]
	v_pk_add_f16 v61, v102, v125 neg_lo:[0,1] neg_hi:[0,1]
	v_exp_f16_sdwa v62, v58 dst_sel:WORD_0 dst_unused:UNUSED_PAD src0_sel:WORD_0
	v_exp_f16_sdwa v63, v59 dst_sel:WORD_0 dst_unused:UNUSED_PAD src0_sel:WORD_0
	v_exp_f16_sdwa v64, v60 dst_sel:WORD_0 dst_unused:UNUSED_PAD src0_sel:WORD_0
	v_exp_f16_sdwa v65, v61 dst_sel:WORD_0 dst_unused:UNUSED_PAD src0_sel:WORD_0
	v_exp_f16_sdwa v62, v58 dst_sel:WORD_1 dst_unused:UNUSED_PRESERVE src0_sel:WORD_1
	v_exp_f16_sdwa v63, v59 dst_sel:WORD_1 dst_unused:UNUSED_PRESERVE src0_sel:WORD_1
	v_exp_f16_sdwa v64, v60 dst_sel:WORD_1 dst_unused:UNUSED_PRESERVE src0_sel:WORD_1
	v_exp_f16_sdwa v65, v61 dst_sel:WORD_1 dst_unused:UNUSED_PRESERVE src0_sel:WORD_1
	v_pk_add_f16 v58, v109, v122 neg_lo:[0,1] neg_hi:[0,1]
	v_pk_add_f16 v45, v45, v62
	v_pk_add_f16 v44, v44, v63
	v_pk_add_f16 v43, v43, v64
	v_pk_add_f16 v42, v42, v65
	v_pk_fma_f16 v30, v18, v62, v30
	v_pk_fma_f16 v31, v19, v63, v31
	v_pk_fma_f16 v32, v20, v64, v32
	v_pk_fma_f16 v33, v21, v65, v33
	v_pk_add_f16 v59, v108, v123 neg_lo:[0,1] neg_hi:[0,1]
	v_pk_add_f16 v60, v107, v124 neg_lo:[0,1] neg_hi:[0,1]
	v_pk_add_f16 v61, v106, v125 neg_lo:[0,1] neg_hi:[0,1]
	v_exp_f16_sdwa v62, v58 dst_sel:WORD_0 dst_unused:UNUSED_PAD src0_sel:WORD_0
	v_exp_f16_sdwa v63, v59 dst_sel:WORD_0 dst_unused:UNUSED_PAD src0_sel:WORD_0
	v_exp_f16_sdwa v64, v60 dst_sel:WORD_0 dst_unused:UNUSED_PAD src0_sel:WORD_0
	v_exp_f16_sdwa v65, v61 dst_sel:WORD_0 dst_unused:UNUSED_PAD src0_sel:WORD_0
	v_exp_f16_sdwa v62, v58 dst_sel:WORD_1 dst_unused:UNUSED_PRESERVE src0_sel:WORD_1
	v_exp_f16_sdwa v63, v59 dst_sel:WORD_1 dst_unused:UNUSED_PRESERVE src0_sel:WORD_1
	v_exp_f16_sdwa v64, v60 dst_sel:WORD_1 dst_unused:UNUSED_PRESERVE src0_sel:WORD_1
	v_exp_f16_sdwa v65, v61 dst_sel:WORD_1 dst_unused:UNUSED_PRESERVE src0_sel:WORD_1
	v_pk_add_f16 v58, v121, v122 neg_lo:[0,1] neg_hi:[0,1]
	v_pk_add_f16 v45, v45, v62
	v_pk_add_f16 v42, v42, v65
	v_pk_add_f16 v43, v43, v64
	v_pk_add_f16 v44, v44, v63
	v_pk_fma_f16 v33, v25, v65, v33
	v_pk_fma_f16 v32, v24, v64, v32
	v_pk_fma_f16 v31, v23, v63, v31
	v_pk_fma_f16 v30, v22, v62, v30
	v_pk_add_f16 v59, v120, v123 neg_lo:[0,1] neg_hi:[0,1]
	v_pk_add_f16 v60, v119, v124 neg_lo:[0,1] neg_hi:[0,1]
	v_pk_add_f16 v61, v118, v125 neg_lo:[0,1] neg_hi:[0,1]
	v_exp_f16_sdwa v62, v58 dst_sel:WORD_0 dst_unused:UNUSED_PAD src0_sel:WORD_0
	v_exp_f16_sdwa v63, v59 dst_sel:WORD_0 dst_unused:UNUSED_PAD src0_sel:WORD_0
	v_exp_f16_sdwa v64, v60 dst_sel:WORD_0 dst_unused:UNUSED_PAD src0_sel:WORD_0
	v_exp_f16_sdwa v65, v61 dst_sel:WORD_0 dst_unused:UNUSED_PAD src0_sel:WORD_0
	v_exp_f16_sdwa v62, v58 dst_sel:WORD_1 dst_unused:UNUSED_PRESERVE src0_sel:WORD_1
	v_exp_f16_sdwa v63, v59 dst_sel:WORD_1 dst_unused:UNUSED_PRESERVE src0_sel:WORD_1
	v_exp_f16_sdwa v64, v60 dst_sel:WORD_1 dst_unused:UNUSED_PRESERVE src0_sel:WORD_1
	v_exp_f16_sdwa v65, v61 dst_sel:WORD_1 dst_unused:UNUSED_PRESERVE src0_sel:WORD_1
	v_exp_f16_sdwa v58, v54 dst_sel:WORD_0 dst_unused:UNUSED_PAD src0_sel:WORD_0
	v_exp_f16_sdwa v59, v55 dst_sel:WORD_0 dst_unused:UNUSED_PAD src0_sel:WORD_0
	v_exp_f16_sdwa v60, v56 dst_sel:WORD_0 dst_unused:UNUSED_PAD src0_sel:WORD_0
	v_exp_f16_sdwa v61, v57 dst_sel:WORD_0 dst_unused:UNUSED_PAD src0_sel:WORD_0
	v_exp_f16_sdwa v58, v54 dst_sel:WORD_1 dst_unused:UNUSED_PRESERVE src0_sel:WORD_1
	v_exp_f16_sdwa v59, v55 dst_sel:WORD_1 dst_unused:UNUSED_PRESERVE src0_sel:WORD_1
	v_exp_f16_sdwa v60, v56 dst_sel:WORD_1 dst_unused:UNUSED_PRESERVE src0_sel:WORD_1
	v_exp_f16_sdwa v61, v57 dst_sel:WORD_1 dst_unused:UNUSED_PRESERVE src0_sel:WORD_1
	v_pk_add_f16 v54, v82, v122 neg_lo:[0,1] neg_hi:[0,1]
	v_pk_add_f16 v45, v45, v62
	v_pk_add_f16 v44, v44, v63
	v_pk_add_f16 v43, v43, v64
	v_pk_add_f16 v42, v42, v65
	v_pk_fma_f16 v30, v26, v62, v30
	v_pk_fma_f16 v31, v27, v63, v31
	v_pk_fma_f16 v32, v28, v64, v32
	v_pk_fma_f16 v33, v29, v65, v33
	v_pk_add_f16 v45, v45, v58
	v_pk_add_f16 v42, v42, v61
	v_pk_add_f16 v43, v43, v60
	v_pk_add_f16 v44, v44, v59
	v_pk_fma_f16 v33, v41, v61, v33
	v_pk_fma_f16 v32, v40, v60, v32
	v_pk_fma_f16 v31, v39, v59, v31
	v_pk_fma_f16 v30, v38, v58, v30
	v_pk_add_f16 v55, v83, v123 neg_lo:[0,1] neg_hi:[0,1]
	v_pk_add_f16 v56, v84, v124 neg_lo:[0,1] neg_hi:[0,1]
	v_pk_add_f16 v57, v85, v125 neg_lo:[0,1] neg_hi:[0,1]
	v_exp_f16_sdwa v58, v54 dst_sel:WORD_0 dst_unused:UNUSED_PAD src0_sel:WORD_0
	v_exp_f16_sdwa v59, v55 dst_sel:WORD_0 dst_unused:UNUSED_PAD src0_sel:WORD_0
	v_exp_f16_sdwa v60, v56 dst_sel:WORD_0 dst_unused:UNUSED_PAD src0_sel:WORD_0
	v_exp_f16_sdwa v61, v57 dst_sel:WORD_0 dst_unused:UNUSED_PAD src0_sel:WORD_0
	v_exp_f16_sdwa v58, v54 dst_sel:WORD_1 dst_unused:UNUSED_PRESERVE src0_sel:WORD_1
	v_exp_f16_sdwa v59, v55 dst_sel:WORD_1 dst_unused:UNUSED_PRESERVE src0_sel:WORD_1
	v_exp_f16_sdwa v60, v56 dst_sel:WORD_1 dst_unused:UNUSED_PRESERVE src0_sel:WORD_1
	v_exp_f16_sdwa v61, v57 dst_sel:WORD_1 dst_unused:UNUSED_PRESERVE src0_sel:WORD_1
	v_pk_add_f16 v54, v94, v122 neg_lo:[0,1] neg_hi:[0,1]
	v_pk_add_f16 v45, v45, v58
	v_pk_add_f16 v44, v44, v59
	v_pk_add_f16 v43, v43, v60
	v_pk_add_f16 v42, v42, v61
	v_pk_fma_f16 v30, v50, v58, v30
	v_pk_fma_f16 v31, v51, v59, v31
	v_pk_fma_f16 v32, v52, v60, v32
	v_pk_fma_f16 v33, v53, v61, v33
	v_pk_add_f16 v55, v95, v123 neg_lo:[0,1] neg_hi:[0,1]
	v_pk_add_f16 v56, v96, v124 neg_lo:[0,1] neg_hi:[0,1]
	v_pk_add_f16 v57, v97, v125 neg_lo:[0,1] neg_hi:[0,1]
	v_exp_f16_sdwa v58, v54 dst_sel:WORD_0 dst_unused:UNUSED_PAD src0_sel:WORD_0
	v_exp_f16_sdwa v59, v55 dst_sel:WORD_0 dst_unused:UNUSED_PAD src0_sel:WORD_0
	v_exp_f16_sdwa v60, v56 dst_sel:WORD_0 dst_unused:UNUSED_PAD src0_sel:WORD_0
	v_exp_f16_sdwa v61, v57 dst_sel:WORD_0 dst_unused:UNUSED_PAD src0_sel:WORD_0
	v_exp_f16_sdwa v58, v54 dst_sel:WORD_1 dst_unused:UNUSED_PRESERVE src0_sel:WORD_1
	v_exp_f16_sdwa v59, v55 dst_sel:WORD_1 dst_unused:UNUSED_PRESERVE src0_sel:WORD_1
	v_exp_f16_sdwa v60, v56 dst_sel:WORD_1 dst_unused:UNUSED_PRESERVE src0_sel:WORD_1
	v_exp_f16_sdwa v61, v57 dst_sel:WORD_1 dst_unused:UNUSED_PRESERVE src0_sel:WORD_1
	v_pk_add_f16 v45, v45, v58
	v_pk_add_f16 v44, v44, v59
	v_rcp_f16_e32 v54, v45
	v_rcp_f16_sdwa v45, v45 dst_sel:DWORD dst_unused:UNUSED_PAD src0_sel:WORD_1
	v_pk_add_f16 v43, v43, v60
	v_rcp_f16_e32 v55, v44
	v_rcp_f16_sdwa v44, v44 dst_sel:DWORD dst_unused:UNUSED_PAD src0_sel:WORD_1
	v_pk_add_f16 v42, v42, v61
	v_pk_fma_f16 v30, v70, v58, v30
	v_rcp_f16_e32 v58, v43
	v_rcp_f16_sdwa v43, v43 dst_sel:DWORD dst_unused:UNUSED_PAD src0_sel:WORD_1
	v_pk_fma_f16 v31, v71, v59, v31
	v_rcp_f16_e32 v59, v42
	v_rcp_f16_sdwa v42, v42 dst_sel:DWORD dst_unused:UNUSED_PAD src0_sel:WORD_1
	v_pack_b32_f16 v45, v54, v45
	v_pk_mul_f16 v57, v30, v45
	v_pack_b32_f16 v30, v55, v44
	v_pk_fma_f16 v32, v72, v60, v32
	v_pk_mul_f16 v56, v31, v30
	v_pack_b32_f16 v30, v58, v43
	v_pk_fma_f16 v33, v73, v61, v33
	v_pk_mul_f16 v55, v32, v30
	v_pack_b32_f16 v30, v59, v42
	v_pk_mul_f16 v54, v33, v30
	s_waitcnt vmcnt(0)
	v_pk_mul_f16 v30, v204, v154 op_sel_hi:[0,1]
	v_pk_mul_f16 v31, v204, v155 op_sel_hi:[0,1]
	v_pk_mul_f16 v32, v204, v156 op_sel_hi:[0,1]
	v_pk_mul_f16 v33, v204, v157 op_sel_hi:[0,1]
	v_pk_mul_f16 v42, v202, v154 op_sel_hi:[0,1]
	v_pk_mul_f16 v43, v202, v155 op_sel_hi:[0,1]
	v_pk_mul_f16 v44, v202, v156 op_sel_hi:[0,1]
	v_pk_mul_f16 v45, v202, v157 op_sel_hi:[0,1]
	v_pk_mul_f16 v58, v203, v154 op_sel_hi:[0,1]
	v_pk_mul_f16 v59, v203, v155 op_sel_hi:[0,1]
	v_pk_mul_f16 v60, v203, v156 op_sel_hi:[0,1]
	v_pk_mul_f16 v61, v203, v157 op_sel_hi:[0,1]
	v_pk_fma_f16 v37, v37, v157, v33
	v_pk_fma_f16 v36, v36, v156, v32
	v_pk_fma_f16 v35, v35, v155, v31
	v_pk_fma_f16 v34, v34, v154, v30
	v_pk_fma_f16 v49, v49, v157, v45
	v_pk_fma_f16 v48, v48, v156, v44
	v_pk_fma_f16 v47, v47, v155, v43
	v_pk_fma_f16 v46, v46, v154, v42
	v_pk_fma_f16 v62, v69, v157, v61
	v_pk_fma_f16 v63, v68, v156, v60
	v_pk_fma_f16 v64, v67, v155, v59
	v_pk_fma_f16 v65, v66, v154, v58
	v_pk_fma_f16 v66, v89, v157, v33
	v_pk_fma_f16 v67, v88, v156, v32
	v_pk_fma_f16 v68, v87, v155, v31
	v_pk_fma_f16 v69, v86, v154, v30
	v_pk_fma_f16 v78, v117, v157, v45
	v_pk_fma_f16 v79, v116, v156, v44
	v_pk_fma_f16 v80, v115, v155, v43
	v_pk_fma_f16 v81, v114, v154, v42
	v_pk_fma_f16 v82, v133, v157, v61
	v_pk_fma_f16 v83, v132, v156, v60
	v_pk_fma_f16 v84, v131, v155, v59
	v_pk_fma_f16 v85, v130, v154, v58
	v_pk_fma_f16 v61, v17, v157, v61
	v_pk_fma_f16 v60, v16, v156, v60
	v_pk_fma_f16 v59, v15, v155, v59
	v_pk_fma_f16 v58, v14, v154, v58
	v_pk_maximum3_f16 v14, v34, v46, v65
	v_pk_maximum3_f16 v15, v35, v47, v64
	v_pk_maximum3_f16 v16, v36, v48, v63
	v_pk_maximum3_f16 v17, v37, v49, v62
	v_pk_maximum3_f16 v86, v69, v81, v85
	v_pk_maximum3_f16 v87, v68, v80, v84
	v_pk_maximum3_f16 v88, v67, v79, v83
	v_pk_maximum3_f16 v89, v66, v78, v82
	v_pk_fma_f16 v33, v145, v157, v33
	v_pk_fma_f16 v32, v144, v156, v32
	v_pk_fma_f16 v31, v143, v155, v31
	v_pk_fma_f16 v30, v142, v154, v30
	v_pk_fma_f16 v45, v153, v157, v45
	v_pk_fma_f16 v44, v152, v156, v44
	v_pk_fma_f16 v43, v151, v155, v43
	v_pk_fma_f16 v42, v150, v154, v42
	v_pk_maximum3_f16 v95, v31, v43, v59
	v_pk_maximum3_f16 v96, v32, v44, v60
	v_pk_maximum3_f16 v97, v33, v45, v61
	v_pk_maximum3_f16 v94, v30, v42, v58
	v_pk_maximum3_f16 v15, v15, v87, v95
	v_pk_maximum3_f16 v16, v16, v88, v96
	v_pk_maximum3_f16 v17, v17, v89, v97
	v_pk_maximum3_f16 v14, v14, v86, v94
	v_xor_b32_e32 v86, 0x80008000, v17
	v_xor_b32_e32 v87, 0x80008000, v16
	v_xor_b32_e32 v88, 0x80008000, v15
	v_xor_b32_e32 v89, 0x80008000, v14
	v_pk_add_f16 v14, v34, v89
	v_pk_add_f16 v15, v35, v88
	v_pk_add_f16 v16, v36, v87
	v_pk_add_f16 v17, v37, v86
	v_exp_f16_sdwa v34, v14 dst_sel:WORD_0 dst_unused:UNUSED_PAD src0_sel:WORD_0
	v_exp_f16_sdwa v35, v15 dst_sel:WORD_0 dst_unused:UNUSED_PAD src0_sel:WORD_0
	v_exp_f16_sdwa v36, v16 dst_sel:WORD_0 dst_unused:UNUSED_PAD src0_sel:WORD_0
	v_exp_f16_sdwa v37, v17 dst_sel:WORD_0 dst_unused:UNUSED_PAD src0_sel:WORD_0
	v_exp_f16_sdwa v34, v14 dst_sel:WORD_1 dst_unused:UNUSED_PRESERVE src0_sel:WORD_1
	v_exp_f16_sdwa v35, v15 dst_sel:WORD_1 dst_unused:UNUSED_PRESERVE src0_sel:WORD_1
	v_exp_f16_sdwa v36, v16 dst_sel:WORD_1 dst_unused:UNUSED_PRESERVE src0_sel:WORD_1
	v_exp_f16_sdwa v37, v17 dst_sel:WORD_1 dst_unused:UNUSED_PRESERVE src0_sel:WORD_1
	v_pk_add_f16 v14, v34, 0
	v_pk_add_f16 v15, v35, 0
	v_pk_add_f16 v16, v36, 0
	v_pk_add_f16 v17, v37, 0
	v_pk_fma_f16 v18, v18, v34, 0
	v_pk_fma_f16 v19, v19, v35, 0
	v_pk_fma_f16 v20, v20, v36, 0
	v_pk_fma_f16 v21, v21, v37, 0
	v_pk_add_f16 v34, v46, v89
	v_pk_add_f16 v35, v47, v88
	v_pk_add_f16 v36, v48, v87
	v_pk_add_f16 v37, v49, v86
	v_exp_f16_sdwa v46, v34 dst_sel:WORD_0 dst_unused:UNUSED_PAD src0_sel:WORD_0
	v_exp_f16_sdwa v47, v35 dst_sel:WORD_0 dst_unused:UNUSED_PAD src0_sel:WORD_0
	v_exp_f16_sdwa v48, v36 dst_sel:WORD_0 dst_unused:UNUSED_PAD src0_sel:WORD_0
	v_exp_f16_sdwa v49, v37 dst_sel:WORD_0 dst_unused:UNUSED_PAD src0_sel:WORD_0
	v_exp_f16_sdwa v46, v34 dst_sel:WORD_1 dst_unused:UNUSED_PRESERVE src0_sel:WORD_1
	v_exp_f16_sdwa v47, v35 dst_sel:WORD_1 dst_unused:UNUSED_PRESERVE src0_sel:WORD_1
	v_exp_f16_sdwa v48, v36 dst_sel:WORD_1 dst_unused:UNUSED_PRESERVE src0_sel:WORD_1
	v_exp_f16_sdwa v49, v37 dst_sel:WORD_1 dst_unused:UNUSED_PRESERVE src0_sel:WORD_1
	s_nop 0
	v_pk_add_f16 v17, v17, v49
	v_pk_add_f16 v16, v16, v48
	v_pk_add_f16 v15, v15, v47
	v_pk_add_f16 v14, v14, v46
	v_pk_fma_f16 v21, v25, v49, v21
	v_pk_fma_f16 v20, v24, v48, v20
	v_pk_fma_f16 v19, v23, v47, v19
	v_pk_fma_f16 v18, v22, v46, v18
	v_pk_add_f16 v22, v65, v89
	v_pk_add_f16 v23, v64, v88
	v_pk_add_f16 v24, v63, v87
	v_pk_add_f16 v25, v62, v86
	v_exp_f16_sdwa v34, v22 dst_sel:WORD_0 dst_unused:UNUSED_PAD src0_sel:WORD_0
	v_exp_f16_sdwa v35, v23 dst_sel:WORD_0 dst_unused:UNUSED_PAD src0_sel:WORD_0
	v_exp_f16_sdwa v36, v24 dst_sel:WORD_0 dst_unused:UNUSED_PAD src0_sel:WORD_0
	v_exp_f16_sdwa v37, v25 dst_sel:WORD_0 dst_unused:UNUSED_PAD src0_sel:WORD_0
	v_exp_f16_sdwa v34, v22 dst_sel:WORD_1 dst_unused:UNUSED_PRESERVE src0_sel:WORD_1
	v_exp_f16_sdwa v35, v23 dst_sel:WORD_1 dst_unused:UNUSED_PRESERVE src0_sel:WORD_1
	v_exp_f16_sdwa v36, v24 dst_sel:WORD_1 dst_unused:UNUSED_PRESERVE src0_sel:WORD_1
	v_exp_f16_sdwa v37, v25 dst_sel:WORD_1 dst_unused:UNUSED_PRESERVE src0_sel:WORD_1
	v_pk_add_f16 v22, v69, v89
	v_pk_add_f16 v14, v14, v34
	v_pk_add_f16 v15, v15, v35
	v_pk_add_f16 v16, v16, v36
	v_pk_add_f16 v17, v17, v37
	v_pk_fma_f16 v18, v26, v34, v18
	v_pk_fma_f16 v19, v27, v35, v19
	v_pk_fma_f16 v20, v28, v36, v20
	v_pk_fma_f16 v21, v29, v37, v21
	v_pk_add_f16 v23, v68, v88
	v_pk_add_f16 v24, v67, v87
	v_pk_add_f16 v25, v66, v86
	v_exp_f16_sdwa v26, v22 dst_sel:WORD_0 dst_unused:UNUSED_PAD src0_sel:WORD_0
	v_exp_f16_sdwa v27, v23 dst_sel:WORD_0 dst_unused:UNUSED_PAD src0_sel:WORD_0
	v_exp_f16_sdwa v28, v24 dst_sel:WORD_0 dst_unused:UNUSED_PAD src0_sel:WORD_0
	v_exp_f16_sdwa v29, v25 dst_sel:WORD_0 dst_unused:UNUSED_PAD src0_sel:WORD_0
	v_exp_f16_sdwa v26, v22 dst_sel:WORD_1 dst_unused:UNUSED_PRESERVE src0_sel:WORD_1
	v_exp_f16_sdwa v27, v23 dst_sel:WORD_1 dst_unused:UNUSED_PRESERVE src0_sel:WORD_1
	v_exp_f16_sdwa v28, v24 dst_sel:WORD_1 dst_unused:UNUSED_PRESERVE src0_sel:WORD_1
	v_exp_f16_sdwa v29, v25 dst_sel:WORD_1 dst_unused:UNUSED_PRESERVE src0_sel:WORD_1
	v_pk_add_f16 v22, v81, v89
	v_pk_add_f16 v17, v17, v29
	v_pk_add_f16 v16, v16, v28
	v_pk_add_f16 v15, v15, v27
	v_pk_add_f16 v14, v14, v26
	v_pk_fma_f16 v21, v41, v29, v21
	v_pk_fma_f16 v20, v40, v28, v20
	v_pk_fma_f16 v19, v39, v27, v19
	v_pk_fma_f16 v18, v38, v26, v18
	v_pk_add_f16 v23, v80, v88
	v_pk_add_f16 v24, v79, v87
	v_pk_add_f16 v25, v78, v86
	v_exp_f16_sdwa v26, v22 dst_sel:WORD_0 dst_unused:UNUSED_PAD src0_sel:WORD_0
	v_exp_f16_sdwa v27, v23 dst_sel:WORD_0 dst_unused:UNUSED_PAD src0_sel:WORD_0
	v_exp_f16_sdwa v28, v24 dst_sel:WORD_0 dst_unused:UNUSED_PAD src0_sel:WORD_0
	v_exp_f16_sdwa v29, v25 dst_sel:WORD_0 dst_unused:UNUSED_PAD src0_sel:WORD_0
	v_exp_f16_sdwa v26, v22 dst_sel:WORD_1 dst_unused:UNUSED_PRESERVE src0_sel:WORD_1
	v_exp_f16_sdwa v27, v23 dst_sel:WORD_1 dst_unused:UNUSED_PRESERVE src0_sel:WORD_1
	v_exp_f16_sdwa v28, v24 dst_sel:WORD_1 dst_unused:UNUSED_PRESERVE src0_sel:WORD_1
	v_exp_f16_sdwa v29, v25 dst_sel:WORD_1 dst_unused:UNUSED_PRESERVE src0_sel:WORD_1
	v_pk_add_f16 v22, v85, v89
	v_pk_add_f16 v14, v14, v26
	v_pk_add_f16 v15, v15, v27
	v_pk_add_f16 v16, v16, v28
	v_pk_add_f16 v17, v17, v29
	v_pk_fma_f16 v18, v50, v26, v18
	v_pk_fma_f16 v19, v51, v27, v19
	v_pk_fma_f16 v20, v52, v28, v20
	v_pk_fma_f16 v21, v53, v29, v21
	v_pk_add_f16 v23, v84, v88
	v_pk_add_f16 v24, v83, v87
	v_pk_add_f16 v25, v82, v86
	v_exp_f16_sdwa v26, v22 dst_sel:WORD_0 dst_unused:UNUSED_PAD src0_sel:WORD_0
	v_exp_f16_sdwa v27, v23 dst_sel:WORD_0 dst_unused:UNUSED_PAD src0_sel:WORD_0
	v_exp_f16_sdwa v28, v24 dst_sel:WORD_0 dst_unused:UNUSED_PAD src0_sel:WORD_0
	v_exp_f16_sdwa v29, v25 dst_sel:WORD_0 dst_unused:UNUSED_PAD src0_sel:WORD_0
	v_exp_f16_sdwa v26, v22 dst_sel:WORD_1 dst_unused:UNUSED_PRESERVE src0_sel:WORD_1
	v_exp_f16_sdwa v27, v23 dst_sel:WORD_1 dst_unused:UNUSED_PRESERVE src0_sel:WORD_1
	v_exp_f16_sdwa v28, v24 dst_sel:WORD_1 dst_unused:UNUSED_PRESERVE src0_sel:WORD_1
	v_exp_f16_sdwa v29, v25 dst_sel:WORD_1 dst_unused:UNUSED_PRESERVE src0_sel:WORD_1
	v_pk_add_f16 v22, v30, v89
	v_pk_add_f16 v17, v17, v29
	v_pk_add_f16 v16, v16, v28
	v_pk_add_f16 v15, v15, v27
	v_pk_add_f16 v14, v14, v26
	v_pk_fma_f16 v21, v73, v29, v21
	v_pk_fma_f16 v20, v72, v28, v20
	v_pk_fma_f16 v19, v71, v27, v19
	v_pk_fma_f16 v18, v70, v26, v18
	v_pk_add_f16 v23, v31, v88
	v_pk_add_f16 v24, v32, v87
	v_pk_add_f16 v25, v33, v86
	v_exp_f16_sdwa v26, v22 dst_sel:WORD_0 dst_unused:UNUSED_PAD src0_sel:WORD_0
	v_exp_f16_sdwa v27, v23 dst_sel:WORD_0 dst_unused:UNUSED_PAD src0_sel:WORD_0
	v_exp_f16_sdwa v28, v24 dst_sel:WORD_0 dst_unused:UNUSED_PAD src0_sel:WORD_0
	v_exp_f16_sdwa v29, v25 dst_sel:WORD_0 dst_unused:UNUSED_PAD src0_sel:WORD_0
	v_exp_f16_sdwa v26, v22 dst_sel:WORD_1 dst_unused:UNUSED_PRESERVE src0_sel:WORD_1
	v_exp_f16_sdwa v27, v23 dst_sel:WORD_1 dst_unused:UNUSED_PRESERVE src0_sel:WORD_1
	v_exp_f16_sdwa v28, v24 dst_sel:WORD_1 dst_unused:UNUSED_PRESERVE src0_sel:WORD_1
	v_exp_f16_sdwa v29, v25 dst_sel:WORD_1 dst_unused:UNUSED_PRESERVE src0_sel:WORD_1
	v_pk_add_f16 v22, v42, v89
	v_pk_add_f16 v14, v14, v26
	v_pk_add_f16 v15, v15, v27
	v_pk_add_f16 v16, v16, v28
	v_pk_add_f16 v17, v17, v29
	v_pk_fma_f16 v18, v90, v26, v18
	v_pk_fma_f16 v19, v91, v27, v19
	v_pk_fma_f16 v20, v92, v28, v20
	v_pk_fma_f16 v21, v93, v29, v21
	v_pk_add_f16 v23, v43, v88
	v_pk_add_f16 v24, v44, v87
	v_pk_add_f16 v25, v45, v86
	v_exp_f16_sdwa v26, v22 dst_sel:WORD_0 dst_unused:UNUSED_PAD src0_sel:WORD_0
	v_exp_f16_sdwa v27, v23 dst_sel:WORD_0 dst_unused:UNUSED_PAD src0_sel:WORD_0
	v_exp_f16_sdwa v28, v24 dst_sel:WORD_0 dst_unused:UNUSED_PAD src0_sel:WORD_0
	v_exp_f16_sdwa v29, v25 dst_sel:WORD_0 dst_unused:UNUSED_PAD src0_sel:WORD_0
	v_exp_f16_sdwa v26, v22 dst_sel:WORD_1 dst_unused:UNUSED_PRESERVE src0_sel:WORD_1
	v_exp_f16_sdwa v27, v23 dst_sel:WORD_1 dst_unused:UNUSED_PRESERVE src0_sel:WORD_1
	v_exp_f16_sdwa v28, v24 dst_sel:WORD_1 dst_unused:UNUSED_PRESERVE src0_sel:WORD_1
	v_exp_f16_sdwa v29, v25 dst_sel:WORD_1 dst_unused:UNUSED_PRESERVE src0_sel:WORD_1
	v_pk_add_f16 v22, v58, v89
	v_pk_add_f16 v17, v17, v29
	v_pk_add_f16 v16, v16, v28
	v_pk_add_f16 v15, v15, v27
	v_pk_add_f16 v14, v14, v26
	v_pk_fma_f16 v21, v113, v29, v21
	v_pk_fma_f16 v20, v112, v28, v20
	v_pk_fma_f16 v19, v111, v27, v19
	v_pk_fma_f16 v18, v110, v26, v18
	v_pk_add_f16 v23, v59, v88
	v_pk_add_f16 v24, v60, v87
	v_pk_add_f16 v25, v61, v86
	v_exp_f16_sdwa v30, v22 dst_sel:WORD_0 dst_unused:UNUSED_PAD src0_sel:WORD_0
	v_exp_f16_sdwa v31, v23 dst_sel:WORD_0 dst_unused:UNUSED_PAD src0_sel:WORD_0
	v_exp_f16_sdwa v32, v24 dst_sel:WORD_0 dst_unused:UNUSED_PAD src0_sel:WORD_0
	v_exp_f16_sdwa v33, v25 dst_sel:WORD_0 dst_unused:UNUSED_PAD src0_sel:WORD_0
	v_exp_f16_sdwa v30, v22 dst_sel:WORD_1 dst_unused:UNUSED_PRESERVE src0_sel:WORD_1
	v_exp_f16_sdwa v31, v23 dst_sel:WORD_1 dst_unused:UNUSED_PRESERVE src0_sel:WORD_1
	v_exp_f16_sdwa v32, v24 dst_sel:WORD_1 dst_unused:UNUSED_PRESERVE src0_sel:WORD_1
	v_exp_f16_sdwa v33, v25 dst_sel:WORD_1 dst_unused:UNUSED_PRESERVE src0_sel:WORD_1
	s_nop 0
.LBB4_42:
	s_and_b64 vcc, exec, s[4:5]
	s_cbranch_vccz .LBB4_80
	global_load_dwordx3 v[146:148], v169, s[8:9]
	v_cmp_lt_u32_e64 s[64:65], 0, v199
	v_cmp_gt_u32_e64 s[66:67], 63, v199
	v_cmp_lt_u32_e64 s[68:69], 0, v180
	v_cmp_gt_u32_e64 s[70:71], 60, v180
	buffer_load_dwordx4 v[162:165], v200, s[36:39], 0 offen
	s_and_b64 s[72:73], s[68:69], s[64:65]
	s_and_b64 s[74:75], s[68:69], s[66:67]
	s_and_b64 s[76:77], s[70:71], s[64:65]
	s_and_b64 s[78:79], s[70:71], s[66:67]
	v_add_u32_e32 v245, 0xfffe7c00, v200
	v_add_u32_e32 v246, 0xfffe8000, v200
	s_mov_b64 exec, s[72:73]
	buffer_load_dwordx4 v[114:117], v245, s[36:39], 0 offen
	buffer_load_dwordx4 v[74:77], v245, s[36:39], 0 offen offset:512
	s_mov_b64 exec, -1
	s_mov_b64 exec, s[68:69]
	buffer_load_dwordx4 v[130:133], v246, s[36:39], 0 offen offset:512
	buffer_load_dwordx4 v[98:101], v246, s[36:39], 0 offen offset:1024
	s_mov_b64 exec, -1
	s_mov_b64 exec, s[74:75]
	buffer_load_dwordx4 v[138:141], v246, s[36:39], 0 offen offset:2048
	buffer_load_dwordx4 v[118:121], v246, s[36:39], 0 offen offset:2560
	s_mov_b64 exec, -1
	v_add_u32_e32 v245, 0xfffffc00, v200
	s_mov_b64 exec, s[64:65]
	buffer_load_dwordx4 v[86:89], v245, s[36:39], 0 offen
	buffer_load_dwordx4 v[46:49], v245, s[36:39], 0 offen offset:512
	s_mov_b64 exec, -1
	buffer_load_dwordx4 v[110:113], v200, s[36:39], 0 offen offset:512
	buffer_load_dwordx4 v[66:69], v200, s[36:39], 0 offen offset:1024
	s_mov_b64 exec, s[66:67]
	buffer_load_dwordx4 v[126:129], v200, s[36:39], 0 offen offset:2048
	buffer_load_dwordx4 v[90:93], v200, s[36:39], 0 offen offset:2560
	s_mov_b64 exec, -1
	v_add_u32_e32 v245, 0x17c00, v200
	v_add_u32_e32 v246, 0x18000, v200
	s_mov_b64 exec, s[64:65]
	buffer_load_dwordx4 v[54:57], v245, s[36:39], 0 offen
	buffer_load_dwordx4 v[22:25], v245, s[36:39], 0 offen offset:512
	s_mov_b64 exec, -1
	buffer_load_dwordx4 v[70:73], v246, s[36:39], 0 offen offset:512
	buffer_load_dwordx4 v[34:37], v246, s[36:39], 0 offen offset:1024
	s_mov_b64 exec, s[66:67]
	buffer_load_dwordx4 v[94:97], v246, s[36:39], 0 offen offset:2048
	buffer_load_dwordx4 v[50:53], v246, s[36:39], 0 offen offset:2560
	s_mov_b64 exec, -1
	v_add_u32_e32 v245, 0x18000, v200
	buffer_load_dwordx4 v[154:157], v245, s[36:39], 0 offen
	v_add_u32_e32 v246, 0x30000, v200
	buffer_load_dwordx4 v[150:153], v246, s[36:39], 0 offen
	v_add_u32_e32 v245, 0x2fc00, v200
	v_add_u32_e32 v246, 0x30000, v200
	v_add_u32_e32 v247, 0x47c00, v200
	v_add_u32_e32 v248, 0x48000, v200
	v_add_u32_e32 v249, 0x5fc00, v200
	v_add_u32_e32 v250, 0x60000, v200
	s_not_b64 exec, s[72:73]
	s_cbranch_execz .Lmyf_C2_0
	v_mov_b32_e32 v114, v6
	v_mov_b32_e32 v115, v7
	v_mov_b32_e32 v116, v8
	v_mov_b32_e32 v117, v9
	v_mov_b32_e32 v74, v2
	v_mov_b32_e32 v75, v3
	v_mov_b32_e32 v76, v4
	v_mov_b32_e32 v77, v5
.Lmyf_C2_0:
	s_not_b64 exec, s[68:69]
	s_cbranch_execz .Lmyf_C2_1
	v_mov_b32_e32 v130, v6
	v_mov_b32_e32 v131, v7
	v_mov_b32_e32 v132, v8
	v_mov_b32_e32 v133, v9
	v_mov_b32_e32 v98, v2
	v_mov_b32_e32 v99, v3
	v_mov_b32_e32 v100, v4
	v_mov_b32_e32 v101, v5
.Lmyf_C2_1:
	s_not_b64 exec, s[74:75]
	s_cbranch_execz .Lmyf_C2_2
	v_mov_b32_e32 v138, v6
	v_mov_b32_e32 v139, v7
	v_mov_b32_e32 v140, v8
	v_mov_b32_e32 v141, v9
	v_mov_b32_e32 v118, v2
	v_mov_b32_e32 v119, v3
	v_mov_b32_e32 v120, v4
	v_mov_b32_e32 v121, v5
.Lmyf_C2_2:
	s_not_b64 exec, s[64:65]
	s_cbranch_execz .Lmyf_C2_3
	v_mov_b32_e32 v86, v6
	v_mov_b32_e32 v87, v7
	v_mov_b32_e32 v88, v8
	v_mov_b32_e32 v89, v9
	v_mov_b32_e32 v46, v2
	v_mov_b32_e32 v47, v3
	v_mov_b32_e32 v48, v4
	v_mov_b32_e32 v49, v5
	v_mov_b32_e32 v54, v6
	v_mov_b32_e32 v55, v7
	v_mov_b32_e32 v56, v8
	v_mov_b32_e32 v57, v9
	v_mov_b32_e32 v22, v2
	v_mov_b32_e32 v23, v3
	v_mov_b32_e32 v24, v4
	v_mov_b32_e32 v25, v5
	v_mov_b32_e32 v26, v6
	v_mov_b32_e32 v27, v7
	v_mov_b32_e32 v28, v8
	v_mov_b32_e32 v29, v9
	v_mov_b32_e32 v10, v2
	v_mov_b32_e32 v11, v3
	v_mov_b32_e32 v12, v4
	v_mov_b32_e32 v13, v5
	v_mov_b32_e32 v78, v6
	v_mov_b32_e32 v79, v7
	v_mov_b32_e32 v80, v8
	v_mov_b32_e32 v81, v9
	v_mov_b32_e32 v30, v2
	v_mov_b32_e32 v31, v3
	v_mov_b32_e32 v32, v4
	v_mov_b32_e32 v33, v5
.Lmyf_C2_3:
	s_not_b64 exec, s[66:67]
	s_cbranch_execz .Lmyf_C2_4
	v_mov_b32_e32 v126, v6
	v_mov_b32_e32 v127, v7
	v_mov_b32_e32 v128, v8
	v_mov_b32_e32 v129, v9
	v_mov_b32_e32 v90, v2
	v_mov_b32_e32 v91, v3
	v_mov_b32_e32 v92, v4
	v_mov_b32_e32 v93, v5
	v_mov_b32_e32 v94, v6
	v_mov_b32_e32 v95, v7
	v_mov_b32_e32 v96, v8
	v_mov_b32_e32 v97, v9
	v_mov_b32_e32 v50, v2
	v_mov_b32_e32 v51, v3
	v_mov_b32_e32 v52, v4
	v_mov_b32_e32 v53, v5
	v_mov_b32_e32 v58, v6
	v_mov_b32_e32 v59, v7
	v_mov_b32_e32 v60, v8
	v_mov_b32_e32 v61, v9
	v_mov_b32_e32 v18, v2
	v_mov_b32_e32 v19, v3
	v_mov_b32_e32 v20, v4
	v_mov_b32_e32 v21, v5
	v_mov_b32_e32 v122, v6
	v_mov_b32_e32 v123, v7
	v_mov_b32_e32 v124, v8
	v_mov_b32_e32 v125, v9
	v_mov_b32_e32 v62, v2
	v_mov_b32_e32 v63, v3
	v_mov_b32_e32 v64, v4
	v_mov_b32_e32 v65, v5
.Lmyf_C2_4:
	s_not_b64 exec, s[76:77]
	s_cbranch_execz .Lmyf_C2_5
	v_mov_b32_e32 v134, v6
	v_mov_b32_e32 v135, v7
	v_mov_b32_e32 v136, v8
	v_mov_b32_e32 v137, v9
	v_mov_b32_e32 v82, v2
	v_mov_b32_e32 v83, v3
	v_mov_b32_e32 v84, v4
	v_mov_b32_e32 v85, v5
.Lmyf_C2_5:
	s_not_b64 exec, s[70:71]
	s_cbranch_execz .Lmyf_C2_6
	v_mov_b32_e32 v142, v6
	v_mov_b32_e32 v143, v7
	v_mov_b32_e32 v144, v8
	v_mov_b32_e32 v145, v9
	v_mov_b32_e32 v102, v2
	v_mov_b32_e32 v103, v3
	v_mov_b32_e32 v104, v4
	v_mov_b32_e32 v105, v5
.Lmyf_C2_6:
	s_not_b64 exec, s[78:79]
	s_cbranch_execz .Lmyf_C2_7
.Lmyf_C2_7:
	s_mov_b64 exec, -1
	s_waitcnt vmcnt(21)
	v_cvt_f16_f32_e32 v158, v147
	v_cvt_f16_f32_e32 v160, v146
	v_cvt_f16_f32_e32 v159, v148
	v_add_u32_e32 v251, 0x48000, v200
	buffer_load_dwordx4 v[146:149], v251, s[36:39], 0 offen
	s_waitcnt vmcnt(3)
	v_pk_mul_f16 v161, v160, v162 op_sel_hi:[0,1]
	v_pk_mul_f16 v204, v160, v165 op_sel_hi:[0,1]
	v_pk_mul_f16 v208, v158, v165 op_sel_hi:[0,1]
	v_pk_mul_f16 v212, v159, v165 op_sel_hi:[0,1]
	v_pk_mul_f16 v202, v160, v163 op_sel_hi:[0,1]
	v_pk_mul_f16 v203, v160, v164 op_sel_hi:[0,1]
	v_pk_mul_f16 v205, v158, v162 op_sel_hi:[0,1]
	s_mov_b64 exec, s[64:65]
	buffer_load_dwordx4 v[26:29], v245, s[36:39], 0 offen
	buffer_load_dwordx4 v[10:13], v245, s[36:39], 0 offen offset:512
	s_mov_b64 exec, -1
	v_pk_mul_f16 v206, v158, v163 op_sel_hi:[0,1]
	v_pk_mul_f16 v207, v158, v164 op_sel_hi:[0,1]
	v_pk_mul_f16 v209, v159, v162 op_sel_hi:[0,1]
	v_pk_mul_f16 v210, v159, v163 op_sel_hi:[0,1]
	v_pk_mul_f16 v211, v159, v164 op_sel_hi:[0,1]
	v_pk_fma_f16 v117, v117, v165, v204
	v_pk_fma_f16 v114, v114, v162, v161
	v_pk_fma_f16 v133, v133, v165, v204
	v_pk_fma_f16 v130, v130, v162, v161
	v_pk_fma_f16 v141, v141, v165, v204
	v_pk_fma_f16 v138, v138, v162, v161
	v_pk_fma_f16 v161, v89, v165, v208
	v_pk_fma_f16 v213, v113, v165, v208
	buffer_load_dwordx4 v[38:41], v246, s[36:39], 0 offen offset:512
	buffer_load_dwordx4 v[14:17], v246, s[36:39], 0 offen offset:1024
	v_pk_fma_f16 v208, v129, v165, v208
	v_pk_fma_f16 v217, v57, v165, v212
	v_pk_fma_f16 v221, v73, v165, v212
	v_pk_fma_f16 v165, v97, v165, v212
	v_pk_maximum3_f16 v212, v117, v133, v141
	v_pk_fma_f16 v116, v116, v164, v203
	v_pk_fma_f16 v115, v115, v163, v202
	v_pk_fma_f16 v132, v132, v164, v203
	v_pk_fma_f16 v131, v131, v163, v202
	v_pk_fma_f16 v140, v140, v164, v203
	v_pk_fma_f16 v139, v139, v163, v202
	v_pk_fma_f16 v202, v88, v164, v207
	v_pk_fma_f16 v203, v87, v163, v206
	v_pk_fma_f16 v204, v86, v162, v205
	v_pk_fma_f16 v214, v112, v164, v207
	v_pk_fma_f16 v215, v111, v163, v206
	s_mov_b64 exec, s[66:67]
	buffer_load_dwordx4 v[58:61], v246, s[36:39], 0 offen offset:2048
	buffer_load_dwordx4 v[18:21], v246, s[36:39], 0 offen offset:2560
	s_mov_b64 exec, -1
	v_pk_fma_f16 v216, v110, v162, v205
	v_pk_fma_f16 v207, v128, v164, v207
	v_pk_fma_f16 v206, v127, v163, v206
	v_pk_fma_f16 v205, v126, v162, v205
	v_pk_fma_f16 v218, v56, v164, v211
	v_pk_fma_f16 v219, v55, v163, v210
	v_pk_fma_f16 v220, v54, v162, v209
	v_pk_fma_f16 v222, v72, v164, v211
	v_pk_fma_f16 v223, v71, v163, v210
	v_pk_fma_f16 v224, v70, v162, v209
	v_pk_fma_f16 v164, v96, v164, v211
	v_pk_fma_f16 v163, v95, v163, v210
	v_pk_fma_f16 v162, v94, v162, v209
	v_pk_maximum3_f16 v209, v114, v130, v138
	v_pk_maximum3_f16 v210, v115, v131, v139
	v_pk_maximum3_f16 v211, v116, v132, v140
	v_pk_maximum3_f16 v228, v161, v213, v208
	v_pk_maximum3_f16 v232, v217, v221, v165
	v_pk_maximum3_f16 v225, v204, v216, v205
	v_pk_maximum3_f16 v226, v203, v215, v206
	v_pk_maximum3_f16 v227, v202, v214, v207
	v_pk_maximum3_f16 v229, v220, v224, v162
	v_pk_maximum3_f16 v230, v219, v223, v163
	v_pk_maximum3_f16 v212, v212, v228, v232
	v_pk_maximum3_f16 v231, v218, v222, v164
	v_pk_maximum3_f16 v209, v209, v225, v229
	v_pk_maximum3_f16 v210, v210, v226, v230
	v_pk_maximum3_f16 v211, v211, v227, v231
	v_pk_add_f16 v117, v117, v212 neg_lo:[0,1] neg_hi:[0,1]
	s_mov_b64 exec, s[64:65]
	buffer_load_dwordx4 v[78:81], v247, s[36:39], 0 offen
	buffer_load_dwordx4 v[30:33], v247, s[36:39], 0 offen offset:512
	s_mov_b64 exec, -1
	v_pk_add_f16 v114, v114, v209 neg_lo:[0,1] neg_hi:[0,1]
	v_pk_add_f16 v115, v115, v210 neg_lo:[0,1] neg_hi:[0,1]
	v_pk_add_f16 v116, v116, v211 neg_lo:[0,1] neg_hi:[0,1]
	v_pk_add_f16 v130, v130, v209 neg_lo:[0,1] neg_hi:[0,1]
	v_exp_f16_sdwa v225, v114 dst_sel:WORD_0 dst_unused:UNUSED_PAD src0_sel:WORD_0
	v_exp_f16_sdwa v226, v115 dst_sel:WORD_0 dst_unused:UNUSED_PAD src0_sel:WORD_0
	v_exp_f16_sdwa v227, v116 dst_sel:WORD_0 dst_unused:UNUSED_PAD src0_sel:WORD_0
	v_exp_f16_sdwa v228, v117 dst_sel:WORD_0 dst_unused:UNUSED_PAD src0_sel:WORD_0
	v_exp_f16_sdwa v225, v114 dst_sel:WORD_1 dst_unused:UNUSED_PRESERVE src0_sel:WORD_1
	v_exp_f16_sdwa v226, v115 dst_sel:WORD_1 dst_unused:UNUSED_PRESERVE src0_sel:WORD_1
	v_exp_f16_sdwa v227, v116 dst_sel:WORD_1 dst_unused:UNUSED_PRESERVE src0_sel:WORD_1
	v_exp_f16_sdwa v228, v117 dst_sel:WORD_1 dst_unused:UNUSED_PRESERVE src0_sel:WORD_1
	v_pk_add_f16 v131, v131, v210 neg_lo:[0,1] neg_hi:[0,1]
	v_pk_add_f16 v117, v225, 0
	v_pk_fma_f16 v77, v77, v228, 0
	v_pk_add_f16 v114, v228, 0
	v_pk_add_f16 v115, v227, 0
	v_pk_add_f16 v116, v226, 0
	v_pk_fma_f16 v76, v76, v227, 0
	v_pk_fma_f16 v75, v75, v226, 0
	v_pk_fma_f16 v74, v74, v225, 0
	v_pk_add_f16 v132, v132, v211 neg_lo:[0,1] neg_hi:[0,1]
	buffer_load_dwordx4 v[106:109], v248, s[36:39], 0 offen offset:512
	buffer_load_dwordx4 v[42:45], v248, s[36:39], 0 offen offset:1024
	v_pk_add_f16 v133, v133, v212 neg_lo:[0,1] neg_hi:[0,1]
	v_exp_f16_sdwa v225, v130 dst_sel:WORD_0 dst_unused:UNUSED_PAD src0_sel:WORD_0
	v_exp_f16_sdwa v226, v131 dst_sel:WORD_0 dst_unused:UNUSED_PAD src0_sel:WORD_0
	v_exp_f16_sdwa v227, v132 dst_sel:WORD_0 dst_unused:UNUSED_PAD src0_sel:WORD_0
	v_exp_f16_sdwa v228, v133 dst_sel:WORD_0 dst_unused:UNUSED_PAD src0_sel:WORD_0
	v_exp_f16_sdwa v225, v130 dst_sel:WORD_1 dst_unused:UNUSED_PRESERVE src0_sel:WORD_1
	v_exp_f16_sdwa v226, v131 dst_sel:WORD_1 dst_unused:UNUSED_PRESERVE src0_sel:WORD_1
	v_exp_f16_sdwa v227, v132 dst_sel:WORD_1 dst_unused:UNUSED_PRESERVE src0_sel:WORD_1
	v_exp_f16_sdwa v228, v133 dst_sel:WORD_1 dst_unused:UNUSED_PRESERVE src0_sel:WORD_1
	v_pk_add_f16 v117, v117, v225
	v_pk_fma_f16 v77, v101, v228, v77
	v_pk_add_f16 v101, v141, v212 neg_lo:[0,1] neg_hi:[0,1]
	v_pk_add_f16 v116, v116, v226
	v_pk_add_f16 v115, v115, v227
	v_pk_add_f16 v114, v114, v228
	v_pk_fma_f16 v74, v98, v225, v74
	v_pk_fma_f16 v75, v99, v226, v75
	v_pk_fma_f16 v76, v100, v227, v76
	v_pk_add_f16 v98, v138, v209 neg_lo:[0,1] neg_hi:[0,1]
	v_pk_add_f16 v99, v139, v210 neg_lo:[0,1] neg_hi:[0,1]
	v_pk_add_f16 v100, v140, v211 neg_lo:[0,1] neg_hi:[0,1]
	v_exp_f16_sdwa v130, v98 dst_sel:WORD_0 dst_unused:UNUSED_PAD src0_sel:WORD_0
	v_exp_f16_sdwa v131, v99 dst_sel:WORD_0 dst_unused:UNUSED_PAD src0_sel:WORD_0
	v_exp_f16_sdwa v132, v100 dst_sel:WORD_0 dst_unused:UNUSED_PAD src0_sel:WORD_0
	v_exp_f16_sdwa v133, v101 dst_sel:WORD_0 dst_unused:UNUSED_PAD src0_sel:WORD_0
	v_exp_f16_sdwa v130, v98 dst_sel:WORD_1 dst_unused:UNUSED_PRESERVE src0_sel:WORD_1
	v_exp_f16_sdwa v131, v99 dst_sel:WORD_1 dst_unused:UNUSED_PRESERVE src0_sel:WORD_1
	v_exp_f16_sdwa v132, v100 dst_sel:WORD_1 dst_unused:UNUSED_PRESERVE src0_sel:WORD_1
	v_exp_f16_sdwa v133, v101 dst_sel:WORD_1 dst_unused:UNUSED_PRESERVE src0_sel:WORD_1
	v_pk_add_f16 v101, v117, v130
	v_pk_add_f16 v98, v114, v133
	s_mov_b64 exec, s[66:67]
	buffer_load_dwordx4 v[122:125], v248, s[36:39], 0 offen offset:2048
	buffer_load_dwordx4 v[62:65], v248, s[36:39], 0 offen offset:2560
	s_mov_b64 exec, -1
	v_pk_add_f16 v99, v115, v132
	v_pk_add_f16 v100, v116, v131
	v_pk_fma_f16 v77, v121, v133, v77
	v_pk_fma_f16 v76, v120, v132, v76
	v_pk_fma_f16 v75, v119, v131, v75
	v_pk_fma_f16 v74, v118, v130, v74
	v_pk_add_f16 v114, v204, v209 neg_lo:[0,1] neg_hi:[0,1]
	v_pk_add_f16 v115, v203, v210 neg_lo:[0,1] neg_hi:[0,1]
	v_pk_add_f16 v116, v202, v211 neg_lo:[0,1] neg_hi:[0,1]
	v_pk_add_f16 v117, v161, v212 neg_lo:[0,1] neg_hi:[0,1]
	v_exp_f16_sdwa v118, v114 dst_sel:WORD_0 dst_unused:UNUSED_PAD src0_sel:WORD_0
	v_exp_f16_sdwa v119, v115 dst_sel:WORD_0 dst_unused:UNUSED_PAD src0_sel:WORD_0
	v_exp_f16_sdwa v120, v116 dst_sel:WORD_0 dst_unused:UNUSED_PAD src0_sel:WORD_0
	v_exp_f16_sdwa v121, v117 dst_sel:WORD_0 dst_unused:UNUSED_PAD src0_sel:WORD_0
	v_exp_f16_sdwa v118, v114 dst_sel:WORD_1 dst_unused:UNUSED_PRESERVE src0_sel:WORD_1
	v_exp_f16_sdwa v119, v115 dst_sel:WORD_1 dst_unused:UNUSED_PRESERVE src0_sel:WORD_1
	v_exp_f16_sdwa v120, v116 dst_sel:WORD_1 dst_unused:UNUSED_PRESERVE src0_sel:WORD_1
	v_exp_f16_sdwa v121, v117 dst_sel:WORD_1 dst_unused:UNUSED_PRESERVE src0_sel:WORD_1
	v_pk_add_f16 v114, v216, v209 neg_lo:[0,1] neg_hi:[0,1]
	v_pk_add_f16 v101, v101, v118
	v_pk_add_f16 v100, v100, v119
	v_pk_add_f16 v99, v99, v120
	s_mov_b64 exec, s[76:77]
	buffer_load_dwordx4 v[134:137], v249, s[36:39], 0 offen
	buffer_load_dwordx4 v[82:85], v249, s[36:39], 0 offen offset:512
	s_mov_b64 exec, -1
	v_pk_add_f16 v98, v98, v121
	v_pk_fma_f16 v74, v46, v118, v74
	v_pk_fma_f16 v75, v47, v119, v75
	v_pk_fma_f16 v76, v48, v120, v76
	v_pk_fma_f16 v77, v49, v121, v77
	v_pk_add_f16 v115, v215, v210 neg_lo:[0,1] neg_hi:[0,1]
	v_pk_add_f16 v116, v214, v211 neg_lo:[0,1] neg_hi:[0,1]
	v_pk_add_f16 v117, v213, v212 neg_lo:[0,1] neg_hi:[0,1]
	v_exp_f16_sdwa v118, v114 dst_sel:WORD_0 dst_unused:UNUSED_PAD src0_sel:WORD_0
	v_exp_f16_sdwa v119, v115 dst_sel:WORD_0 dst_unused:UNUSED_PAD src0_sel:WORD_0
	v_exp_f16_sdwa v120, v116 dst_sel:WORD_0 dst_unused:UNUSED_PAD src0_sel:WORD_0
	v_exp_f16_sdwa v121, v117 dst_sel:WORD_0 dst_unused:UNUSED_PAD src0_sel:WORD_0
	v_exp_f16_sdwa v118, v114 dst_sel:WORD_1 dst_unused:UNUSED_PRESERVE src0_sel:WORD_1
	v_exp_f16_sdwa v119, v115 dst_sel:WORD_1 dst_unused:UNUSED_PRESERVE src0_sel:WORD_1
	v_exp_f16_sdwa v120, v116 dst_sel:WORD_1 dst_unused:UNUSED_PRESERVE src0_sel:WORD_1
	v_exp_f16_sdwa v121, v117 dst_sel:WORD_1 dst_unused:UNUSED_PRESERVE src0_sel:WORD_1
	v_pk_add_f16 v114, v205, v209 neg_lo:[0,1] neg_hi:[0,1]
	v_pk_add_f16 v101, v101, v118
	v_pk_add_f16 v98, v98, v121
	v_pk_add_f16 v99, v99, v120
	v_pk_add_f16 v100, v100, v119
	v_pk_fma_f16 v77, v69, v121, v77
	v_pk_fma_f16 v76, v68, v120, v76
	s_mov_b64 exec, s[70:71]
	buffer_load_dwordx4 v[142:145], v250, s[36:39], 0 offen offset:512
	buffer_load_dwordx4 v[102:105], v250, s[36:39], 0 offen offset:1024
	s_mov_b64 exec, -1
	v_pk_fma_f16 v75, v67, v119, v75
	v_pk_fma_f16 v74, v66, v118, v74
	v_pk_add_f16 v115, v206, v210 neg_lo:[0,1] neg_hi:[0,1]
	v_pk_add_f16 v116, v207, v211 neg_lo:[0,1] neg_hi:[0,1]
	v_pk_add_f16 v117, v208, v212 neg_lo:[0,1] neg_hi:[0,1]
	v_exp_f16_sdwa v118, v114 dst_sel:WORD_0 dst_unused:UNUSED_PAD src0_sel:WORD_0
	v_exp_f16_sdwa v119, v115 dst_sel:WORD_0 dst_unused:UNUSED_PAD src0_sel:WORD_0
	v_exp_f16_sdwa v120, v116 dst_sel:WORD_0 dst_unused:UNUSED_PAD src0_sel:WORD_0
	v_exp_f16_sdwa v121, v117 dst_sel:WORD_0 dst_unused:UNUSED_PAD src0_sel:WORD_0
	v_exp_f16_sdwa v118, v114 dst_sel:WORD_1 dst_unused:UNUSED_PRESERVE src0_sel:WORD_1
	v_exp_f16_sdwa v119, v115 dst_sel:WORD_1 dst_unused:UNUSED_PRESERVE src0_sel:WORD_1
	v_exp_f16_sdwa v120, v116 dst_sel:WORD_1 dst_unused:UNUSED_PRESERVE src0_sel:WORD_1
	v_exp_f16_sdwa v121, v117 dst_sel:WORD_1 dst_unused:UNUSED_PRESERVE src0_sel:WORD_1
	v_pk_add_f16 v114, v220, v209 neg_lo:[0,1] neg_hi:[0,1]
	v_pk_add_f16 v101, v101, v118
	v_pk_add_f16 v100, v100, v119
	v_pk_add_f16 v99, v99, v120
	v_pk_add_f16 v98, v98, v121
	v_pk_fma_f16 v74, v90, v118, v74
	v_pk_fma_f16 v75, v91, v119, v75
	v_pk_fma_f16 v76, v92, v120, v76
	v_pk_fma_f16 v77, v93, v121, v77
	s_mov_b64 exec, s[78:79]
	buffer_load_dwordx4 v[6:9], v250, s[36:39], 0 offen offset:2048
	buffer_load_dwordx4 v[2:5], v250, s[36:39], 0 offen offset:2560
	s_mov_b64 exec, -1
	v_pk_add_f16 v115, v219, v210 neg_lo:[0,1] neg_hi:[0,1]
	v_pk_add_f16 v116, v218, v211 neg_lo:[0,1] neg_hi:[0,1]
	v_pk_add_f16 v117, v217, v212 neg_lo:[0,1] neg_hi:[0,1]
	v_exp_f16_sdwa v118, v114 dst_sel:WORD_0 dst_unused:UNUSED_PAD src0_sel:WORD_0
	v_exp_f16_sdwa v119, v115 dst_sel:WORD_0 dst_unused:UNUSED_PAD src0_sel:WORD_0
	v_exp_f16_sdwa v120, v116 dst_sel:WORD_0 dst_unused:UNUSED_PAD src0_sel:WORD_0
	v_exp_f16_sdwa v121, v117 dst_sel:WORD_0 dst_unused:UNUSED_PAD src0_sel:WORD_0
	v_exp_f16_sdwa v118, v114 dst_sel:WORD_1 dst_unused:UNUSED_PRESERVE src0_sel:WORD_1
	v_exp_f16_sdwa v119, v115 dst_sel:WORD_1 dst_unused:UNUSED_PRESERVE src0_sel:WORD_1
	v_exp_f16_sdwa v120, v116 dst_sel:WORD_1 dst_unused:UNUSED_PRESERVE src0_sel:WORD_1
	v_exp_f16_sdwa v121, v117 dst_sel:WORD_1 dst_unused:UNUSED_PRESERVE src0_sel:WORD_1
	v_pk_add_f16 v114, v224, v209 neg_lo:[0,1] neg_hi:[0,1]
	v_pk_add_f16 v101, v101, v118
	v_pk_add_f16 v98, v98, v121
	v_pk_add_f16 v99, v99, v120
	v_pk_add_f16 v100, v100, v119
	v_pk_fma_f16 v77, v25, v121, v77
	v_pk_fma_f16 v76, v24, v120, v76
	v_pk_fma_f16 v75, v23, v119, v75
	v_pk_fma_f16 v74, v22, v118, v74
	v_pk_add_f16 v115, v223, v210 neg_lo:[0,1] neg_hi:[0,1]
	v_pk_add_f16 v116, v222, v211 neg_lo:[0,1] neg_hi:[0,1]
	v_pk_add_f16 v117, v221, v212 neg_lo:[0,1] neg_hi:[0,1]
	v_exp_f16_sdwa v118, v114 dst_sel:WORD_0 dst_unused:UNUSED_PAD src0_sel:WORD_0
	v_exp_f16_sdwa v119, v115 dst_sel:WORD_0 dst_unused:UNUSED_PAD src0_sel:WORD_0
	v_exp_f16_sdwa v120, v116 dst_sel:WORD_0 dst_unused:UNUSED_PAD src0_sel:WORD_0
	v_exp_f16_sdwa v121, v117 dst_sel:WORD_0 dst_unused:UNUSED_PAD src0_sel:WORD_0
	v_exp_f16_sdwa v118, v114 dst_sel:WORD_1 dst_unused:UNUSED_PRESERVE src0_sel:WORD_1
	v_exp_f16_sdwa v119, v115 dst_sel:WORD_1 dst_unused:UNUSED_PRESERVE src0_sel:WORD_1
	v_exp_f16_sdwa v120, v116 dst_sel:WORD_1 dst_unused:UNUSED_PRESERVE src0_sel:WORD_1
	v_exp_f16_sdwa v121, v117 dst_sel:WORD_1 dst_unused:UNUSED_PRESERVE src0_sel:WORD_1
	v_pk_add_f16 v114, v162, v209 neg_lo:[0,1] neg_hi:[0,1]
	v_pk_add_f16 v101, v101, v118
	v_pk_add_f16 v100, v100, v119
	v_pk_add_f16 v99, v99, v120
	v_pk_add_f16 v98, v98, v121
	v_pk_fma_f16 v74, v34, v118, v74
	v_pk_fma_f16 v75, v35, v119, v75
	v_pk_fma_f16 v76, v36, v120, v76
	v_pk_fma_f16 v77, v37, v121, v77
	v_pk_add_f16 v115, v163, v210 neg_lo:[0,1] neg_hi:[0,1]
	v_pk_add_f16 v116, v164, v211 neg_lo:[0,1] neg_hi:[0,1]
	v_pk_add_f16 v117, v165, v212 neg_lo:[0,1] neg_hi:[0,1]
	v_exp_f16_sdwa v118, v114 dst_sel:WORD_0 dst_unused:UNUSED_PAD src0_sel:WORD_0
	v_exp_f16_sdwa v119, v115 dst_sel:WORD_0 dst_unused:UNUSED_PAD src0_sel:WORD_0
	v_exp_f16_sdwa v120, v116 dst_sel:WORD_0 dst_unused:UNUSED_PAD src0_sel:WORD_0
	v_exp_f16_sdwa v121, v117 dst_sel:WORD_0 dst_unused:UNUSED_PAD src0_sel:WORD_0
	v_exp_f16_sdwa v118, v114 dst_sel:WORD_1 dst_unused:UNUSED_PRESERVE src0_sel:WORD_1
	v_exp_f16_sdwa v119, v115 dst_sel:WORD_1 dst_unused:UNUSED_PRESERVE src0_sel:WORD_1
	v_exp_f16_sdwa v120, v116 dst_sel:WORD_1 dst_unused:UNUSED_PRESERVE src0_sel:WORD_1
	v_exp_f16_sdwa v121, v117 dst_sel:WORD_1 dst_unused:UNUSED_PRESERVE src0_sel:WORD_1
	v_pk_add_f16 v101, v101, v118
	v_pk_add_f16 v100, v100, v119
	v_rcp_f16_e32 v114, v101
	v_rcp_f16_sdwa v101, v101 dst_sel:DWORD dst_unused:UNUSED_PAD src0_sel:WORD_1
	v_pk_add_f16 v99, v99, v120
	v_rcp_f16_e32 v115, v100
	v_rcp_f16_sdwa v100, v100 dst_sel:DWORD dst_unused:UNUSED_PAD src0_sel:WORD_1
	v_pk_add_f16 v98, v98, v121
	v_rcp_f16_e32 v116, v99
	v_rcp_f16_sdwa v99, v99 dst_sel:DWORD dst_unused:UNUSED_PAD src0_sel:WORD_1
	v_rcp_f16_e32 v117, v98
	v_rcp_f16_sdwa v98, v98 dst_sel:DWORD dst_unused:UNUSED_PAD src0_sel:WORD_1
	v_pk_fma_f16 v74, v50, v118, v74
	v_pack_b32_f16 v101, v114, v101
	v_pk_fma_f16 v75, v51, v119, v75
	v_pk_mul_f16 v138, v74, v101
	v_pack_b32_f16 v74, v115, v100
	v_pk_fma_f16 v76, v52, v120, v76
	v_pk_mul_f16 v139, v75, v74
	v_pack_b32_f16 v74, v116, v99
	v_pk_fma_f16 v77, v53, v121, v77
	v_pk_mul_f16 v140, v76, v74
	v_pack_b32_f16 v74, v117, v98
	v_pk_mul_f16 v141, v77, v74
	s_waitcnt vmcnt(12)
	v_pk_mul_f16 v74, v160, v154 op_sel_hi:[0,1]
	v_pk_mul_f16 v77, v160, v157 op_sel_hi:[0,1]
	v_pk_mul_f16 v101, v158, v157 op_sel_hi:[0,1]
	v_pk_mul_f16 v117, v159, v157 op_sel_hi:[0,1]
	v_pk_mul_f16 v75, v160, v155 op_sel_hi:[0,1]
	v_pk_mul_f16 v76, v160, v156 op_sel_hi:[0,1]
	v_pk_mul_f16 v98, v158, v154 op_sel_hi:[0,1]
	v_pk_mul_f16 v99, v158, v155 op_sel_hi:[0,1]
	v_pk_mul_f16 v100, v158, v156 op_sel_hi:[0,1]
	v_pk_mul_f16 v114, v159, v154 op_sel_hi:[0,1]
	v_pk_mul_f16 v115, v159, v155 op_sel_hi:[0,1]
	v_pk_mul_f16 v116, v159, v156 op_sel_hi:[0,1]
	v_pk_fma_f16 v89, v89, v157, v77
	v_pk_fma_f16 v86, v86, v154, v74
	v_pk_fma_f16 v113, v113, v157, v77
	v_pk_fma_f16 v110, v110, v154, v74
	v_pk_fma_f16 v77, v129, v157, v77
	v_pk_fma_f16 v74, v126, v154, v74
	v_pk_fma_f16 v118, v57, v157, v101
	v_pk_fma_f16 v126, v73, v157, v101
	v_pk_fma_f16 v101, v97, v157, v101
	v_pk_fma_f16 v130, v29, v157, v117
	v_pk_fma_f16 v161, v41, v157, v117
	v_pk_fma_f16 v117, v61, v157, v117
	v_pk_maximum3_f16 v157, v89, v113, v77
	v_pk_fma_f16 v88, v88, v156, v76
	v_pk_fma_f16 v87, v87, v155, v75
	v_pk_fma_f16 v112, v112, v156, v76
	v_pk_fma_f16 v111, v111, v155, v75
	v_pk_fma_f16 v76, v128, v156, v76
	v_pk_fma_f16 v75, v127, v155, v75
	v_pk_fma_f16 v119, v56, v156, v100
	v_pk_fma_f16 v120, v55, v155, v99
	v_pk_fma_f16 v121, v54, v154, v98
	v_pk_fma_f16 v127, v72, v156, v100
	v_pk_fma_f16 v128, v71, v155, v99
	v_pk_fma_f16 v129, v70, v154, v98
	v_pk_fma_f16 v100, v96, v156, v100
	v_pk_fma_f16 v99, v95, v155, v99
	v_pk_fma_f16 v98, v94, v154, v98
	v_pk_fma_f16 v131, v28, v156, v116
	v_pk_fma_f16 v132, v27, v155, v115
	v_pk_fma_f16 v133, v26, v154, v114
	v_pk_fma_f16 v162, v40, v156, v116
	v_pk_fma_f16 v163, v39, v155, v115
	v_pk_fma_f16 v164, v38, v154, v114
	v_pk_fma_f16 v116, v60, v156, v116
	v_pk_fma_f16 v115, v59, v155, v115
	v_pk_fma_f16 v114, v58, v154, v114
	v_pk_maximum3_f16 v154, v86, v110, v74
	v_pk_maximum3_f16 v155, v87, v111, v75
	v_pk_maximum3_f16 v156, v88, v112, v76
	v_pk_maximum3_f16 v204, v118, v126, v101
	v_pk_maximum3_f16 v208, v130, v161, v117
	v_pk_maximum3_f16 v165, v121, v129, v98
	v_pk_maximum3_f16 v202, v120, v128, v99
	v_pk_maximum3_f16 v203, v119, v127, v100
	v_pk_maximum3_f16 v205, v133, v164, v114
	v_pk_maximum3_f16 v206, v132, v163, v115
	v_pk_maximum3_f16 v157, v157, v204, v208
	v_pk_maximum3_f16 v207, v131, v162, v116
	v_pk_maximum3_f16 v154, v154, v165, v205
	v_pk_maximum3_f16 v155, v155, v202, v206
	v_pk_maximum3_f16 v156, v156, v203, v207
	v_pk_add_f16 v89, v89, v157 neg_lo:[0,1] neg_hi:[0,1]
	v_pk_add_f16 v86, v86, v154 neg_lo:[0,1] neg_hi:[0,1]
	v_pk_add_f16 v87, v87, v155 neg_lo:[0,1] neg_hi:[0,1]
	v_pk_add_f16 v88, v88, v156 neg_lo:[0,1] neg_hi:[0,1]
	v_pk_add_f16 v110, v110, v154 neg_lo:[0,1] neg_hi:[0,1]
	v_exp_f16_sdwa v165, v86 dst_sel:WORD_0 dst_unused:UNUSED_PAD src0_sel:WORD_0
	v_exp_f16_sdwa v202, v87 dst_sel:WORD_0 dst_unused:UNUSED_PAD src0_sel:WORD_0
	v_exp_f16_sdwa v203, v88 dst_sel:WORD_0 dst_unused:UNUSED_PAD src0_sel:WORD_0
	v_exp_f16_sdwa v204, v89 dst_sel:WORD_0 dst_unused:UNUSED_PAD src0_sel:WORD_0
	v_exp_f16_sdwa v165, v86 dst_sel:WORD_1 dst_unused:UNUSED_PRESERVE src0_sel:WORD_1
	v_exp_f16_sdwa v202, v87 dst_sel:WORD_1 dst_unused:UNUSED_PRESERVE src0_sel:WORD_1
	v_exp_f16_sdwa v203, v88 dst_sel:WORD_1 dst_unused:UNUSED_PRESERVE src0_sel:WORD_1
	v_exp_f16_sdwa v204, v89 dst_sel:WORD_1 dst_unused:UNUSED_PRESERVE src0_sel:WORD_1
	v_pk_add_f16 v111, v111, v155 neg_lo:[0,1] neg_hi:[0,1]
	v_pk_add_f16 v89, v165, 0
	v_pk_fma_f16 v49, v49, v204, 0
	v_pk_add_f16 v86, v204, 0
	v_pk_add_f16 v87, v203, 0
	v_pk_add_f16 v88, v202, 0
	v_pk_fma_f16 v48, v48, v203, 0
	v_pk_fma_f16 v47, v47, v202, 0
	v_pk_fma_f16 v46, v46, v165, 0
	v_pk_add_f16 v112, v112, v156 neg_lo:[0,1] neg_hi:[0,1]
	v_pk_add_f16 v113, v113, v157 neg_lo:[0,1] neg_hi:[0,1]
	v_exp_f16_sdwa v165, v110 dst_sel:WORD_0 dst_unused:UNUSED_PAD src0_sel:WORD_0
	v_exp_f16_sdwa v202, v111 dst_sel:WORD_0 dst_unused:UNUSED_PAD src0_sel:WORD_0
	v_exp_f16_sdwa v203, v112 dst_sel:WORD_0 dst_unused:UNUSED_PAD src0_sel:WORD_0
	v_exp_f16_sdwa v204, v113 dst_sel:WORD_0 dst_unused:UNUSED_PAD src0_sel:WORD_0
	v_exp_f16_sdwa v165, v110 dst_sel:WORD_1 dst_unused:UNUSED_PRESERVE src0_sel:WORD_1
	v_exp_f16_sdwa v202, v111 dst_sel:WORD_1 dst_unused:UNUSED_PRESERVE src0_sel:WORD_1
	v_exp_f16_sdwa v203, v112 dst_sel:WORD_1 dst_unused:UNUSED_PRESERVE src0_sel:WORD_1
	v_exp_f16_sdwa v204, v113 dst_sel:WORD_1 dst_unused:UNUSED_PRESERVE src0_sel:WORD_1
	v_pk_add_f16 v89, v89, v165
	v_pk_fma_f16 v49, v69, v204, v49
	v_pk_add_f16 v69, v77, v157 neg_lo:[0,1] neg_hi:[0,1]
	v_pk_add_f16 v88, v88, v202
	v_pk_add_f16 v87, v87, v203
	v_pk_add_f16 v86, v86, v204
	v_pk_fma_f16 v46, v66, v165, v46
	v_pk_fma_f16 v47, v67, v202, v47
	v_pk_fma_f16 v48, v68, v203, v48
	v_pk_add_f16 v66, v74, v154 neg_lo:[0,1] neg_hi:[0,1]
	v_pk_add_f16 v67, v75, v155 neg_lo:[0,1] neg_hi:[0,1]
	v_pk_add_f16 v68, v76, v156 neg_lo:[0,1] neg_hi:[0,1]
	v_exp_f16_sdwa v74, v66 dst_sel:WORD_0 dst_unused:UNUSED_PAD src0_sel:WORD_0
	v_exp_f16_sdwa v75, v67 dst_sel:WORD_0 dst_unused:UNUSED_PAD src0_sel:WORD_0
	v_exp_f16_sdwa v76, v68 dst_sel:WORD_0 dst_unused:UNUSED_PAD src0_sel:WORD_0
	v_exp_f16_sdwa v77, v69 dst_sel:WORD_0 dst_unused:UNUSED_PAD src0_sel:WORD_0
	v_exp_f16_sdwa v74, v66 dst_sel:WORD_1 dst_unused:UNUSED_PRESERVE src0_sel:WORD_1
	v_exp_f16_sdwa v75, v67 dst_sel:WORD_1 dst_unused:UNUSED_PRESERVE src0_sel:WORD_1
	v_exp_f16_sdwa v76, v68 dst_sel:WORD_1 dst_unused:UNUSED_PRESERVE src0_sel:WORD_1
	v_exp_f16_sdwa v77, v69 dst_sel:WORD_1 dst_unused:UNUSED_PRESERVE src0_sel:WORD_1
	v_pk_add_f16 v69, v89, v74
	v_pk_add_f16 v66, v86, v77
	v_pk_add_f16 v67, v87, v76
	v_pk_add_f16 v68, v88, v75
	v_pk_fma_f16 v49, v93, v77, v49
	v_pk_fma_f16 v48, v92, v76, v48
	v_pk_fma_f16 v47, v91, v75, v47
	v_pk_fma_f16 v46, v90, v74, v46
	v_pk_add_f16 v74, v121, v154 neg_lo:[0,1] neg_hi:[0,1]
	v_pk_add_f16 v75, v120, v155 neg_lo:[0,1] neg_hi:[0,1]
	v_pk_add_f16 v76, v119, v156 neg_lo:[0,1] neg_hi:[0,1]
	v_pk_add_f16 v77, v118, v157 neg_lo:[0,1] neg_hi:[0,1]
	v_exp_f16_sdwa v86, v74 dst_sel:WORD_0 dst_unused:UNUSED_PAD src0_sel:WORD_0
	v_exp_f16_sdwa v87, v75 dst_sel:WORD_0 dst_unused:UNUSED_PAD src0_sel:WORD_0
	v_exp_f16_sdwa v88, v76 dst_sel:WORD_0 dst_unused:UNUSED_PAD src0_sel:WORD_0
	v_exp_f16_sdwa v89, v77 dst_sel:WORD_0 dst_unused:UNUSED_PAD src0_sel:WORD_0
	v_exp_f16_sdwa v86, v74 dst_sel:WORD_1 dst_unused:UNUSED_PRESERVE src0_sel:WORD_1
	v_exp_f16_sdwa v87, v75 dst_sel:WORD_1 dst_unused:UNUSED_PRESERVE src0_sel:WORD_1
	v_exp_f16_sdwa v88, v76 dst_sel:WORD_1 dst_unused:UNUSED_PRESERVE src0_sel:WORD_1
	v_exp_f16_sdwa v89, v77 dst_sel:WORD_1 dst_unused:UNUSED_PRESERVE src0_sel:WORD_1
	v_pk_add_f16 v74, v129, v154 neg_lo:[0,1] neg_hi:[0,1]
	v_pk_add_f16 v69, v69, v86
	v_pk_add_f16 v68, v68, v87
	v_pk_add_f16 v67, v67, v88
	v_pk_add_f16 v66, v66, v89
	v_pk_fma_f16 v46, v22, v86, v46
	v_pk_fma_f16 v47, v23, v87, v47
	v_pk_fma_f16 v48, v24, v88, v48
	v_pk_fma_f16 v49, v25, v89, v49
	v_pk_add_f16 v75, v128, v155 neg_lo:[0,1] neg_hi:[0,1]
	v_pk_add_f16 v76, v127, v156 neg_lo:[0,1] neg_hi:[0,1]
	v_pk_add_f16 v77, v126, v157 neg_lo:[0,1] neg_hi:[0,1]
	v_exp_f16_sdwa v86, v74 dst_sel:WORD_0 dst_unused:UNUSED_PAD src0_sel:WORD_0
	v_exp_f16_sdwa v87, v75 dst_sel:WORD_0 dst_unused:UNUSED_PAD src0_sel:WORD_0
	v_exp_f16_sdwa v88, v76 dst_sel:WORD_0 dst_unused:UNUSED_PAD src0_sel:WORD_0
	v_exp_f16_sdwa v89, v77 dst_sel:WORD_0 dst_unused:UNUSED_PAD src0_sel:WORD_0
	v_exp_f16_sdwa v86, v74 dst_sel:WORD_1 dst_unused:UNUSED_PRESERVE src0_sel:WORD_1
	v_exp_f16_sdwa v87, v75 dst_sel:WORD_1 dst_unused:UNUSED_PRESERVE src0_sel:WORD_1
	v_exp_f16_sdwa v88, v76 dst_sel:WORD_1 dst_unused:UNUSED_PRESERVE src0_sel:WORD_1
	v_exp_f16_sdwa v89, v77 dst_sel:WORD_1 dst_unused:UNUSED_PRESERVE src0_sel:WORD_1
	v_pk_add_f16 v74, v98, v154 neg_lo:[0,1] neg_hi:[0,1]
	v_pk_add_f16 v69, v69, v86
	v_pk_add_f16 v66, v66, v89
	v_pk_add_f16 v67, v67, v88
	v_pk_add_f16 v68, v68, v87
	v_pk_fma_f16 v49, v37, v89, v49
	v_pk_fma_f16 v48, v36, v88, v48
	v_pk_fma_f16 v47, v35, v87, v47
	v_pk_fma_f16 v46, v34, v86, v46
	v_pk_add_f16 v75, v99, v155 neg_lo:[0,1] neg_hi:[0,1]
	v_pk_add_f16 v76, v100, v156 neg_lo:[0,1] neg_hi:[0,1]
	v_pk_add_f16 v77, v101, v157 neg_lo:[0,1] neg_hi:[0,1]
	v_exp_f16_sdwa v86, v74 dst_sel:WORD_0 dst_unused:UNUSED_PAD src0_sel:WORD_0
	v_exp_f16_sdwa v87, v75 dst_sel:WORD_0 dst_unused:UNUSED_PAD src0_sel:WORD_0
	v_exp_f16_sdwa v88, v76 dst_sel:WORD_0 dst_unused:UNUSED_PAD src0_sel:WORD_0
	v_exp_f16_sdwa v89, v77 dst_sel:WORD_0 dst_unused:UNUSED_PAD src0_sel:WORD_0
	v_exp_f16_sdwa v86, v74 dst_sel:WORD_1 dst_unused:UNUSED_PRESERVE src0_sel:WORD_1
	v_exp_f16_sdwa v87, v75 dst_sel:WORD_1 dst_unused:UNUSED_PRESERVE src0_sel:WORD_1
	v_exp_f16_sdwa v88, v76 dst_sel:WORD_1 dst_unused:UNUSED_PRESERVE src0_sel:WORD_1
	v_exp_f16_sdwa v89, v77 dst_sel:WORD_1 dst_unused:UNUSED_PRESERVE src0_sel:WORD_1
	v_pk_add_f16 v74, v133, v154 neg_lo:[0,1] neg_hi:[0,1]
	v_pk_add_f16 v69, v69, v86
	v_pk_add_f16 v68, v68, v87
	v_pk_add_f16 v67, v67, v88
	v_pk_add_f16 v66, v66, v89
	v_pk_fma_f16 v46, v50, v86, v46
	v_pk_fma_f16 v47, v51, v87, v47
	v_pk_fma_f16 v48, v52, v88, v48
	v_pk_fma_f16 v49, v53, v89, v49
	v_pk_add_f16 v75, v132, v155 neg_lo:[0,1] neg_hi:[0,1]
	v_pk_add_f16 v76, v131, v156 neg_lo:[0,1] neg_hi:[0,1]
	v_pk_add_f16 v77, v130, v157 neg_lo:[0,1] neg_hi:[0,1]
	v_exp_f16_sdwa v86, v74 dst_sel:WORD_0 dst_unused:UNUSED_PAD src0_sel:WORD_0
	v_exp_f16_sdwa v87, v75 dst_sel:WORD_0 dst_unused:UNUSED_PAD src0_sel:WORD_0
	v_exp_f16_sdwa v88, v76 dst_sel:WORD_0 dst_unused:UNUSED_PAD src0_sel:WORD_0
	v_exp_f16_sdwa v89, v77 dst_sel:WORD_0 dst_unused:UNUSED_PAD src0_sel:WORD_0
	v_exp_f16_sdwa v86, v74 dst_sel:WORD_1 dst_unused:UNUSED_PRESERVE src0_sel:WORD_1
	v_exp_f16_sdwa v87, v75 dst_sel:WORD_1 dst_unused:UNUSED_PRESERVE src0_sel:WORD_1
	v_exp_f16_sdwa v88, v76 dst_sel:WORD_1 dst_unused:UNUSED_PRESERVE src0_sel:WORD_1
	v_exp_f16_sdwa v89, v77 dst_sel:WORD_1 dst_unused:UNUSED_PRESERVE src0_sel:WORD_1
	v_pk_add_f16 v74, v164, v154 neg_lo:[0,1] neg_hi:[0,1]
	v_pk_add_f16 v69, v69, v86
	v_pk_add_f16 v66, v66, v89
	v_pk_add_f16 v67, v67, v88
	v_pk_add_f16 v68, v68, v87
	v_pk_fma_f16 v49, v13, v89, v49
	v_pk_fma_f16 v48, v12, v88, v48
	v_pk_fma_f16 v47, v11, v87, v47
	v_pk_fma_f16 v46, v10, v86, v46
	v_pk_add_f16 v75, v163, v155 neg_lo:[0,1] neg_hi:[0,1]
	v_pk_add_f16 v76, v162, v156 neg_lo:[0,1] neg_hi:[0,1]
	v_pk_add_f16 v77, v161, v157 neg_lo:[0,1] neg_hi:[0,1]
	v_exp_f16_sdwa v86, v74 dst_sel:WORD_0 dst_unused:UNUSED_PAD src0_sel:WORD_0
	v_exp_f16_sdwa v87, v75 dst_sel:WORD_0 dst_unused:UNUSED_PAD src0_sel:WORD_0
	v_exp_f16_sdwa v88, v76 dst_sel:WORD_0 dst_unused:UNUSED_PAD src0_sel:WORD_0
	v_exp_f16_sdwa v89, v77 dst_sel:WORD_0 dst_unused:UNUSED_PAD src0_sel:WORD_0
	v_exp_f16_sdwa v86, v74 dst_sel:WORD_1 dst_unused:UNUSED_PRESERVE src0_sel:WORD_1
	v_exp_f16_sdwa v87, v75 dst_sel:WORD_1 dst_unused:UNUSED_PRESERVE src0_sel:WORD_1
	v_exp_f16_sdwa v88, v76 dst_sel:WORD_1 dst_unused:UNUSED_PRESERVE src0_sel:WORD_1
	v_exp_f16_sdwa v89, v77 dst_sel:WORD_1 dst_unused:UNUSED_PRESERVE src0_sel:WORD_1
	v_pk_add_f16 v74, v114, v154 neg_lo:[0,1] neg_hi:[0,1]
	v_pk_add_f16 v69, v69, v86
	v_pk_add_f16 v68, v68, v87
	v_pk_add_f16 v67, v67, v88
	v_pk_add_f16 v66, v66, v89
	v_pk_fma_f16 v46, v14, v86, v46
	v_pk_fma_f16 v47, v15, v87, v47
	v_pk_fma_f16 v48, v16, v88, v48
	v_pk_fma_f16 v49, v17, v89, v49
	v_pk_add_f16 v75, v115, v155 neg_lo:[0,1] neg_hi:[0,1]
	v_pk_add_f16 v76, v116, v156 neg_lo:[0,1] neg_hi:[0,1]
	v_pk_add_f16 v77, v117, v157 neg_lo:[0,1] neg_hi:[0,1]
	v_exp_f16_sdwa v86, v74 dst_sel:WORD_0 dst_unused:UNUSED_PAD src0_sel:WORD_0
	v_exp_f16_sdwa v87, v75 dst_sel:WORD_0 dst_unused:UNUSED_PAD src0_sel:WORD_0
	v_exp_f16_sdwa v88, v76 dst_sel:WORD_0 dst_unused:UNUSED_PAD src0_sel:WORD_0
	v_exp_f16_sdwa v89, v77 dst_sel:WORD_0 dst_unused:UNUSED_PAD src0_sel:WORD_0
	v_exp_f16_sdwa v86, v74 dst_sel:WORD_1 dst_unused:UNUSED_PRESERVE src0_sel:WORD_1
	v_exp_f16_sdwa v87, v75 dst_sel:WORD_1 dst_unused:UNUSED_PRESERVE src0_sel:WORD_1
	v_exp_f16_sdwa v88, v76 dst_sel:WORD_1 dst_unused:UNUSED_PRESERVE src0_sel:WORD_1
	v_exp_f16_sdwa v89, v77 dst_sel:WORD_1 dst_unused:UNUSED_PRESERVE src0_sel:WORD_1
	v_pk_add_f16 v69, v69, v86
	v_pk_add_f16 v68, v68, v87
	v_rcp_f16_e32 v74, v69
	v_rcp_f16_sdwa v69, v69 dst_sel:DWORD dst_unused:UNUSED_PAD src0_sel:WORD_1
	v_pk_add_f16 v67, v67, v88
	v_rcp_f16_e32 v75, v68
	v_rcp_f16_sdwa v68, v68 dst_sel:DWORD dst_unused:UNUSED_PAD src0_sel:WORD_1
	v_pk_add_f16 v66, v66, v89
	v_pk_fma_f16 v46, v18, v86, v46
	v_rcp_f16_e32 v86, v67
	v_rcp_f16_sdwa v67, v67 dst_sel:DWORD dst_unused:UNUSED_PAD src0_sel:WORD_1
	v_pk_fma_f16 v47, v19, v87, v47
	v_rcp_f16_e32 v87, v66
	v_rcp_f16_sdwa v66, v66 dst_sel:DWORD dst_unused:UNUSED_PAD src0_sel:WORD_1
	v_pack_b32_f16 v69, v74, v69
	v_pk_mul_f16 v77, v46, v69
	v_pack_b32_f16 v46, v75, v68
	v_pk_fma_f16 v48, v20, v88, v48
	v_pk_mul_f16 v76, v47, v46
	v_pack_b32_f16 v46, v86, v67
	v_pk_fma_f16 v49, v21, v89, v49
	v_pk_mul_f16 v75, v48, v46
	v_pack_b32_f16 v46, v87, v66
	v_pk_mul_f16 v74, v49, v46
	s_waitcnt vmcnt(6)
	v_pk_mul_f16 v49, v160, v153 op_sel_hi:[0,1]
	v_pk_mul_f16 v46, v160, v150 op_sel_hi:[0,1]
	v_pk_mul_f16 v47, v160, v151 op_sel_hi:[0,1]
	v_pk_mul_f16 v48, v160, v152 op_sel_hi:[0,1]
	v_pk_mul_f16 v69, v158, v153 op_sel_hi:[0,1]
	v_pk_mul_f16 v89, v159, v153 op_sel_hi:[0,1]
	v_pk_fma_f16 v57, v57, v153, v49
	v_pk_fma_f16 v73, v73, v153, v49
	v_pk_fma_f16 v49, v97, v153, v49
	v_pk_mul_f16 v66, v158, v150 op_sel_hi:[0,1]
	v_pk_maximum3_f16 v117, v57, v73, v49
	v_pk_mul_f16 v67, v158, v151 op_sel_hi:[0,1]
	v_pk_mul_f16 v68, v158, v152 op_sel_hi:[0,1]
	v_pk_mul_f16 v86, v159, v150 op_sel_hi:[0,1]
	v_pk_mul_f16 v87, v159, v151 op_sel_hi:[0,1]
	v_pk_mul_f16 v88, v159, v152 op_sel_hi:[0,1]
	v_pk_fma_f16 v56, v56, v152, v48
	v_pk_fma_f16 v55, v55, v151, v47
	v_pk_fma_f16 v54, v54, v150, v46
	v_pk_fma_f16 v72, v72, v152, v48
	v_pk_fma_f16 v71, v71, v151, v47
	v_pk_fma_f16 v70, v70, v150, v46
	v_pk_fma_f16 v48, v96, v152, v48
	v_pk_fma_f16 v47, v95, v151, v47
	v_pk_fma_f16 v46, v94, v150, v46
	v_pk_fma_f16 v90, v29, v153, v69
	v_pk_fma_f16 v94, v41, v153, v69
	v_pk_fma_f16 v69, v61, v153, v69
	v_pk_fma_f16 v98, v81, v153, v89
	v_pk_fma_f16 v110, v109, v153, v89
	v_pk_fma_f16 v89, v125, v153, v89
	v_pk_maximum3_f16 v114, v54, v70, v46
	v_pk_maximum3_f16 v115, v55, v71, v47
	v_pk_maximum3_f16 v116, v56, v72, v48
	v_pk_maximum3_f16 v121, v90, v94, v69
	v_pk_fma_f16 v91, v28, v152, v68
	v_pk_maximum3_f16 v129, v98, v110, v89
	v_pk_fma_f16 v92, v27, v151, v67
	v_pk_maximum3_f16 v117, v117, v121, v129
	v_pk_fma_f16 v93, v26, v150, v66
	v_pk_fma_f16 v95, v40, v152, v68
	v_pk_fma_f16 v96, v39, v151, v67
	v_pk_fma_f16 v97, v38, v150, v66
	v_pk_fma_f16 v68, v60, v152, v68
	v_pk_fma_f16 v67, v59, v151, v67
	v_pk_fma_f16 v66, v58, v150, v66
	v_pk_fma_f16 v99, v80, v152, v88
	v_pk_fma_f16 v100, v79, v151, v87
	v_pk_fma_f16 v101, v78, v150, v86
	v_pk_fma_f16 v111, v108, v152, v88
	v_pk_fma_f16 v112, v107, v151, v87
	v_pk_fma_f16 v113, v106, v150, v86
	v_pk_fma_f16 v88, v124, v152, v88
	v_pk_fma_f16 v87, v123, v151, v87
	v_pk_fma_f16 v86, v122, v150, v86
	v_pk_maximum3_f16 v118, v93, v97, v66
	v_pk_maximum3_f16 v119, v92, v96, v67
	v_pk_maximum3_f16 v120, v91, v95, v68
	v_pk_maximum3_f16 v127, v100, v112, v87
	v_pk_maximum3_f16 v128, v99, v111, v88
	v_pk_maximum3_f16 v126, v101, v113, v86
	v_pk_maximum3_f16 v114, v114, v118, v126
	v_pk_maximum3_f16 v115, v115, v119, v127
	v_pk_maximum3_f16 v116, v116, v120, v128
	v_pk_add_f16 v57, v57, v117 neg_lo:[0,1] neg_hi:[0,1]
	v_pk_add_f16 v54, v54, v114 neg_lo:[0,1] neg_hi:[0,1]
	v_pk_add_f16 v55, v55, v115 neg_lo:[0,1] neg_hi:[0,1]
	v_pk_add_f16 v56, v56, v116 neg_lo:[0,1] neg_hi:[0,1]
	v_pk_add_f16 v70, v70, v114 neg_lo:[0,1] neg_hi:[0,1]
	v_exp_f16_sdwa v118, v54 dst_sel:WORD_0 dst_unused:UNUSED_PAD src0_sel:WORD_0
	v_exp_f16_sdwa v119, v55 dst_sel:WORD_0 dst_unused:UNUSED_PAD src0_sel:WORD_0
	v_exp_f16_sdwa v120, v56 dst_sel:WORD_0 dst_unused:UNUSED_PAD src0_sel:WORD_0
	v_exp_f16_sdwa v121, v57 dst_sel:WORD_0 dst_unused:UNUSED_PAD src0_sel:WORD_0
	v_exp_f16_sdwa v118, v54 dst_sel:WORD_1 dst_unused:UNUSED_PRESERVE src0_sel:WORD_1
	v_exp_f16_sdwa v119, v55 dst_sel:WORD_1 dst_unused:UNUSED_PRESERVE src0_sel:WORD_1
	v_exp_f16_sdwa v120, v56 dst_sel:WORD_1 dst_unused:UNUSED_PRESERVE src0_sel:WORD_1
	v_exp_f16_sdwa v121, v57 dst_sel:WORD_1 dst_unused:UNUSED_PRESERVE src0_sel:WORD_1
	v_pk_add_f16 v71, v71, v115 neg_lo:[0,1] neg_hi:[0,1]
	v_pk_add_f16 v57, v118, 0
	v_pk_fma_f16 v25, v25, v121, 0
	v_pk_add_f16 v54, v121, 0
	v_pk_add_f16 v55, v120, 0
	v_pk_add_f16 v56, v119, 0
	v_pk_fma_f16 v24, v24, v120, 0
	v_pk_fma_f16 v23, v23, v119, 0
	v_pk_fma_f16 v22, v22, v118, 0
	v_pk_add_f16 v72, v72, v116 neg_lo:[0,1] neg_hi:[0,1]
	v_pk_add_f16 v73, v73, v117 neg_lo:[0,1] neg_hi:[0,1]
	v_exp_f16_sdwa v118, v70 dst_sel:WORD_0 dst_unused:UNUSED_PAD src0_sel:WORD_0
	v_exp_f16_sdwa v119, v71 dst_sel:WORD_0 dst_unused:UNUSED_PAD src0_sel:WORD_0
	v_exp_f16_sdwa v120, v72 dst_sel:WORD_0 dst_unused:UNUSED_PAD src0_sel:WORD_0
	v_exp_f16_sdwa v121, v73 dst_sel:WORD_0 dst_unused:UNUSED_PAD src0_sel:WORD_0
	v_exp_f16_sdwa v118, v70 dst_sel:WORD_1 dst_unused:UNUSED_PRESERVE src0_sel:WORD_1
	v_exp_f16_sdwa v119, v71 dst_sel:WORD_1 dst_unused:UNUSED_PRESERVE src0_sel:WORD_1
	v_exp_f16_sdwa v120, v72 dst_sel:WORD_1 dst_unused:UNUSED_PRESERVE src0_sel:WORD_1
	v_exp_f16_sdwa v121, v73 dst_sel:WORD_1 dst_unused:UNUSED_PRESERVE src0_sel:WORD_1
	v_pk_add_f16 v57, v57, v118
	v_pk_fma_f16 v25, v37, v121, v25
	v_pk_add_f16 v37, v49, v117 neg_lo:[0,1] neg_hi:[0,1]
	v_pk_add_f16 v56, v56, v119
	v_pk_add_f16 v55, v55, v120
	v_pk_add_f16 v54, v54, v121
	v_pk_fma_f16 v22, v34, v118, v22
	v_pk_fma_f16 v23, v35, v119, v23
	v_pk_fma_f16 v24, v36, v120, v24
	v_pk_add_f16 v34, v46, v114 neg_lo:[0,1] neg_hi:[0,1]
	v_pk_add_f16 v35, v47, v115 neg_lo:[0,1] neg_hi:[0,1]
	v_pk_add_f16 v36, v48, v116 neg_lo:[0,1] neg_hi:[0,1]
	v_exp_f16_sdwa v46, v34 dst_sel:WORD_0 dst_unused:UNUSED_PAD src0_sel:WORD_0
	v_exp_f16_sdwa v47, v35 dst_sel:WORD_0 dst_unused:UNUSED_PAD src0_sel:WORD_0
	v_exp_f16_sdwa v48, v36 dst_sel:WORD_0 dst_unused:UNUSED_PAD src0_sel:WORD_0
	v_exp_f16_sdwa v49, v37 dst_sel:WORD_0 dst_unused:UNUSED_PAD src0_sel:WORD_0
	v_exp_f16_sdwa v46, v34 dst_sel:WORD_1 dst_unused:UNUSED_PRESERVE src0_sel:WORD_1
	v_exp_f16_sdwa v47, v35 dst_sel:WORD_1 dst_unused:UNUSED_PRESERVE src0_sel:WORD_1
	v_exp_f16_sdwa v48, v36 dst_sel:WORD_1 dst_unused:UNUSED_PRESERVE src0_sel:WORD_1
	v_exp_f16_sdwa v49, v37 dst_sel:WORD_1 dst_unused:UNUSED_PRESERVE src0_sel:WORD_1
	v_pk_add_f16 v37, v57, v46
	v_pk_add_f16 v34, v54, v49
	v_pk_add_f16 v35, v55, v48
	v_pk_add_f16 v36, v56, v47
	v_pk_fma_f16 v25, v53, v49, v25
	v_pk_fma_f16 v24, v52, v48, v24
	v_pk_fma_f16 v23, v51, v47, v23
	v_pk_fma_f16 v22, v50, v46, v22
	v_pk_add_f16 v46, v93, v114 neg_lo:[0,1] neg_hi:[0,1]
	v_pk_add_f16 v47, v92, v115 neg_lo:[0,1] neg_hi:[0,1]
	v_pk_add_f16 v48, v91, v116 neg_lo:[0,1] neg_hi:[0,1]
	v_pk_add_f16 v49, v90, v117 neg_lo:[0,1] neg_hi:[0,1]
	v_exp_f16_sdwa v50, v46 dst_sel:WORD_0 dst_unused:UNUSED_PAD src0_sel:WORD_0
	v_exp_f16_sdwa v51, v47 dst_sel:WORD_0 dst_unused:UNUSED_PAD src0_sel:WORD_0
	v_exp_f16_sdwa v52, v48 dst_sel:WORD_0 dst_unused:UNUSED_PAD src0_sel:WORD_0
	v_exp_f16_sdwa v53, v49 dst_sel:WORD_0 dst_unused:UNUSED_PAD src0_sel:WORD_0
	v_exp_f16_sdwa v50, v46 dst_sel:WORD_1 dst_unused:UNUSED_PRESERVE src0_sel:WORD_1
	v_exp_f16_sdwa v51, v47 dst_sel:WORD_1 dst_unused:UNUSED_PRESERVE src0_sel:WORD_1
	v_exp_f16_sdwa v52, v48 dst_sel:WORD_1 dst_unused:UNUSED_PRESERVE src0_sel:WORD_1
	v_exp_f16_sdwa v53, v49 dst_sel:WORD_1 dst_unused:UNUSED_PRESERVE src0_sel:WORD_1
	v_pk_add_f16 v46, v97, v114 neg_lo:[0,1] neg_hi:[0,1]
	v_pk_add_f16 v37, v37, v50
	v_pk_add_f16 v36, v36, v51
	v_pk_add_f16 v35, v35, v52
	v_pk_add_f16 v34, v34, v53
	v_pk_fma_f16 v22, v10, v50, v22
	v_pk_fma_f16 v23, v11, v51, v23
	v_pk_fma_f16 v24, v12, v52, v24
	v_pk_fma_f16 v25, v13, v53, v25
	v_pk_add_f16 v47, v96, v115 neg_lo:[0,1] neg_hi:[0,1]
	v_pk_add_f16 v48, v95, v116 neg_lo:[0,1] neg_hi:[0,1]
	v_pk_add_f16 v49, v94, v117 neg_lo:[0,1] neg_hi:[0,1]
	v_exp_f16_sdwa v50, v46 dst_sel:WORD_0 dst_unused:UNUSED_PAD src0_sel:WORD_0
	v_exp_f16_sdwa v51, v47 dst_sel:WORD_0 dst_unused:UNUSED_PAD src0_sel:WORD_0
	v_exp_f16_sdwa v52, v48 dst_sel:WORD_0 dst_unused:UNUSED_PAD src0_sel:WORD_0
	v_exp_f16_sdwa v53, v49 dst_sel:WORD_0 dst_unused:UNUSED_PAD src0_sel:WORD_0
	v_exp_f16_sdwa v50, v46 dst_sel:WORD_1 dst_unused:UNUSED_PRESERVE src0_sel:WORD_1
	v_exp_f16_sdwa v51, v47 dst_sel:WORD_1 dst_unused:UNUSED_PRESERVE src0_sel:WORD_1
	v_exp_f16_sdwa v52, v48 dst_sel:WORD_1 dst_unused:UNUSED_PRESERVE src0_sel:WORD_1
	v_exp_f16_sdwa v53, v49 dst_sel:WORD_1 dst_unused:UNUSED_PRESERVE src0_sel:WORD_1
	v_pk_add_f16 v46, v66, v114 neg_lo:[0,1] neg_hi:[0,1]
	v_pk_add_f16 v37, v37, v50
	v_pk_add_f16 v34, v34, v53
	v_pk_add_f16 v35, v35, v52
	v_pk_add_f16 v36, v36, v51
	v_pk_fma_f16 v25, v17, v53, v25
	v_pk_fma_f16 v24, v16, v52, v24
	v_pk_fma_f16 v23, v15, v51, v23
	v_pk_fma_f16 v22, v14, v50, v22
	v_pk_add_f16 v47, v67, v115 neg_lo:[0,1] neg_hi:[0,1]
	v_pk_add_f16 v48, v68, v116 neg_lo:[0,1] neg_hi:[0,1]
	v_pk_add_f16 v49, v69, v117 neg_lo:[0,1] neg_hi:[0,1]
	v_exp_f16_sdwa v50, v46 dst_sel:WORD_0 dst_unused:UNUSED_PAD src0_sel:WORD_0
	v_exp_f16_sdwa v51, v47 dst_sel:WORD_0 dst_unused:UNUSED_PAD src0_sel:WORD_0
	v_exp_f16_sdwa v52, v48 dst_sel:WORD_0 dst_unused:UNUSED_PAD src0_sel:WORD_0
	v_exp_f16_sdwa v53, v49 dst_sel:WORD_0 dst_unused:UNUSED_PAD src0_sel:WORD_0
	v_exp_f16_sdwa v50, v46 dst_sel:WORD_1 dst_unused:UNUSED_PRESERVE src0_sel:WORD_1
	v_exp_f16_sdwa v51, v47 dst_sel:WORD_1 dst_unused:UNUSED_PRESERVE src0_sel:WORD_1
	v_exp_f16_sdwa v52, v48 dst_sel:WORD_1 dst_unused:UNUSED_PRESERVE src0_sel:WORD_1
	v_exp_f16_sdwa v53, v49 dst_sel:WORD_1 dst_unused:UNUSED_PRESERVE src0_sel:WORD_1
	v_pk_add_f16 v46, v101, v114 neg_lo:[0,1] neg_hi:[0,1]
	v_pk_add_f16 v37, v37, v50
	v_pk_add_f16 v36, v36, v51
	v_pk_add_f16 v35, v35, v52
	v_pk_add_f16 v34, v34, v53
	v_pk_fma_f16 v22, v18, v50, v22
	v_pk_fma_f16 v23, v19, v51, v23
	v_pk_fma_f16 v24, v20, v52, v24
	v_pk_fma_f16 v25, v21, v53, v25
	v_pk_add_f16 v47, v100, v115 neg_lo:[0,1] neg_hi:[0,1]
	v_pk_add_f16 v48, v99, v116 neg_lo:[0,1] neg_hi:[0,1]
	v_pk_add_f16 v49, v98, v117 neg_lo:[0,1] neg_hi:[0,1]
	v_exp_f16_sdwa v50, v46 dst_sel:WORD_0 dst_unused:UNUSED_PAD src0_sel:WORD_0
	v_exp_f16_sdwa v51, v47 dst_sel:WORD_0 dst_unused:UNUSED_PAD src0_sel:WORD_0
	v_exp_f16_sdwa v52, v48 dst_sel:WORD_0 dst_unused:UNUSED_PAD src0_sel:WORD_0
	v_exp_f16_sdwa v53, v49 dst_sel:WORD_0 dst_unused:UNUSED_PAD src0_sel:WORD_0
	v_exp_f16_sdwa v50, v46 dst_sel:WORD_1 dst_unused:UNUSED_PRESERVE src0_sel:WORD_1
	v_exp_f16_sdwa v51, v47 dst_sel:WORD_1 dst_unused:UNUSED_PRESERVE src0_sel:WORD_1
	v_exp_f16_sdwa v52, v48 dst_sel:WORD_1 dst_unused:UNUSED_PRESERVE src0_sel:WORD_1
	v_exp_f16_sdwa v53, v49 dst_sel:WORD_1 dst_unused:UNUSED_PRESERVE src0_sel:WORD_1
	v_pk_add_f16 v46, v113, v114 neg_lo:[0,1] neg_hi:[0,1]
	v_pk_add_f16 v37, v37, v50
	v_pk_add_f16 v34, v34, v53
	v_pk_add_f16 v35, v35, v52
	v_pk_add_f16 v36, v36, v51
	v_pk_fma_f16 v25, v33, v53, v25
	v_pk_fma_f16 v24, v32, v52, v24
	v_pk_fma_f16 v23, v31, v51, v23
	v_pk_fma_f16 v22, v30, v50, v22
	v_pk_add_f16 v47, v112, v115 neg_lo:[0,1] neg_hi:[0,1]
	v_pk_add_f16 v48, v111, v116 neg_lo:[0,1] neg_hi:[0,1]
	v_pk_add_f16 v49, v110, v117 neg_lo:[0,1] neg_hi:[0,1]
	v_exp_f16_sdwa v50, v46 dst_sel:WORD_0 dst_unused:UNUSED_PAD src0_sel:WORD_0
	v_exp_f16_sdwa v51, v47 dst_sel:WORD_0 dst_unused:UNUSED_PAD src0_sel:WORD_0
	v_exp_f16_sdwa v52, v48 dst_sel:WORD_0 dst_unused:UNUSED_PAD src0_sel:WORD_0
	v_exp_f16_sdwa v53, v49 dst_sel:WORD_0 dst_unused:UNUSED_PAD src0_sel:WORD_0
	v_exp_f16_sdwa v50, v46 dst_sel:WORD_1 dst_unused:UNUSED_PRESERVE src0_sel:WORD_1
	v_exp_f16_sdwa v51, v47 dst_sel:WORD_1 dst_unused:UNUSED_PRESERVE src0_sel:WORD_1
	v_exp_f16_sdwa v52, v48 dst_sel:WORD_1 dst_unused:UNUSED_PRESERVE src0_sel:WORD_1
	v_exp_f16_sdwa v53, v49 dst_sel:WORD_1 dst_unused:UNUSED_PRESERVE src0_sel:WORD_1
	v_pk_add_f16 v46, v86, v114 neg_lo:[0,1] neg_hi:[0,1]
	v_pk_add_f16 v37, v37, v50
	v_pk_add_f16 v36, v36, v51
	v_pk_add_f16 v35, v35, v52
	v_pk_add_f16 v34, v34, v53
	v_pk_fma_f16 v22, v42, v50, v22
	v_pk_fma_f16 v23, v43, v51, v23
	v_pk_fma_f16 v24, v44, v52, v24
	v_pk_fma_f16 v25, v45, v53, v25
	v_pk_add_f16 v47, v87, v115 neg_lo:[0,1] neg_hi:[0,1]
	v_pk_add_f16 v48, v88, v116 neg_lo:[0,1] neg_hi:[0,1]
	v_pk_add_f16 v49, v89, v117 neg_lo:[0,1] neg_hi:[0,1]
	v_exp_f16_sdwa v50, v46 dst_sel:WORD_0 dst_unused:UNUSED_PAD src0_sel:WORD_0
	v_exp_f16_sdwa v51, v47 dst_sel:WORD_0 dst_unused:UNUSED_PAD src0_sel:WORD_0
	v_exp_f16_sdwa v52, v48 dst_sel:WORD_0 dst_unused:UNUSED_PAD src0_sel:WORD_0
	v_exp_f16_sdwa v53, v49 dst_sel:WORD_0 dst_unused:UNUSED_PAD src0_sel:WORD_0
	v_exp_f16_sdwa v50, v46 dst_sel:WORD_1 dst_unused:UNUSED_PRESERVE src0_sel:WORD_1
	v_exp_f16_sdwa v51, v47 dst_sel:WORD_1 dst_unused:UNUSED_PRESERVE src0_sel:WORD_1
	v_exp_f16_sdwa v52, v48 dst_sel:WORD_1 dst_unused:UNUSED_PRESERVE src0_sel:WORD_1
	v_exp_f16_sdwa v53, v49 dst_sel:WORD_1 dst_unused:UNUSED_PRESERVE src0_sel:WORD_1
	v_pk_add_f16 v37, v37, v50
	v_pk_add_f16 v36, v36, v51
	v_rcp_f16_e32 v46, v37
	v_rcp_f16_sdwa v37, v37 dst_sel:DWORD dst_unused:UNUSED_PAD src0_sel:WORD_1
	v_pk_add_f16 v35, v35, v52
	v_rcp_f16_e32 v47, v36
	v_rcp_f16_sdwa v36, v36 dst_sel:DWORD dst_unused:UNUSED_PAD src0_sel:WORD_1
	v_pk_add_f16 v34, v34, v53
	v_rcp_f16_e32 v48, v35
	v_rcp_f16_sdwa v35, v35 dst_sel:DWORD dst_unused:UNUSED_PAD src0_sel:WORD_1
	v_rcp_f16_e32 v49, v34
	v_rcp_f16_sdwa v34, v34 dst_sel:DWORD dst_unused:UNUSED_PAD src0_sel:WORD_1
	v_pk_fma_f16 v22, v62, v50, v22
	v_pack_b32_f16 v37, v46, v37
	v_pk_fma_f16 v23, v63, v51, v23
	v_pk_mul_f16 v57, v22, v37
	v_pack_b32_f16 v22, v47, v36
	v_pk_fma_f16 v24, v64, v52, v24
	v_pk_mul_f16 v56, v23, v22
	v_pack_b32_f16 v22, v48, v35
	v_pk_fma_f16 v25, v65, v53, v25
	v_pk_mul_f16 v55, v24, v22
	v_pack_b32_f16 v22, v49, v34
	v_pk_mul_f16 v54, v25, v22
	s_waitcnt vmcnt(0)
	v_pk_mul_f16 v22, v160, v146 op_sel_hi:[0,1]
	v_pk_mul_f16 v23, v160, v147 op_sel_hi:[0,1]
	v_pk_mul_f16 v24, v160, v148 op_sel_hi:[0,1]
	v_pk_mul_f16 v25, v160, v149 op_sel_hi:[0,1]
	v_pk_mul_f16 v46, v159, v146 op_sel_hi:[0,1]
	v_pk_mul_f16 v47, v159, v147 op_sel_hi:[0,1]
	v_pk_mul_f16 v48, v159, v148 op_sel_hi:[0,1]
	v_pk_mul_f16 v49, v159, v149 op_sel_hi:[0,1]
	v_pk_mul_f16 v34, v158, v146 op_sel_hi:[0,1]
	v_pk_mul_f16 v35, v158, v147 op_sel_hi:[0,1]
	v_pk_mul_f16 v36, v158, v148 op_sel_hi:[0,1]
	v_pk_mul_f16 v37, v158, v149 op_sel_hi:[0,1]
	v_pk_fma_f16 v29, v29, v149, v25
	v_pk_fma_f16 v28, v28, v148, v24
	v_pk_fma_f16 v27, v27, v147, v23
	v_pk_fma_f16 v26, v26, v146, v22
	v_pk_fma_f16 v41, v41, v149, v25
	v_pk_fma_f16 v40, v40, v148, v24
	v_pk_fma_f16 v39, v39, v147, v23
	v_pk_fma_f16 v38, v38, v146, v22
	v_pk_fma_f16 v25, v61, v149, v25
	v_pk_fma_f16 v24, v60, v148, v24
	v_pk_fma_f16 v23, v59, v147, v23
	v_pk_fma_f16 v22, v58, v146, v22
	v_pk_fma_f16 v66, v137, v149, v49
	v_pk_fma_f16 v67, v136, v148, v48
	v_pk_fma_f16 v68, v135, v147, v47
	v_pk_fma_f16 v69, v134, v146, v46
	v_pk_fma_f16 v70, v145, v149, v49
	v_pk_fma_f16 v71, v144, v148, v48
	v_pk_fma_f16 v72, v143, v147, v47
	v_pk_fma_f16 v73, v142, v146, v46
	v_pk_fma_f16 v9, v9, v149, v49
	v_pk_fma_f16 v8, v8, v148, v48
	v_pk_fma_f16 v7, v7, v147, v47
	v_pk_fma_f16 v6, v6, v146, v46
	v_pk_maximum3_f16 v46, v26, v38, v22
	v_pk_maximum3_f16 v47, v27, v39, v23
	v_pk_maximum3_f16 v48, v28, v40, v24
	v_pk_maximum3_f16 v49, v29, v41, v25
	v_pk_fma_f16 v50, v81, v149, v37
	v_pk_fma_f16 v51, v80, v148, v36
	v_pk_fma_f16 v52, v79, v147, v35
	v_pk_fma_f16 v53, v78, v146, v34
	v_pk_fma_f16 v58, v109, v149, v37
	v_pk_fma_f16 v59, v108, v148, v36
	v_pk_fma_f16 v60, v107, v147, v35
	v_pk_fma_f16 v61, v106, v146, v34
	v_pk_fma_f16 v37, v125, v149, v37
	v_pk_fma_f16 v36, v124, v148, v36
	v_pk_fma_f16 v35, v123, v147, v35
	v_pk_fma_f16 v34, v122, v146, v34
	v_pk_maximum3_f16 v79, v52, v60, v35
	v_pk_maximum3_f16 v80, v51, v59, v36
	v_pk_maximum3_f16 v81, v50, v58, v37
	v_pk_maximum3_f16 v86, v69, v73, v6
	v_pk_maximum3_f16 v87, v68, v72, v7
	v_pk_maximum3_f16 v78, v53, v61, v34
	v_pk_maximum3_f16 v88, v67, v71, v8
	v_pk_maximum3_f16 v89, v66, v70, v9
	v_pk_maximum3_f16 v46, v46, v78, v86
	v_pk_maximum3_f16 v47, v47, v79, v87
	v_pk_maximum3_f16 v48, v48, v80, v88
	v_pk_maximum3_f16 v49, v49, v81, v89
	s_nop 0
	v_pk_add_f16 v26, v26, v46 neg_lo:[0,1] neg_hi:[0,1]
	v_pk_add_f16 v27, v27, v47 neg_lo:[0,1] neg_hi:[0,1]
	v_pk_add_f16 v28, v28, v48 neg_lo:[0,1] neg_hi:[0,1]
	v_pk_add_f16 v29, v29, v49 neg_lo:[0,1] neg_hi:[0,1]
	v_pk_add_f16 v38, v38, v46 neg_lo:[0,1] neg_hi:[0,1]
	v_exp_f16_sdwa v78, v26 dst_sel:WORD_0 dst_unused:UNUSED_PAD src0_sel:WORD_0
	v_exp_f16_sdwa v79, v27 dst_sel:WORD_0 dst_unused:UNUSED_PAD src0_sel:WORD_0
	v_exp_f16_sdwa v80, v28 dst_sel:WORD_0 dst_unused:UNUSED_PAD src0_sel:WORD_0
	v_exp_f16_sdwa v81, v29 dst_sel:WORD_0 dst_unused:UNUSED_PAD src0_sel:WORD_0
	v_exp_f16_sdwa v78, v26 dst_sel:WORD_1 dst_unused:UNUSED_PRESERVE src0_sel:WORD_1
	v_exp_f16_sdwa v79, v27 dst_sel:WORD_1 dst_unused:UNUSED_PRESERVE src0_sel:WORD_1
	v_exp_f16_sdwa v80, v28 dst_sel:WORD_1 dst_unused:UNUSED_PRESERVE src0_sel:WORD_1
	v_exp_f16_sdwa v81, v29 dst_sel:WORD_1 dst_unused:UNUSED_PRESERVE src0_sel:WORD_1
	v_pk_add_f16 v39, v39, v47 neg_lo:[0,1] neg_hi:[0,1]
	v_pk_add_f16 v26, v78, 0
	v_pk_add_f16 v27, v79, 0
	v_pk_add_f16 v28, v80, 0
	v_pk_add_f16 v29, v81, 0
	v_pk_fma_f16 v10, v10, v78, 0
	v_pk_fma_f16 v11, v11, v79, 0
	v_pk_fma_f16 v12, v12, v80, 0
	v_pk_fma_f16 v13, v13, v81, 0
	v_pk_add_f16 v40, v40, v48 neg_lo:[0,1] neg_hi:[0,1]
	v_pk_add_f16 v41, v41, v49 neg_lo:[0,1] neg_hi:[0,1]
	v_pk_add_f16 v6, v6, v46 neg_lo:[0,1] neg_hi:[0,1]
	v_exp_f16_sdwa v78, v38 dst_sel:WORD_0 dst_unused:UNUSED_PAD src0_sel:WORD_0
	v_exp_f16_sdwa v79, v39 dst_sel:WORD_0 dst_unused:UNUSED_PAD src0_sel:WORD_0
	v_exp_f16_sdwa v80, v40 dst_sel:WORD_0 dst_unused:UNUSED_PAD src0_sel:WORD_0
	v_exp_f16_sdwa v81, v41 dst_sel:WORD_0 dst_unused:UNUSED_PAD src0_sel:WORD_0
	v_exp_f16_sdwa v78, v38 dst_sel:WORD_1 dst_unused:UNUSED_PRESERVE src0_sel:WORD_1
	v_exp_f16_sdwa v79, v39 dst_sel:WORD_1 dst_unused:UNUSED_PRESERVE src0_sel:WORD_1
	v_exp_f16_sdwa v80, v40 dst_sel:WORD_1 dst_unused:UNUSED_PRESERVE src0_sel:WORD_1
	v_exp_f16_sdwa v81, v41 dst_sel:WORD_1 dst_unused:UNUSED_PRESERVE src0_sel:WORD_1
	v_pk_add_f16 v7, v7, v47 neg_lo:[0,1] neg_hi:[0,1]
	v_pk_add_f16 v29, v29, v81
	v_pk_add_f16 v28, v28, v80
	v_pk_add_f16 v27, v27, v79
	v_pk_add_f16 v26, v26, v78
	v_pk_fma_f16 v13, v17, v81, v13
	v_pk_fma_f16 v12, v16, v80, v12
	v_pk_fma_f16 v11, v15, v79, v11
	v_pk_fma_f16 v10, v14, v78, v10
	v_pk_add_f16 v14, v22, v46 neg_lo:[0,1] neg_hi:[0,1]
	v_pk_add_f16 v15, v23, v47 neg_lo:[0,1] neg_hi:[0,1]
	v_pk_add_f16 v16, v24, v48 neg_lo:[0,1] neg_hi:[0,1]
	v_pk_add_f16 v17, v25, v49 neg_lo:[0,1] neg_hi:[0,1]
	v_pk_add_f16 v8, v8, v48 neg_lo:[0,1] neg_hi:[0,1]
	v_exp_f16_sdwa v22, v14 dst_sel:WORD_0 dst_unused:UNUSED_PAD src0_sel:WORD_0
	v_exp_f16_sdwa v23, v15 dst_sel:WORD_0 dst_unused:UNUSED_PAD src0_sel:WORD_0
	v_exp_f16_sdwa v24, v16 dst_sel:WORD_0 dst_unused:UNUSED_PAD src0_sel:WORD_0
	v_exp_f16_sdwa v25, v17 dst_sel:WORD_0 dst_unused:UNUSED_PAD src0_sel:WORD_0
	v_exp_f16_sdwa v22, v14 dst_sel:WORD_1 dst_unused:UNUSED_PRESERVE src0_sel:WORD_1
	v_exp_f16_sdwa v23, v15 dst_sel:WORD_1 dst_unused:UNUSED_PRESERVE src0_sel:WORD_1
	v_exp_f16_sdwa v24, v16 dst_sel:WORD_1 dst_unused:UNUSED_PRESERVE src0_sel:WORD_1
	v_exp_f16_sdwa v25, v17 dst_sel:WORD_1 dst_unused:UNUSED_PRESERVE src0_sel:WORD_1
	v_pk_add_f16 v9, v9, v49 neg_lo:[0,1] neg_hi:[0,1]
	v_pk_add_f16 v14, v26, v22
	v_pk_add_f16 v15, v27, v23
	v_pk_add_f16 v16, v28, v24
	v_pk_add_f16 v17, v29, v25
	v_pk_fma_f16 v10, v18, v22, v10
	v_pk_fma_f16 v11, v19, v23, v11
	v_pk_fma_f16 v12, v20, v24, v12
	v_pk_fma_f16 v13, v21, v25, v13
	v_pk_add_f16 v18, v53, v46 neg_lo:[0,1] neg_hi:[0,1]
	v_pk_add_f16 v19, v52, v47 neg_lo:[0,1] neg_hi:[0,1]
	v_pk_add_f16 v20, v51, v48 neg_lo:[0,1] neg_hi:[0,1]
	v_pk_add_f16 v21, v50, v49 neg_lo:[0,1] neg_hi:[0,1]
	v_exp_f16_sdwa v22, v18 dst_sel:WORD_0 dst_unused:UNUSED_PAD src0_sel:WORD_0
	v_exp_f16_sdwa v23, v19 dst_sel:WORD_0 dst_unused:UNUSED_PAD src0_sel:WORD_0
	v_exp_f16_sdwa v24, v20 dst_sel:WORD_0 dst_unused:UNUSED_PAD src0_sel:WORD_0
	v_exp_f16_sdwa v25, v21 dst_sel:WORD_0 dst_unused:UNUSED_PAD src0_sel:WORD_0
	v_exp_f16_sdwa v22, v18 dst_sel:WORD_1 dst_unused:UNUSED_PRESERVE src0_sel:WORD_1
	v_exp_f16_sdwa v23, v19 dst_sel:WORD_1 dst_unused:UNUSED_PRESERVE src0_sel:WORD_1
	v_exp_f16_sdwa v24, v20 dst_sel:WORD_1 dst_unused:UNUSED_PRESERVE src0_sel:WORD_1
	v_exp_f16_sdwa v25, v21 dst_sel:WORD_1 dst_unused:UNUSED_PRESERVE src0_sel:WORD_1
	v_pk_add_f16 v18, v61, v46 neg_lo:[0,1] neg_hi:[0,1]
	v_pk_add_f16 v17, v17, v25
	v_pk_add_f16 v16, v16, v24
	v_pk_add_f16 v15, v15, v23
	v_pk_add_f16 v14, v14, v22
	v_pk_fma_f16 v13, v33, v25, v13
	v_pk_fma_f16 v12, v32, v24, v12
	v_pk_fma_f16 v11, v31, v23, v11
	v_pk_fma_f16 v10, v30, v22, v10
	v_pk_add_f16 v19, v60, v47 neg_lo:[0,1] neg_hi:[0,1]
	v_pk_add_f16 v20, v59, v48 neg_lo:[0,1] neg_hi:[0,1]
	v_pk_add_f16 v21, v58, v49 neg_lo:[0,1] neg_hi:[0,1]
	v_exp_f16_sdwa v30, v6 dst_sel:WORD_0 dst_unused:UNUSED_PAD src0_sel:WORD_0
	v_exp_f16_sdwa v31, v7 dst_sel:WORD_0 dst_unused:UNUSED_PAD src0_sel:WORD_0
	v_exp_f16_sdwa v32, v8 dst_sel:WORD_0 dst_unused:UNUSED_PAD src0_sel:WORD_0
	v_exp_f16_sdwa v33, v9 dst_sel:WORD_0 dst_unused:UNUSED_PAD src0_sel:WORD_0
	v_exp_f16_sdwa v30, v6 dst_sel:WORD_1 dst_unused:UNUSED_PRESERVE src0_sel:WORD_1
	v_exp_f16_sdwa v31, v7 dst_sel:WORD_1 dst_unused:UNUSED_PRESERVE src0_sel:WORD_1
	v_exp_f16_sdwa v32, v8 dst_sel:WORD_1 dst_unused:UNUSED_PRESERVE src0_sel:WORD_1
	v_exp_f16_sdwa v33, v9 dst_sel:WORD_1 dst_unused:UNUSED_PRESERVE src0_sel:WORD_1
	v_exp_f16_sdwa v22, v18 dst_sel:WORD_0 dst_unused:UNUSED_PAD src0_sel:WORD_0
	v_exp_f16_sdwa v23, v19 dst_sel:WORD_0 dst_unused:UNUSED_PAD src0_sel:WORD_0
	v_exp_f16_sdwa v24, v20 dst_sel:WORD_0 dst_unused:UNUSED_PAD src0_sel:WORD_0
	v_exp_f16_sdwa v25, v21 dst_sel:WORD_0 dst_unused:UNUSED_PAD src0_sel:WORD_0
	v_exp_f16_sdwa v22, v18 dst_sel:WORD_1 dst_unused:UNUSED_PRESERVE src0_sel:WORD_1
	v_exp_f16_sdwa v23, v19 dst_sel:WORD_1 dst_unused:UNUSED_PRESERVE src0_sel:WORD_1
	v_exp_f16_sdwa v24, v20 dst_sel:WORD_1 dst_unused:UNUSED_PRESERVE src0_sel:WORD_1
	v_exp_f16_sdwa v25, v21 dst_sel:WORD_1 dst_unused:UNUSED_PRESERVE src0_sel:WORD_1
	v_pk_add_f16 v18, v34, v46 neg_lo:[0,1] neg_hi:[0,1]
	v_pk_add_f16 v14, v14, v22
	v_pk_add_f16 v15, v15, v23
	v_pk_add_f16 v16, v16, v24
	v_pk_add_f16 v17, v17, v25
	v_pk_fma_f16 v10, v42, v22, v10
	v_pk_fma_f16 v11, v43, v23, v11
	v_pk_fma_f16 v12, v44, v24, v12
	v_pk_fma_f16 v13, v45, v25, v13
	v_pk_add_f16 v19, v35, v47 neg_lo:[0,1] neg_hi:[0,1]
	v_pk_add_f16 v20, v36, v48 neg_lo:[0,1] neg_hi:[0,1]
	v_pk_add_f16 v21, v37, v49 neg_lo:[0,1] neg_hi:[0,1]
	v_exp_f16_sdwa v22, v18 dst_sel:WORD_0 dst_unused:UNUSED_PAD src0_sel:WORD_0
	v_exp_f16_sdwa v23, v19 dst_sel:WORD_0 dst_unused:UNUSED_PAD src0_sel:WORD_0
	v_exp_f16_sdwa v24, v20 dst_sel:WORD_0 dst_unused:UNUSED_PAD src0_sel:WORD_0
	v_exp_f16_sdwa v25, v21 dst_sel:WORD_0 dst_unused:UNUSED_PAD src0_sel:WORD_0
	v_exp_f16_sdwa v22, v18 dst_sel:WORD_1 dst_unused:UNUSED_PRESERVE src0_sel:WORD_1
	v_exp_f16_sdwa v23, v19 dst_sel:WORD_1 dst_unused:UNUSED_PRESERVE src0_sel:WORD_1
	v_exp_f16_sdwa v24, v20 dst_sel:WORD_1 dst_unused:UNUSED_PRESERVE src0_sel:WORD_1
	v_exp_f16_sdwa v25, v21 dst_sel:WORD_1 dst_unused:UNUSED_PRESERVE src0_sel:WORD_1
	v_pk_add_f16 v18, v69, v46 neg_lo:[0,1] neg_hi:[0,1]
	v_pk_add_f16 v17, v17, v25
	v_pk_add_f16 v16, v16, v24
	v_pk_add_f16 v15, v15, v23
	v_pk_add_f16 v14, v14, v22
	v_pk_fma_f16 v13, v65, v25, v13
	v_pk_fma_f16 v12, v64, v24, v12
	v_pk_fma_f16 v11, v63, v23, v11
	v_pk_fma_f16 v10, v62, v22, v10
	v_pk_add_f16 v19, v68, v47 neg_lo:[0,1] neg_hi:[0,1]
	v_pk_add_f16 v20, v67, v48 neg_lo:[0,1] neg_hi:[0,1]
	v_pk_add_f16 v21, v66, v49 neg_lo:[0,1] neg_hi:[0,1]
	v_exp_f16_sdwa v22, v18 dst_sel:WORD_0 dst_unused:UNUSED_PAD src0_sel:WORD_0
	v_exp_f16_sdwa v23, v19 dst_sel:WORD_0 dst_unused:UNUSED_PAD src0_sel:WORD_0
	v_exp_f16_sdwa v24, v20 dst_sel:WORD_0 dst_unused:UNUSED_PAD src0_sel:WORD_0
	v_exp_f16_sdwa v25, v21 dst_sel:WORD_0 dst_unused:UNUSED_PAD src0_sel:WORD_0
	v_exp_f16_sdwa v22, v18 dst_sel:WORD_1 dst_unused:UNUSED_PRESERVE src0_sel:WORD_1
	v_exp_f16_sdwa v23, v19 dst_sel:WORD_1 dst_unused:UNUSED_PRESERVE src0_sel:WORD_1
	v_exp_f16_sdwa v24, v20 dst_sel:WORD_1 dst_unused:UNUSED_PRESERVE src0_sel:WORD_1
	v_exp_f16_sdwa v25, v21 dst_sel:WORD_1 dst_unused:UNUSED_PRESERVE src0_sel:WORD_1
	v_pk_add_f16 v18, v73, v46 neg_lo:[0,1] neg_hi:[0,1]
	v_pk_add_f16 v14, v14, v22
	v_pk_add_f16 v15, v15, v23
	v_pk_add_f16 v16, v16, v24
	v_pk_add_f16 v17, v17, v25
	v_pk_fma_f16 v10, v82, v22, v10
	v_pk_fma_f16 v11, v83, v23, v11
	v_pk_fma_f16 v12, v84, v24, v12
	v_pk_fma_f16 v13, v85, v25, v13
	v_pk_add_f16 v19, v72, v47 neg_lo:[0,1] neg_hi:[0,1]
	v_pk_add_f16 v20, v71, v48 neg_lo:[0,1] neg_hi:[0,1]
	v_pk_add_f16 v21, v70, v49 neg_lo:[0,1] neg_hi:[0,1]
	v_exp_f16_sdwa v22, v18 dst_sel:WORD_0 dst_unused:UNUSED_PAD src0_sel:WORD_0
	v_exp_f16_sdwa v23, v19 dst_sel:WORD_0 dst_unused:UNUSED_PAD src0_sel:WORD_0
	v_exp_f16_sdwa v24, v20 dst_sel:WORD_0 dst_unused:UNUSED_PAD src0_sel:WORD_0
	v_exp_f16_sdwa v25, v21 dst_sel:WORD_0 dst_unused:UNUSED_PAD src0_sel:WORD_0
	v_exp_f16_sdwa v22, v18 dst_sel:WORD_1 dst_unused:UNUSED_PRESERVE src0_sel:WORD_1
	v_exp_f16_sdwa v23, v19 dst_sel:WORD_1 dst_unused:UNUSED_PRESERVE src0_sel:WORD_1
	v_exp_f16_sdwa v24, v20 dst_sel:WORD_1 dst_unused:UNUSED_PRESERVE src0_sel:WORD_1
	v_exp_f16_sdwa v25, v21 dst_sel:WORD_1 dst_unused:UNUSED_PRESERVE src0_sel:WORD_1
	s_nop 0
	v_pk_add_f16 v17, v17, v25
	v_pk_add_f16 v16, v16, v24
	v_pk_add_f16 v15, v15, v23
	v_pk_add_f16 v14, v14, v22
	v_pk_fma_f16 v21, v105, v25, v13
	v_pk_fma_f16 v20, v104, v24, v12
	v_pk_fma_f16 v19, v103, v23, v11
	v_pk_fma_f16 v18, v102, v22, v10
	v_mov_b32_e32 v13, v5
	v_mov_b32_e32 v12, v4
	v_mov_b32_e32 v11, v3
	v_mov_b32_e32 v10, v2
.LBB4_80:
	v_lshlrev_b64 v[6:7], 9, v[168:169]
	v_or_b32_e32 v6, v6, v198
	v_lshl_add_u64 v[2:3], s[20:21], 0, v[6:7]
	global_load_dwordx4 v[2:5], v[2:3], off nt
	v_lshl_add_u64 v[6:7], s[22:23], 0, v[6:7]
	global_load_dwordx4 v[6:9], v[6:7], off nt
	v_add_u32_e32 v168, v185, v199
	v_lshlrev_b64 v[26:27], 9, v[168:169]
	v_or_b32_e32 v26, v26, v198
	v_lshl_add_u64 v[22:23], s[20:21], 0, v[26:27]
	global_load_dwordx4 v[22:25], v[22:23], off nt
	v_lshl_add_u64 v[26:27], s[22:23], 0, v[26:27]
	global_load_dwordx4 v[26:29], v[26:27], off nt
	v_pk_add_f16 v17, v17, v33
	v_pk_add_f16 v16, v16, v32
	v_pk_add_f16 v15, v15, v31
	v_pk_add_f16 v14, v14, v30
	v_pk_fma_f16 v42, v13, v33, v21
	v_pk_fma_f16 v43, v12, v32, v20
	v_rcp_f16_e32 v12, v14
	v_rcp_f16_sdwa v13, v14 dst_sel:DWORD dst_unused:UNUSED_PAD src0_sel:WORD_1
	v_rcp_f16_e32 v14, v15
	v_rcp_f16_sdwa v15, v15 dst_sel:DWORD dst_unused:UNUSED_PAD src0_sel:WORD_1
	v_rcp_f16_e32 v46, v16
	v_rcp_f16_sdwa v16, v16 dst_sel:DWORD dst_unused:UNUSED_PAD src0_sel:WORD_1
	v_rcp_f16_e32 v47, v17
	v_rcp_f16_sdwa v17, v17 dst_sel:DWORD dst_unused:UNUSED_PAD src0_sel:WORD_1
	v_add_u32_e32 v168, v187, v199
	v_pk_fma_f16 v44, v10, v30, v18
	v_pk_fma_f16 v45, v11, v31, v19
	v_lshlrev_b64 v[10:11], 9, v[168:169]
	v_or_b32_e32 v10, v10, v198
	v_lshl_add_u64 v[38:39], s[20:21], 0, v[10:11]
	v_lshl_add_u64 v[40:41], s[22:23], 0, v[10:11]
	v_pack_b32_f16 v48, v14, v15
	v_pack_b32_f16 v49, v12, v13
	v_pack_b32_f16 v46, v46, v16
	v_pack_b32_f16 v47, v47, v17
	global_load_dwordx4 v[10:13], v[38:39], off nt
	global_load_dwordx4 v[14:17], v[40:41], off nt
	v_cvt_f32_f16_sdwa v21, v139 dst_sel:DWORD dst_unused:UNUSED_PAD src0_sel:WORD_1
	v_cvt_f32_f16_e32 v20, v139
	v_cvt_f32_f16_sdwa v19, v138 dst_sel:DWORD dst_unused:UNUSED_PAD src0_sel:WORD_1
	v_cvt_f32_f16_e32 v18, v138
	v_cvt_f32_f16_sdwa v33, v141 dst_sel:DWORD dst_unused:UNUSED_PAD src0_sel:WORD_1
	v_cvt_f32_f16_e32 v32, v141
	v_pk_mul_f16 v58, v43, v46
	v_pk_mul_f16 v59, v42, v47
	v_cvt_f32_f16_sdwa v31, v140 dst_sel:DWORD dst_unused:UNUSED_PAD src0_sel:WORD_1
	v_cvt_f32_f16_e32 v30, v140
	v_pk_mul_f16 v52, v45, v48
	v_pk_mul_f16 v53, v44, v49
	v_add_u32_e32 v168, v190, v199
	v_lshlrev_b64 v[36:37], 9, v[168:169]
	v_or_b32_e32 v36, v36, v198
	v_lshl_or_b32 v50, s46, 6, v178
	v_lshlrev_b32_e32 v51, 9, v50
	v_add_u32_e32 v203, v184, v51
	v_cvt_f32_f16_sdwa v35, v77 dst_sel:DWORD dst_unused:UNUSED_PAD src0_sel:WORD_1
	v_cvt_f32_f16_e32 v34, v77
	v_add_lshl_u32 v202, v188, v50, 9
	s_mov_b64 s[4:5], -1
	s_and_b64 vcc, exec, s[26:27]
	s_waitcnt vmcnt(5)
	v_cvt_f32_f16_e32 v38, v2
	v_cvt_f32_f16_sdwa v39, v2 dst_sel:DWORD dst_unused:UNUSED_PAD src0_sel:WORD_1
	v_cvt_f32_f16_e32 v2, v3
	v_cvt_f32_f16_sdwa v3, v3 dst_sel:DWORD dst_unused:UNUSED_PAD src0_sel:WORD_1
	s_waitcnt vmcnt(4)
	v_cvt_f32_f16_e32 v40, v6
	v_cvt_f32_f16_sdwa v41, v6 dst_sel:DWORD dst_unused:UNUSED_PAD src0_sel:WORD_1
	v_cvt_f32_f16_e32 v6, v7
	v_cvt_f32_f16_sdwa v7, v7 dst_sel:DWORD dst_unused:UNUSED_PAD src0_sel:WORD_1
	v_cvt_f32_f16_e32 v42, v4
	v_cvt_f32_f16_sdwa v43, v4 dst_sel:DWORD dst_unused:UNUSED_PAD src0_sel:WORD_1
	v_cvt_f32_f16_e32 v4, v5
	v_cvt_f32_f16_sdwa v5, v5 dst_sel:DWORD dst_unused:UNUSED_PAD src0_sel:WORD_1
	v_cvt_f32_f16_e32 v44, v8
	v_cvt_f32_f16_sdwa v45, v8 dst_sel:DWORD dst_unused:UNUSED_PAD src0_sel:WORD_1
	v_cvt_f32_f16_e32 v8, v9
	v_cvt_f32_f16_sdwa v9, v9 dst_sel:DWORD dst_unused:UNUSED_PAD src0_sel:WORD_1
	v_pk_add_f32 v[2:3], v[20:21], v[2:3]
	v_pk_add_f32 v[18:19], v[18:19], v[38:39]
	v_pk_add_f32 v[4:5], v[32:33], v[4:5]
	v_pk_add_f32 v[6:7], v[2:3], v[6:7]
	v_pk_add_f32 v[20:21], v[30:31], v[42:43]
	v_pk_add_f32 v[18:19], v[18:19], v[40:41]
	v_pk_add_f32 v[8:9], v[4:5], v[8:9]
	v_cvt_pk_f16_f32 v3, v6, v7
	v_lshl_add_u64 v[6:7], s[20:21], 0, v[36:37]
	v_pk_add_f32 v[20:21], v[20:21], v[44:45]
	v_cvt_pk_f16_f32 v2, v18, v19
	v_cvt_pk_f16_f32 v5, v8, v9
	global_load_dwordx4 v[6:9], v[6:7], off nt
	v_lshl_add_u64 v[18:19], s[22:23], 0, v[36:37]
	v_cvt_pk_f16_f32 v4, v20, v21
	global_load_dwordx4 v[18:21], v[18:19], off nt
	s_waitcnt vmcnt(5)
	v_cvt_f32_f16_e32 v46, v22
	v_cvt_f32_f16_sdwa v47, v22 dst_sel:DWORD dst_unused:UNUSED_PAD src0_sel:WORD_1
	ds_write_b128 v203, v[2:5]
	v_cvt_f32_f16_sdwa v5, v76 dst_sel:DWORD dst_unused:UNUSED_PAD src0_sel:WORD_1
	v_cvt_f32_f16_e32 v4, v76
	v_cvt_f32_f16_e32 v22, v23
	v_cvt_f32_f16_sdwa v23, v23 dst_sel:DWORD dst_unused:UNUSED_PAD src0_sel:WORD_1
	s_waitcnt vmcnt(4)
	v_cvt_f32_f16_e32 v48, v26
	v_cvt_f32_f16_sdwa v49, v26 dst_sel:DWORD dst_unused:UNUSED_PAD src0_sel:WORD_1
	v_cvt_f32_f16_e32 v26, v27
	v_cvt_f32_f16_sdwa v27, v27 dst_sel:DWORD dst_unused:UNUSED_PAD src0_sel:WORD_1
	v_cvt_f32_f16_sdwa v31, v75 dst_sel:DWORD dst_unused:UNUSED_PAD src0_sel:WORD_1
	v_cvt_f32_f16_e32 v30, v75
	v_cvt_f32_f16_e32 v32, v24
	v_cvt_f32_f16_sdwa v33, v24 dst_sel:DWORD dst_unused:UNUSED_PAD src0_sel:WORD_1
	v_pk_add_f32 v[4:5], v[4:5], v[22:23]
	v_cvt_f32_f16_e32 v22, v28
	v_pk_add_f32 v[4:5], v[4:5], v[26:27]
	v_cvt_f32_f16_sdwa v23, v28 dst_sel:DWORD dst_unused:UNUSED_PAD src0_sel:WORD_1
	v_cvt_f32_f16_sdwa v27, v74 dst_sel:DWORD dst_unused:UNUSED_PAD src0_sel:WORD_1
	v_cvt_f32_f16_e32 v26, v74
	v_cvt_f32_f16_e32 v24, v25
	v_cvt_f32_f16_sdwa v25, v25 dst_sel:DWORD dst_unused:UNUSED_PAD src0_sel:WORD_1
	v_pk_add_f32 v[2:3], v[34:35], v[46:47]
	v_cvt_f32_f16_e32 v28, v29
	v_cvt_f32_f16_sdwa v29, v29 dst_sel:DWORD dst_unused:UNUSED_PAD src0_sel:WORD_1
	v_pk_add_f32 v[2:3], v[2:3], v[48:49]
	s_nop 0
	v_cvt_pk_f16_f32 v2, v2, v3
	v_cvt_pk_f16_f32 v3, v4, v5
	v_pk_add_f32 v[4:5], v[30:31], v[32:33]
	s_nop 0
	v_pk_add_f32 v[4:5], v[4:5], v[22:23]
	v_pk_add_f32 v[22:23], v[26:27], v[24:25]
	v_cvt_pk_f16_f32 v4, v4, v5
	v_pk_add_f32 v[22:23], v[22:23], v[28:29]
	s_waitcnt vmcnt(3)
	v_cvt_f32_f16_e32 v24, v10
	v_cvt_pk_f16_f32 v5, v22, v23
	v_add_u32_e32 v22, v186, v50
	v_lshlrev_b32_e32 v204, 9, v22
	v_bitop3_b32 v22, v22, v179, 15 bitop3:0x6c
	v_lshlrev_b32_e32 v205, 4, v22
	v_cvt_f32_f16_sdwa v25, v10 dst_sel:DWORD dst_unused:UNUSED_PAD src0_sel:WORD_1
	v_or_b32_e32 v10, v205, v204
	v_cvt_f32_f16_sdwa v23, v57 dst_sel:DWORD dst_unused:UNUSED_PAD src0_sel:WORD_1
	v_cvt_f32_f16_e32 v22, v57
	ds_write_b128 v10, v[2:5]
	v_cvt_f32_f16_sdwa v5, v56 dst_sel:DWORD dst_unused:UNUSED_PAD src0_sel:WORD_1
	v_cvt_f32_f16_e32 v4, v56
	v_cvt_f32_f16_e32 v10, v11
	v_cvt_f32_f16_sdwa v11, v11 dst_sel:DWORD dst_unused:UNUSED_PAD src0_sel:WORD_1
	s_waitcnt vmcnt(2)
	v_cvt_f32_f16_e32 v26, v14
	v_cvt_f32_f16_sdwa v27, v14 dst_sel:DWORD dst_unused:UNUSED_PAD src0_sel:WORD_1
	v_cvt_f32_f16_e32 v14, v15
	v_cvt_f32_f16_sdwa v15, v15 dst_sel:DWORD dst_unused:UNUSED_PAD src0_sel:WORD_1
	v_pk_add_f32 v[2:3], v[22:23], v[24:25]
	v_cvt_f32_f16_sdwa v23, v55 dst_sel:DWORD dst_unused:UNUSED_PAD src0_sel:WORD_1
	v_cvt_f32_f16_e32 v22, v55
	v_cvt_f32_f16_e32 v24, v12
	v_cvt_f32_f16_sdwa v25, v12 dst_sel:DWORD dst_unused:UNUSED_PAD src0_sel:WORD_1
	v_pk_add_f32 v[4:5], v[4:5], v[10:11]
	v_cvt_f32_f16_e32 v10, v16
	v_pk_add_f32 v[4:5], v[4:5], v[14:15]
	v_cvt_f32_f16_sdwa v11, v16 dst_sel:DWORD dst_unused:UNUSED_PAD src0_sel:WORD_1
	v_cvt_f32_f16_sdwa v15, v54 dst_sel:DWORD dst_unused:UNUSED_PAD src0_sel:WORD_1
	v_cvt_f32_f16_e32 v14, v54
	v_cvt_f32_f16_e32 v12, v13
	v_cvt_f32_f16_sdwa v13, v13 dst_sel:DWORD dst_unused:UNUSED_PAD src0_sel:WORD_1
	v_cvt_f32_f16_e32 v16, v17
	v_cvt_f32_f16_sdwa v17, v17 dst_sel:DWORD dst_unused:UNUSED_PAD src0_sel:WORD_1
	v_pk_add_f32 v[2:3], v[2:3], v[26:27]
	s_nop 0
	v_cvt_pk_f16_f32 v2, v2, v3
	v_cvt_pk_f16_f32 v3, v4, v5
	v_pk_add_f32 v[4:5], v[22:23], v[24:25]
	s_nop 0
	v_pk_add_f32 v[4:5], v[4:5], v[10:11]
	v_pk_add_f32 v[10:11], v[14:15], v[12:13]
	v_cvt_pk_f16_f32 v4, v4, v5
	v_pk_add_f32 v[10:11], v[10:11], v[16:17]
	s_waitcnt vmcnt(1)
	v_cvt_f32_f16_e32 v12, v6
	v_cvt_pk_f16_f32 v5, v10, v11
	v_cvt_f32_f16_e32 v10, v53
	v_cvt_f32_f16_sdwa v11, v53 dst_sel:DWORD dst_unused:UNUSED_PAD src0_sel:WORD_1
	v_cvt_f32_f16_sdwa v13, v6 dst_sel:DWORD dst_unused:UNUSED_PAD src0_sel:WORD_1
	s_waitcnt vmcnt(0)
	v_cvt_f32_f16_e32 v14, v18
	v_cvt_f32_f16_sdwa v15, v18 dst_sel:DWORD dst_unused:UNUSED_PAD src0_sel:WORD_1
	v_or_b32_e32 v6, v189, v202
	ds_write_b128 v6, v[2:5]
	v_cvt_f32_f16_e32 v4, v52
	v_cvt_f32_f16_sdwa v5, v52 dst_sel:DWORD dst_unused:UNUSED_PAD src0_sel:WORD_1
	v_cvt_f32_f16_e32 v6, v7
	v_cvt_f32_f16_sdwa v7, v7 dst_sel:DWORD dst_unused:UNUSED_PAD src0_sel:WORD_1
	v_pk_add_f32 v[2:3], v[10:11], v[12:13]
	v_cvt_f32_f16_e32 v10, v19
	v_cvt_f32_f16_sdwa v11, v19 dst_sel:DWORD dst_unused:UNUSED_PAD src0_sel:WORD_1
	v_pk_add_f32 v[2:3], v[2:3], v[14:15]
	v_cvt_f32_f16_e32 v12, v58
	v_cvt_f32_f16_sdwa v13, v58 dst_sel:DWORD dst_unused:UNUSED_PAD src0_sel:WORD_1
	v_cvt_f32_f16_e32 v14, v8
	v_cvt_f32_f16_sdwa v15, v8 dst_sel:DWORD dst_unused:UNUSED_PAD src0_sel:WORD_1
	v_pk_add_f32 v[4:5], v[4:5], v[6:7]
	v_cvt_f32_f16_e32 v6, v20
	v_pk_add_f32 v[4:5], v[4:5], v[10:11]
	v_cvt_f32_f16_sdwa v7, v20 dst_sel:DWORD dst_unused:UNUSED_PAD src0_sel:WORD_1
	v_cvt_f32_f16_e32 v10, v59
	v_cvt_f32_f16_sdwa v11, v59 dst_sel:DWORD dst_unused:UNUSED_PAD src0_sel:WORD_1
	v_cvt_f32_f16_e32 v8, v9
	v_cvt_f32_f16_sdwa v9, v9 dst_sel:DWORD dst_unused:UNUSED_PAD src0_sel:WORD_1
	v_cvt_pk_f16_f32 v2, v2, v3
	v_cvt_pk_f16_f32 v3, v4, v5
	v_pk_add_f32 v[4:5], v[12:13], v[14:15]
	v_cvt_f32_f16_e32 v12, v21
	v_cvt_f32_f16_sdwa v13, v21 dst_sel:DWORD dst_unused:UNUSED_PAD src0_sel:WORD_1
	v_pk_add_f32 v[4:5], v[4:5], v[6:7]
	v_pk_add_f32 v[6:7], v[10:11], v[8:9]
	v_cvt_pk_f16_f32 v4, v4, v5
	v_pk_add_f32 v[6:7], v[6:7], v[12:13]
	s_nop 0
	v_cvt_pk_f16_f32 v5, v6, v7
	v_add_lshl_u32 v6, v191, v50, 9
	v_add_u32_e32 v168, v192, v6
	ds_write_b128 v168, v[2:5]
	global_load_dwordx4 v[2:5], v[174:175], off
	global_load_dwordx4 v[8:11], v[176:177], off
	global_load_dwordx4 v[12:15], v[174:175], off offset:16
	global_load_dwordx4 v[16:19], v[176:177], off offset:16
	s_waitcnt vmcnt(3)
	v_cvt_pk_f16_f32 v6, v2, v3
	s_waitcnt vmcnt(2)
	v_cvt_pk_f16_f32 v2, v8, v9
	v_cvt_pk_f16_f32 v7, v4, v5
	v_cvt_pk_f16_f32 v3, v10, v11
	s_waitcnt vmcnt(1)
	v_cvt_pk_f16_f32 v8, v12, v13
	s_waitcnt vmcnt(0)
	v_cvt_pk_f16_f32 v4, v16, v17
	v_cvt_pk_f16_f32 v9, v14, v15
	v_cvt_pk_f16_f32 v5, v18, v19
	s_cbranch_vccz .LBB4_118
	global_load_dwordx3 v[154:156], v169, s[18:19]
	s_mov_b32 s14, s38
	s_mov_b32 s15, s39
	v_cmp_lt_u32_e64 s[64:65], 0, v199
	v_cmp_gt_u32_e64 s[66:67], 63, v199
	v_cmp_lt_u32_e64 s[68:69], 0, v180
	v_cmp_gt_u32_e64 s[70:71], 60, v180
	buffer_load_dwordx4 v[210:213], v200, s[12:15], 0 offen
	s_and_b64 s[72:73], s[68:69], s[64:65]
	s_and_b64 s[74:75], s[68:69], s[66:67]
	s_and_b64 s[76:77], s[70:71], s[64:65]
	s_and_b64 s[78:79], s[70:71], s[66:67]
	v_add_u32_e32 v245, 0xfffe7c00, v200
	v_add_u32_e32 v246, 0xfffe8000, v200
	s_mov_b64 exec, s[72:73]
	buffer_load_dwordx4 v[122:125], v245, s[12:15], 0 offen
	buffer_load_dwordx4 v[82:85], v245, s[12:15], 0 offen offset:512
	s_mov_b64 exec, -1
	s_mov_b64 exec, s[68:69]
	buffer_load_dwordx4 v[138:141], v246, s[12:15], 0 offen offset:512
	buffer_load_dwordx4 v[106:109], v246, s[12:15], 0 offen offset:1024
	s_mov_b64 exec, -1
	s_mov_b64 exec, s[74:75]
	buffer_load_dwordx4 v[146:149], v246, s[12:15], 0 offen offset:2048
	buffer_load_dwordx4 v[126:129], v246, s[12:15], 0 offen offset:2560
	s_mov_b64 exec, -1
	v_add_u32_e32 v245, 0xfffffc00, v200
	s_mov_b64 exec, s[64:65]
	buffer_load_dwordx4 v[94:97], v245, s[12:15], 0 offen
	buffer_load_dwordx4 v[54:57], v245, s[12:15], 0 offen offset:512
	s_mov_b64 exec, -1
	buffer_load_dwordx4 v[118:121], v200, s[12:15], 0 offen offset:512
	buffer_load_dwordx4 v[74:77], v200, s[12:15], 0 offen offset:1024
	s_mov_b64 exec, s[66:67]
	buffer_load_dwordx4 v[134:137], v200, s[12:15], 0 offen offset:2048
	buffer_load_dwordx4 v[98:101], v200, s[12:15], 0 offen offset:2560
	s_mov_b64 exec, -1
	v_add_u32_e32 v245, 0x17c00, v200
	v_add_u32_e32 v246, 0x18000, v200
	s_mov_b64 exec, s[64:65]
	buffer_load_dwordx4 v[62:65], v245, s[12:15], 0 offen
	buffer_load_dwordx4 v[30:33], v245, s[12:15], 0 offen offset:512
	s_mov_b64 exec, -1
	buffer_load_dwordx4 v[78:81], v246, s[12:15], 0 offen offset:512
	buffer_load_dwordx4 v[42:45], v246, s[12:15], 0 offen offset:1024
	s_mov_b64 exec, s[66:67]
	buffer_load_dwordx4 v[102:105], v246, s[12:15], 0 offen offset:2048
	buffer_load_dwordx4 v[58:61], v246, s[12:15], 0 offen offset:2560
	s_mov_b64 exec, -1
	v_add_u32_e32 v245, 0x18000, v200
	buffer_load_dwordx4 v[162:165], v245, s[12:15], 0 offen
	v_add_u32_e32 v246, 0x30000, v200
	buffer_load_dwordx4 v[158:161], v246, s[12:15], 0 offen
	v_add_u32_e32 v245, 0x2fc00, v200
	v_add_u32_e32 v246, 0x30000, v200
	v_add_u32_e32 v247, 0x47c00, v200
	v_add_u32_e32 v248, 0x48000, v200
	v_add_u32_e32 v249, 0x5fc00, v200
	v_add_u32_e32 v250, 0x60000, v200
	s_not_b64 exec, s[72:73]
	s_cbranch_execz .Lmyf_C3_0
	v_mov_b32_e32 v122, v6
	v_mov_b32_e32 v123, v7
	v_mov_b32_e32 v124, v8
	v_mov_b32_e32 v125, v9
	v_mov_b32_e32 v82, v2
	v_mov_b32_e32 v83, v3
	v_mov_b32_e32 v84, v4
	v_mov_b32_e32 v85, v5

.Lmyf_C3_7:
	s_mov_b64 exec, -1
	s_waitcnt vmcnt(21)
	v_cvt_f16_f32_e32 v206, v155
	v_cvt_f16_f32_e32 v208, v154
	v_cvt_f16_f32_e32 v207, v156
	v_add_u32_e32 v251, 0x48000, v200
	buffer_load_dwordx4 v[154:157], v251, s[12:15], 0 offen
	s_mov_b64 s[4:5], 0
	s_waitcnt vmcnt(3)
	v_pk_mul_f16 v216, v208, v213 op_sel_hi:[0,1]
	v_pk_mul_f16 v220, v206, v213 op_sel_hi:[0,1]
	v_pk_mul_f16 v224, v207, v213 op_sel_hi:[0,1]
	v_pk_mul_f16 v209, v208, v210 op_sel_hi:[0,1]
	v_pk_mul_f16 v214, v208, v211 op_sel_hi:[0,1]
	v_pk_mul_f16 v215, v208, v212 op_sel_hi:[0,1]
	v_pk_mul_f16 v217, v206, v210 op_sel_hi:[0,1]
	s_mov_b64 exec, s[64:65]
	buffer_load_dwordx4 v[34:37], v245, s[12:15], 0 offen
	buffer_load_dwordx4 v[18:21], v245, s[12:15], 0 offen offset:512
	s_mov_b64 exec, -1
	v_pk_mul_f16 v218, v206, v211 op_sel_hi:[0,1]
	v_pk_mul_f16 v219, v206, v212 op_sel_hi:[0,1]
	v_pk_mul_f16 v221, v207, v210 op_sel_hi:[0,1]
	v_pk_mul_f16 v222, v207, v211 op_sel_hi:[0,1]
	v_pk_mul_f16 v223, v207, v212 op_sel_hi:[0,1]
	v_pk_fma_f16 v125, v125, v213, v216
	v_pk_fma_f16 v141, v141, v213, v220
	v_pk_fma_f16 v149, v149, v213, v224
	v_pk_fma_f16 v225, v97, v213, v216
	v_pk_fma_f16 v229, v121, v213, v220
	v_pk_fma_f16 v233, v137, v213, v224
	v_pk_fma_f16 v216, v65, v213, v216
	v_pk_fma_f16 v220, v81, v213, v220
	buffer_load_dwordx4 v[46:49], v246, s[12:15], 0 offen offset:512
	buffer_load_dwordx4 v[22:25], v246, s[12:15], 0 offen offset:1024
	v_pk_fma_f16 v213, v105, v213, v224
	v_pk_maximum3_f16 v224, v125, v141, v149
	v_pk_fma_f16 v124, v124, v212, v215
	v_pk_fma_f16 v123, v123, v211, v214
	v_pk_fma_f16 v122, v122, v210, v209
	v_pk_fma_f16 v140, v140, v212, v219
	v_pk_fma_f16 v139, v139, v211, v218
	v_pk_fma_f16 v138, v138, v210, v217
	v_pk_fma_f16 v148, v148, v212, v223
	v_pk_fma_f16 v147, v147, v211, v222
	v_pk_fma_f16 v146, v146, v210, v221
	v_pk_fma_f16 v226, v96, v212, v215
	v_pk_fma_f16 v227, v95, v211, v214
	v_pk_fma_f16 v228, v94, v210, v209
	v_pk_fma_f16 v230, v120, v212, v219
	v_pk_fma_f16 v231, v119, v211, v218
	s_mov_b64 exec, s[66:67]
	buffer_load_dwordx4 v[66:69], v246, s[12:15], 0 offen offset:2048
	buffer_load_dwordx4 v[26:29], v246, s[12:15], 0 offen offset:2560
	s_mov_b64 exec, -1
	v_pk_fma_f16 v232, v118, v210, v217
	v_pk_fma_f16 v234, v136, v212, v223
	v_pk_fma_f16 v235, v135, v211, v222
	v_pk_fma_f16 v236, v134, v210, v221
	v_pk_fma_f16 v215, v64, v212, v215
	v_pk_fma_f16 v214, v63, v211, v214
	v_pk_fma_f16 v209, v62, v210, v209
	v_pk_fma_f16 v219, v80, v212, v219
	v_pk_fma_f16 v218, v79, v211, v218
	v_pk_fma_f16 v217, v78, v210, v217
	v_pk_fma_f16 v212, v104, v212, v223
	v_pk_fma_f16 v211, v103, v211, v222
	v_pk_fma_f16 v210, v102, v210, v221
	v_pk_maximum3_f16 v221, v122, v138, v146
	v_pk_maximum3_f16 v222, v123, v139, v147
	v_pk_maximum3_f16 v223, v124, v140, v148
	v_pk_maximum3_f16 v240, v225, v229, v233
	v_pk_maximum3_f16 v244, v216, v220, v213
	v_pk_maximum3_f16 v237, v228, v232, v236
	v_pk_maximum3_f16 v238, v227, v231, v235
	v_pk_maximum3_f16 v239, v226, v230, v234
	v_pk_maximum3_f16 v241, v209, v217, v210
	v_pk_maximum3_f16 v242, v214, v218, v211
	v_pk_maximum3_f16 v224, v224, v240, v244
	v_pk_maximum3_f16 v243, v215, v219, v212
	v_pk_maximum3_f16 v221, v221, v237, v241
	v_pk_maximum3_f16 v222, v222, v238, v242
	v_pk_maximum3_f16 v223, v223, v239, v243
	v_pk_add_f16 v125, v125, v224 neg_lo:[0,1] neg_hi:[0,1]
	s_mov_b64 exec, s[64:65]
	buffer_load_dwordx4 v[86:89], v247, s[12:15], 0 offen
	buffer_load_dwordx4 v[38:41], v247, s[12:15], 0 offen offset:512
	s_mov_b64 exec, -1
	v_pk_add_f16 v122, v122, v221 neg_lo:[0,1] neg_hi:[0,1]
	v_pk_add_f16 v123, v123, v222 neg_lo:[0,1] neg_hi:[0,1]
	v_pk_add_f16 v124, v124, v223 neg_lo:[0,1] neg_hi:[0,1]
	v_pk_add_f16 v138, v138, v221 neg_lo:[0,1] neg_hi:[0,1]
	v_exp_f16_sdwa v237, v122 dst_sel:WORD_0 dst_unused:UNUSED_PAD src0_sel:WORD_0
	v_exp_f16_sdwa v238, v123 dst_sel:WORD_0 dst_unused:UNUSED_PAD src0_sel:WORD_0
	v_exp_f16_sdwa v239, v124 dst_sel:WORD_0 dst_unused:UNUSED_PAD src0_sel:WORD_0
	v_exp_f16_sdwa v240, v125 dst_sel:WORD_0 dst_unused:UNUSED_PAD src0_sel:WORD_0
	v_exp_f16_sdwa v237, v122 dst_sel:WORD_1 dst_unused:UNUSED_PRESERVE src0_sel:WORD_1
	v_exp_f16_sdwa v238, v123 dst_sel:WORD_1 dst_unused:UNUSED_PRESERVE src0_sel:WORD_1
	v_exp_f16_sdwa v239, v124 dst_sel:WORD_1 dst_unused:UNUSED_PRESERVE src0_sel:WORD_1
	v_exp_f16_sdwa v240, v125 dst_sel:WORD_1 dst_unused:UNUSED_PRESERVE src0_sel:WORD_1
	v_pk_add_f16 v139, v139, v222 neg_lo:[0,1] neg_hi:[0,1]
	v_pk_add_f16 v125, v237, 0
	v_pk_fma_f16 v85, v85, v240, 0
	v_pk_add_f16 v122, v240, 0
	v_pk_add_f16 v123, v239, 0
	v_pk_add_f16 v124, v238, 0
	v_pk_fma_f16 v84, v84, v239, 0
	v_pk_fma_f16 v83, v83, v238, 0
	v_pk_fma_f16 v82, v82, v237, 0
	v_pk_add_f16 v140, v140, v223 neg_lo:[0,1] neg_hi:[0,1]
	buffer_load_dwordx4 v[114:117], v248, s[12:15], 0 offen offset:512
	buffer_load_dwordx4 v[50:53], v248, s[12:15], 0 offen offset:1024
	v_pk_add_f16 v141, v141, v224 neg_lo:[0,1] neg_hi:[0,1]
	v_exp_f16_sdwa v237, v138 dst_sel:WORD_0 dst_unused:UNUSED_PAD src0_sel:WORD_0
	v_exp_f16_sdwa v238, v139 dst_sel:WORD_0 dst_unused:UNUSED_PAD src0_sel:WORD_0
	v_exp_f16_sdwa v239, v140 dst_sel:WORD_0 dst_unused:UNUSED_PAD src0_sel:WORD_0
	v_exp_f16_sdwa v240, v141 dst_sel:WORD_0 dst_unused:UNUSED_PAD src0_sel:WORD_0
	v_exp_f16_sdwa v237, v138 dst_sel:WORD_1 dst_unused:UNUSED_PRESERVE src0_sel:WORD_1
	v_exp_f16_sdwa v238, v139 dst_sel:WORD_1 dst_unused:UNUSED_PRESERVE src0_sel:WORD_1
	v_exp_f16_sdwa v239, v140 dst_sel:WORD_1 dst_unused:UNUSED_PRESERVE src0_sel:WORD_1
	v_exp_f16_sdwa v240, v141 dst_sel:WORD_1 dst_unused:UNUSED_PRESERVE src0_sel:WORD_1
	v_pk_add_f16 v125, v125, v237
	v_pk_fma_f16 v85, v109, v240, v85
	v_pk_add_f16 v109, v149, v224 neg_lo:[0,1] neg_hi:[0,1]
	v_pk_add_f16 v124, v124, v238
	v_pk_add_f16 v123, v123, v239
	v_pk_add_f16 v122, v122, v240
	v_pk_fma_f16 v82, v106, v237, v82
	v_pk_fma_f16 v83, v107, v238, v83
	v_pk_fma_f16 v84, v108, v239, v84
	v_pk_add_f16 v106, v146, v221 neg_lo:[0,1] neg_hi:[0,1]
	v_pk_add_f16 v107, v147, v222 neg_lo:[0,1] neg_hi:[0,1]
	v_pk_add_f16 v108, v148, v223 neg_lo:[0,1] neg_hi:[0,1]
	v_exp_f16_sdwa v138, v106 dst_sel:WORD_0 dst_unused:UNUSED_PAD src0_sel:WORD_0
	v_exp_f16_sdwa v139, v107 dst_sel:WORD_0 dst_unused:UNUSED_PAD src0_sel:WORD_0
	v_exp_f16_sdwa v140, v108 dst_sel:WORD_0 dst_unused:UNUSED_PAD src0_sel:WORD_0
	v_exp_f16_sdwa v141, v109 dst_sel:WORD_0 dst_unused:UNUSED_PAD src0_sel:WORD_0
	v_exp_f16_sdwa v138, v106 dst_sel:WORD_1 dst_unused:UNUSED_PRESERVE src0_sel:WORD_1
	v_exp_f16_sdwa v139, v107 dst_sel:WORD_1 dst_unused:UNUSED_PRESERVE src0_sel:WORD_1
	v_exp_f16_sdwa v140, v108 dst_sel:WORD_1 dst_unused:UNUSED_PRESERVE src0_sel:WORD_1
	v_exp_f16_sdwa v141, v109 dst_sel:WORD_1 dst_unused:UNUSED_PRESERVE src0_sel:WORD_1
	v_pk_add_f16 v109, v125, v138
	v_pk_add_f16 v106, v122, v141
	s_mov_b64 exec, s[66:67]
	buffer_load_dwordx4 v[130:133], v248, s[12:15], 0 offen offset:2048
	buffer_load_dwordx4 v[70:73], v248, s[12:15], 0 offen offset:2560
	s_mov_b64 exec, -1
	v_pk_add_f16 v107, v123, v140
	v_pk_add_f16 v108, v124, v139
	v_pk_fma_f16 v85, v129, v141, v85
	v_pk_fma_f16 v84, v128, v140, v84
	v_pk_fma_f16 v83, v127, v139, v83
	v_pk_fma_f16 v82, v126, v138, v82
	v_pk_add_f16 v122, v228, v221 neg_lo:[0,1] neg_hi:[0,1]
	v_pk_add_f16 v123, v227, v222 neg_lo:[0,1] neg_hi:[0,1]
	v_pk_add_f16 v124, v226, v223 neg_lo:[0,1] neg_hi:[0,1]
	v_pk_add_f16 v125, v225, v224 neg_lo:[0,1] neg_hi:[0,1]
	v_exp_f16_sdwa v126, v122 dst_sel:WORD_0 dst_unused:UNUSED_PAD src0_sel:WORD_0
	v_exp_f16_sdwa v127, v123 dst_sel:WORD_0 dst_unused:UNUSED_PAD src0_sel:WORD_0
	v_exp_f16_sdwa v128, v124 dst_sel:WORD_0 dst_unused:UNUSED_PAD src0_sel:WORD_0
	v_exp_f16_sdwa v129, v125 dst_sel:WORD_0 dst_unused:UNUSED_PAD src0_sel:WORD_0
	v_exp_f16_sdwa v126, v122 dst_sel:WORD_1 dst_unused:UNUSED_PRESERVE src0_sel:WORD_1
	v_exp_f16_sdwa v127, v123 dst_sel:WORD_1 dst_unused:UNUSED_PRESERVE src0_sel:WORD_1
	v_exp_f16_sdwa v128, v124 dst_sel:WORD_1 dst_unused:UNUSED_PRESERVE src0_sel:WORD_1
	v_exp_f16_sdwa v129, v125 dst_sel:WORD_1 dst_unused:UNUSED_PRESERVE src0_sel:WORD_1
	v_pk_add_f16 v122, v232, v221 neg_lo:[0,1] neg_hi:[0,1]
	v_pk_add_f16 v109, v109, v126
	v_pk_add_f16 v108, v108, v127
	v_pk_add_f16 v107, v107, v128
	s_mov_b64 exec, s[76:77]
	buffer_load_dwordx4 v[142:145], v249, s[12:15], 0 offen
	buffer_load_dwordx4 v[90:93], v249, s[12:15], 0 offen offset:512
	s_mov_b64 exec, -1
	v_pk_add_f16 v106, v106, v129
	v_pk_fma_f16 v82, v54, v126, v82
	v_pk_fma_f16 v83, v55, v127, v83
	v_pk_fma_f16 v84, v56, v128, v84
	v_pk_fma_f16 v85, v57, v129, v85
	v_pk_add_f16 v123, v231, v222 neg_lo:[0,1] neg_hi:[0,1]
	v_pk_add_f16 v124, v230, v223 neg_lo:[0,1] neg_hi:[0,1]
	v_pk_add_f16 v125, v229, v224 neg_lo:[0,1] neg_hi:[0,1]
	v_exp_f16_sdwa v126, v122 dst_sel:WORD_0 dst_unused:UNUSED_PAD src0_sel:WORD_0
	v_exp_f16_sdwa v127, v123 dst_sel:WORD_0 dst_unused:UNUSED_PAD src0_sel:WORD_0
	v_exp_f16_sdwa v128, v124 dst_sel:WORD_0 dst_unused:UNUSED_PAD src0_sel:WORD_0
	v_exp_f16_sdwa v129, v125 dst_sel:WORD_0 dst_unused:UNUSED_PAD src0_sel:WORD_0
	v_exp_f16_sdwa v126, v122 dst_sel:WORD_1 dst_unused:UNUSED_PRESERVE src0_sel:WORD_1
	v_exp_f16_sdwa v127, v123 dst_sel:WORD_1 dst_unused:UNUSED_PRESERVE src0_sel:WORD_1
	v_exp_f16_sdwa v128, v124 dst_sel:WORD_1 dst_unused:UNUSED_PRESERVE src0_sel:WORD_1
	v_exp_f16_sdwa v129, v125 dst_sel:WORD_1 dst_unused:UNUSED_PRESERVE src0_sel:WORD_1
	v_pk_add_f16 v122, v236, v221 neg_lo:[0,1] neg_hi:[0,1]
	v_pk_add_f16 v109, v109, v126
	v_pk_add_f16 v106, v106, v129
	v_pk_add_f16 v107, v107, v128
	v_pk_add_f16 v108, v108, v127
	v_pk_fma_f16 v85, v77, v129, v85
	v_pk_fma_f16 v84, v76, v128, v84
	s_mov_b64 exec, s[70:71]
	buffer_load_dwordx4 v[150:153], v250, s[12:15], 0 offen offset:512
	buffer_load_dwordx4 v[110:113], v250, s[12:15], 0 offen offset:1024
	s_mov_b64 exec, -1
	v_pk_fma_f16 v83, v75, v127, v83
	v_pk_fma_f16 v82, v74, v126, v82
	v_pk_add_f16 v123, v235, v222 neg_lo:[0,1] neg_hi:[0,1]
	v_pk_add_f16 v124, v234, v223 neg_lo:[0,1] neg_hi:[0,1]
	v_pk_add_f16 v125, v233, v224 neg_lo:[0,1] neg_hi:[0,1]
	v_exp_f16_sdwa v126, v122 dst_sel:WORD_0 dst_unused:UNUSED_PAD src0_sel:WORD_0
	v_exp_f16_sdwa v127, v123 dst_sel:WORD_0 dst_unused:UNUSED_PAD src0_sel:WORD_0
	v_exp_f16_sdwa v128, v124 dst_sel:WORD_0 dst_unused:UNUSED_PAD src0_sel:WORD_0
	v_exp_f16_sdwa v129, v125 dst_sel:WORD_0 dst_unused:UNUSED_PAD src0_sel:WORD_0
	v_exp_f16_sdwa v126, v122 dst_sel:WORD_1 dst_unused:UNUSED_PRESERVE src0_sel:WORD_1
	v_exp_f16_sdwa v127, v123 dst_sel:WORD_1 dst_unused:UNUSED_PRESERVE src0_sel:WORD_1
	v_exp_f16_sdwa v128, v124 dst_sel:WORD_1 dst_unused:UNUSED_PRESERVE src0_sel:WORD_1
	v_exp_f16_sdwa v129, v125 dst_sel:WORD_1 dst_unused:UNUSED_PRESERVE src0_sel:WORD_1
	v_pk_add_f16 v122, v209, v221 neg_lo:[0,1] neg_hi:[0,1]
	v_pk_add_f16 v109, v109, v126
	v_pk_add_f16 v108, v108, v127
	v_pk_add_f16 v107, v107, v128
	v_pk_add_f16 v106, v106, v129
	v_pk_fma_f16 v82, v98, v126, v82
	v_pk_fma_f16 v83, v99, v127, v83
	v_pk_fma_f16 v84, v100, v128, v84
	v_pk_fma_f16 v85, v101, v129, v85
	s_mov_b64 exec, s[78:79]
	buffer_load_dwordx4 v[14:17], v250, s[12:15], 0 offen offset:2048
	buffer_load_dwordx4 v[10:13], v250, s[12:15], 0 offen offset:2560
	s_mov_b64 exec, -1
	v_pk_add_f16 v123, v214, v222 neg_lo:[0,1] neg_hi:[0,1]
	v_pk_add_f16 v124, v215, v223 neg_lo:[0,1] neg_hi:[0,1]
	v_pk_add_f16 v125, v216, v224 neg_lo:[0,1] neg_hi:[0,1]
	v_exp_f16_sdwa v126, v122 dst_sel:WORD_0 dst_unused:UNUSED_PAD src0_sel:WORD_0
	v_exp_f16_sdwa v127, v123 dst_sel:WORD_0 dst_unused:UNUSED_PAD src0_sel:WORD_0
	v_exp_f16_sdwa v128, v124 dst_sel:WORD_0 dst_unused:UNUSED_PAD src0_sel:WORD_0
	v_exp_f16_sdwa v129, v125 dst_sel:WORD_0 dst_unused:UNUSED_PAD src0_sel:WORD_0
	v_exp_f16_sdwa v126, v122 dst_sel:WORD_1 dst_unused:UNUSED_PRESERVE src0_sel:WORD_1
	v_exp_f16_sdwa v127, v123 dst_sel:WORD_1 dst_unused:UNUSED_PRESERVE src0_sel:WORD_1
	v_exp_f16_sdwa v128, v124 dst_sel:WORD_1 dst_unused:UNUSED_PRESERVE src0_sel:WORD_1
	v_exp_f16_sdwa v129, v125 dst_sel:WORD_1 dst_unused:UNUSED_PRESERVE src0_sel:WORD_1
	v_pk_add_f16 v122, v217, v221 neg_lo:[0,1] neg_hi:[0,1]
	v_pk_add_f16 v109, v109, v126
	v_pk_add_f16 v106, v106, v129
	v_pk_add_f16 v107, v107, v128
	v_pk_add_f16 v108, v108, v127
	v_pk_fma_f16 v85, v33, v129, v85
	v_pk_fma_f16 v84, v32, v128, v84
	v_pk_fma_f16 v83, v31, v127, v83
	v_pk_fma_f16 v82, v30, v126, v82
	v_pk_add_f16 v123, v218, v222 neg_lo:[0,1] neg_hi:[0,1]
	v_pk_add_f16 v124, v219, v223 neg_lo:[0,1] neg_hi:[0,1]
	v_pk_add_f16 v125, v220, v224 neg_lo:[0,1] neg_hi:[0,1]
	v_exp_f16_sdwa v126, v122 dst_sel:WORD_0 dst_unused:UNUSED_PAD src0_sel:WORD_0
	v_exp_f16_sdwa v127, v123 dst_sel:WORD_0 dst_unused:UNUSED_PAD src0_sel:WORD_0
	v_exp_f16_sdwa v128, v124 dst_sel:WORD_0 dst_unused:UNUSED_PAD src0_sel:WORD_0
	v_exp_f16_sdwa v129, v125 dst_sel:WORD_0 dst_unused:UNUSED_PAD src0_sel:WORD_0
	v_exp_f16_sdwa v126, v122 dst_sel:WORD_1 dst_unused:UNUSED_PRESERVE src0_sel:WORD_1
	v_exp_f16_sdwa v127, v123 dst_sel:WORD_1 dst_unused:UNUSED_PRESERVE src0_sel:WORD_1
	v_exp_f16_sdwa v128, v124 dst_sel:WORD_1 dst_unused:UNUSED_PRESERVE src0_sel:WORD_1
	v_exp_f16_sdwa v129, v125 dst_sel:WORD_1 dst_unused:UNUSED_PRESERVE src0_sel:WORD_1
	v_pk_add_f16 v122, v210, v221 neg_lo:[0,1] neg_hi:[0,1]
	v_pk_add_f16 v109, v109, v126
	v_pk_add_f16 v108, v108, v127
	v_pk_add_f16 v107, v107, v128
	v_pk_add_f16 v106, v106, v129
	v_pk_fma_f16 v82, v42, v126, v82
	v_pk_fma_f16 v83, v43, v127, v83
	v_pk_fma_f16 v84, v44, v128, v84
	v_pk_fma_f16 v85, v45, v129, v85
	v_pk_add_f16 v123, v211, v222 neg_lo:[0,1] neg_hi:[0,1]
	v_pk_add_f16 v124, v212, v223 neg_lo:[0,1] neg_hi:[0,1]
	v_pk_add_f16 v125, v213, v224 neg_lo:[0,1] neg_hi:[0,1]
	v_exp_f16_sdwa v126, v122 dst_sel:WORD_0 dst_unused:UNUSED_PAD src0_sel:WORD_0
	v_exp_f16_sdwa v127, v123 dst_sel:WORD_0 dst_unused:UNUSED_PAD src0_sel:WORD_0
	v_exp_f16_sdwa v128, v124 dst_sel:WORD_0 dst_unused:UNUSED_PAD src0_sel:WORD_0
	v_exp_f16_sdwa v129, v125 dst_sel:WORD_0 dst_unused:UNUSED_PAD src0_sel:WORD_0
	v_exp_f16_sdwa v126, v122 dst_sel:WORD_1 dst_unused:UNUSED_PRESERVE src0_sel:WORD_1
	v_exp_f16_sdwa v127, v123 dst_sel:WORD_1 dst_unused:UNUSED_PRESERVE src0_sel:WORD_1
	v_exp_f16_sdwa v128, v124 dst_sel:WORD_1 dst_unused:UNUSED_PRESERVE src0_sel:WORD_1
	v_exp_f16_sdwa v129, v125 dst_sel:WORD_1 dst_unused:UNUSED_PRESERVE src0_sel:WORD_1
	v_pk_add_f16 v109, v109, v126
	v_pk_add_f16 v108, v108, v127
	v_rcp_f16_e32 v122, v109
	v_rcp_f16_sdwa v109, v109 dst_sel:DWORD dst_unused:UNUSED_PAD src0_sel:WORD_1
	v_pk_add_f16 v107, v107, v128
	v_rcp_f16_e32 v123, v108
	v_rcp_f16_sdwa v108, v108 dst_sel:DWORD dst_unused:UNUSED_PAD src0_sel:WORD_1
	v_pk_add_f16 v106, v106, v129
	v_rcp_f16_e32 v124, v107
	v_rcp_f16_sdwa v107, v107 dst_sel:DWORD dst_unused:UNUSED_PAD src0_sel:WORD_1
	v_rcp_f16_e32 v125, v106
	v_rcp_f16_sdwa v106, v106 dst_sel:DWORD dst_unused:UNUSED_PAD src0_sel:WORD_1
	v_pk_fma_f16 v82, v58, v126, v82
	v_pack_b32_f16 v109, v122, v109
	v_pk_fma_f16 v83, v59, v127, v83
	v_pk_mul_f16 v141, v82, v109
	v_pack_b32_f16 v82, v123, v108
	v_pk_fma_f16 v84, v60, v128, v84
	v_pk_mul_f16 v140, v83, v82
	v_pack_b32_f16 v82, v124, v107
	v_pk_fma_f16 v85, v61, v129, v85
	v_pk_mul_f16 v139, v84, v82
	v_pack_b32_f16 v82, v125, v106
	v_pk_mul_f16 v138, v85, v82
	s_waitcnt vmcnt(12)
	v_pk_mul_f16 v85, v208, v165 op_sel_hi:[0,1]
	v_pk_mul_f16 v109, v206, v165 op_sel_hi:[0,1]
	v_pk_mul_f16 v122, v207, v162 op_sel_hi:[0,1]
	v_pk_mul_f16 v125, v207, v165 op_sel_hi:[0,1]
	v_pk_mul_f16 v82, v208, v162 op_sel_hi:[0,1]
	v_pk_mul_f16 v83, v208, v163 op_sel_hi:[0,1]
	v_pk_mul_f16 v84, v208, v164 op_sel_hi:[0,1]
	v_pk_mul_f16 v106, v206, v162 op_sel_hi:[0,1]
	v_pk_mul_f16 v107, v206, v163 op_sel_hi:[0,1]
	v_pk_mul_f16 v108, v206, v164 op_sel_hi:[0,1]
	v_pk_mul_f16 v123, v207, v163 op_sel_hi:[0,1]
	v_pk_mul_f16 v124, v207, v164 op_sel_hi:[0,1]
	v_pk_fma_f16 v97, v97, v165, v85
	v_pk_fma_f16 v121, v121, v165, v109
	v_pk_fma_f16 v126, v137, v165, v125
	v_pk_fma_f16 v129, v134, v162, v122
	v_pk_fma_f16 v134, v65, v165, v85
	v_pk_fma_f16 v146, v81, v165, v109
	v_pk_fma_f16 v209, v105, v165, v125
	v_pk_fma_f16 v85, v37, v165, v85
	v_pk_fma_f16 v109, v49, v165, v109
	v_pk_fma_f16 v125, v69, v165, v125
	v_pk_maximum3_f16 v165, v97, v121, v126
	v_pk_fma_f16 v96, v96, v164, v84
	v_pk_fma_f16 v95, v95, v163, v83
	v_pk_fma_f16 v94, v94, v162, v82
	v_pk_fma_f16 v120, v120, v164, v108
	v_pk_fma_f16 v119, v119, v163, v107
	v_pk_fma_f16 v118, v118, v162, v106
	v_pk_fma_f16 v127, v136, v164, v124
	v_pk_fma_f16 v128, v135, v163, v123
	v_pk_fma_f16 v135, v64, v164, v84
	v_pk_fma_f16 v136, v63, v163, v83
	v_pk_fma_f16 v137, v62, v162, v82
	v_pk_fma_f16 v147, v80, v164, v108
	v_pk_fma_f16 v148, v79, v163, v107
	v_pk_fma_f16 v149, v78, v162, v106
	v_pk_fma_f16 v210, v104, v164, v124
	v_pk_fma_f16 v211, v103, v163, v123
	v_pk_fma_f16 v212, v102, v162, v122
	v_pk_fma_f16 v84, v36, v164, v84
	v_pk_fma_f16 v83, v35, v163, v83
	v_pk_fma_f16 v82, v34, v162, v82
	v_pk_fma_f16 v108, v48, v164, v108
	v_pk_fma_f16 v107, v47, v163, v107
	v_pk_fma_f16 v106, v46, v162, v106
	v_pk_fma_f16 v124, v68, v164, v124
	v_pk_fma_f16 v123, v67, v163, v123
	v_pk_fma_f16 v122, v66, v162, v122
	v_pk_maximum3_f16 v162, v94, v118, v129
	v_pk_maximum3_f16 v163, v95, v119, v128
	v_pk_maximum3_f16 v164, v96, v120, v127
	v_pk_maximum3_f16 v216, v134, v146, v209
	v_pk_maximum3_f16 v220, v85, v109, v125
	v_pk_maximum3_f16 v213, v137, v149, v212
	v_pk_maximum3_f16 v214, v136, v148, v211
	v_pk_maximum3_f16 v215, v135, v147, v210
	v_pk_maximum3_f16 v217, v82, v106, v122
	v_pk_maximum3_f16 v218, v83, v107, v123
	v_pk_maximum3_f16 v165, v165, v216, v220
	v_pk_maximum3_f16 v219, v84, v108, v124
	v_pk_maximum3_f16 v162, v162, v213, v217
	v_pk_maximum3_f16 v163, v163, v214, v218
	v_pk_maximum3_f16 v164, v164, v215, v219
	v_pk_add_f16 v97, v97, v165 neg_lo:[0,1] neg_hi:[0,1]
	v_pk_add_f16 v94, v94, v162 neg_lo:[0,1] neg_hi:[0,1]
	v_pk_add_f16 v95, v95, v163 neg_lo:[0,1] neg_hi:[0,1]
	v_pk_add_f16 v96, v96, v164 neg_lo:[0,1] neg_hi:[0,1]
	v_pk_add_f16 v118, v118, v162 neg_lo:[0,1] neg_hi:[0,1]
	v_exp_f16_sdwa v213, v94 dst_sel:WORD_0 dst_unused:UNUSED_PAD src0_sel:WORD_0
	v_exp_f16_sdwa v214, v95 dst_sel:WORD_0 dst_unused:UNUSED_PAD src0_sel:WORD_0
	v_exp_f16_sdwa v215, v96 dst_sel:WORD_0 dst_unused:UNUSED_PAD src0_sel:WORD_0
	v_exp_f16_sdwa v216, v97 dst_sel:WORD_0 dst_unused:UNUSED_PAD src0_sel:WORD_0
	v_exp_f16_sdwa v213, v94 dst_sel:WORD_1 dst_unused:UNUSED_PRESERVE src0_sel:WORD_1
	v_exp_f16_sdwa v214, v95 dst_sel:WORD_1 dst_unused:UNUSED_PRESERVE src0_sel:WORD_1
	v_exp_f16_sdwa v215, v96 dst_sel:WORD_1 dst_unused:UNUSED_PRESERVE src0_sel:WORD_1
	v_exp_f16_sdwa v216, v97 dst_sel:WORD_1 dst_unused:UNUSED_PRESERVE src0_sel:WORD_1
	v_pk_add_f16 v119, v119, v163 neg_lo:[0,1] neg_hi:[0,1]
	v_pk_add_f16 v97, v213, 0
	v_pk_fma_f16 v57, v57, v216, 0
	v_pk_add_f16 v94, v216, 0
	v_pk_add_f16 v95, v215, 0
	v_pk_add_f16 v96, v214, 0
	v_pk_fma_f16 v56, v56, v215, 0
	v_pk_fma_f16 v55, v55, v214, 0
	v_pk_fma_f16 v54, v54, v213, 0
	v_pk_add_f16 v120, v120, v164 neg_lo:[0,1] neg_hi:[0,1]
	v_pk_add_f16 v121, v121, v165 neg_lo:[0,1] neg_hi:[0,1]
	v_pk_add_f16 v82, v82, v162 neg_lo:[0,1] neg_hi:[0,1]
	v_exp_f16_sdwa v213, v118 dst_sel:WORD_0 dst_unused:UNUSED_PAD src0_sel:WORD_0
	v_exp_f16_sdwa v214, v119 dst_sel:WORD_0 dst_unused:UNUSED_PAD src0_sel:WORD_0
	v_exp_f16_sdwa v215, v120 dst_sel:WORD_0 dst_unused:UNUSED_PAD src0_sel:WORD_0
	v_exp_f16_sdwa v216, v121 dst_sel:WORD_0 dst_unused:UNUSED_PAD src0_sel:WORD_0
	v_exp_f16_sdwa v213, v118 dst_sel:WORD_1 dst_unused:UNUSED_PRESERVE src0_sel:WORD_1
	v_exp_f16_sdwa v214, v119 dst_sel:WORD_1 dst_unused:UNUSED_PRESERVE src0_sel:WORD_1
	v_exp_f16_sdwa v215, v120 dst_sel:WORD_1 dst_unused:UNUSED_PRESERVE src0_sel:WORD_1
	v_exp_f16_sdwa v216, v121 dst_sel:WORD_1 dst_unused:UNUSED_PRESERVE src0_sel:WORD_1
	v_pk_add_f16 v83, v83, v163 neg_lo:[0,1] neg_hi:[0,1]
	v_pk_add_f16 v97, v97, v213
	v_pk_fma_f16 v57, v77, v216, v57
	v_pk_add_f16 v77, v126, v165 neg_lo:[0,1] neg_hi:[0,1]
	v_pk_add_f16 v96, v96, v214
	v_pk_add_f16 v95, v95, v215
	v_pk_add_f16 v94, v94, v216
	v_pk_fma_f16 v54, v74, v213, v54
	v_pk_fma_f16 v55, v75, v214, v55
	v_pk_fma_f16 v56, v76, v215, v56
	v_pk_add_f16 v74, v129, v162 neg_lo:[0,1] neg_hi:[0,1]
	v_pk_add_f16 v75, v128, v163 neg_lo:[0,1] neg_hi:[0,1]
	v_pk_add_f16 v76, v127, v164 neg_lo:[0,1] neg_hi:[0,1]
	v_pk_add_f16 v84, v84, v164 neg_lo:[0,1] neg_hi:[0,1]
	v_exp_f16_sdwa v118, v74 dst_sel:WORD_0 dst_unused:UNUSED_PAD src0_sel:WORD_0
	v_exp_f16_sdwa v119, v75 dst_sel:WORD_0 dst_unused:UNUSED_PAD src0_sel:WORD_0
	v_exp_f16_sdwa v120, v76 dst_sel:WORD_0 dst_unused:UNUSED_PAD src0_sel:WORD_0
	v_exp_f16_sdwa v121, v77 dst_sel:WORD_0 dst_unused:UNUSED_PAD src0_sel:WORD_0
	v_exp_f16_sdwa v118, v74 dst_sel:WORD_1 dst_unused:UNUSED_PRESERVE src0_sel:WORD_1
	v_exp_f16_sdwa v119, v75 dst_sel:WORD_1 dst_unused:UNUSED_PRESERVE src0_sel:WORD_1
	v_exp_f16_sdwa v120, v76 dst_sel:WORD_1 dst_unused:UNUSED_PRESERVE src0_sel:WORD_1
	v_exp_f16_sdwa v121, v77 dst_sel:WORD_1 dst_unused:UNUSED_PRESERVE src0_sel:WORD_1
	v_pk_add_f16 v85, v85, v165 neg_lo:[0,1] neg_hi:[0,1]
	v_pk_add_f16 v77, v97, v118
	v_pk_add_f16 v74, v94, v121
	v_pk_add_f16 v75, v95, v120
	v_pk_add_f16 v76, v96, v119
	v_pk_fma_f16 v57, v101, v121, v57
	v_pk_fma_f16 v56, v100, v120, v56
	v_pk_fma_f16 v55, v99, v119, v55
	v_pk_fma_f16 v54, v98, v118, v54
	v_pk_add_f16 v94, v137, v162 neg_lo:[0,1] neg_hi:[0,1]
	v_pk_add_f16 v95, v136, v163 neg_lo:[0,1] neg_hi:[0,1]
	v_pk_add_f16 v96, v135, v164 neg_lo:[0,1] neg_hi:[0,1]
	v_pk_add_f16 v97, v134, v165 neg_lo:[0,1] neg_hi:[0,1]
	v_exp_f16_sdwa v98, v94 dst_sel:WORD_0 dst_unused:UNUSED_PAD src0_sel:WORD_0
	v_exp_f16_sdwa v99, v95 dst_sel:WORD_0 dst_unused:UNUSED_PAD src0_sel:WORD_0
	v_exp_f16_sdwa v100, v96 dst_sel:WORD_0 dst_unused:UNUSED_PAD src0_sel:WORD_0
	v_exp_f16_sdwa v101, v97 dst_sel:WORD_0 dst_unused:UNUSED_PAD src0_sel:WORD_0
	v_exp_f16_sdwa v98, v94 dst_sel:WORD_1 dst_unused:UNUSED_PRESERVE src0_sel:WORD_1
	v_exp_f16_sdwa v99, v95 dst_sel:WORD_1 dst_unused:UNUSED_PRESERVE src0_sel:WORD_1
	v_exp_f16_sdwa v100, v96 dst_sel:WORD_1 dst_unused:UNUSED_PRESERVE src0_sel:WORD_1
	v_exp_f16_sdwa v101, v97 dst_sel:WORD_1 dst_unused:UNUSED_PRESERVE src0_sel:WORD_1
	v_pk_add_f16 v94, v149, v162 neg_lo:[0,1] neg_hi:[0,1]
	v_pk_add_f16 v77, v77, v98
	v_pk_add_f16 v76, v76, v99
	v_pk_add_f16 v75, v75, v100
	v_pk_add_f16 v74, v74, v101
	v_pk_fma_f16 v54, v30, v98, v54
	v_pk_fma_f16 v55, v31, v99, v55
	v_pk_fma_f16 v56, v32, v100, v56
	v_pk_fma_f16 v57, v33, v101, v57
	v_pk_add_f16 v95, v148, v163 neg_lo:[0,1] neg_hi:[0,1]
	v_pk_add_f16 v96, v147, v164 neg_lo:[0,1] neg_hi:[0,1]
	v_pk_add_f16 v97, v146, v165 neg_lo:[0,1] neg_hi:[0,1]
	v_exp_f16_sdwa v98, v94 dst_sel:WORD_0 dst_unused:UNUSED_PAD src0_sel:WORD_0
	v_exp_f16_sdwa v99, v95 dst_sel:WORD_0 dst_unused:UNUSED_PAD src0_sel:WORD_0
	v_exp_f16_sdwa v100, v96 dst_sel:WORD_0 dst_unused:UNUSED_PAD src0_sel:WORD_0
	v_exp_f16_sdwa v101, v97 dst_sel:WORD_0 dst_unused:UNUSED_PAD src0_sel:WORD_0
	v_exp_f16_sdwa v98, v94 dst_sel:WORD_1 dst_unused:UNUSED_PRESERVE src0_sel:WORD_1
	v_exp_f16_sdwa v99, v95 dst_sel:WORD_1 dst_unused:UNUSED_PRESERVE src0_sel:WORD_1
	v_exp_f16_sdwa v100, v96 dst_sel:WORD_1 dst_unused:UNUSED_PRESERVE src0_sel:WORD_1
	v_exp_f16_sdwa v101, v97 dst_sel:WORD_1 dst_unused:UNUSED_PRESERVE src0_sel:WORD_1
	v_pk_add_f16 v94, v212, v162 neg_lo:[0,1] neg_hi:[0,1]
	v_pk_add_f16 v77, v77, v98
	v_pk_add_f16 v74, v74, v101
	v_pk_add_f16 v75, v75, v100
	v_pk_add_f16 v76, v76, v99
	v_pk_fma_f16 v57, v45, v101, v57
	v_pk_fma_f16 v56, v44, v100, v56
	v_pk_fma_f16 v55, v43, v99, v55
	v_pk_fma_f16 v54, v42, v98, v54
	v_pk_add_f16 v95, v211, v163 neg_lo:[0,1] neg_hi:[0,1]
	v_pk_add_f16 v96, v210, v164 neg_lo:[0,1] neg_hi:[0,1]
	v_pk_add_f16 v97, v209, v165 neg_lo:[0,1] neg_hi:[0,1]
	v_exp_f16_sdwa v98, v94 dst_sel:WORD_0 dst_unused:UNUSED_PAD src0_sel:WORD_0
	v_exp_f16_sdwa v99, v95 dst_sel:WORD_0 dst_unused:UNUSED_PAD src0_sel:WORD_0
	v_exp_f16_sdwa v100, v96 dst_sel:WORD_0 dst_unused:UNUSED_PAD src0_sel:WORD_0
	v_exp_f16_sdwa v101, v97 dst_sel:WORD_0 dst_unused:UNUSED_PAD src0_sel:WORD_0
	v_exp_f16_sdwa v98, v94 dst_sel:WORD_1 dst_unused:UNUSED_PRESERVE src0_sel:WORD_1
	v_exp_f16_sdwa v99, v95 dst_sel:WORD_1 dst_unused:UNUSED_PRESERVE src0_sel:WORD_1
	v_exp_f16_sdwa v100, v96 dst_sel:WORD_1 dst_unused:UNUSED_PRESERVE src0_sel:WORD_1
	v_exp_f16_sdwa v101, v97 dst_sel:WORD_1 dst_unused:UNUSED_PRESERVE src0_sel:WORD_1
	v_exp_f16_sdwa v94, v82 dst_sel:WORD_0 dst_unused:UNUSED_PAD src0_sel:WORD_0
	v_exp_f16_sdwa v95, v83 dst_sel:WORD_0 dst_unused:UNUSED_PAD src0_sel:WORD_0
	v_exp_f16_sdwa v96, v84 dst_sel:WORD_0 dst_unused:UNUSED_PAD src0_sel:WORD_0
	v_exp_f16_sdwa v97, v85 dst_sel:WORD_0 dst_unused:UNUSED_PAD src0_sel:WORD_0
	v_exp_f16_sdwa v94, v82 dst_sel:WORD_1 dst_unused:UNUSED_PRESERVE src0_sel:WORD_1
	v_exp_f16_sdwa v95, v83 dst_sel:WORD_1 dst_unused:UNUSED_PRESERVE src0_sel:WORD_1
	v_exp_f16_sdwa v96, v84 dst_sel:WORD_1 dst_unused:UNUSED_PRESERVE src0_sel:WORD_1
	v_exp_f16_sdwa v97, v85 dst_sel:WORD_1 dst_unused:UNUSED_PRESERVE src0_sel:WORD_1
	v_pk_add_f16 v82, v106, v162 neg_lo:[0,1] neg_hi:[0,1]
	v_pk_add_f16 v77, v77, v98
	v_pk_add_f16 v76, v76, v99
	v_pk_add_f16 v75, v75, v100
	v_pk_add_f16 v74, v74, v101
	v_pk_fma_f16 v54, v58, v98, v54
	v_pk_fma_f16 v55, v59, v99, v55
	v_pk_fma_f16 v56, v60, v100, v56
	v_pk_fma_f16 v57, v61, v101, v57
	v_pk_add_f16 v77, v77, v94
	v_pk_add_f16 v74, v74, v97
	v_pk_add_f16 v75, v75, v96
	v_pk_add_f16 v76, v76, v95
	v_pk_fma_f16 v57, v21, v97, v57
	v_pk_fma_f16 v56, v20, v96, v56
	v_pk_fma_f16 v55, v19, v95, v55
	v_pk_fma_f16 v54, v18, v94, v54
	v_pk_add_f16 v83, v107, v163 neg_lo:[0,1] neg_hi:[0,1]
	v_pk_add_f16 v84, v108, v164 neg_lo:[0,1] neg_hi:[0,1]
	v_pk_add_f16 v85, v109, v165 neg_lo:[0,1] neg_hi:[0,1]
	v_exp_f16_sdwa v94, v82 dst_sel:WORD_0 dst_unused:UNUSED_PAD src0_sel:WORD_0
	v_exp_f16_sdwa v95, v83 dst_sel:WORD_0 dst_unused:UNUSED_PAD src0_sel:WORD_0
	v_exp_f16_sdwa v96, v84 dst_sel:WORD_0 dst_unused:UNUSED_PAD src0_sel:WORD_0
	v_exp_f16_sdwa v97, v85 dst_sel:WORD_0 dst_unused:UNUSED_PAD src0_sel:WORD_0
	v_exp_f16_sdwa v94, v82 dst_sel:WORD_1 dst_unused:UNUSED_PRESERVE src0_sel:WORD_1
	v_exp_f16_sdwa v95, v83 dst_sel:WORD_1 dst_unused:UNUSED_PRESERVE src0_sel:WORD_1
	v_exp_f16_sdwa v96, v84 dst_sel:WORD_1 dst_unused:UNUSED_PRESERVE src0_sel:WORD_1
	v_exp_f16_sdwa v97, v85 dst_sel:WORD_1 dst_unused:UNUSED_PRESERVE src0_sel:WORD_1
	v_pk_add_f16 v82, v122, v162 neg_lo:[0,1] neg_hi:[0,1]
	v_pk_add_f16 v77, v77, v94
	v_pk_add_f16 v76, v76, v95
	v_pk_add_f16 v75, v75, v96
	v_pk_add_f16 v74, v74, v97
	v_pk_fma_f16 v54, v22, v94, v54
	v_pk_fma_f16 v55, v23, v95, v55
	v_pk_fma_f16 v56, v24, v96, v56
	v_pk_fma_f16 v57, v25, v97, v57
	v_pk_add_f16 v83, v123, v163 neg_lo:[0,1] neg_hi:[0,1]
	v_pk_add_f16 v84, v124, v164 neg_lo:[0,1] neg_hi:[0,1]
	v_pk_add_f16 v85, v125, v165 neg_lo:[0,1] neg_hi:[0,1]
	v_exp_f16_sdwa v94, v82 dst_sel:WORD_0 dst_unused:UNUSED_PAD src0_sel:WORD_0
	v_exp_f16_sdwa v95, v83 dst_sel:WORD_0 dst_unused:UNUSED_PAD src0_sel:WORD_0
	v_exp_f16_sdwa v96, v84 dst_sel:WORD_0 dst_unused:UNUSED_PAD src0_sel:WORD_0
	v_exp_f16_sdwa v97, v85 dst_sel:WORD_0 dst_unused:UNUSED_PAD src0_sel:WORD_0
	v_exp_f16_sdwa v94, v82 dst_sel:WORD_1 dst_unused:UNUSED_PRESERVE src0_sel:WORD_1
	v_exp_f16_sdwa v95, v83 dst_sel:WORD_1 dst_unused:UNUSED_PRESERVE src0_sel:WORD_1
	v_exp_f16_sdwa v96, v84 dst_sel:WORD_1 dst_unused:UNUSED_PRESERVE src0_sel:WORD_1
	v_exp_f16_sdwa v97, v85 dst_sel:WORD_1 dst_unused:UNUSED_PRESERVE src0_sel:WORD_1
	v_pk_add_f16 v77, v77, v94
	v_pk_add_f16 v76, v76, v95
	v_rcp_f16_e32 v82, v77
	v_rcp_f16_sdwa v77, v77 dst_sel:DWORD dst_unused:UNUSED_PAD src0_sel:WORD_1
	v_pk_add_f16 v75, v75, v96
	v_rcp_f16_e32 v83, v76
	v_rcp_f16_sdwa v76, v76 dst_sel:DWORD dst_unused:UNUSED_PAD src0_sel:WORD_1
	v_pk_add_f16 v74, v74, v97
	v_rcp_f16_e32 v84, v75
	v_rcp_f16_sdwa v75, v75 dst_sel:DWORD dst_unused:UNUSED_PAD src0_sel:WORD_1
	v_rcp_f16_e32 v85, v74
	v_rcp_f16_sdwa v74, v74 dst_sel:DWORD dst_unused:UNUSED_PAD src0_sel:WORD_1
	v_pk_fma_f16 v54, v26, v94, v54
	v_pack_b32_f16 v77, v82, v77
	v_pk_fma_f16 v57, v29, v97, v57
	v_pk_fma_f16 v55, v27, v95, v55
	v_pk_mul_f16 v97, v54, v77
	v_pack_b32_f16 v54, v83, v76
	v_pk_fma_f16 v56, v28, v96, v56
	v_pk_mul_f16 v96, v55, v54
	v_pack_b32_f16 v54, v84, v75
	v_pk_mul_f16 v95, v56, v54
	v_pack_b32_f16 v54, v85, v74
	v_pk_mul_f16 v94, v57, v54
	s_waitcnt vmcnt(6)
	v_pk_mul_f16 v57, v208, v161 op_sel_hi:[0,1]
	v_pk_mul_f16 v77, v206, v161 op_sel_hi:[0,1]
	v_pk_mul_f16 v85, v207, v161 op_sel_hi:[0,1]
	v_pk_mul_f16 v54, v208, v158 op_sel_hi:[0,1]
	v_pk_mul_f16 v55, v208, v159 op_sel_hi:[0,1]
	v_pk_mul_f16 v56, v208, v160 op_sel_hi:[0,1]
	v_pk_mul_f16 v74, v206, v158 op_sel_hi:[0,1]
	v_pk_mul_f16 v75, v206, v159 op_sel_hi:[0,1]
	v_pk_mul_f16 v76, v206, v160 op_sel_hi:[0,1]
	v_pk_mul_f16 v82, v207, v158 op_sel_hi:[0,1]
	v_pk_mul_f16 v83, v207, v159 op_sel_hi:[0,1]
	v_pk_mul_f16 v84, v207, v160 op_sel_hi:[0,1]
	v_pk_fma_f16 v65, v65, v161, v57
	v_pk_fma_f16 v81, v81, v161, v77
	v_pk_fma_f16 v98, v105, v161, v85
	v_pk_fma_f16 v64, v64, v160, v56
	v_pk_maximum3_f16 v125, v65, v81, v98
	v_pk_fma_f16 v63, v63, v159, v55
	v_pk_fma_f16 v62, v62, v158, v54
	v_pk_fma_f16 v80, v80, v160, v76
	v_pk_fma_f16 v79, v79, v159, v75
	v_pk_fma_f16 v78, v78, v158, v74
	v_pk_fma_f16 v99, v104, v160, v84
	v_pk_fma_f16 v100, v103, v159, v83
	v_pk_fma_f16 v101, v102, v158, v82
	v_pk_fma_f16 v102, v37, v161, v57
	v_pk_fma_f16 v106, v49, v161, v77
	v_pk_fma_f16 v118, v69, v161, v85
	v_pk_fma_f16 v57, v89, v161, v57
	v_pk_fma_f16 v77, v117, v161, v77
	v_pk_fma_f16 v85, v133, v161, v85
	v_pk_maximum3_f16 v122, v62, v78, v101
	v_pk_maximum3_f16 v123, v63, v79, v100
	v_pk_maximum3_f16 v124, v64, v80, v99
	v_pk_maximum3_f16 v129, v102, v106, v118
	v_pk_fma_f16 v103, v36, v160, v56
	v_pk_maximum3_f16 v137, v57, v77, v85
	v_pk_fma_f16 v104, v35, v159, v55
	v_pk_maximum3_f16 v125, v125, v129, v137
	v_pk_fma_f16 v105, v34, v158, v54
	v_pk_fma_f16 v107, v48, v160, v76
	v_pk_fma_f16 v108, v47, v159, v75
	v_pk_fma_f16 v109, v46, v158, v74
	v_pk_fma_f16 v119, v68, v160, v84
	v_pk_fma_f16 v120, v67, v159, v83
	v_pk_fma_f16 v121, v66, v158, v82
	v_pk_fma_f16 v56, v88, v160, v56
	v_pk_fma_f16 v55, v87, v159, v55
	v_pk_fma_f16 v54, v86, v158, v54
	v_pk_fma_f16 v76, v116, v160, v76
	v_pk_fma_f16 v75, v115, v159, v75
	v_pk_fma_f16 v74, v114, v158, v74
	v_pk_fma_f16 v84, v132, v160, v84
	v_pk_fma_f16 v83, v131, v159, v83
	v_pk_fma_f16 v82, v130, v158, v82
	v_pk_maximum3_f16 v126, v105, v109, v121
	v_pk_maximum3_f16 v127, v104, v108, v120
	v_pk_maximum3_f16 v128, v103, v107, v119
	v_pk_maximum3_f16 v135, v55, v75, v83
	v_pk_maximum3_f16 v136, v56, v76, v84
	v_pk_maximum3_f16 v134, v54, v74, v82
	v_pk_maximum3_f16 v122, v122, v126, v134
	v_pk_maximum3_f16 v123, v123, v127, v135
	v_pk_maximum3_f16 v124, v124, v128, v136
	v_pk_add_f16 v65, v65, v125 neg_lo:[0,1] neg_hi:[0,1]
	v_pk_add_f16 v62, v62, v122 neg_lo:[0,1] neg_hi:[0,1]
	v_pk_add_f16 v63, v63, v123 neg_lo:[0,1] neg_hi:[0,1]
	v_pk_add_f16 v64, v64, v124 neg_lo:[0,1] neg_hi:[0,1]
	v_pk_add_f16 v78, v78, v122 neg_lo:[0,1] neg_hi:[0,1]
	v_exp_f16_sdwa v126, v62 dst_sel:WORD_0 dst_unused:UNUSED_PAD src0_sel:WORD_0
	v_exp_f16_sdwa v127, v63 dst_sel:WORD_0 dst_unused:UNUSED_PAD src0_sel:WORD_0
	v_exp_f16_sdwa v128, v64 dst_sel:WORD_0 dst_unused:UNUSED_PAD src0_sel:WORD_0
	v_exp_f16_sdwa v129, v65 dst_sel:WORD_0 dst_unused:UNUSED_PAD src0_sel:WORD_0
	v_exp_f16_sdwa v126, v62 dst_sel:WORD_1 dst_unused:UNUSED_PRESERVE src0_sel:WORD_1
	v_exp_f16_sdwa v127, v63 dst_sel:WORD_1 dst_unused:UNUSED_PRESERVE src0_sel:WORD_1
	v_exp_f16_sdwa v128, v64 dst_sel:WORD_1 dst_unused:UNUSED_PRESERVE src0_sel:WORD_1
	v_exp_f16_sdwa v129, v65 dst_sel:WORD_1 dst_unused:UNUSED_PRESERVE src0_sel:WORD_1
	v_pk_add_f16 v79, v79, v123 neg_lo:[0,1] neg_hi:[0,1]
	v_pk_add_f16 v65, v126, 0
	v_pk_fma_f16 v33, v33, v129, 0
	v_pk_add_f16 v62, v129, 0
	v_pk_add_f16 v63, v128, 0
	v_pk_add_f16 v64, v127, 0
	v_pk_fma_f16 v32, v32, v128, 0
	v_pk_fma_f16 v31, v31, v127, 0
	v_pk_fma_f16 v30, v30, v126, 0
	v_pk_add_f16 v80, v80, v124 neg_lo:[0,1] neg_hi:[0,1]
	v_pk_add_f16 v81, v81, v125 neg_lo:[0,1] neg_hi:[0,1]
	v_pk_add_f16 v54, v54, v122 neg_lo:[0,1] neg_hi:[0,1]
	v_exp_f16_sdwa v126, v78 dst_sel:WORD_0 dst_unused:UNUSED_PAD src0_sel:WORD_0
	v_exp_f16_sdwa v127, v79 dst_sel:WORD_0 dst_unused:UNUSED_PAD src0_sel:WORD_0
	v_exp_f16_sdwa v128, v80 dst_sel:WORD_0 dst_unused:UNUSED_PAD src0_sel:WORD_0
	v_exp_f16_sdwa v129, v81 dst_sel:WORD_0 dst_unused:UNUSED_PAD src0_sel:WORD_0
	v_exp_f16_sdwa v126, v78 dst_sel:WORD_1 dst_unused:UNUSED_PRESERVE src0_sel:WORD_1
	v_exp_f16_sdwa v127, v79 dst_sel:WORD_1 dst_unused:UNUSED_PRESERVE src0_sel:WORD_1
	v_exp_f16_sdwa v128, v80 dst_sel:WORD_1 dst_unused:UNUSED_PRESERVE src0_sel:WORD_1
	v_exp_f16_sdwa v129, v81 dst_sel:WORD_1 dst_unused:UNUSED_PRESERVE src0_sel:WORD_1
	v_pk_add_f16 v55, v55, v123 neg_lo:[0,1] neg_hi:[0,1]
	v_pk_add_f16 v65, v65, v126
	v_pk_fma_f16 v33, v45, v129, v33
	v_pk_add_f16 v45, v98, v125 neg_lo:[0,1] neg_hi:[0,1]
	v_pk_add_f16 v64, v64, v127
	v_pk_add_f16 v63, v63, v128
	v_pk_add_f16 v62, v62, v129
	v_pk_fma_f16 v30, v42, v126, v30
	v_pk_fma_f16 v31, v43, v127, v31
	v_pk_fma_f16 v32, v44, v128, v32
	v_pk_add_f16 v42, v101, v122 neg_lo:[0,1] neg_hi:[0,1]
	v_pk_add_f16 v43, v100, v123 neg_lo:[0,1] neg_hi:[0,1]
	v_pk_add_f16 v44, v99, v124 neg_lo:[0,1] neg_hi:[0,1]
	v_pk_add_f16 v56, v56, v124 neg_lo:[0,1] neg_hi:[0,1]
	v_exp_f16_sdwa v78, v42 dst_sel:WORD_0 dst_unused:UNUSED_PAD src0_sel:WORD_0
	v_exp_f16_sdwa v79, v43 dst_sel:WORD_0 dst_unused:UNUSED_PAD src0_sel:WORD_0
	v_exp_f16_sdwa v80, v44 dst_sel:WORD_0 dst_unused:UNUSED_PAD src0_sel:WORD_0
	v_exp_f16_sdwa v81, v45 dst_sel:WORD_0 dst_unused:UNUSED_PAD src0_sel:WORD_0
	v_exp_f16_sdwa v78, v42 dst_sel:WORD_1 dst_unused:UNUSED_PRESERVE src0_sel:WORD_1
	v_exp_f16_sdwa v79, v43 dst_sel:WORD_1 dst_unused:UNUSED_PRESERVE src0_sel:WORD_1
	v_exp_f16_sdwa v80, v44 dst_sel:WORD_1 dst_unused:UNUSED_PRESERVE src0_sel:WORD_1
	v_exp_f16_sdwa v81, v45 dst_sel:WORD_1 dst_unused:UNUSED_PRESERVE src0_sel:WORD_1
	v_pk_add_f16 v57, v57, v125 neg_lo:[0,1] neg_hi:[0,1]
	v_pk_add_f16 v45, v65, v78
	v_pk_add_f16 v42, v62, v81
	v_pk_add_f16 v43, v63, v80
	v_pk_add_f16 v44, v64, v79
	v_pk_fma_f16 v33, v61, v81, v33
	v_pk_fma_f16 v32, v60, v80, v32
	v_pk_fma_f16 v31, v59, v79, v31
	v_pk_fma_f16 v30, v58, v78, v30
	v_pk_add_f16 v58, v105, v122 neg_lo:[0,1] neg_hi:[0,1]
	v_pk_add_f16 v59, v104, v123 neg_lo:[0,1] neg_hi:[0,1]
	v_pk_add_f16 v60, v103, v124 neg_lo:[0,1] neg_hi:[0,1]
	v_pk_add_f16 v61, v102, v125 neg_lo:[0,1] neg_hi:[0,1]
	v_exp_f16_sdwa v62, v58 dst_sel:WORD_0 dst_unused:UNUSED_PAD src0_sel:WORD_0
	v_exp_f16_sdwa v63, v59 dst_sel:WORD_0 dst_unused:UNUSED_PAD src0_sel:WORD_0
	v_exp_f16_sdwa v64, v60 dst_sel:WORD_0 dst_unused:UNUSED_PAD src0_sel:WORD_0
	v_exp_f16_sdwa v65, v61 dst_sel:WORD_0 dst_unused:UNUSED_PAD src0_sel:WORD_0
	v_exp_f16_sdwa v62, v58 dst_sel:WORD_1 dst_unused:UNUSED_PRESERVE src0_sel:WORD_1
	v_exp_f16_sdwa v63, v59 dst_sel:WORD_1 dst_unused:UNUSED_PRESERVE src0_sel:WORD_1
	v_exp_f16_sdwa v64, v60 dst_sel:WORD_1 dst_unused:UNUSED_PRESERVE src0_sel:WORD_1
	v_exp_f16_sdwa v65, v61 dst_sel:WORD_1 dst_unused:UNUSED_PRESERVE src0_sel:WORD_1
	v_pk_add_f16 v58, v109, v122 neg_lo:[0,1] neg_hi:[0,1]
	v_pk_add_f16 v45, v45, v62
	v_pk_add_f16 v44, v44, v63
	v_pk_add_f16 v43, v43, v64
	v_pk_add_f16 v42, v42, v65
	v_pk_fma_f16 v30, v18, v62, v30
	v_pk_fma_f16 v31, v19, v63, v31
	v_pk_fma_f16 v32, v20, v64, v32
	v_pk_fma_f16 v33, v21, v65, v33
	v_pk_add_f16 v59, v108, v123 neg_lo:[0,1] neg_hi:[0,1]
	v_pk_add_f16 v60, v107, v124 neg_lo:[0,1] neg_hi:[0,1]
	v_pk_add_f16 v61, v106, v125 neg_lo:[0,1] neg_hi:[0,1]
	v_exp_f16_sdwa v62, v58 dst_sel:WORD_0 dst_unused:UNUSED_PAD src0_sel:WORD_0
	v_exp_f16_sdwa v63, v59 dst_sel:WORD_0 dst_unused:UNUSED_PAD src0_sel:WORD_0
	v_exp_f16_sdwa v64, v60 dst_sel:WORD_0 dst_unused:UNUSED_PAD src0_sel:WORD_0
	v_exp_f16_sdwa v65, v61 dst_sel:WORD_0 dst_unused:UNUSED_PAD src0_sel:WORD_0
	v_exp_f16_sdwa v62, v58 dst_sel:WORD_1 dst_unused:UNUSED_PRESERVE src0_sel:WORD_1
	v_exp_f16_sdwa v63, v59 dst_sel:WORD_1 dst_unused:UNUSED_PRESERVE src0_sel:WORD_1
	v_exp_f16_sdwa v64, v60 dst_sel:WORD_1 dst_unused:UNUSED_PRESERVE src0_sel:WORD_1
	v_exp_f16_sdwa v65, v61 dst_sel:WORD_1 dst_unused:UNUSED_PRESERVE src0_sel:WORD_1
	v_pk_add_f16 v58, v121, v122 neg_lo:[0,1] neg_hi:[0,1]
	v_pk_add_f16 v45, v45, v62
	v_pk_add_f16 v42, v42, v65
	v_pk_add_f16 v43, v43, v64
	v_pk_add_f16 v44, v44, v63
	v_pk_fma_f16 v33, v25, v65, v33
	v_pk_fma_f16 v32, v24, v64, v32
	v_pk_fma_f16 v31, v23, v63, v31
	v_pk_fma_f16 v30, v22, v62, v30
	v_pk_add_f16 v59, v120, v123 neg_lo:[0,1] neg_hi:[0,1]
	v_pk_add_f16 v60, v119, v124 neg_lo:[0,1] neg_hi:[0,1]
	v_pk_add_f16 v61, v118, v125 neg_lo:[0,1] neg_hi:[0,1]
	v_exp_f16_sdwa v62, v58 dst_sel:WORD_0 dst_unused:UNUSED_PAD src0_sel:WORD_0
	v_exp_f16_sdwa v63, v59 dst_sel:WORD_0 dst_unused:UNUSED_PAD src0_sel:WORD_0
	v_exp_f16_sdwa v64, v60 dst_sel:WORD_0 dst_unused:UNUSED_PAD src0_sel:WORD_0
	v_exp_f16_sdwa v65, v61 dst_sel:WORD_0 dst_unused:UNUSED_PAD src0_sel:WORD_0
	v_exp_f16_sdwa v62, v58 dst_sel:WORD_1 dst_unused:UNUSED_PRESERVE src0_sel:WORD_1
	v_exp_f16_sdwa v63, v59 dst_sel:WORD_1 dst_unused:UNUSED_PRESERVE src0_sel:WORD_1
	v_exp_f16_sdwa v64, v60 dst_sel:WORD_1 dst_unused:UNUSED_PRESERVE src0_sel:WORD_1
	v_exp_f16_sdwa v65, v61 dst_sel:WORD_1 dst_unused:UNUSED_PRESERVE src0_sel:WORD_1
	v_exp_f16_sdwa v58, v54 dst_sel:WORD_0 dst_unused:UNUSED_PAD src0_sel:WORD_0
	v_exp_f16_sdwa v59, v55 dst_sel:WORD_0 dst_unused:UNUSED_PAD src0_sel:WORD_0
	v_exp_f16_sdwa v60, v56 dst_sel:WORD_0 dst_unused:UNUSED_PAD src0_sel:WORD_0
	v_exp_f16_sdwa v61, v57 dst_sel:WORD_0 dst_unused:UNUSED_PAD src0_sel:WORD_0
	v_exp_f16_sdwa v58, v54 dst_sel:WORD_1 dst_unused:UNUSED_PRESERVE src0_sel:WORD_1
	v_exp_f16_sdwa v59, v55 dst_sel:WORD_1 dst_unused:UNUSED_PRESERVE src0_sel:WORD_1
	v_exp_f16_sdwa v60, v56 dst_sel:WORD_1 dst_unused:UNUSED_PRESERVE src0_sel:WORD_1
	v_exp_f16_sdwa v61, v57 dst_sel:WORD_1 dst_unused:UNUSED_PRESERVE src0_sel:WORD_1
	v_pk_add_f16 v54, v74, v122 neg_lo:[0,1] neg_hi:[0,1]
	v_pk_add_f16 v45, v45, v62
	v_pk_add_f16 v44, v44, v63
	v_pk_add_f16 v43, v43, v64
	v_pk_add_f16 v42, v42, v65
	v_pk_fma_f16 v30, v26, v62, v30
	v_pk_fma_f16 v31, v27, v63, v31
	v_pk_fma_f16 v32, v28, v64, v32
	v_pk_fma_f16 v33, v29, v65, v33
	v_pk_add_f16 v45, v45, v58
	v_pk_add_f16 v42, v42, v61
	v_pk_add_f16 v43, v43, v60
	v_pk_add_f16 v44, v44, v59
	v_pk_fma_f16 v33, v41, v61, v33
	v_pk_fma_f16 v32, v40, v60, v32
	v_pk_fma_f16 v31, v39, v59, v31
	v_pk_fma_f16 v30, v38, v58, v30
	v_pk_add_f16 v55, v75, v123 neg_lo:[0,1] neg_hi:[0,1]
	v_pk_add_f16 v56, v76, v124 neg_lo:[0,1] neg_hi:[0,1]
	v_pk_add_f16 v57, v77, v125 neg_lo:[0,1] neg_hi:[0,1]
	v_exp_f16_sdwa v58, v54 dst_sel:WORD_0 dst_unused:UNUSED_PAD src0_sel:WORD_0
	v_exp_f16_sdwa v59, v55 dst_sel:WORD_0 dst_unused:UNUSED_PAD src0_sel:WORD_0
	v_exp_f16_sdwa v60, v56 dst_sel:WORD_0 dst_unused:UNUSED_PAD src0_sel:WORD_0
	v_exp_f16_sdwa v61, v57 dst_sel:WORD_0 dst_unused:UNUSED_PAD src0_sel:WORD_0
	v_exp_f16_sdwa v58, v54 dst_sel:WORD_1 dst_unused:UNUSED_PRESERVE src0_sel:WORD_1
	v_exp_f16_sdwa v59, v55 dst_sel:WORD_1 dst_unused:UNUSED_PRESERVE src0_sel:WORD_1
	v_exp_f16_sdwa v60, v56 dst_sel:WORD_1 dst_unused:UNUSED_PRESERVE src0_sel:WORD_1
	v_exp_f16_sdwa v61, v57 dst_sel:WORD_1 dst_unused:UNUSED_PRESERVE src0_sel:WORD_1
	v_pk_add_f16 v54, v82, v122 neg_lo:[0,1] neg_hi:[0,1]
	v_pk_add_f16 v45, v45, v58
	v_pk_add_f16 v44, v44, v59
	v_pk_add_f16 v43, v43, v60
	v_pk_add_f16 v42, v42, v61
	v_pk_fma_f16 v30, v50, v58, v30
	v_pk_fma_f16 v31, v51, v59, v31
	v_pk_fma_f16 v32, v52, v60, v32
	v_pk_fma_f16 v33, v53, v61, v33
	v_pk_add_f16 v55, v83, v123 neg_lo:[0,1] neg_hi:[0,1]
	v_pk_add_f16 v56, v84, v124 neg_lo:[0,1] neg_hi:[0,1]
	v_pk_add_f16 v57, v85, v125 neg_lo:[0,1] neg_hi:[0,1]
	v_exp_f16_sdwa v58, v54 dst_sel:WORD_0 dst_unused:UNUSED_PAD src0_sel:WORD_0
	v_exp_f16_sdwa v59, v55 dst_sel:WORD_0 dst_unused:UNUSED_PAD src0_sel:WORD_0
	v_exp_f16_sdwa v60, v56 dst_sel:WORD_0 dst_unused:UNUSED_PAD src0_sel:WORD_0
	v_exp_f16_sdwa v61, v57 dst_sel:WORD_0 dst_unused:UNUSED_PAD src0_sel:WORD_0
	v_exp_f16_sdwa v58, v54 dst_sel:WORD_1 dst_unused:UNUSED_PRESERVE src0_sel:WORD_1
	v_exp_f16_sdwa v59, v55 dst_sel:WORD_1 dst_unused:UNUSED_PRESERVE src0_sel:WORD_1
	v_exp_f16_sdwa v60, v56 dst_sel:WORD_1 dst_unused:UNUSED_PRESERVE src0_sel:WORD_1
	v_exp_f16_sdwa v61, v57 dst_sel:WORD_1 dst_unused:UNUSED_PRESERVE src0_sel:WORD_1
	v_pk_add_f16 v45, v45, v58
	v_pk_add_f16 v44, v44, v59
	v_rcp_f16_e32 v54, v45
	v_rcp_f16_sdwa v45, v45 dst_sel:DWORD dst_unused:UNUSED_PAD src0_sel:WORD_1
	v_pk_add_f16 v43, v43, v60
	v_rcp_f16_e32 v55, v44
	v_rcp_f16_sdwa v44, v44 dst_sel:DWORD dst_unused:UNUSED_PAD src0_sel:WORD_1
	v_pk_add_f16 v42, v42, v61
	v_rcp_f16_e32 v56, v43
	v_rcp_f16_sdwa v43, v43 dst_sel:DWORD dst_unused:UNUSED_PAD src0_sel:WORD_1
	v_rcp_f16_e32 v57, v42
	v_rcp_f16_sdwa v42, v42 dst_sel:DWORD dst_unused:UNUSED_PAD src0_sel:WORD_1
	v_pk_fma_f16 v30, v70, v58, v30
	v_pack_b32_f16 v45, v54, v45
	v_pk_fma_f16 v31, v71, v59, v31
	v_pk_mul_f16 v45, v30, v45
	v_pack_b32_f16 v30, v55, v44
	v_pk_fma_f16 v32, v72, v60, v32
	v_pk_mul_f16 v44, v31, v30
	v_pack_b32_f16 v30, v56, v43
	v_pk_fma_f16 v33, v73, v61, v33
	v_pk_mul_f16 v43, v32, v30
	v_pack_b32_f16 v30, v57, v42
	v_pk_mul_f16 v42, v33, v30
	s_waitcnt vmcnt(0)
	v_pk_mul_f16 v30, v208, v154 op_sel_hi:[0,1]
	v_pk_mul_f16 v31, v208, v155 op_sel_hi:[0,1]
	v_pk_mul_f16 v32, v208, v156 op_sel_hi:[0,1]
	v_pk_mul_f16 v33, v208, v157 op_sel_hi:[0,1]
	v_pk_mul_f16 v54, v206, v154 op_sel_hi:[0,1]
	v_pk_mul_f16 v55, v206, v155 op_sel_hi:[0,1]
	v_pk_mul_f16 v56, v206, v156 op_sel_hi:[0,1]
	v_pk_mul_f16 v57, v206, v157 op_sel_hi:[0,1]
	v_pk_mul_f16 v58, v207, v154 op_sel_hi:[0,1]
	v_pk_mul_f16 v59, v207, v155 op_sel_hi:[0,1]
	v_pk_mul_f16 v60, v207, v156 op_sel_hi:[0,1]
	v_pk_mul_f16 v61, v207, v157 op_sel_hi:[0,1]
	v_pk_fma_f16 v37, v37, v157, v33
	v_pk_fma_f16 v36, v36, v156, v32
	v_pk_fma_f16 v35, v35, v155, v31
	v_pk_fma_f16 v34, v34, v154, v30
	v_pk_fma_f16 v49, v49, v157, v57
	v_pk_fma_f16 v48, v48, v156, v56
	v_pk_fma_f16 v47, v47, v155, v55
	v_pk_fma_f16 v46, v46, v154, v54
	v_pk_fma_f16 v62, v69, v157, v61
	v_pk_fma_f16 v63, v68, v156, v60
	v_pk_fma_f16 v64, v67, v155, v59
	v_pk_fma_f16 v65, v66, v154, v58
	v_pk_fma_f16 v66, v89, v157, v33
	v_pk_fma_f16 v67, v88, v156, v32
	v_pk_fma_f16 v68, v87, v155, v31
	v_pk_fma_f16 v69, v86, v154, v30
	v_pk_fma_f16 v74, v117, v157, v57
	v_pk_fma_f16 v75, v116, v156, v56
	v_pk_fma_f16 v76, v115, v155, v55
	v_pk_fma_f16 v77, v114, v154, v54
	v_pk_fma_f16 v78, v133, v157, v61
	v_pk_fma_f16 v79, v132, v156, v60
	v_pk_fma_f16 v80, v131, v155, v59
	v_pk_fma_f16 v81, v130, v154, v58
	v_pk_fma_f16 v61, v17, v157, v61
	v_pk_fma_f16 v60, v16, v156, v60
	v_pk_fma_f16 v59, v15, v155, v59
	v_pk_fma_f16 v58, v14, v154, v58
	v_pk_maximum3_f16 v14, v34, v46, v65
	v_pk_maximum3_f16 v15, v35, v47, v64
	v_pk_maximum3_f16 v16, v36, v48, v63
	v_pk_maximum3_f16 v17, v37, v49, v62
	v_pk_maximum3_f16 v82, v69, v77, v81
	v_pk_maximum3_f16 v83, v68, v76, v80
	v_pk_maximum3_f16 v84, v67, v75, v79
	v_pk_maximum3_f16 v85, v66, v74, v78
	v_pk_fma_f16 v33, v145, v157, v33
	v_pk_fma_f16 v32, v144, v156, v32
	v_pk_fma_f16 v31, v143, v155, v31
	v_pk_fma_f16 v30, v142, v154, v30
	v_pk_fma_f16 v57, v153, v157, v57
	v_pk_fma_f16 v56, v152, v156, v56
	v_pk_fma_f16 v55, v151, v155, v55
	v_pk_fma_f16 v54, v150, v154, v54
	v_pk_maximum3_f16 v87, v31, v55, v59
	v_pk_maximum3_f16 v88, v32, v56, v60
	v_pk_maximum3_f16 v89, v33, v57, v61
	v_pk_maximum3_f16 v86, v30, v54, v58
	v_pk_maximum3_f16 v15, v15, v83, v87
	v_pk_maximum3_f16 v16, v16, v84, v88
	v_pk_maximum3_f16 v17, v17, v85, v89
	v_pk_maximum3_f16 v14, v14, v82, v86
	v_xor_b32_e32 v82, 0x80008000, v17
	v_xor_b32_e32 v83, 0x80008000, v16
	v_xor_b32_e32 v84, 0x80008000, v15
	v_xor_b32_e32 v85, 0x80008000, v14
	v_pk_add_f16 v14, v34, v85
	v_pk_add_f16 v15, v35, v84
	v_pk_add_f16 v16, v36, v83
	v_pk_add_f16 v17, v37, v82
	v_exp_f16_sdwa v34, v14 dst_sel:WORD_0 dst_unused:UNUSED_PAD src0_sel:WORD_0
	v_exp_f16_sdwa v35, v15 dst_sel:WORD_0 dst_unused:UNUSED_PAD src0_sel:WORD_0
	v_exp_f16_sdwa v36, v16 dst_sel:WORD_0 dst_unused:UNUSED_PAD src0_sel:WORD_0
	v_exp_f16_sdwa v37, v17 dst_sel:WORD_0 dst_unused:UNUSED_PAD src0_sel:WORD_0
	v_exp_f16_sdwa v34, v14 dst_sel:WORD_1 dst_unused:UNUSED_PRESERVE src0_sel:WORD_1
	v_exp_f16_sdwa v35, v15 dst_sel:WORD_1 dst_unused:UNUSED_PRESERVE src0_sel:WORD_1
	v_exp_f16_sdwa v36, v16 dst_sel:WORD_1 dst_unused:UNUSED_PRESERVE src0_sel:WORD_1
	v_exp_f16_sdwa v37, v17 dst_sel:WORD_1 dst_unused:UNUSED_PRESERVE src0_sel:WORD_1
	v_pk_add_f16 v14, v34, 0
	v_pk_add_f16 v15, v35, 0
	v_pk_add_f16 v16, v36, 0
	v_pk_add_f16 v17, v37, 0
	v_pk_fma_f16 v18, v18, v34, 0
	v_pk_fma_f16 v19, v19, v35, 0
	v_pk_fma_f16 v20, v20, v36, 0
	v_pk_fma_f16 v21, v21, v37, 0
	v_pk_add_f16 v34, v46, v85
	v_pk_add_f16 v35, v47, v84
	v_pk_add_f16 v36, v48, v83
	v_pk_add_f16 v37, v49, v82
	v_exp_f16_sdwa v46, v34 dst_sel:WORD_0 dst_unused:UNUSED_PAD src0_sel:WORD_0
	v_exp_f16_sdwa v47, v35 dst_sel:WORD_0 dst_unused:UNUSED_PAD src0_sel:WORD_0
	v_exp_f16_sdwa v48, v36 dst_sel:WORD_0 dst_unused:UNUSED_PAD src0_sel:WORD_0
	v_exp_f16_sdwa v49, v37 dst_sel:WORD_0 dst_unused:UNUSED_PAD src0_sel:WORD_0
	v_exp_f16_sdwa v46, v34 dst_sel:WORD_1 dst_unused:UNUSED_PRESERVE src0_sel:WORD_1
	v_exp_f16_sdwa v47, v35 dst_sel:WORD_1 dst_unused:UNUSED_PRESERVE src0_sel:WORD_1
	v_exp_f16_sdwa v48, v36 dst_sel:WORD_1 dst_unused:UNUSED_PRESERVE src0_sel:WORD_1
	v_exp_f16_sdwa v49, v37 dst_sel:WORD_1 dst_unused:UNUSED_PRESERVE src0_sel:WORD_1
	s_nop 0
	v_pk_add_f16 v17, v17, v49
	v_pk_add_f16 v16, v16, v48
	v_pk_add_f16 v15, v15, v47
	v_pk_add_f16 v14, v14, v46
	v_pk_fma_f16 v21, v25, v49, v21
	v_pk_fma_f16 v20, v24, v48, v20
	v_pk_fma_f16 v19, v23, v47, v19
	v_pk_fma_f16 v18, v22, v46, v18
	v_pk_add_f16 v22, v65, v85
	v_pk_add_f16 v23, v64, v84
	v_pk_add_f16 v24, v63, v83
	v_pk_add_f16 v25, v62, v82
	v_exp_f16_sdwa v34, v22 dst_sel:WORD_0 dst_unused:UNUSED_PAD src0_sel:WORD_0
	v_exp_f16_sdwa v35, v23 dst_sel:WORD_0 dst_unused:UNUSED_PAD src0_sel:WORD_0
	v_exp_f16_sdwa v36, v24 dst_sel:WORD_0 dst_unused:UNUSED_PAD src0_sel:WORD_0
	v_exp_f16_sdwa v37, v25 dst_sel:WORD_0 dst_unused:UNUSED_PAD src0_sel:WORD_0
	v_exp_f16_sdwa v34, v22 dst_sel:WORD_1 dst_unused:UNUSED_PRESERVE src0_sel:WORD_1
	v_exp_f16_sdwa v35, v23 dst_sel:WORD_1 dst_unused:UNUSED_PRESERVE src0_sel:WORD_1
	v_exp_f16_sdwa v36, v24 dst_sel:WORD_1 dst_unused:UNUSED_PRESERVE src0_sel:WORD_1
	v_exp_f16_sdwa v37, v25 dst_sel:WORD_1 dst_unused:UNUSED_PRESERVE src0_sel:WORD_1
	v_pk_add_f16 v22, v69, v85
	v_pk_add_f16 v14, v14, v34
	v_pk_add_f16 v15, v15, v35
	v_pk_add_f16 v16, v16, v36
	v_pk_add_f16 v17, v17, v37
	v_pk_fma_f16 v18, v26, v34, v18
	v_pk_fma_f16 v19, v27, v35, v19
	v_pk_fma_f16 v20, v28, v36, v20
	v_pk_fma_f16 v21, v29, v37, v21
	v_pk_add_f16 v23, v68, v84
	v_pk_add_f16 v24, v67, v83
	v_pk_add_f16 v25, v66, v82
	v_exp_f16_sdwa v26, v22 dst_sel:WORD_0 dst_unused:UNUSED_PAD src0_sel:WORD_0
	v_exp_f16_sdwa v27, v23 dst_sel:WORD_0 dst_unused:UNUSED_PAD src0_sel:WORD_0
	v_exp_f16_sdwa v28, v24 dst_sel:WORD_0 dst_unused:UNUSED_PAD src0_sel:WORD_0
	v_exp_f16_sdwa v29, v25 dst_sel:WORD_0 dst_unused:UNUSED_PAD src0_sel:WORD_0
	v_exp_f16_sdwa v26, v22 dst_sel:WORD_1 dst_unused:UNUSED_PRESERVE src0_sel:WORD_1
	v_exp_f16_sdwa v27, v23 dst_sel:WORD_1 dst_unused:UNUSED_PRESERVE src0_sel:WORD_1
	v_exp_f16_sdwa v28, v24 dst_sel:WORD_1 dst_unused:UNUSED_PRESERVE src0_sel:WORD_1
	v_exp_f16_sdwa v29, v25 dst_sel:WORD_1 dst_unused:UNUSED_PRESERVE src0_sel:WORD_1
	v_pk_add_f16 v22, v77, v85
	v_pk_add_f16 v17, v17, v29
	v_pk_add_f16 v16, v16, v28
	v_pk_add_f16 v15, v15, v27
	v_pk_add_f16 v14, v14, v26
	v_pk_fma_f16 v21, v41, v29, v21
	v_pk_fma_f16 v20, v40, v28, v20
	v_pk_fma_f16 v19, v39, v27, v19
	v_pk_fma_f16 v18, v38, v26, v18
	v_pk_add_f16 v23, v76, v84
	v_pk_add_f16 v24, v75, v83
	v_pk_add_f16 v25, v74, v82
	v_exp_f16_sdwa v26, v22 dst_sel:WORD_0 dst_unused:UNUSED_PAD src0_sel:WORD_0
	v_exp_f16_sdwa v27, v23 dst_sel:WORD_0 dst_unused:UNUSED_PAD src0_sel:WORD_0
	v_exp_f16_sdwa v28, v24 dst_sel:WORD_0 dst_unused:UNUSED_PAD src0_sel:WORD_0
	v_exp_f16_sdwa v29, v25 dst_sel:WORD_0 dst_unused:UNUSED_PAD src0_sel:WORD_0
	v_exp_f16_sdwa v26, v22 dst_sel:WORD_1 dst_unused:UNUSED_PRESERVE src0_sel:WORD_1
	v_exp_f16_sdwa v27, v23 dst_sel:WORD_1 dst_unused:UNUSED_PRESERVE src0_sel:WORD_1
	v_exp_f16_sdwa v28, v24 dst_sel:WORD_1 dst_unused:UNUSED_PRESERVE src0_sel:WORD_1
	v_exp_f16_sdwa v29, v25 dst_sel:WORD_1 dst_unused:UNUSED_PRESERVE src0_sel:WORD_1
	v_pk_add_f16 v22, v81, v85
	v_pk_add_f16 v14, v14, v26
	v_pk_add_f16 v15, v15, v27
	v_pk_add_f16 v16, v16, v28
	v_pk_add_f16 v17, v17, v29
	v_pk_fma_f16 v18, v50, v26, v18
	v_pk_fma_f16 v19, v51, v27, v19
	v_pk_fma_f16 v20, v52, v28, v20
	v_pk_fma_f16 v21, v53, v29, v21
	v_pk_add_f16 v23, v80, v84
	v_pk_add_f16 v24, v79, v83
	v_pk_add_f16 v25, v78, v82
	v_exp_f16_sdwa v26, v22 dst_sel:WORD_0 dst_unused:UNUSED_PAD src0_sel:WORD_0
	v_exp_f16_sdwa v27, v23 dst_sel:WORD_0 dst_unused:UNUSED_PAD src0_sel:WORD_0
	v_exp_f16_sdwa v28, v24 dst_sel:WORD_0 dst_unused:UNUSED_PAD src0_sel:WORD_0
	v_exp_f16_sdwa v29, v25 dst_sel:WORD_0 dst_unused:UNUSED_PAD src0_sel:WORD_0
	v_exp_f16_sdwa v26, v22 dst_sel:WORD_1 dst_unused:UNUSED_PRESERVE src0_sel:WORD_1
	v_exp_f16_sdwa v27, v23 dst_sel:WORD_1 dst_unused:UNUSED_PRESERVE src0_sel:WORD_1
	v_exp_f16_sdwa v28, v24 dst_sel:WORD_1 dst_unused:UNUSED_PRESERVE src0_sel:WORD_1
	v_exp_f16_sdwa v29, v25 dst_sel:WORD_1 dst_unused:UNUSED_PRESERVE src0_sel:WORD_1
	v_pk_add_f16 v22, v30, v85
	v_pk_add_f16 v17, v17, v29
	v_pk_add_f16 v16, v16, v28
	v_pk_add_f16 v15, v15, v27
	v_pk_add_f16 v14, v14, v26
	v_pk_fma_f16 v21, v73, v29, v21
	v_pk_fma_f16 v20, v72, v28, v20
	v_pk_fma_f16 v19, v71, v27, v19
	v_pk_fma_f16 v18, v70, v26, v18
	v_pk_add_f16 v23, v31, v84
	v_pk_add_f16 v24, v32, v83
	v_pk_add_f16 v25, v33, v82
	v_exp_f16_sdwa v26, v22 dst_sel:WORD_0 dst_unused:UNUSED_PAD src0_sel:WORD_0
	v_exp_f16_sdwa v27, v23 dst_sel:WORD_0 dst_unused:UNUSED_PAD src0_sel:WORD_0
	v_exp_f16_sdwa v28, v24 dst_sel:WORD_0 dst_unused:UNUSED_PAD src0_sel:WORD_0
	v_exp_f16_sdwa v29, v25 dst_sel:WORD_0 dst_unused:UNUSED_PAD src0_sel:WORD_0
	v_exp_f16_sdwa v26, v22 dst_sel:WORD_1 dst_unused:UNUSED_PRESERVE src0_sel:WORD_1
	v_exp_f16_sdwa v27, v23 dst_sel:WORD_1 dst_unused:UNUSED_PRESERVE src0_sel:WORD_1
	v_exp_f16_sdwa v28, v24 dst_sel:WORD_1 dst_unused:UNUSED_PRESERVE src0_sel:WORD_1
	v_exp_f16_sdwa v29, v25 dst_sel:WORD_1 dst_unused:UNUSED_PRESERVE src0_sel:WORD_1
	v_pk_add_f16 v22, v54, v85
	v_pk_add_f16 v14, v14, v26
	v_pk_add_f16 v15, v15, v27
	v_pk_add_f16 v16, v16, v28
	v_pk_add_f16 v17, v17, v29
	v_pk_fma_f16 v18, v90, v26, v18
	v_pk_fma_f16 v19, v91, v27, v19
	v_pk_fma_f16 v20, v92, v28, v20
	v_pk_fma_f16 v21, v93, v29, v21
	v_pk_add_f16 v23, v55, v84
	v_pk_add_f16 v24, v56, v83
	v_pk_add_f16 v25, v57, v82
	v_exp_f16_sdwa v26, v22 dst_sel:WORD_0 dst_unused:UNUSED_PAD src0_sel:WORD_0
	v_exp_f16_sdwa v27, v23 dst_sel:WORD_0 dst_unused:UNUSED_PAD src0_sel:WORD_0
	v_exp_f16_sdwa v28, v24 dst_sel:WORD_0 dst_unused:UNUSED_PAD src0_sel:WORD_0
	v_exp_f16_sdwa v29, v25 dst_sel:WORD_0 dst_unused:UNUSED_PAD src0_sel:WORD_0
	v_exp_f16_sdwa v26, v22 dst_sel:WORD_1 dst_unused:UNUSED_PRESERVE src0_sel:WORD_1
	v_exp_f16_sdwa v27, v23 dst_sel:WORD_1 dst_unused:UNUSED_PRESERVE src0_sel:WORD_1
	v_exp_f16_sdwa v28, v24 dst_sel:WORD_1 dst_unused:UNUSED_PRESERVE src0_sel:WORD_1
	v_exp_f16_sdwa v29, v25 dst_sel:WORD_1 dst_unused:UNUSED_PRESERVE src0_sel:WORD_1
	s_nop 0
	v_pk_add_f16 v17, v17, v29
	v_pk_add_f16 v16, v16, v28
	v_pk_add_f16 v15, v15, v27
	v_pk_add_f16 v14, v14, v26
	v_pk_fma_f16 v21, v113, v29, v21
	v_pk_fma_f16 v20, v112, v28, v20
	v_pk_fma_f16 v19, v111, v27, v19
	v_pk_fma_f16 v18, v110, v26, v18
	v_pk_add_f16 v26, v58, v85
	v_pk_add_f16 v27, v59, v84
	v_pk_add_f16 v28, v60, v83
	v_pk_add_f16 v29, v61, v82
	v_exp_f16_sdwa v22, v26 dst_sel:WORD_0 dst_unused:UNUSED_PAD src0_sel:WORD_0
	v_exp_f16_sdwa v23, v27 dst_sel:WORD_0 dst_unused:UNUSED_PAD src0_sel:WORD_0
	v_exp_f16_sdwa v24, v28 dst_sel:WORD_0 dst_unused:UNUSED_PAD src0_sel:WORD_0
	v_exp_f16_sdwa v25, v29 dst_sel:WORD_0 dst_unused:UNUSED_PAD src0_sel:WORD_0
	v_exp_f16_sdwa v22, v26 dst_sel:WORD_1 dst_unused:UNUSED_PRESERVE src0_sel:WORD_1
	v_exp_f16_sdwa v23, v27 dst_sel:WORD_1 dst_unused:UNUSED_PRESERVE src0_sel:WORD_1
	v_exp_f16_sdwa v24, v28 dst_sel:WORD_1 dst_unused:UNUSED_PRESERVE src0_sel:WORD_1
	v_exp_f16_sdwa v25, v29 dst_sel:WORD_1 dst_unused:UNUSED_PRESERVE src0_sel:WORD_1
	s_nop 0
.LBB4_118:
	s_and_b64 vcc, exec, s[4:5]
	s_cbranch_vccz .LBB4_3
	global_load_dwordx3 v[146:148], v169, s[16:17]
	s_mov_b32 s14, s38
	s_mov_b32 s15, s39
	v_cmp_lt_u32_e64 s[64:65], 0, v199
	v_cmp_gt_u32_e64 s[66:67], 63, v199
	v_cmp_lt_u32_e64 s[68:69], 0, v180
	v_cmp_gt_u32_e64 s[70:71], 60, v180
	buffer_load_dwordx4 v[162:165], v200, s[12:15], 0 offen
	s_and_b64 s[72:73], s[68:69], s[64:65]
	s_and_b64 s[74:75], s[68:69], s[66:67]
	s_and_b64 s[76:77], s[70:71], s[64:65]
	s_and_b64 s[78:79], s[70:71], s[66:67]
	v_add_u32_e32 v245, 0xfffe7c00, v200
	v_add_u32_e32 v246, 0xfffe8000, v200
	s_mov_b64 exec, s[72:73]
	buffer_load_dwordx4 v[114:117], v245, s[12:15], 0 offen
	buffer_load_dwordx4 v[70:73], v245, s[12:15], 0 offen offset:512
	s_mov_b64 exec, -1
	s_mov_b64 exec, s[68:69]
	buffer_load_dwordx4 v[130:133], v246, s[12:15], 0 offen offset:512
	buffer_load_dwordx4 v[94:97], v246, s[12:15], 0 offen offset:1024
	s_mov_b64 exec, -1
	s_mov_b64 exec, s[74:75]
	buffer_load_dwordx4 v[138:141], v246, s[12:15], 0 offen offset:2048
	buffer_load_dwordx4 v[118:121], v246, s[12:15], 0 offen offset:2560
	s_mov_b64 exec, -1
	v_add_u32_e32 v245, 0xfffffc00, v200
	s_mov_b64 exec, s[64:65]
	buffer_load_dwordx4 v[86:89], v245, s[12:15], 0 offen
	buffer_load_dwordx4 v[42:45], v245, s[12:15], 0 offen offset:512
	s_mov_b64 exec, -1
	buffer_load_dwordx4 v[110:113], v200, s[12:15], 0 offen offset:512
	buffer_load_dwordx4 v[66:69], v200, s[12:15], 0 offen offset:1024
	s_mov_b64 exec, s[66:67]
	buffer_load_dwordx4 v[126:129], v200, s[12:15], 0 offen offset:2048
	buffer_load_dwordx4 v[90:93], v200, s[12:15], 0 offen offset:2560
	s_mov_b64 exec, -1
	v_add_u32_e32 v245, 0x17c00, v200
	v_add_u32_e32 v246, 0x18000, v200
	s_mov_b64 exec, s[64:65]
	buffer_load_dwordx4 v[54:57], v245, s[12:15], 0 offen
	buffer_load_dwordx4 v[22:25], v245, s[12:15], 0 offen offset:512
	s_mov_b64 exec, -1
	buffer_load_dwordx4 v[74:77], v246, s[12:15], 0 offen offset:512
	buffer_load_dwordx4 v[34:37], v246, s[12:15], 0 offen offset:1024
	s_mov_b64 exec, s[66:67]
	buffer_load_dwordx4 v[98:101], v246, s[12:15], 0 offen offset:2048
	buffer_load_dwordx4 v[50:53], v246, s[12:15], 0 offen offset:2560
	s_mov_b64 exec, -1
	v_add_u32_e32 v245, 0x18000, v200
	buffer_load_dwordx4 v[154:157], v245, s[12:15], 0 offen
	v_add_u32_e32 v246, 0x30000, v200
	buffer_load_dwordx4 v[150:153], v246, s[12:15], 0 offen
	v_add_u32_e32 v245, 0x2fc00, v200
	v_add_u32_e32 v246, 0x30000, v200
	v_add_u32_e32 v247, 0x47c00, v200
	v_add_u32_e32 v248, 0x48000, v200
	v_add_u32_e32 v249, 0x5fc00, v200
	v_add_u32_e32 v250, 0x60000, v200
	s_not_b64 exec, s[72:73]
	s_cbranch_execz .Lmyf_C4_0
	v_mov_b32_e32 v114, v6
	v_mov_b32_e32 v115, v7
	v_mov_b32_e32 v116, v8
	v_mov_b32_e32 v117, v9
	v_mov_b32_e32 v70, v2
	v_mov_b32_e32 v71, v3
	v_mov_b32_e32 v72, v4
	v_mov_b32_e32 v73, v5
.Lmyf_C4_0:
	s_not_b64 exec, s[68:69]
	s_cbranch_execz .Lmyf_C4_1
	v_mov_b32_e32 v130, v6
	v_mov_b32_e32 v131, v7
	v_mov_b32_e32 v132, v8
	v_mov_b32_e32 v133, v9
	v_mov_b32_e32 v94, v2
	v_mov_b32_e32 v95, v3
	v_mov_b32_e32 v96, v4
	v_mov_b32_e32 v97, v5

.Lmyf_C4_2:
	s_not_b64 exec, s[64:65]
	s_cbranch_execz .Lmyf_C4_3
	v_mov_b32_e32 v86, v6
	v_mov_b32_e32 v87, v7
	v_mov_b32_e32 v88, v8
	v_mov_b32_e32 v89, v9
	v_mov_b32_e32 v42, v2
	v_mov_b32_e32 v43, v3
	v_mov_b32_e32 v44, v4
	v_mov_b32_e32 v45, v5
	v_mov_b32_e32 v54, v6
	v_mov_b32_e32 v55, v7
	v_mov_b32_e32 v56, v8
	v_mov_b32_e32 v57, v9
	v_mov_b32_e32 v22, v2
	v_mov_b32_e32 v23, v3
	v_mov_b32_e32 v24, v4
	v_mov_b32_e32 v25, v5
	v_mov_b32_e32 v26, v6
	v_mov_b32_e32 v27, v7
	v_mov_b32_e32 v28, v8
	v_mov_b32_e32 v29, v9
	v_mov_b32_e32 v10, v2
	v_mov_b32_e32 v11, v3
	v_mov_b32_e32 v12, v4
	v_mov_b32_e32 v13, v5
	v_mov_b32_e32 v78, v6
	v_mov_b32_e32 v79, v7
	v_mov_b32_e32 v80, v8
	v_mov_b32_e32 v81, v9
	v_mov_b32_e32 v30, v2
	v_mov_b32_e32 v31, v3
	v_mov_b32_e32 v32, v4
	v_mov_b32_e32 v33, v5
.Lmyf_C4_3:
	s_not_b64 exec, s[66:67]
	s_cbranch_execz .Lmyf_C4_4
	v_mov_b32_e32 v126, v6
	v_mov_b32_e32 v127, v7
	v_mov_b32_e32 v128, v8
	v_mov_b32_e32 v129, v9
	v_mov_b32_e32 v90, v2
	v_mov_b32_e32 v91, v3
	v_mov_b32_e32 v92, v4
	v_mov_b32_e32 v93, v5
	v_mov_b32_e32 v98, v6
	v_mov_b32_e32 v99, v7
	v_mov_b32_e32 v100, v8
	v_mov_b32_e32 v101, v9
	v_mov_b32_e32 v50, v2
	v_mov_b32_e32 v51, v3
	v_mov_b32_e32 v52, v4
	v_mov_b32_e32 v53, v5
	v_mov_b32_e32 v58, v6
	v_mov_b32_e32 v59, v7
	v_mov_b32_e32 v60, v8
	v_mov_b32_e32 v61, v9
	v_mov_b32_e32 v18, v2
	v_mov_b32_e32 v19, v3
	v_mov_b32_e32 v20, v4
	v_mov_b32_e32 v21, v5
	v_mov_b32_e32 v122, v6
	v_mov_b32_e32 v123, v7
	v_mov_b32_e32 v124, v8
	v_mov_b32_e32 v125, v9
	v_mov_b32_e32 v62, v2
	v_mov_b32_e32 v63, v3
	v_mov_b32_e32 v64, v4
	v_mov_b32_e32 v65, v5

.Lmyf_C4_7:
	s_mov_b64 exec, -1
	s_waitcnt vmcnt(21)
	v_cvt_f16_f32_e32 v158, v147
	v_cvt_f16_f32_e32 v160, v146
	v_cvt_f16_f32_e32 v159, v148
	v_add_u32_e32 v251, 0x48000, v200
	buffer_load_dwordx4 v[146:149], v251, s[12:15], 0 offen
	s_branch .LBB4_2

.LBB5_4:
	v_add_u32_e32 v182, s30, v161
	v_add_u32_e32 v181, -1, v182
	v_or_b32_e32 v2, v181, v164
	v_add_u32_e32 v180, 0x18400, v171
	v_cmp_gt_u32_e64 s[0:1], 64, v2
	s_mov_b64 s[4:5], -1
	s_and_b64 vcc, exec, s[24:25]
	s_cbranch_vccz .LBB5_42
	s_load_dwordx2 s[4:5], s[22:23], 0x20
	s_waitcnt lgkmcnt(0)
	s_load_dwordx2 s[26:27], s[4:5], 0x0
	s_load_dword s31, s[4:5], 0x8
	v_cmp_lt_u32_e64 s[64:65], 0, v182
	v_cmp_gt_u32_e64 s[66:67], 63, v182
	v_cmp_lt_u32_e64 s[68:69], 0, v162
	v_cmp_gt_u32_e64 s[70:71], 60, v162
	buffer_load_dwordx4 v[186:189], v180, s[16:19], 0 offen
	s_and_b64 s[72:73], s[68:69], s[64:65]
	s_and_b64 s[74:75], s[68:69], s[66:67]
	s_and_b64 s[76:77], s[70:71], s[64:65]
	s_and_b64 s[78:79], s[70:71], s[66:67]
	v_add_u32_e32 v224, 0xfffe7c00, v180
	v_add_u32_e32 v225, 0xfffe8000, v180
	s_mov_b64 exec, s[72:73]
	buffer_load_dwordx4 v[110:113], v224, s[16:19], 0 offen
	buffer_load_dwordx4 v[70:73], v224, s[16:19], 0 offen offset:512
	s_mov_b64 exec, -1
	s_mov_b64 exec, s[68:69]
	buffer_load_dwordx4 v[126:129], v225, s[16:19], 0 offen offset:512
	buffer_load_dwordx4 v[98:101], v225, s[16:19], 0 offen offset:1024
	s_mov_b64 exec, -1
	s_mov_b64 exec, s[74:75]
	buffer_load_dwordx4 v[134:137], v225, s[16:19], 0 offen offset:2048
	buffer_load_dwordx4 v[114:117], v225, s[16:19], 0 offen offset:2560
	s_mov_b64 exec, -1
	v_add_u32_e32 v224, 0xfffffc00, v180
	s_mov_b64 exec, s[64:65]
	buffer_load_dwordx4 v[82:85], v224, s[16:19], 0 offen
	buffer_load_dwordx4 v[42:45], v224, s[16:19], 0 offen offset:512
	s_mov_b64 exec, -1
	buffer_load_dwordx4 v[106:109], v180, s[16:19], 0 offen offset:512
	buffer_load_dwordx4 v[62:65], v180, s[16:19], 0 offen offset:1024
	s_mov_b64 exec, s[66:67]
	buffer_load_dwordx4 v[122:125], v180, s[16:19], 0 offen offset:2048
	buffer_load_dwordx4 v[86:89], v180, s[16:19], 0 offen offset:2560
	s_mov_b64 exec, -1
	v_add_u32_e32 v224, 0x17c00, v180
	v_add_u32_e32 v225, 0x18000, v180
	s_mov_b64 exec, s[64:65]
	buffer_load_dwordx4 v[50:53], v224, s[16:19], 0 offen
	buffer_load_dwordx4 v[22:25], v224, s[16:19], 0 offen offset:512
	s_mov_b64 exec, -1
	buffer_load_dwordx4 v[66:69], v225, s[16:19], 0 offen offset:512
	buffer_load_dwordx4 v[30:33], v225, s[16:19], 0 offen offset:1024
	s_mov_b64 exec, s[66:67]
	buffer_load_dwordx4 v[94:97], v225, s[16:19], 0 offen offset:2048
	buffer_load_dwordx4 v[46:49], v225, s[16:19], 0 offen offset:2560
	s_mov_b64 exec, -1
	v_add_u32_e32 v224, 0x18000, v180
	buffer_load_dwordx4 v[154:157], v224, s[16:19], 0 offen
	v_add_u32_e32 v225, 0x30000, v180
	buffer_load_dwordx4 v[150:153], v225, s[16:19], 0 offen
	v_add_u32_e32 v224, 0x48000, v180
	buffer_load_dwordx4 v[146:149], v224, s[16:19], 0 offen
	v_add_u32_e32 v224, 0x2fc00, v180
	v_add_u32_e32 v225, 0x30000, v180
	v_add_u32_e32 v226, 0x47c00, v180
	v_add_u32_e32 v227, 0x48000, v180
	v_add_u32_e32 v228, 0x5fc00, v180
	v_add_u32_e32 v229, 0x60000, v180
	s_not_b64 exec, s[72:73]
	s_cbranch_execz .Lmyf_D1_0
	v_mov_b32_e32 v110, v172
	v_mov_b32_e32 v111, v174
	v_mov_b32_e32 v112, v176
	v_mov_b32_e32 v113, v178
	v_mov_b32_e32 v70, v173
	v_mov_b32_e32 v71, v175
	v_mov_b32_e32 v72, v177
	v_mov_b32_e32 v73, v179

.Lmyf_D1_7:
	s_mov_b64 exec, -1
	s_waitcnt lgkmcnt(0)
	v_cvt_f16_f32_e32 v183, s27
	v_cvt_f16_f32_e32 v185, s26
	v_cvt_f16_f32_e32 v184, s31
	s_mov_b64 s[4:5], 0
	s_waitcnt vmcnt(3)
	v_pk_mul_f16 v193, v185, v189 op_sel_hi:[0,1]
	v_pk_mul_f16 v197, v183, v189 op_sel_hi:[0,1]
	v_pk_mul_f16 v201, v184, v189 op_sel_hi:[0,1]
	v_pk_mul_f16 v190, v185, v186 op_sel_hi:[0,1]
	v_pk_mul_f16 v191, v185, v187 op_sel_hi:[0,1]
	v_pk_mul_f16 v192, v185, v188 op_sel_hi:[0,1]
	v_pk_mul_f16 v194, v183, v186 op_sel_hi:[0,1]
	s_mov_b64 exec, s[64:65]
	buffer_load_dwordx4 v[18:21], v224, s[16:19], 0 offen
	buffer_load_dwordx4 v[6:9], v224, s[16:19], 0 offen offset:512
	s_mov_b64 exec, -1
	v_pk_mul_f16 v195, v183, v187 op_sel_hi:[0,1]
	v_pk_mul_f16 v196, v183, v188 op_sel_hi:[0,1]
	v_pk_mul_f16 v198, v184, v186 op_sel_hi:[0,1]
	v_pk_mul_f16 v199, v184, v187 op_sel_hi:[0,1]
	v_pk_mul_f16 v200, v184, v188 op_sel_hi:[0,1]
	v_pk_fma_f16 v113, v113, v189, v193
	v_pk_fma_f16 v129, v129, v189, v197
	v_pk_fma_f16 v137, v137, v189, v201
	v_pk_fma_f16 v202, v85, v189, v193
	v_pk_fma_f16 v206, v109, v189, v197
	v_pk_fma_f16 v210, v125, v189, v201
	v_pk_fma_f16 v193, v53, v189, v193
	v_pk_fma_f16 v197, v69, v189, v197
	buffer_load_dwordx4 v[34:37], v225, s[16:19], 0 offen offset:512
	buffer_load_dwordx4 v[10:13], v225, s[16:19], 0 offen offset:1024
	v_pk_fma_f16 v189, v97, v189, v201
	v_pk_maximum3_f16 v201, v113, v129, v137
	v_pk_fma_f16 v112, v112, v188, v192
	v_pk_fma_f16 v111, v111, v187, v191
	v_pk_fma_f16 v110, v110, v186, v190
	v_pk_fma_f16 v128, v128, v188, v196
	v_pk_fma_f16 v127, v127, v187, v195
	v_pk_fma_f16 v126, v126, v186, v194
	v_pk_fma_f16 v136, v136, v188, v200
	v_pk_fma_f16 v135, v135, v187, v199
	v_pk_fma_f16 v134, v134, v186, v198
	v_pk_fma_f16 v203, v84, v188, v192
	v_pk_fma_f16 v204, v83, v187, v191
	v_pk_fma_f16 v205, v82, v186, v190
	v_pk_fma_f16 v207, v108, v188, v196
	v_pk_fma_f16 v208, v107, v187, v195
	s_mov_b64 exec, s[66:67]
	buffer_load_dwordx4 v[54:57], v225, s[16:19], 0 offen offset:2048
	buffer_load_dwordx4 v[14:17], v225, s[16:19], 0 offen offset:2560
	s_mov_b64 exec, -1
	v_pk_fma_f16 v209, v106, v186, v194
	v_pk_fma_f16 v211, v124, v188, v200
	v_pk_fma_f16 v212, v123, v187, v199
	v_pk_fma_f16 v213, v122, v186, v198
	v_pk_fma_f16 v192, v52, v188, v192
	v_pk_fma_f16 v191, v51, v187, v191
	v_pk_fma_f16 v190, v50, v186, v190
	v_pk_fma_f16 v196, v68, v188, v196
	v_pk_fma_f16 v195, v67, v187, v195
	v_pk_fma_f16 v194, v66, v186, v194
	v_pk_fma_f16 v188, v96, v188, v200
	v_pk_fma_f16 v187, v95, v187, v199
	v_pk_fma_f16 v186, v94, v186, v198
	v_pk_maximum3_f16 v198, v110, v126, v134
	v_pk_maximum3_f16 v199, v111, v127, v135
	v_pk_maximum3_f16 v200, v112, v128, v136
	v_pk_maximum3_f16 v217, v202, v206, v210
	v_pk_maximum3_f16 v221, v193, v197, v189
	v_pk_maximum3_f16 v214, v205, v209, v213
	v_pk_maximum3_f16 v215, v204, v208, v212
	v_pk_maximum3_f16 v216, v203, v207, v211
	v_pk_maximum3_f16 v218, v190, v194, v186
	v_pk_maximum3_f16 v219, v191, v195, v187
	v_pk_maximum3_f16 v201, v201, v217, v221
	v_pk_maximum3_f16 v220, v192, v196, v188
	v_pk_maximum3_f16 v198, v198, v214, v218
	v_pk_maximum3_f16 v199, v199, v215, v219
	v_pk_maximum3_f16 v200, v200, v216, v220
	v_pk_add_f16 v113, v113, v201 neg_lo:[0,1] neg_hi:[0,1]
	s_mov_b64 exec, s[64:65]
	buffer_load_dwordx4 v[74:77], v226, s[16:19], 0 offen
	buffer_load_dwordx4 v[26:29], v226, s[16:19], 0 offen offset:512
	s_mov_b64 exec, -1
	v_pk_add_f16 v110, v110, v198 neg_lo:[0,1] neg_hi:[0,1]
	v_pk_add_f16 v111, v111, v199 neg_lo:[0,1] neg_hi:[0,1]
	v_pk_add_f16 v112, v112, v200 neg_lo:[0,1] neg_hi:[0,1]
	v_pk_add_f16 v126, v126, v198 neg_lo:[0,1] neg_hi:[0,1]
	v_exp_f16_sdwa v214, v110 dst_sel:WORD_0 dst_unused:UNUSED_PAD src0_sel:WORD_0
	v_exp_f16_sdwa v215, v111 dst_sel:WORD_0 dst_unused:UNUSED_PAD src0_sel:WORD_0
	v_exp_f16_sdwa v216, v112 dst_sel:WORD_0 dst_unused:UNUSED_PAD src0_sel:WORD_0
	v_exp_f16_sdwa v217, v113 dst_sel:WORD_0 dst_unused:UNUSED_PAD src0_sel:WORD_0
	v_exp_f16_sdwa v214, v110 dst_sel:WORD_1 dst_unused:UNUSED_PRESERVE src0_sel:WORD_1
	v_exp_f16_sdwa v215, v111 dst_sel:WORD_1 dst_unused:UNUSED_PRESERVE src0_sel:WORD_1
	v_exp_f16_sdwa v216, v112 dst_sel:WORD_1 dst_unused:UNUSED_PRESERVE src0_sel:WORD_1
	v_exp_f16_sdwa v217, v113 dst_sel:WORD_1 dst_unused:UNUSED_PRESERVE src0_sel:WORD_1
	v_pk_add_f16 v127, v127, v199 neg_lo:[0,1] neg_hi:[0,1]
	v_pk_add_f16 v113, v214, 0
	v_pk_fma_f16 v73, v73, v217, 0
	v_pk_add_f16 v110, v217, 0
	v_pk_add_f16 v111, v216, 0
	v_pk_add_f16 v112, v215, 0
	v_pk_fma_f16 v72, v72, v216, 0
	v_pk_fma_f16 v71, v71, v215, 0
	v_pk_fma_f16 v70, v70, v214, 0
	v_pk_add_f16 v128, v128, v200 neg_lo:[0,1] neg_hi:[0,1]
	buffer_load_dwordx4 v[102:105], v227, s[16:19], 0 offen offset:512
	buffer_load_dwordx4 v[38:41], v227, s[16:19], 0 offen offset:1024
	v_pk_add_f16 v129, v129, v201 neg_lo:[0,1] neg_hi:[0,1]
	v_exp_f16_sdwa v214, v126 dst_sel:WORD_0 dst_unused:UNUSED_PAD src0_sel:WORD_0
	v_exp_f16_sdwa v215, v127 dst_sel:WORD_0 dst_unused:UNUSED_PAD src0_sel:WORD_0
	v_exp_f16_sdwa v216, v128 dst_sel:WORD_0 dst_unused:UNUSED_PAD src0_sel:WORD_0
	v_exp_f16_sdwa v217, v129 dst_sel:WORD_0 dst_unused:UNUSED_PAD src0_sel:WORD_0
	v_exp_f16_sdwa v214, v126 dst_sel:WORD_1 dst_unused:UNUSED_PRESERVE src0_sel:WORD_1
	v_exp_f16_sdwa v215, v127 dst_sel:WORD_1 dst_unused:UNUSED_PRESERVE src0_sel:WORD_1
	v_exp_f16_sdwa v216, v128 dst_sel:WORD_1 dst_unused:UNUSED_PRESERVE src0_sel:WORD_1
	v_exp_f16_sdwa v217, v129 dst_sel:WORD_1 dst_unused:UNUSED_PRESERVE src0_sel:WORD_1
	v_pk_add_f16 v113, v113, v214
	v_pk_fma_f16 v73, v101, v217, v73
	v_pk_add_f16 v101, v137, v201 neg_lo:[0,1] neg_hi:[0,1]
	v_pk_add_f16 v112, v112, v215
	v_pk_add_f16 v111, v111, v216
	v_pk_add_f16 v110, v110, v217
	v_pk_fma_f16 v70, v98, v214, v70
	v_pk_fma_f16 v71, v99, v215, v71
	v_pk_fma_f16 v72, v100, v216, v72
	v_pk_add_f16 v98, v134, v198 neg_lo:[0,1] neg_hi:[0,1]
	v_pk_add_f16 v99, v135, v199 neg_lo:[0,1] neg_hi:[0,1]
	v_pk_add_f16 v100, v136, v200 neg_lo:[0,1] neg_hi:[0,1]
	v_exp_f16_sdwa v126, v98 dst_sel:WORD_0 dst_unused:UNUSED_PAD src0_sel:WORD_0
	v_exp_f16_sdwa v127, v99 dst_sel:WORD_0 dst_unused:UNUSED_PAD src0_sel:WORD_0
	v_exp_f16_sdwa v128, v100 dst_sel:WORD_0 dst_unused:UNUSED_PAD src0_sel:WORD_0
	v_exp_f16_sdwa v129, v101 dst_sel:WORD_0 dst_unused:UNUSED_PAD src0_sel:WORD_0
	v_exp_f16_sdwa v126, v98 dst_sel:WORD_1 dst_unused:UNUSED_PRESERVE src0_sel:WORD_1
	v_exp_f16_sdwa v127, v99 dst_sel:WORD_1 dst_unused:UNUSED_PRESERVE src0_sel:WORD_1
	v_exp_f16_sdwa v128, v100 dst_sel:WORD_1 dst_unused:UNUSED_PRESERVE src0_sel:WORD_1
	v_exp_f16_sdwa v129, v101 dst_sel:WORD_1 dst_unused:UNUSED_PRESERVE src0_sel:WORD_1
	v_pk_add_f16 v101, v113, v126
	v_pk_add_f16 v98, v110, v129
	s_mov_b64 exec, s[66:67]
	buffer_load_dwordx4 v[118:121], v227, s[16:19], 0 offen offset:2048
	buffer_load_dwordx4 v[58:61], v227, s[16:19], 0 offen offset:2560
	s_mov_b64 exec, -1
	v_pk_add_f16 v99, v111, v128
	v_pk_add_f16 v100, v112, v127
	v_pk_fma_f16 v73, v117, v129, v73
	v_pk_fma_f16 v72, v116, v128, v72
	v_pk_fma_f16 v71, v115, v127, v71
	v_pk_fma_f16 v70, v114, v126, v70
	v_pk_add_f16 v110, v205, v198 neg_lo:[0,1] neg_hi:[0,1]
	v_pk_add_f16 v111, v204, v199 neg_lo:[0,1] neg_hi:[0,1]
	v_pk_add_f16 v112, v203, v200 neg_lo:[0,1] neg_hi:[0,1]
	v_pk_add_f16 v113, v202, v201 neg_lo:[0,1] neg_hi:[0,1]
	v_exp_f16_sdwa v114, v110 dst_sel:WORD_0 dst_unused:UNUSED_PAD src0_sel:WORD_0
	v_exp_f16_sdwa v115, v111 dst_sel:WORD_0 dst_unused:UNUSED_PAD src0_sel:WORD_0
	v_exp_f16_sdwa v116, v112 dst_sel:WORD_0 dst_unused:UNUSED_PAD src0_sel:WORD_0
	v_exp_f16_sdwa v117, v113 dst_sel:WORD_0 dst_unused:UNUSED_PAD src0_sel:WORD_0
	v_exp_f16_sdwa v114, v110 dst_sel:WORD_1 dst_unused:UNUSED_PRESERVE src0_sel:WORD_1
	v_exp_f16_sdwa v115, v111 dst_sel:WORD_1 dst_unused:UNUSED_PRESERVE src0_sel:WORD_1
	v_exp_f16_sdwa v116, v112 dst_sel:WORD_1 dst_unused:UNUSED_PRESERVE src0_sel:WORD_1
	v_exp_f16_sdwa v117, v113 dst_sel:WORD_1 dst_unused:UNUSED_PRESERVE src0_sel:WORD_1
	v_pk_add_f16 v110, v209, v198 neg_lo:[0,1] neg_hi:[0,1]
	v_pk_add_f16 v101, v101, v114
	v_pk_add_f16 v100, v100, v115
	v_pk_add_f16 v99, v99, v116
	s_mov_b64 exec, s[76:77]
	buffer_load_dwordx4 v[130:133], v228, s[16:19], 0 offen
	buffer_load_dwordx4 v[78:81], v228, s[16:19], 0 offen offset:512
	s_mov_b64 exec, -1
	v_pk_add_f16 v98, v98, v117
	v_pk_fma_f16 v70, v42, v114, v70
	v_pk_fma_f16 v71, v43, v115, v71
	v_pk_fma_f16 v72, v44, v116, v72
	v_pk_fma_f16 v73, v45, v117, v73
	v_pk_add_f16 v111, v208, v199 neg_lo:[0,1] neg_hi:[0,1]
	v_pk_add_f16 v112, v207, v200 neg_lo:[0,1] neg_hi:[0,1]
	v_pk_add_f16 v113, v206, v201 neg_lo:[0,1] neg_hi:[0,1]
	v_exp_f16_sdwa v114, v110 dst_sel:WORD_0 dst_unused:UNUSED_PAD src0_sel:WORD_0
	v_exp_f16_sdwa v115, v111 dst_sel:WORD_0 dst_unused:UNUSED_PAD src0_sel:WORD_0
	v_exp_f16_sdwa v116, v112 dst_sel:WORD_0 dst_unused:UNUSED_PAD src0_sel:WORD_0
	v_exp_f16_sdwa v117, v113 dst_sel:WORD_0 dst_unused:UNUSED_PAD src0_sel:WORD_0
	v_exp_f16_sdwa v114, v110 dst_sel:WORD_1 dst_unused:UNUSED_PRESERVE src0_sel:WORD_1
	v_exp_f16_sdwa v115, v111 dst_sel:WORD_1 dst_unused:UNUSED_PRESERVE src0_sel:WORD_1
	v_exp_f16_sdwa v116, v112 dst_sel:WORD_1 dst_unused:UNUSED_PRESERVE src0_sel:WORD_1
	v_exp_f16_sdwa v117, v113 dst_sel:WORD_1 dst_unused:UNUSED_PRESERVE src0_sel:WORD_1
	v_pk_add_f16 v110, v213, v198 neg_lo:[0,1] neg_hi:[0,1]
	v_pk_add_f16 v101, v101, v114
	v_pk_add_f16 v98, v98, v117
	v_pk_add_f16 v99, v99, v116
	v_pk_add_f16 v100, v100, v115
	v_pk_fma_f16 v73, v65, v117, v73
	v_pk_fma_f16 v72, v64, v116, v72
	s_mov_b64 exec, s[70:71]
	buffer_load_dwordx4 v[138:141], v229, s[16:19], 0 offen offset:512
	buffer_load_dwordx4 v[90:93], v229, s[16:19], 0 offen offset:1024
	s_mov_b64 exec, -1
	v_pk_fma_f16 v71, v63, v115, v71
	v_pk_fma_f16 v70, v62, v114, v70
	v_pk_add_f16 v111, v212, v199 neg_lo:[0,1] neg_hi:[0,1]
	v_pk_add_f16 v112, v211, v200 neg_lo:[0,1] neg_hi:[0,1]
	v_pk_add_f16 v113, v210, v201 neg_lo:[0,1] neg_hi:[0,1]
	v_exp_f16_sdwa v114, v110 dst_sel:WORD_0 dst_unused:UNUSED_PAD src0_sel:WORD_0
	v_exp_f16_sdwa v115, v111 dst_sel:WORD_0 dst_unused:UNUSED_PAD src0_sel:WORD_0
	v_exp_f16_sdwa v116, v112 dst_sel:WORD_0 dst_unused:UNUSED_PAD src0_sel:WORD_0
	v_exp_f16_sdwa v117, v113 dst_sel:WORD_0 dst_unused:UNUSED_PAD src0_sel:WORD_0
	v_exp_f16_sdwa v114, v110 dst_sel:WORD_1 dst_unused:UNUSED_PRESERVE src0_sel:WORD_1
	v_exp_f16_sdwa v115, v111 dst_sel:WORD_1 dst_unused:UNUSED_PRESERVE src0_sel:WORD_1
	v_exp_f16_sdwa v116, v112 dst_sel:WORD_1 dst_unused:UNUSED_PRESERVE src0_sel:WORD_1
	v_exp_f16_sdwa v117, v113 dst_sel:WORD_1 dst_unused:UNUSED_PRESERVE src0_sel:WORD_1
	v_pk_add_f16 v110, v190, v198 neg_lo:[0,1] neg_hi:[0,1]
	v_pk_add_f16 v101, v101, v114
	v_pk_add_f16 v100, v100, v115
	v_pk_add_f16 v99, v99, v116
	v_pk_add_f16 v98, v98, v117
	v_pk_fma_f16 v70, v86, v114, v70
	v_pk_fma_f16 v71, v87, v115, v71
	v_pk_fma_f16 v72, v88, v116, v72
	v_pk_fma_f16 v73, v89, v117, v73
	s_mov_b64 exec, s[78:79]
	buffer_load_dwordx4 v[142:145], v229, s[16:19], 0 offen offset:2048
	buffer_load_dwordx4 v[2:5], v229, s[16:19], 0 offen offset:2560
	s_mov_b64 exec, -1
	v_pk_add_f16 v111, v191, v199 neg_lo:[0,1] neg_hi:[0,1]
	v_pk_add_f16 v112, v192, v200 neg_lo:[0,1] neg_hi:[0,1]
	v_pk_add_f16 v113, v193, v201 neg_lo:[0,1] neg_hi:[0,1]
	v_exp_f16_sdwa v114, v110 dst_sel:WORD_0 dst_unused:UNUSED_PAD src0_sel:WORD_0
	v_exp_f16_sdwa v115, v111 dst_sel:WORD_0 dst_unused:UNUSED_PAD src0_sel:WORD_0
	v_exp_f16_sdwa v116, v112 dst_sel:WORD_0 dst_unused:UNUSED_PAD src0_sel:WORD_0
	v_exp_f16_sdwa v117, v113 dst_sel:WORD_0 dst_unused:UNUSED_PAD src0_sel:WORD_0
	v_exp_f16_sdwa v114, v110 dst_sel:WORD_1 dst_unused:UNUSED_PRESERVE src0_sel:WORD_1
	v_exp_f16_sdwa v115, v111 dst_sel:WORD_1 dst_unused:UNUSED_PRESERVE src0_sel:WORD_1
	v_exp_f16_sdwa v116, v112 dst_sel:WORD_1 dst_unused:UNUSED_PRESERVE src0_sel:WORD_1
	v_exp_f16_sdwa v117, v113 dst_sel:WORD_1 dst_unused:UNUSED_PRESERVE src0_sel:WORD_1
	v_pk_add_f16 v110, v194, v198 neg_lo:[0,1] neg_hi:[0,1]
	v_pk_add_f16 v101, v101, v114
	v_pk_add_f16 v98, v98, v117
	v_pk_add_f16 v99, v99, v116
	v_pk_add_f16 v100, v100, v115
	v_pk_fma_f16 v73, v25, v117, v73
	v_pk_fma_f16 v72, v24, v116, v72
	v_pk_fma_f16 v71, v23, v115, v71
	v_pk_fma_f16 v70, v22, v114, v70
	v_pk_add_f16 v111, v195, v199 neg_lo:[0,1] neg_hi:[0,1]
	v_pk_add_f16 v112, v196, v200 neg_lo:[0,1] neg_hi:[0,1]
	v_pk_add_f16 v113, v197, v201 neg_lo:[0,1] neg_hi:[0,1]
	v_exp_f16_sdwa v114, v110 dst_sel:WORD_0 dst_unused:UNUSED_PAD src0_sel:WORD_0
	v_exp_f16_sdwa v115, v111 dst_sel:WORD_0 dst_unused:UNUSED_PAD src0_sel:WORD_0
	v_exp_f16_sdwa v116, v112 dst_sel:WORD_0 dst_unused:UNUSED_PAD src0_sel:WORD_0
	v_exp_f16_sdwa v117, v113 dst_sel:WORD_0 dst_unused:UNUSED_PAD src0_sel:WORD_0
	v_exp_f16_sdwa v114, v110 dst_sel:WORD_1 dst_unused:UNUSED_PRESERVE src0_sel:WORD_1
	v_exp_f16_sdwa v115, v111 dst_sel:WORD_1 dst_unused:UNUSED_PRESERVE src0_sel:WORD_1
	v_exp_f16_sdwa v116, v112 dst_sel:WORD_1 dst_unused:UNUSED_PRESERVE src0_sel:WORD_1
	v_exp_f16_sdwa v117, v113 dst_sel:WORD_1 dst_unused:UNUSED_PRESERVE src0_sel:WORD_1
	v_pk_add_f16 v110, v186, v198 neg_lo:[0,1] neg_hi:[0,1]
	v_pk_add_f16 v101, v101, v114
	v_pk_add_f16 v100, v100, v115
	v_pk_add_f16 v99, v99, v116
	v_pk_add_f16 v98, v98, v117
	v_pk_fma_f16 v70, v30, v114, v70
	v_pk_fma_f16 v71, v31, v115, v71
	v_pk_fma_f16 v72, v32, v116, v72
	v_pk_fma_f16 v73, v33, v117, v73
	v_pk_add_f16 v111, v187, v199 neg_lo:[0,1] neg_hi:[0,1]
	v_pk_add_f16 v112, v188, v200 neg_lo:[0,1] neg_hi:[0,1]
	v_pk_add_f16 v113, v189, v201 neg_lo:[0,1] neg_hi:[0,1]
	v_exp_f16_sdwa v114, v110 dst_sel:WORD_0 dst_unused:UNUSED_PAD src0_sel:WORD_0
	v_exp_f16_sdwa v115, v111 dst_sel:WORD_0 dst_unused:UNUSED_PAD src0_sel:WORD_0
	v_exp_f16_sdwa v116, v112 dst_sel:WORD_0 dst_unused:UNUSED_PAD src0_sel:WORD_0
	v_exp_f16_sdwa v117, v113 dst_sel:WORD_0 dst_unused:UNUSED_PAD src0_sel:WORD_0
	v_exp_f16_sdwa v114, v110 dst_sel:WORD_1 dst_unused:UNUSED_PRESERVE src0_sel:WORD_1
	v_exp_f16_sdwa v115, v111 dst_sel:WORD_1 dst_unused:UNUSED_PRESERVE src0_sel:WORD_1
	v_exp_f16_sdwa v116, v112 dst_sel:WORD_1 dst_unused:UNUSED_PRESERVE src0_sel:WORD_1
	v_exp_f16_sdwa v117, v113 dst_sel:WORD_1 dst_unused:UNUSED_PRESERVE src0_sel:WORD_1
	v_pk_add_f16 v101, v101, v114
	v_pk_add_f16 v100, v100, v115
	v_rcp_f16_e32 v110, v101
	v_rcp_f16_sdwa v101, v101 dst_sel:DWORD dst_unused:UNUSED_PAD src0_sel:WORD_1
	v_pk_add_f16 v99, v99, v116
	v_rcp_f16_e32 v111, v100
	v_rcp_f16_sdwa v100, v100 dst_sel:DWORD dst_unused:UNUSED_PAD src0_sel:WORD_1
	v_pk_add_f16 v98, v98, v117
	v_rcp_f16_e32 v112, v99
	v_rcp_f16_sdwa v99, v99 dst_sel:DWORD dst_unused:UNUSED_PAD src0_sel:WORD_1
	v_rcp_f16_e32 v113, v98
	v_rcp_f16_sdwa v98, v98 dst_sel:DWORD dst_unused:UNUSED_PAD src0_sel:WORD_1
	v_pk_fma_f16 v70, v46, v114, v70
	v_pack_b32_f16 v101, v110, v101
	v_pk_fma_f16 v71, v47, v115, v71
	v_pk_mul_f16 v110, v70, v101
	v_pack_b32_f16 v70, v111, v100
	v_pk_fma_f16 v72, v48, v116, v72
	v_pk_mul_f16 v111, v71, v70
	v_pack_b32_f16 v70, v112, v99
	v_pk_fma_f16 v73, v49, v117, v73
	v_pk_mul_f16 v112, v72, v70
	v_pack_b32_f16 v70, v113, v98
	v_pk_mul_f16 v113, v73, v70
	s_waitcnt vmcnt(12)
	v_pk_mul_f16 v70, v185, v154 op_sel_hi:[0,1]
	v_pk_mul_f16 v98, v183, v154 op_sel_hi:[0,1]
	v_pk_mul_f16 v114, v184, v154 op_sel_hi:[0,1]
	v_pk_mul_f16 v71, v185, v155 op_sel_hi:[0,1]
	v_pk_mul_f16 v72, v185, v156 op_sel_hi:[0,1]
	v_pk_mul_f16 v73, v185, v157 op_sel_hi:[0,1]
	v_pk_mul_f16 v99, v183, v155 op_sel_hi:[0,1]
	v_pk_mul_f16 v100, v183, v156 op_sel_hi:[0,1]
	v_pk_mul_f16 v101, v183, v157 op_sel_hi:[0,1]
	v_pk_mul_f16 v115, v184, v155 op_sel_hi:[0,1]
	v_pk_mul_f16 v116, v184, v156 op_sel_hi:[0,1]
	v_pk_mul_f16 v117, v184, v157 op_sel_hi:[0,1]
	v_pk_fma_f16 v82, v82, v154, v70
	v_pk_fma_f16 v106, v106, v154, v98
	v_pk_fma_f16 v122, v122, v154, v114
	v_pk_fma_f16 v129, v50, v154, v70
	v_pk_fma_f16 v137, v66, v154, v98
	v_pk_fma_f16 v189, v94, v154, v114
	v_pk_fma_f16 v70, v18, v154, v70
	v_pk_fma_f16 v98, v34, v154, v98
	v_pk_fma_f16 v114, v54, v154, v114
	v_pk_maximum3_f16 v154, v82, v106, v122
	v_pk_fma_f16 v85, v85, v157, v73
	v_pk_fma_f16 v84, v84, v156, v72
	v_pk_fma_f16 v83, v83, v155, v71
	v_pk_fma_f16 v109, v109, v157, v101
	v_pk_fma_f16 v108, v108, v156, v100
	v_pk_fma_f16 v107, v107, v155, v99
	v_pk_fma_f16 v125, v125, v157, v117
	v_pk_fma_f16 v124, v124, v156, v116
	v_pk_fma_f16 v123, v123, v155, v115
	v_pk_fma_f16 v126, v53, v157, v73
	v_pk_fma_f16 v127, v52, v156, v72
	v_pk_fma_f16 v128, v51, v155, v71
	v_pk_fma_f16 v134, v69, v157, v101
	v_pk_fma_f16 v135, v68, v156, v100
	v_pk_fma_f16 v136, v67, v155, v99
	v_pk_fma_f16 v186, v97, v157, v117
	v_pk_fma_f16 v187, v96, v156, v116
	v_pk_fma_f16 v188, v95, v155, v115
	v_pk_fma_f16 v73, v21, v157, v73
	v_pk_fma_f16 v72, v20, v156, v72
	v_pk_fma_f16 v71, v19, v155, v71
	v_pk_fma_f16 v101, v37, v157, v101
	v_pk_fma_f16 v100, v36, v156, v100
	v_pk_fma_f16 v99, v35, v155, v99
	v_pk_fma_f16 v117, v57, v157, v117
	v_pk_fma_f16 v116, v56, v156, v116
	v_pk_fma_f16 v115, v55, v155, v115
	v_pk_maximum3_f16 v155, v83, v107, v123
	v_pk_maximum3_f16 v156, v84, v108, v124
	v_pk_maximum3_f16 v157, v85, v109, v125
	v_pk_maximum3_f16 v190, v129, v137, v189
	v_pk_maximum3_f16 v194, v70, v98, v114
	v_pk_maximum3_f16 v191, v128, v136, v188
	v_pk_maximum3_f16 v192, v127, v135, v187
	v_pk_maximum3_f16 v193, v126, v134, v186
	v_pk_maximum3_f16 v195, v71, v99, v115
	v_pk_maximum3_f16 v196, v72, v100, v116
	v_pk_maximum3_f16 v154, v154, v190, v194
	v_pk_maximum3_f16 v197, v73, v101, v117
	v_pk_maximum3_f16 v155, v155, v191, v195
	v_pk_maximum3_f16 v156, v156, v192, v196
	v_pk_maximum3_f16 v157, v157, v193, v197
	v_pk_add_f16 v82, v82, v154 neg_lo:[0,1] neg_hi:[0,1]
	v_pk_add_f16 v83, v83, v155 neg_lo:[0,1] neg_hi:[0,1]
	v_pk_add_f16 v84, v84, v156 neg_lo:[0,1] neg_hi:[0,1]
	v_pk_add_f16 v85, v85, v157 neg_lo:[0,1] neg_hi:[0,1]
	v_pk_add_f16 v106, v106, v154 neg_lo:[0,1] neg_hi:[0,1]
	v_exp_f16_sdwa v190, v82 dst_sel:WORD_0 dst_unused:UNUSED_PAD src0_sel:WORD_0
	v_exp_f16_sdwa v191, v83 dst_sel:WORD_0 dst_unused:UNUSED_PAD src0_sel:WORD_0
	v_exp_f16_sdwa v192, v84 dst_sel:WORD_0 dst_unused:UNUSED_PAD src0_sel:WORD_0
	v_exp_f16_sdwa v193, v85 dst_sel:WORD_0 dst_unused:UNUSED_PAD src0_sel:WORD_0
	v_exp_f16_sdwa v190, v82 dst_sel:WORD_1 dst_unused:UNUSED_PRESERVE src0_sel:WORD_1
	v_exp_f16_sdwa v191, v83 dst_sel:WORD_1 dst_unused:UNUSED_PRESERVE src0_sel:WORD_1
	v_exp_f16_sdwa v192, v84 dst_sel:WORD_1 dst_unused:UNUSED_PRESERVE src0_sel:WORD_1
	v_exp_f16_sdwa v193, v85 dst_sel:WORD_1 dst_unused:UNUSED_PRESERVE src0_sel:WORD_1
	v_pk_add_f16 v107, v107, v155 neg_lo:[0,1] neg_hi:[0,1]
	v_pk_add_f16 v82, v193, 0
	v_pk_fma_f16 v42, v42, v190, 0
	v_pk_add_f16 v83, v192, 0
	v_pk_add_f16 v84, v191, 0
	v_pk_add_f16 v85, v190, 0
	v_pk_fma_f16 v45, v45, v193, 0
	v_pk_fma_f16 v44, v44, v192, 0
	v_pk_fma_f16 v43, v43, v191, 0
	v_pk_add_f16 v108, v108, v156 neg_lo:[0,1] neg_hi:[0,1]
	v_pk_add_f16 v109, v109, v157 neg_lo:[0,1] neg_hi:[0,1]
	v_pk_add_f16 v70, v70, v154 neg_lo:[0,1] neg_hi:[0,1]
	v_exp_f16_sdwa v190, v106 dst_sel:WORD_0 dst_unused:UNUSED_PAD src0_sel:WORD_0
	v_exp_f16_sdwa v191, v107 dst_sel:WORD_0 dst_unused:UNUSED_PAD src0_sel:WORD_0
	v_exp_f16_sdwa v192, v108 dst_sel:WORD_0 dst_unused:UNUSED_PAD src0_sel:WORD_0
	v_exp_f16_sdwa v193, v109 dst_sel:WORD_0 dst_unused:UNUSED_PAD src0_sel:WORD_0
	v_exp_f16_sdwa v190, v106 dst_sel:WORD_1 dst_unused:UNUSED_PRESERVE src0_sel:WORD_1
	v_exp_f16_sdwa v191, v107 dst_sel:WORD_1 dst_unused:UNUSED_PRESERVE src0_sel:WORD_1
	v_exp_f16_sdwa v192, v108 dst_sel:WORD_1 dst_unused:UNUSED_PRESERVE src0_sel:WORD_1
	v_exp_f16_sdwa v193, v109 dst_sel:WORD_1 dst_unused:UNUSED_PRESERVE src0_sel:WORD_1
	v_pk_add_f16 v71, v71, v155 neg_lo:[0,1] neg_hi:[0,1]
	v_pk_add_f16 v82, v82, v193
	v_pk_fma_f16 v42, v62, v190, v42
	v_pk_add_f16 v62, v122, v154 neg_lo:[0,1] neg_hi:[0,1]
	v_pk_add_f16 v85, v85, v190
	v_pk_add_f16 v84, v84, v191
	v_pk_add_f16 v83, v83, v192
	v_pk_fma_f16 v43, v63, v191, v43
	v_pk_fma_f16 v44, v64, v192, v44
	v_pk_fma_f16 v45, v65, v193, v45
	v_pk_add_f16 v63, v123, v155 neg_lo:[0,1] neg_hi:[0,1]
	v_pk_add_f16 v64, v124, v156 neg_lo:[0,1] neg_hi:[0,1]
	v_pk_add_f16 v65, v125, v157 neg_lo:[0,1] neg_hi:[0,1]
	v_pk_add_f16 v72, v72, v156 neg_lo:[0,1] neg_hi:[0,1]
	v_exp_f16_sdwa v106, v62 dst_sel:WORD_0 dst_unused:UNUSED_PAD src0_sel:WORD_0
	v_exp_f16_sdwa v107, v63 dst_sel:WORD_0 dst_unused:UNUSED_PAD src0_sel:WORD_0
	v_exp_f16_sdwa v108, v64 dst_sel:WORD_0 dst_unused:UNUSED_PAD src0_sel:WORD_0
	v_exp_f16_sdwa v109, v65 dst_sel:WORD_0 dst_unused:UNUSED_PAD src0_sel:WORD_0
	v_exp_f16_sdwa v106, v62 dst_sel:WORD_1 dst_unused:UNUSED_PRESERVE src0_sel:WORD_1
	v_exp_f16_sdwa v107, v63 dst_sel:WORD_1 dst_unused:UNUSED_PRESERVE src0_sel:WORD_1
	v_exp_f16_sdwa v108, v64 dst_sel:WORD_1 dst_unused:UNUSED_PRESERVE src0_sel:WORD_1
	v_exp_f16_sdwa v109, v65 dst_sel:WORD_1 dst_unused:UNUSED_PRESERVE src0_sel:WORD_1
	v_pk_add_f16 v73, v73, v157 neg_lo:[0,1] neg_hi:[0,1]
	v_pk_add_f16 v62, v82, v109
	v_pk_add_f16 v63, v83, v108
	v_pk_add_f16 v64, v84, v107
	v_pk_add_f16 v65, v85, v106
	v_pk_fma_f16 v45, v89, v109, v45
	v_pk_fma_f16 v44, v88, v108, v44
	v_pk_fma_f16 v43, v87, v107, v43
	v_pk_fma_f16 v42, v86, v106, v42
	v_pk_add_f16 v82, v129, v154 neg_lo:[0,1] neg_hi:[0,1]
	v_pk_add_f16 v83, v128, v155 neg_lo:[0,1] neg_hi:[0,1]
	v_pk_add_f16 v84, v127, v156 neg_lo:[0,1] neg_hi:[0,1]
	v_pk_add_f16 v85, v126, v157 neg_lo:[0,1] neg_hi:[0,1]
	v_exp_f16_sdwa v86, v82 dst_sel:WORD_0 dst_unused:UNUSED_PAD src0_sel:WORD_0
	v_exp_f16_sdwa v87, v83 dst_sel:WORD_0 dst_unused:UNUSED_PAD src0_sel:WORD_0
	v_exp_f16_sdwa v88, v84 dst_sel:WORD_0 dst_unused:UNUSED_PAD src0_sel:WORD_0
	v_exp_f16_sdwa v89, v85 dst_sel:WORD_0 dst_unused:UNUSED_PAD src0_sel:WORD_0
	v_exp_f16_sdwa v86, v82 dst_sel:WORD_1 dst_unused:UNUSED_PRESERVE src0_sel:WORD_1
	v_exp_f16_sdwa v87, v83 dst_sel:WORD_1 dst_unused:UNUSED_PRESERVE src0_sel:WORD_1
	v_exp_f16_sdwa v88, v84 dst_sel:WORD_1 dst_unused:UNUSED_PRESERVE src0_sel:WORD_1
	v_exp_f16_sdwa v89, v85 dst_sel:WORD_1 dst_unused:UNUSED_PRESERVE src0_sel:WORD_1
	v_pk_add_f16 v82, v137, v154 neg_lo:[0,1] neg_hi:[0,1]
	v_pk_add_f16 v62, v62, v89
	v_pk_add_f16 v65, v65, v86
	v_pk_add_f16 v64, v64, v87
	v_pk_add_f16 v63, v63, v88
	v_pk_fma_f16 v42, v22, v86, v42
	v_pk_fma_f16 v43, v23, v87, v43
	v_pk_fma_f16 v44, v24, v88, v44
	v_pk_fma_f16 v45, v25, v89, v45
	v_pk_add_f16 v83, v136, v155 neg_lo:[0,1] neg_hi:[0,1]
	v_pk_add_f16 v84, v135, v156 neg_lo:[0,1] neg_hi:[0,1]
	v_pk_add_f16 v85, v134, v157 neg_lo:[0,1] neg_hi:[0,1]
	v_exp_f16_sdwa v86, v82 dst_sel:WORD_0 dst_unused:UNUSED_PAD src0_sel:WORD_0
	v_exp_f16_sdwa v87, v83 dst_sel:WORD_0 dst_unused:UNUSED_PAD src0_sel:WORD_0
	v_exp_f16_sdwa v88, v84 dst_sel:WORD_0 dst_unused:UNUSED_PAD src0_sel:WORD_0
	v_exp_f16_sdwa v89, v85 dst_sel:WORD_0 dst_unused:UNUSED_PAD src0_sel:WORD_0
	v_exp_f16_sdwa v86, v82 dst_sel:WORD_1 dst_unused:UNUSED_PRESERVE src0_sel:WORD_1
	v_exp_f16_sdwa v87, v83 dst_sel:WORD_1 dst_unused:UNUSED_PRESERVE src0_sel:WORD_1
	v_exp_f16_sdwa v88, v84 dst_sel:WORD_1 dst_unused:UNUSED_PRESERVE src0_sel:WORD_1
	v_exp_f16_sdwa v89, v85 dst_sel:WORD_1 dst_unused:UNUSED_PRESERVE src0_sel:WORD_1
	v_pk_add_f16 v82, v189, v154 neg_lo:[0,1] neg_hi:[0,1]
	v_pk_add_f16 v62, v62, v89
	v_pk_add_f16 v63, v63, v88
	v_pk_add_f16 v64, v64, v87
	v_pk_add_f16 v65, v65, v86
	v_pk_fma_f16 v45, v33, v89, v45
	v_pk_fma_f16 v44, v32, v88, v44
	v_pk_fma_f16 v43, v31, v87, v43
	v_pk_fma_f16 v42, v30, v86, v42
	v_pk_add_f16 v83, v188, v155 neg_lo:[0,1] neg_hi:[0,1]
	v_pk_add_f16 v84, v187, v156 neg_lo:[0,1] neg_hi:[0,1]
	v_pk_add_f16 v85, v186, v157 neg_lo:[0,1] neg_hi:[0,1]
	v_exp_f16_sdwa v86, v82 dst_sel:WORD_0 dst_unused:UNUSED_PAD src0_sel:WORD_0
	v_exp_f16_sdwa v87, v83 dst_sel:WORD_0 dst_unused:UNUSED_PAD src0_sel:WORD_0
	v_exp_f16_sdwa v88, v84 dst_sel:WORD_0 dst_unused:UNUSED_PAD src0_sel:WORD_0
	v_exp_f16_sdwa v89, v85 dst_sel:WORD_0 dst_unused:UNUSED_PAD src0_sel:WORD_0
	v_exp_f16_sdwa v86, v82 dst_sel:WORD_1 dst_unused:UNUSED_PRESERVE src0_sel:WORD_1
	v_exp_f16_sdwa v87, v83 dst_sel:WORD_1 dst_unused:UNUSED_PRESERVE src0_sel:WORD_1
	v_exp_f16_sdwa v88, v84 dst_sel:WORD_1 dst_unused:UNUSED_PRESERVE src0_sel:WORD_1
	v_exp_f16_sdwa v89, v85 dst_sel:WORD_1 dst_unused:UNUSED_PRESERVE src0_sel:WORD_1
	v_exp_f16_sdwa v82, v70 dst_sel:WORD_0 dst_unused:UNUSED_PAD src0_sel:WORD_0
	v_exp_f16_sdwa v83, v71 dst_sel:WORD_0 dst_unused:UNUSED_PAD src0_sel:WORD_0
	v_exp_f16_sdwa v84, v72 dst_sel:WORD_0 dst_unused:UNUSED_PAD src0_sel:WORD_0
	v_exp_f16_sdwa v85, v73 dst_sel:WORD_0 dst_unused:UNUSED_PAD src0_sel:WORD_0
	v_exp_f16_sdwa v82, v70 dst_sel:WORD_1 dst_unused:UNUSED_PRESERVE src0_sel:WORD_1
	v_exp_f16_sdwa v83, v71 dst_sel:WORD_1 dst_unused:UNUSED_PRESERVE src0_sel:WORD_1
	v_exp_f16_sdwa v84, v72 dst_sel:WORD_1 dst_unused:UNUSED_PRESERVE src0_sel:WORD_1
	v_exp_f16_sdwa v85, v73 dst_sel:WORD_1 dst_unused:UNUSED_PRESERVE src0_sel:WORD_1
	v_pk_add_f16 v70, v98, v154 neg_lo:[0,1] neg_hi:[0,1]
	v_pk_add_f16 v62, v62, v89
	v_pk_add_f16 v65, v65, v86
	v_pk_add_f16 v64, v64, v87
	v_pk_add_f16 v63, v63, v88
	v_pk_fma_f16 v42, v46, v86, v42
	v_pk_fma_f16 v43, v47, v87, v43
	v_pk_fma_f16 v44, v48, v88, v44
	v_pk_fma_f16 v45, v49, v89, v45
	v_pk_add_f16 v62, v62, v85
	v_pk_add_f16 v63, v63, v84
	v_pk_add_f16 v64, v64, v83
	v_pk_add_f16 v65, v65, v82
	v_pk_fma_f16 v45, v9, v85, v45
	v_pk_fma_f16 v44, v8, v84, v44
	v_pk_fma_f16 v43, v7, v83, v43
	v_pk_fma_f16 v42, v6, v82, v42
	v_pk_add_f16 v71, v99, v155 neg_lo:[0,1] neg_hi:[0,1]
	v_pk_add_f16 v72, v100, v156 neg_lo:[0,1] neg_hi:[0,1]
	v_pk_add_f16 v73, v101, v157 neg_lo:[0,1] neg_hi:[0,1]
	v_exp_f16_sdwa v82, v70 dst_sel:WORD_0 dst_unused:UNUSED_PAD src0_sel:WORD_0
	v_exp_f16_sdwa v83, v71 dst_sel:WORD_0 dst_unused:UNUSED_PAD src0_sel:WORD_0
	v_exp_f16_sdwa v84, v72 dst_sel:WORD_0 dst_unused:UNUSED_PAD src0_sel:WORD_0
	v_exp_f16_sdwa v85, v73 dst_sel:WORD_0 dst_unused:UNUSED_PAD src0_sel:WORD_0
	v_exp_f16_sdwa v82, v70 dst_sel:WORD_1 dst_unused:UNUSED_PRESERVE src0_sel:WORD_1
	v_exp_f16_sdwa v83, v71 dst_sel:WORD_1 dst_unused:UNUSED_PRESERVE src0_sel:WORD_1
	v_exp_f16_sdwa v84, v72 dst_sel:WORD_1 dst_unused:UNUSED_PRESERVE src0_sel:WORD_1
	v_exp_f16_sdwa v85, v73 dst_sel:WORD_1 dst_unused:UNUSED_PRESERVE src0_sel:WORD_1
	v_pk_add_f16 v70, v114, v154 neg_lo:[0,1] neg_hi:[0,1]
	v_pk_add_f16 v62, v62, v85
	v_pk_add_f16 v65, v65, v82
	v_pk_add_f16 v64, v64, v83
	v_pk_add_f16 v63, v63, v84
	v_pk_fma_f16 v42, v10, v82, v42
	v_pk_fma_f16 v43, v11, v83, v43
	v_pk_fma_f16 v44, v12, v84, v44
	v_pk_fma_f16 v45, v13, v85, v45
	v_pk_add_f16 v71, v115, v155 neg_lo:[0,1] neg_hi:[0,1]
	v_pk_add_f16 v72, v116, v156 neg_lo:[0,1] neg_hi:[0,1]
	v_pk_add_f16 v73, v117, v157 neg_lo:[0,1] neg_hi:[0,1]
	v_exp_f16_sdwa v82, v70 dst_sel:WORD_0 dst_unused:UNUSED_PAD src0_sel:WORD_0
	v_exp_f16_sdwa v83, v71 dst_sel:WORD_0 dst_unused:UNUSED_PAD src0_sel:WORD_0
	v_exp_f16_sdwa v84, v72 dst_sel:WORD_0 dst_unused:UNUSED_PAD src0_sel:WORD_0
	v_exp_f16_sdwa v85, v73 dst_sel:WORD_0 dst_unused:UNUSED_PAD src0_sel:WORD_0
	v_exp_f16_sdwa v82, v70 dst_sel:WORD_1 dst_unused:UNUSED_PRESERVE src0_sel:WORD_1
	v_exp_f16_sdwa v83, v71 dst_sel:WORD_1 dst_unused:UNUSED_PRESERVE src0_sel:WORD_1
	v_exp_f16_sdwa v84, v72 dst_sel:WORD_1 dst_unused:UNUSED_PRESERVE src0_sel:WORD_1
	v_exp_f16_sdwa v85, v73 dst_sel:WORD_1 dst_unused:UNUSED_PRESERVE src0_sel:WORD_1
	s_nop 0
	v_pk_add_f16 v62, v62, v85
	v_pk_add_f16 v63, v63, v84
	v_pk_add_f16 v64, v64, v83
	v_pk_add_f16 v65, v65, v82
	v_rcp_f16_e32 v73, v62
	v_rcp_f16_sdwa v62, v62 dst_sel:DWORD dst_unused:UNUSED_PAD src0_sel:WORD_1
	v_rcp_f16_e32 v70, v65
	v_rcp_f16_sdwa v65, v65 dst_sel:DWORD dst_unused:UNUSED_PAD src0_sel:WORD_1
	v_rcp_f16_e32 v71, v64
	v_rcp_f16_sdwa v64, v64 dst_sel:DWORD dst_unused:UNUSED_PAD src0_sel:WORD_1
	v_rcp_f16_e32 v72, v63
	v_rcp_f16_sdwa v63, v63 dst_sel:DWORD dst_unused:UNUSED_PAD src0_sel:WORD_1
	v_pk_fma_f16 v45, v17, v85, v45
	v_pack_b32_f16 v62, v73, v62
	v_pk_fma_f16 v44, v16, v84, v44
	v_pk_fma_f16 v43, v15, v83, v43
	v_pk_fma_f16 v42, v14, v82, v42
	v_pack_b32_f16 v65, v70, v65
	v_pack_b32_f16 v64, v71, v64
	v_pack_b32_f16 v63, v72, v63
	v_pk_mul_f16 v45, v45, v62
	s_waitcnt vmcnt(6)
	v_pk_mul_f16 v62, v185, v150 op_sel_hi:[0,1]
	v_pk_mul_f16 v70, v183, v150 op_sel_hi:[0,1]
	v_pk_mul_f16 v82, v184, v150 op_sel_hi:[0,1]
	v_pk_mul_f16 v42, v42, v65
	v_pk_mul_f16 v43, v43, v64
	v_pk_mul_f16 v44, v44, v63
	v_pk_mul_f16 v63, v185, v151 op_sel_hi:[0,1]
	v_pk_mul_f16 v64, v185, v152 op_sel_hi:[0,1]
	v_pk_mul_f16 v65, v185, v153 op_sel_hi:[0,1]
	v_pk_mul_f16 v71, v183, v151 op_sel_hi:[0,1]
	v_pk_mul_f16 v72, v183, v152 op_sel_hi:[0,1]
	v_pk_mul_f16 v73, v183, v153 op_sel_hi:[0,1]
	v_pk_mul_f16 v83, v184, v151 op_sel_hi:[0,1]
	v_pk_mul_f16 v84, v184, v152 op_sel_hi:[0,1]
	v_pk_mul_f16 v85, v184, v153 op_sel_hi:[0,1]
	v_pk_fma_f16 v50, v50, v150, v62
	v_pk_fma_f16 v66, v66, v150, v70
	v_pk_fma_f16 v89, v94, v150, v82
	v_pk_fma_f16 v53, v53, v153, v65
	v_pk_maximum3_f16 v114, v50, v66, v89
	v_pk_fma_f16 v52, v52, v152, v64
	v_pk_fma_f16 v51, v51, v151, v63
	v_pk_fma_f16 v69, v69, v153, v73
	v_pk_fma_f16 v68, v68, v152, v72
	v_pk_fma_f16 v67, v67, v151, v71
	v_pk_fma_f16 v86, v97, v153, v85
	v_pk_fma_f16 v87, v96, v152, v84
	v_pk_fma_f16 v88, v95, v151, v83
	v_pk_fma_f16 v97, v18, v150, v62
	v_pk_fma_f16 v101, v34, v150, v70
	v_pk_fma_f16 v109, v54, v150, v82
	v_pk_fma_f16 v62, v74, v150, v62
	v_pk_fma_f16 v70, v102, v150, v70
	v_pk_fma_f16 v82, v118, v150, v82
	v_pk_maximum3_f16 v115, v51, v67, v88
	v_pk_maximum3_f16 v116, v52, v68, v87
	v_pk_maximum3_f16 v117, v53, v69, v86
	v_pk_maximum3_f16 v122, v97, v101, v109
	v_pk_fma_f16 v94, v21, v153, v65
	v_pk_maximum3_f16 v126, v62, v70, v82
	v_pk_fma_f16 v95, v20, v152, v64
	v_pk_maximum3_f16 v114, v114, v122, v126
	v_pk_fma_f16 v96, v19, v151, v63
	v_pk_fma_f16 v98, v37, v153, v73
	v_pk_fma_f16 v99, v36, v152, v72
	v_pk_fma_f16 v100, v35, v151, v71
	v_pk_fma_f16 v106, v57, v153, v85
	v_pk_fma_f16 v107, v56, v152, v84
	v_pk_fma_f16 v108, v55, v151, v83
	v_pk_fma_f16 v65, v77, v153, v65
	v_pk_fma_f16 v64, v76, v152, v64
	v_pk_fma_f16 v63, v75, v151, v63
	v_pk_fma_f16 v73, v105, v153, v73
	v_pk_fma_f16 v72, v104, v152, v72
	v_pk_fma_f16 v71, v103, v151, v71
	v_pk_fma_f16 v85, v121, v153, v85
	v_pk_fma_f16 v84, v120, v152, v84
	v_pk_fma_f16 v83, v119, v151, v83
	v_pk_maximum3_f16 v123, v96, v100, v108
	v_pk_maximum3_f16 v124, v95, v99, v107
	v_pk_maximum3_f16 v125, v94, v98, v106
	v_pk_maximum3_f16 v128, v64, v72, v84
	v_pk_maximum3_f16 v129, v65, v73, v85
	v_pk_maximum3_f16 v127, v63, v71, v83
	v_pk_maximum3_f16 v115, v115, v123, v127
	v_pk_maximum3_f16 v116, v116, v124, v128
	v_pk_maximum3_f16 v117, v117, v125, v129
	v_pk_add_f16 v50, v50, v114 neg_lo:[0,1] neg_hi:[0,1]
	v_pk_add_f16 v51, v51, v115 neg_lo:[0,1] neg_hi:[0,1]
	v_pk_add_f16 v52, v52, v116 neg_lo:[0,1] neg_hi:[0,1]
	v_pk_add_f16 v53, v53, v117 neg_lo:[0,1] neg_hi:[0,1]
	v_pk_add_f16 v66, v66, v114 neg_lo:[0,1] neg_hi:[0,1]
	v_exp_f16_sdwa v122, v50 dst_sel:WORD_0 dst_unused:UNUSED_PAD src0_sel:WORD_0
	v_exp_f16_sdwa v123, v51 dst_sel:WORD_0 dst_unused:UNUSED_PAD src0_sel:WORD_0
	v_exp_f16_sdwa v124, v52 dst_sel:WORD_0 dst_unused:UNUSED_PAD src0_sel:WORD_0
	v_exp_f16_sdwa v125, v53 dst_sel:WORD_0 dst_unused:UNUSED_PAD src0_sel:WORD_0
	v_exp_f16_sdwa v122, v50 dst_sel:WORD_1 dst_unused:UNUSED_PRESERVE src0_sel:WORD_1
	v_exp_f16_sdwa v123, v51 dst_sel:WORD_1 dst_unused:UNUSED_PRESERVE src0_sel:WORD_1
	v_exp_f16_sdwa v124, v52 dst_sel:WORD_1 dst_unused:UNUSED_PRESERVE src0_sel:WORD_1
	v_exp_f16_sdwa v125, v53 dst_sel:WORD_1 dst_unused:UNUSED_PRESERVE src0_sel:WORD_1
	v_pk_add_f16 v67, v67, v115 neg_lo:[0,1] neg_hi:[0,1]
	v_pk_add_f16 v50, v125, 0
	v_pk_fma_f16 v22, v22, v122, 0
	v_pk_add_f16 v51, v124, 0
	v_pk_add_f16 v52, v123, 0
	v_pk_add_f16 v53, v122, 0
	v_pk_fma_f16 v23, v23, v123, 0
	v_pk_fma_f16 v24, v24, v124, 0
	v_pk_fma_f16 v25, v25, v125, 0
	v_pk_add_f16 v68, v68, v116 neg_lo:[0,1] neg_hi:[0,1]
	v_pk_add_f16 v69, v69, v117 neg_lo:[0,1] neg_hi:[0,1]
	v_exp_f16_sdwa v122, v66 dst_sel:WORD_0 dst_unused:UNUSED_PAD src0_sel:WORD_0
	v_exp_f16_sdwa v123, v67 dst_sel:WORD_0 dst_unused:UNUSED_PAD src0_sel:WORD_0
	v_exp_f16_sdwa v124, v68 dst_sel:WORD_0 dst_unused:UNUSED_PAD src0_sel:WORD_0
	v_exp_f16_sdwa v125, v69 dst_sel:WORD_0 dst_unused:UNUSED_PAD src0_sel:WORD_0
	v_exp_f16_sdwa v122, v66 dst_sel:WORD_1 dst_unused:UNUSED_PRESERVE src0_sel:WORD_1
	v_exp_f16_sdwa v123, v67 dst_sel:WORD_1 dst_unused:UNUSED_PRESERVE src0_sel:WORD_1
	v_exp_f16_sdwa v124, v68 dst_sel:WORD_1 dst_unused:UNUSED_PRESERVE src0_sel:WORD_1
	v_exp_f16_sdwa v125, v69 dst_sel:WORD_1 dst_unused:UNUSED_PRESERVE src0_sel:WORD_1
	s_nop 0
	v_pk_add_f16 v50, v50, v125
	v_pk_fma_f16 v22, v30, v122, v22
	v_pk_add_f16 v30, v89, v114 neg_lo:[0,1] neg_hi:[0,1]
	v_pk_add_f16 v53, v53, v122
	v_pk_add_f16 v52, v52, v123
	v_pk_add_f16 v51, v51, v124
	v_pk_fma_f16 v25, v33, v125, v25
	v_pk_fma_f16 v24, v32, v124, v24
	v_pk_fma_f16 v23, v31, v123, v23
	v_pk_add_f16 v31, v88, v115 neg_lo:[0,1] neg_hi:[0,1]
	v_pk_add_f16 v32, v87, v116 neg_lo:[0,1] neg_hi:[0,1]
	v_pk_add_f16 v33, v86, v117 neg_lo:[0,1] neg_hi:[0,1]
	v_exp_f16_sdwa v66, v30 dst_sel:WORD_0 dst_unused:UNUSED_PAD src0_sel:WORD_0
	v_exp_f16_sdwa v67, v31 dst_sel:WORD_0 dst_unused:UNUSED_PAD src0_sel:WORD_0
	v_exp_f16_sdwa v68, v32 dst_sel:WORD_0 dst_unused:UNUSED_PAD src0_sel:WORD_0
	v_exp_f16_sdwa v69, v33 dst_sel:WORD_0 dst_unused:UNUSED_PAD src0_sel:WORD_0
	v_exp_f16_sdwa v66, v30 dst_sel:WORD_1 dst_unused:UNUSED_PRESERVE src0_sel:WORD_1
	v_exp_f16_sdwa v67, v31 dst_sel:WORD_1 dst_unused:UNUSED_PRESERVE src0_sel:WORD_1
	v_exp_f16_sdwa v68, v32 dst_sel:WORD_1 dst_unused:UNUSED_PRESERVE src0_sel:WORD_1
	v_exp_f16_sdwa v69, v33 dst_sel:WORD_1 dst_unused:UNUSED_PRESERVE src0_sel:WORD_1
	s_nop 0
	v_pk_add_f16 v30, v50, v69
	v_pk_add_f16 v31, v51, v68
	v_pk_add_f16 v32, v52, v67
	v_pk_add_f16 v33, v53, v66
	v_pk_fma_f16 v22, v46, v66, v22
	v_pk_fma_f16 v23, v47, v67, v23
	v_pk_fma_f16 v24, v48, v68, v24
	v_pk_fma_f16 v25, v49, v69, v25
	v_pk_add_f16 v46, v97, v114 neg_lo:[0,1] neg_hi:[0,1]
	v_pk_add_f16 v47, v96, v115 neg_lo:[0,1] neg_hi:[0,1]
	v_pk_add_f16 v48, v95, v116 neg_lo:[0,1] neg_hi:[0,1]
	v_pk_add_f16 v49, v94, v117 neg_lo:[0,1] neg_hi:[0,1]
	v_exp_f16_sdwa v50, v46 dst_sel:WORD_0 dst_unused:UNUSED_PAD src0_sel:WORD_0
	v_exp_f16_sdwa v51, v47 dst_sel:WORD_0 dst_unused:UNUSED_PAD src0_sel:WORD_0
	v_exp_f16_sdwa v52, v48 dst_sel:WORD_0 dst_unused:UNUSED_PAD src0_sel:WORD_0
	v_exp_f16_sdwa v53, v49 dst_sel:WORD_0 dst_unused:UNUSED_PAD src0_sel:WORD_0
	v_exp_f16_sdwa v50, v46 dst_sel:WORD_1 dst_unused:UNUSED_PRESERVE src0_sel:WORD_1
	v_exp_f16_sdwa v51, v47 dst_sel:WORD_1 dst_unused:UNUSED_PRESERVE src0_sel:WORD_1
	v_exp_f16_sdwa v52, v48 dst_sel:WORD_1 dst_unused:UNUSED_PRESERVE src0_sel:WORD_1
	v_exp_f16_sdwa v53, v49 dst_sel:WORD_1 dst_unused:UNUSED_PRESERVE src0_sel:WORD_1
	v_pk_add_f16 v46, v101, v114 neg_lo:[0,1] neg_hi:[0,1]
	v_pk_add_f16 v30, v30, v53
	v_pk_add_f16 v33, v33, v50
	v_pk_add_f16 v32, v32, v51
	v_pk_add_f16 v31, v31, v52
	v_pk_fma_f16 v25, v9, v53, v25
	v_pk_fma_f16 v24, v8, v52, v24
	v_pk_fma_f16 v23, v7, v51, v23
	v_pk_fma_f16 v22, v6, v50, v22
	v_pk_add_f16 v47, v100, v115 neg_lo:[0,1] neg_hi:[0,1]
	v_pk_add_f16 v48, v99, v116 neg_lo:[0,1] neg_hi:[0,1]
	v_pk_add_f16 v49, v98, v117 neg_lo:[0,1] neg_hi:[0,1]
	v_exp_f16_sdwa v50, v46 dst_sel:WORD_0 dst_unused:UNUSED_PAD src0_sel:WORD_0
	v_exp_f16_sdwa v51, v47 dst_sel:WORD_0 dst_unused:UNUSED_PAD src0_sel:WORD_0
	v_exp_f16_sdwa v52, v48 dst_sel:WORD_0 dst_unused:UNUSED_PAD src0_sel:WORD_0
	v_exp_f16_sdwa v53, v49 dst_sel:WORD_0 dst_unused:UNUSED_PAD src0_sel:WORD_0
	v_exp_f16_sdwa v50, v46 dst_sel:WORD_1 dst_unused:UNUSED_PRESERVE src0_sel:WORD_1
	v_exp_f16_sdwa v51, v47 dst_sel:WORD_1 dst_unused:UNUSED_PRESERVE src0_sel:WORD_1
	v_exp_f16_sdwa v52, v48 dst_sel:WORD_1 dst_unused:UNUSED_PRESERVE src0_sel:WORD_1
	v_exp_f16_sdwa v53, v49 dst_sel:WORD_1 dst_unused:UNUSED_PRESERVE src0_sel:WORD_1
	v_pk_add_f16 v46, v109, v114 neg_lo:[0,1] neg_hi:[0,1]
	v_pk_add_f16 v30, v30, v53
	v_pk_add_f16 v31, v31, v52
	v_pk_add_f16 v32, v32, v51
	v_pk_add_f16 v33, v33, v50
	v_pk_fma_f16 v22, v10, v50, v22
	v_pk_fma_f16 v23, v11, v51, v23
	v_pk_fma_f16 v24, v12, v52, v24
	v_pk_fma_f16 v25, v13, v53, v25
	v_pk_add_f16 v47, v108, v115 neg_lo:[0,1] neg_hi:[0,1]
	v_pk_add_f16 v48, v107, v116 neg_lo:[0,1] neg_hi:[0,1]
	v_pk_add_f16 v49, v106, v117 neg_lo:[0,1] neg_hi:[0,1]
	v_exp_f16_sdwa v50, v46 dst_sel:WORD_0 dst_unused:UNUSED_PAD src0_sel:WORD_0
	v_exp_f16_sdwa v51, v47 dst_sel:WORD_0 dst_unused:UNUSED_PAD src0_sel:WORD_0
	v_exp_f16_sdwa v52, v48 dst_sel:WORD_0 dst_unused:UNUSED_PAD src0_sel:WORD_0
	v_exp_f16_sdwa v53, v49 dst_sel:WORD_0 dst_unused:UNUSED_PAD src0_sel:WORD_0
	v_exp_f16_sdwa v50, v46 dst_sel:WORD_1 dst_unused:UNUSED_PRESERVE src0_sel:WORD_1
	v_exp_f16_sdwa v51, v47 dst_sel:WORD_1 dst_unused:UNUSED_PRESERVE src0_sel:WORD_1
	v_exp_f16_sdwa v52, v48 dst_sel:WORD_1 dst_unused:UNUSED_PRESERVE src0_sel:WORD_1
	v_exp_f16_sdwa v53, v49 dst_sel:WORD_1 dst_unused:UNUSED_PRESERVE src0_sel:WORD_1
	v_pk_add_f16 v46, v62, v114 neg_lo:[0,1] neg_hi:[0,1]
	v_pk_add_f16 v30, v30, v53
	v_pk_add_f16 v33, v33, v50
	v_pk_add_f16 v32, v32, v51
	v_pk_add_f16 v31, v31, v52
	v_pk_fma_f16 v25, v17, v53, v25
	v_pk_fma_f16 v24, v16, v52, v24
	v_pk_fma_f16 v23, v15, v51, v23
	v_pk_fma_f16 v22, v14, v50, v22
	v_pk_add_f16 v47, v63, v115 neg_lo:[0,1] neg_hi:[0,1]
	v_pk_add_f16 v48, v64, v116 neg_lo:[0,1] neg_hi:[0,1]
	v_pk_add_f16 v49, v65, v117 neg_lo:[0,1] neg_hi:[0,1]
	v_exp_f16_sdwa v50, v46 dst_sel:WORD_0 dst_unused:UNUSED_PAD src0_sel:WORD_0
	v_exp_f16_sdwa v51, v47 dst_sel:WORD_0 dst_unused:UNUSED_PAD src0_sel:WORD_0
	v_exp_f16_sdwa v52, v48 dst_sel:WORD_0 dst_unused:UNUSED_PAD src0_sel:WORD_0
	v_exp_f16_sdwa v53, v49 dst_sel:WORD_0 dst_unused:UNUSED_PAD src0_sel:WORD_0
	v_exp_f16_sdwa v50, v46 dst_sel:WORD_1 dst_unused:UNUSED_PRESERVE src0_sel:WORD_1
	v_exp_f16_sdwa v51, v47 dst_sel:WORD_1 dst_unused:UNUSED_PRESERVE src0_sel:WORD_1
	v_exp_f16_sdwa v52, v48 dst_sel:WORD_1 dst_unused:UNUSED_PRESERVE src0_sel:WORD_1
	v_exp_f16_sdwa v53, v49 dst_sel:WORD_1 dst_unused:UNUSED_PRESERVE src0_sel:WORD_1
	v_pk_add_f16 v46, v70, v114 neg_lo:[0,1] neg_hi:[0,1]
	v_pk_add_f16 v30, v30, v53
	v_pk_add_f16 v31, v31, v52
	v_pk_add_f16 v32, v32, v51
	v_pk_add_f16 v33, v33, v50
	v_pk_fma_f16 v22, v26, v50, v22
	v_pk_fma_f16 v23, v27, v51, v23
	v_pk_fma_f16 v24, v28, v52, v24
	v_pk_fma_f16 v25, v29, v53, v25
	v_pk_add_f16 v47, v71, v115 neg_lo:[0,1] neg_hi:[0,1]
	v_pk_add_f16 v48, v72, v116 neg_lo:[0,1] neg_hi:[0,1]
	v_pk_add_f16 v49, v73, v117 neg_lo:[0,1] neg_hi:[0,1]
	v_exp_f16_sdwa v50, v46 dst_sel:WORD_0 dst_unused:UNUSED_PAD src0_sel:WORD_0
	v_exp_f16_sdwa v51, v47 dst_sel:WORD_0 dst_unused:UNUSED_PAD src0_sel:WORD_0
	v_exp_f16_sdwa v52, v48 dst_sel:WORD_0 dst_unused:UNUSED_PAD src0_sel:WORD_0
	v_exp_f16_sdwa v53, v49 dst_sel:WORD_0 dst_unused:UNUSED_PAD src0_sel:WORD_0
	v_exp_f16_sdwa v50, v46 dst_sel:WORD_1 dst_unused:UNUSED_PRESERVE src0_sel:WORD_1
	v_exp_f16_sdwa v51, v47 dst_sel:WORD_1 dst_unused:UNUSED_PRESERVE src0_sel:WORD_1
	v_exp_f16_sdwa v52, v48 dst_sel:WORD_1 dst_unused:UNUSED_PRESERVE src0_sel:WORD_1
	v_exp_f16_sdwa v53, v49 dst_sel:WORD_1 dst_unused:UNUSED_PRESERVE src0_sel:WORD_1
	v_pk_add_f16 v46, v82, v114 neg_lo:[0,1] neg_hi:[0,1]
	v_pk_add_f16 v30, v30, v53
	v_pk_add_f16 v33, v33, v50
	v_pk_add_f16 v32, v32, v51
	v_pk_add_f16 v31, v31, v52
	v_pk_fma_f16 v25, v41, v53, v25
	v_pk_fma_f16 v24, v40, v52, v24
	v_pk_fma_f16 v23, v39, v51, v23
	v_pk_fma_f16 v22, v38, v50, v22
	v_pk_add_f16 v47, v83, v115 neg_lo:[0,1] neg_hi:[0,1]
	v_pk_add_f16 v48, v84, v116 neg_lo:[0,1] neg_hi:[0,1]
	v_pk_add_f16 v49, v85, v117 neg_lo:[0,1] neg_hi:[0,1]
	v_exp_f16_sdwa v50, v46 dst_sel:WORD_0 dst_unused:UNUSED_PAD src0_sel:WORD_0
	v_exp_f16_sdwa v51, v47 dst_sel:WORD_0 dst_unused:UNUSED_PAD src0_sel:WORD_0
	v_exp_f16_sdwa v52, v48 dst_sel:WORD_0 dst_unused:UNUSED_PAD src0_sel:WORD_0
	v_exp_f16_sdwa v53, v49 dst_sel:WORD_0 dst_unused:UNUSED_PAD src0_sel:WORD_0
	v_exp_f16_sdwa v50, v46 dst_sel:WORD_1 dst_unused:UNUSED_PRESERVE src0_sel:WORD_1
	v_exp_f16_sdwa v51, v47 dst_sel:WORD_1 dst_unused:UNUSED_PRESERVE src0_sel:WORD_1
	v_exp_f16_sdwa v52, v48 dst_sel:WORD_1 dst_unused:UNUSED_PRESERVE src0_sel:WORD_1
	v_exp_f16_sdwa v53, v49 dst_sel:WORD_1 dst_unused:UNUSED_PRESERVE src0_sel:WORD_1
	s_nop 0
	v_pk_add_f16 v30, v30, v53
	v_pk_add_f16 v31, v31, v52
	v_rcp_f16_e32 v48, v30
	v_rcp_f16_sdwa v30, v30 dst_sel:DWORD dst_unused:UNUSED_PAD src0_sel:WORD_1
	v_pk_add_f16 v32, v32, v51
	v_rcp_f16_e32 v49, v31
	v_rcp_f16_sdwa v31, v31 dst_sel:DWORD dst_unused:UNUSED_PAD src0_sel:WORD_1
	v_pk_add_f16 v33, v33, v50
	v_rcp_f16_e32 v47, v32
	v_rcp_f16_sdwa v32, v32 dst_sel:DWORD dst_unused:UNUSED_PAD src0_sel:WORD_1
	v_rcp_f16_e32 v46, v33
	v_rcp_f16_sdwa v33, v33 dst_sel:DWORD dst_unused:UNUSED_PAD src0_sel:WORD_1
	v_pk_fma_f16 v25, v61, v53, v25
	v_pack_b32_f16 v30, v48, v30
	v_pk_fma_f16 v24, v60, v52, v24
	v_pk_mul_f16 v25, v25, v30
	v_pack_b32_f16 v30, v49, v31
	v_pk_fma_f16 v23, v59, v51, v23
	v_pk_mul_f16 v24, v24, v30
	v_pack_b32_f16 v30, v47, v32
	v_pk_fma_f16 v22, v58, v50, v22
	v_pk_mul_f16 v23, v23, v30
	v_pack_b32_f16 v30, v46, v33
	v_pk_mul_f16 v22, v22, v30
	s_waitcnt vmcnt(0)
	v_pk_mul_f16 v30, v185, v146 op_sel_hi:[0,1]
	v_pk_mul_f16 v31, v185, v147 op_sel_hi:[0,1]
	v_pk_mul_f16 v32, v185, v148 op_sel_hi:[0,1]
	v_pk_mul_f16 v33, v185, v149 op_sel_hi:[0,1]
	v_pk_mul_f16 v46, v183, v146 op_sel_hi:[0,1]
	v_pk_mul_f16 v47, v183, v147 op_sel_hi:[0,1]
	v_pk_mul_f16 v48, v183, v148 op_sel_hi:[0,1]
	v_pk_mul_f16 v49, v183, v149 op_sel_hi:[0,1]
	v_pk_mul_f16 v50, v184, v146 op_sel_hi:[0,1]
	v_pk_mul_f16 v51, v184, v147 op_sel_hi:[0,1]
	v_pk_mul_f16 v52, v184, v148 op_sel_hi:[0,1]
	v_pk_mul_f16 v53, v184, v149 op_sel_hi:[0,1]
	v_pk_fma_f16 v21, v21, v149, v33
	v_pk_fma_f16 v20, v20, v148, v32
	v_pk_fma_f16 v19, v19, v147, v31
	v_pk_fma_f16 v18, v18, v146, v30
	v_pk_fma_f16 v37, v37, v149, v49
	v_pk_fma_f16 v36, v36, v148, v48
	v_pk_fma_f16 v35, v35, v147, v47
	v_pk_fma_f16 v34, v34, v146, v46
	v_pk_fma_f16 v57, v57, v149, v53
	v_pk_fma_f16 v56, v56, v148, v52
	v_pk_fma_f16 v55, v55, v147, v51
	v_pk_fma_f16 v54, v54, v146, v50
	v_pk_fma_f16 v62, v77, v149, v33
	v_pk_fma_f16 v63, v76, v148, v32
	v_pk_fma_f16 v64, v75, v147, v31
	v_pk_fma_f16 v65, v74, v146, v30
	v_pk_maximum3_f16 v74, v18, v34, v54
	v_pk_maximum3_f16 v75, v19, v35, v55
	v_pk_maximum3_f16 v76, v20, v36, v56
	v_pk_maximum3_f16 v77, v21, v37, v57
	v_pk_fma_f16 v66, v105, v149, v49
	v_pk_fma_f16 v67, v104, v148, v48
	v_pk_fma_f16 v68, v103, v147, v47
	v_pk_fma_f16 v69, v102, v146, v46
	v_pk_fma_f16 v70, v121, v149, v53
	v_pk_fma_f16 v71, v120, v148, v52
	v_pk_fma_f16 v72, v119, v147, v51
	v_pk_fma_f16 v73, v118, v146, v50
	v_pk_fma_f16 v33, v133, v149, v33
	v_pk_fma_f16 v32, v132, v148, v32
	v_pk_fma_f16 v31, v131, v147, v31
	v_pk_fma_f16 v30, v130, v146, v30
	v_pk_fma_f16 v49, v141, v149, v49
	v_pk_fma_f16 v48, v140, v148, v48
	v_pk_fma_f16 v47, v139, v147, v47
	v_pk_fma_f16 v46, v138, v146, v46
	v_pk_fma_f16 v53, v145, v149, v53
	v_pk_fma_f16 v52, v144, v148, v52
	v_pk_fma_f16 v51, v143, v147, v51
	v_pk_fma_f16 v50, v142, v146, v50
	v_pk_maximum3_f16 v82, v65, v69, v73
	v_pk_maximum3_f16 v83, v64, v68, v72
	v_pk_maximum3_f16 v84, v63, v67, v71
	v_pk_maximum3_f16 v85, v62, v66, v70
	v_pk_maximum3_f16 v87, v31, v47, v51
	v_pk_maximum3_f16 v86, v30, v46, v50
	v_pk_maximum3_f16 v88, v32, v48, v52
	v_pk_maximum3_f16 v89, v33, v49, v53
	v_pk_maximum3_f16 v74, v74, v82, v86
	v_pk_maximum3_f16 v75, v75, v83, v87
	v_pk_maximum3_f16 v76, v76, v84, v88
	v_pk_maximum3_f16 v77, v77, v85, v89
	s_nop 0
	v_pk_add_f16 v18, v18, v74 neg_lo:[0,1] neg_hi:[0,1]
	v_pk_add_f16 v19, v19, v75 neg_lo:[0,1] neg_hi:[0,1]
	v_pk_add_f16 v20, v20, v76 neg_lo:[0,1] neg_hi:[0,1]
	v_pk_add_f16 v21, v21, v77 neg_lo:[0,1] neg_hi:[0,1]
	v_pk_add_f16 v34, v34, v74 neg_lo:[0,1] neg_hi:[0,1]
	v_exp_f16_sdwa v82, v18 dst_sel:WORD_0 dst_unused:UNUSED_PAD src0_sel:WORD_0
	v_exp_f16_sdwa v83, v19 dst_sel:WORD_0 dst_unused:UNUSED_PAD src0_sel:WORD_0
	v_exp_f16_sdwa v84, v20 dst_sel:WORD_0 dst_unused:UNUSED_PAD src0_sel:WORD_0
	v_exp_f16_sdwa v85, v21 dst_sel:WORD_0 dst_unused:UNUSED_PAD src0_sel:WORD_0
	v_exp_f16_sdwa v82, v18 dst_sel:WORD_1 dst_unused:UNUSED_PRESERVE src0_sel:WORD_1
	v_exp_f16_sdwa v83, v19 dst_sel:WORD_1 dst_unused:UNUSED_PRESERVE src0_sel:WORD_1
	v_exp_f16_sdwa v84, v20 dst_sel:WORD_1 dst_unused:UNUSED_PRESERVE src0_sel:WORD_1
	v_exp_f16_sdwa v85, v21 dst_sel:WORD_1 dst_unused:UNUSED_PRESERVE src0_sel:WORD_1
	v_pk_add_f16 v35, v35, v75 neg_lo:[0,1] neg_hi:[0,1]
	v_pk_add_f16 v18, v82, 0
	v_pk_add_f16 v19, v83, 0
	v_pk_add_f16 v20, v84, 0
	v_pk_add_f16 v21, v85, 0
	v_pk_fma_f16 v6, v6, v82, 0
	v_pk_fma_f16 v7, v7, v83, 0
	v_pk_fma_f16 v8, v8, v84, 0
	v_pk_fma_f16 v9, v9, v85, 0
	v_pk_add_f16 v36, v36, v76 neg_lo:[0,1] neg_hi:[0,1]
	v_pk_add_f16 v37, v37, v77 neg_lo:[0,1] neg_hi:[0,1]
	v_exp_f16_sdwa v82, v34 dst_sel:WORD_0 dst_unused:UNUSED_PAD src0_sel:WORD_0
	v_exp_f16_sdwa v83, v35 dst_sel:WORD_0 dst_unused:UNUSED_PAD src0_sel:WORD_0
	v_exp_f16_sdwa v84, v36 dst_sel:WORD_0 dst_unused:UNUSED_PAD src0_sel:WORD_0
	v_exp_f16_sdwa v85, v37 dst_sel:WORD_0 dst_unused:UNUSED_PAD src0_sel:WORD_0
	v_exp_f16_sdwa v82, v34 dst_sel:WORD_1 dst_unused:UNUSED_PRESERVE src0_sel:WORD_1
	v_exp_f16_sdwa v83, v35 dst_sel:WORD_1 dst_unused:UNUSED_PRESERVE src0_sel:WORD_1
	v_exp_f16_sdwa v84, v36 dst_sel:WORD_1 dst_unused:UNUSED_PRESERVE src0_sel:WORD_1
	v_exp_f16_sdwa v85, v37 dst_sel:WORD_1 dst_unused:UNUSED_PRESERVE src0_sel:WORD_1
	s_nop 0
	v_pk_add_f16 v21, v21, v85
	v_pk_add_f16 v20, v20, v84
	v_pk_add_f16 v19, v19, v83
	v_pk_add_f16 v18, v18, v82
	v_pk_fma_f16 v9, v13, v85, v9
	v_pk_fma_f16 v8, v12, v84, v8
	v_pk_fma_f16 v7, v11, v83, v7
	v_pk_fma_f16 v6, v10, v82, v6
	v_pk_add_f16 v10, v54, v74 neg_lo:[0,1] neg_hi:[0,1]
	v_pk_add_f16 v11, v55, v75 neg_lo:[0,1] neg_hi:[0,1]
	v_pk_add_f16 v12, v56, v76 neg_lo:[0,1] neg_hi:[0,1]
	v_pk_add_f16 v13, v57, v77 neg_lo:[0,1] neg_hi:[0,1]
	v_exp_f16_sdwa v34, v10 dst_sel:WORD_0 dst_unused:UNUSED_PAD src0_sel:WORD_0
	v_exp_f16_sdwa v35, v11 dst_sel:WORD_0 dst_unused:UNUSED_PAD src0_sel:WORD_0
	v_exp_f16_sdwa v36, v12 dst_sel:WORD_0 dst_unused:UNUSED_PAD src0_sel:WORD_0
	v_exp_f16_sdwa v37, v13 dst_sel:WORD_0 dst_unused:UNUSED_PAD src0_sel:WORD_0
	v_exp_f16_sdwa v34, v10 dst_sel:WORD_1 dst_unused:UNUSED_PRESERVE src0_sel:WORD_1
	v_exp_f16_sdwa v35, v11 dst_sel:WORD_1 dst_unused:UNUSED_PRESERVE src0_sel:WORD_1
	v_exp_f16_sdwa v36, v12 dst_sel:WORD_1 dst_unused:UNUSED_PRESERVE src0_sel:WORD_1
	v_exp_f16_sdwa v37, v13 dst_sel:WORD_1 dst_unused:UNUSED_PRESERVE src0_sel:WORD_1
	v_pk_add_f16 v10, v18, v34
	v_pk_add_f16 v11, v19, v35
	v_pk_add_f16 v12, v20, v36
	v_pk_add_f16 v13, v21, v37
	v_pk_fma_f16 v6, v14, v34, v6
	v_pk_fma_f16 v7, v15, v35, v7
	v_pk_fma_f16 v8, v16, v36, v8
	v_pk_fma_f16 v9, v17, v37, v9
	v_pk_add_f16 v14, v65, v74 neg_lo:[0,1] neg_hi:[0,1]
	v_pk_add_f16 v15, v64, v75 neg_lo:[0,1] neg_hi:[0,1]
	v_pk_add_f16 v16, v63, v76 neg_lo:[0,1] neg_hi:[0,1]
	v_pk_add_f16 v17, v62, v77 neg_lo:[0,1] neg_hi:[0,1]
	v_exp_f16_sdwa v18, v14 dst_sel:WORD_0 dst_unused:UNUSED_PAD src0_sel:WORD_0
	v_exp_f16_sdwa v19, v15 dst_sel:WORD_0 dst_unused:UNUSED_PAD src0_sel:WORD_0
	v_exp_f16_sdwa v20, v16 dst_sel:WORD_0 dst_unused:UNUSED_PAD src0_sel:WORD_0
	v_exp_f16_sdwa v21, v17 dst_sel:WORD_0 dst_unused:UNUSED_PAD src0_sel:WORD_0
	v_exp_f16_sdwa v18, v14 dst_sel:WORD_1 dst_unused:UNUSED_PRESERVE src0_sel:WORD_1
	v_exp_f16_sdwa v19, v15 dst_sel:WORD_1 dst_unused:UNUSED_PRESERVE src0_sel:WORD_1
	v_exp_f16_sdwa v20, v16 dst_sel:WORD_1 dst_unused:UNUSED_PRESERVE src0_sel:WORD_1
	v_exp_f16_sdwa v21, v17 dst_sel:WORD_1 dst_unused:UNUSED_PRESERVE src0_sel:WORD_1
	v_pk_add_f16 v14, v69, v74 neg_lo:[0,1] neg_hi:[0,1]
	v_pk_add_f16 v13, v13, v21
	v_pk_add_f16 v12, v12, v20
	v_pk_add_f16 v11, v11, v19
	v_pk_add_f16 v10, v10, v18
	v_pk_fma_f16 v9, v29, v21, v9
	v_pk_fma_f16 v8, v28, v20, v8
	v_pk_fma_f16 v7, v27, v19, v7
	v_pk_fma_f16 v6, v26, v18, v6
	v_pk_add_f16 v15, v68, v75 neg_lo:[0,1] neg_hi:[0,1]
	v_pk_add_f16 v16, v67, v76 neg_lo:[0,1] neg_hi:[0,1]
	v_pk_add_f16 v17, v66, v77 neg_lo:[0,1] neg_hi:[0,1]
	v_exp_f16_sdwa v18, v14 dst_sel:WORD_0 dst_unused:UNUSED_PAD src0_sel:WORD_0
	v_exp_f16_sdwa v19, v15 dst_sel:WORD_0 dst_unused:UNUSED_PAD src0_sel:WORD_0
	v_exp_f16_sdwa v20, v16 dst_sel:WORD_0 dst_unused:UNUSED_PAD src0_sel:WORD_0
	v_exp_f16_sdwa v21, v17 dst_sel:WORD_0 dst_unused:UNUSED_PAD src0_sel:WORD_0
	v_exp_f16_sdwa v18, v14 dst_sel:WORD_1 dst_unused:UNUSED_PRESERVE src0_sel:WORD_1
	v_exp_f16_sdwa v19, v15 dst_sel:WORD_1 dst_unused:UNUSED_PRESERVE src0_sel:WORD_1
	v_exp_f16_sdwa v20, v16 dst_sel:WORD_1 dst_unused:UNUSED_PRESERVE src0_sel:WORD_1
	v_exp_f16_sdwa v21, v17 dst_sel:WORD_1 dst_unused:UNUSED_PRESERVE src0_sel:WORD_1
	v_pk_add_f16 v14, v73, v74 neg_lo:[0,1] neg_hi:[0,1]
	v_pk_add_f16 v10, v10, v18
	v_pk_add_f16 v11, v11, v19
	v_pk_add_f16 v12, v12, v20
	v_pk_add_f16 v13, v13, v21
	v_pk_fma_f16 v6, v38, v18, v6
	v_pk_fma_f16 v7, v39, v19, v7
	v_pk_fma_f16 v8, v40, v20, v8
	v_pk_fma_f16 v9, v41, v21, v9
	v_pk_add_f16 v15, v72, v75 neg_lo:[0,1] neg_hi:[0,1]
	v_pk_add_f16 v16, v71, v76 neg_lo:[0,1] neg_hi:[0,1]
	v_pk_add_f16 v17, v70, v77 neg_lo:[0,1] neg_hi:[0,1]
	v_exp_f16_sdwa v18, v14 dst_sel:WORD_0 dst_unused:UNUSED_PAD src0_sel:WORD_0
	v_exp_f16_sdwa v19, v15 dst_sel:WORD_0 dst_unused:UNUSED_PAD src0_sel:WORD_0
	v_exp_f16_sdwa v20, v16 dst_sel:WORD_0 dst_unused:UNUSED_PAD src0_sel:WORD_0
	v_exp_f16_sdwa v21, v17 dst_sel:WORD_0 dst_unused:UNUSED_PAD src0_sel:WORD_0
	v_exp_f16_sdwa v18, v14 dst_sel:WORD_1 dst_unused:UNUSED_PRESERVE src0_sel:WORD_1
	v_exp_f16_sdwa v19, v15 dst_sel:WORD_1 dst_unused:UNUSED_PRESERVE src0_sel:WORD_1
	v_exp_f16_sdwa v20, v16 dst_sel:WORD_1 dst_unused:UNUSED_PRESERVE src0_sel:WORD_1
	v_exp_f16_sdwa v21, v17 dst_sel:WORD_1 dst_unused:UNUSED_PRESERVE src0_sel:WORD_1
	v_pk_add_f16 v14, v30, v74 neg_lo:[0,1] neg_hi:[0,1]
	v_pk_add_f16 v13, v13, v21
	v_pk_add_f16 v12, v12, v20
	v_pk_add_f16 v11, v11, v19
	v_pk_add_f16 v10, v10, v18
	v_pk_fma_f16 v9, v61, v21, v9
	v_pk_fma_f16 v8, v60, v20, v8
	v_pk_fma_f16 v7, v59, v19, v7
	v_pk_fma_f16 v6, v58, v18, v6
	v_pk_add_f16 v15, v31, v75 neg_lo:[0,1] neg_hi:[0,1]
	v_pk_add_f16 v16, v32, v76 neg_lo:[0,1] neg_hi:[0,1]
	v_pk_add_f16 v17, v33, v77 neg_lo:[0,1] neg_hi:[0,1]
	v_exp_f16_sdwa v18, v14 dst_sel:WORD_0 dst_unused:UNUSED_PAD src0_sel:WORD_0
	v_exp_f16_sdwa v19, v15 dst_sel:WORD_0 dst_unused:UNUSED_PAD src0_sel:WORD_0
	v_exp_f16_sdwa v20, v16 dst_sel:WORD_0 dst_unused:UNUSED_PAD src0_sel:WORD_0
	v_exp_f16_sdwa v21, v17 dst_sel:WORD_0 dst_unused:UNUSED_PAD src0_sel:WORD_0
	v_exp_f16_sdwa v18, v14 dst_sel:WORD_1 dst_unused:UNUSED_PRESERVE src0_sel:WORD_1
	v_exp_f16_sdwa v19, v15 dst_sel:WORD_1 dst_unused:UNUSED_PRESERVE src0_sel:WORD_1
	v_exp_f16_sdwa v20, v16 dst_sel:WORD_1 dst_unused:UNUSED_PRESERVE src0_sel:WORD_1
	v_exp_f16_sdwa v21, v17 dst_sel:WORD_1 dst_unused:UNUSED_PRESERVE src0_sel:WORD_1
	v_pk_add_f16 v10, v10, v18
	v_pk_add_f16 v11, v11, v19
	v_pk_add_f16 v12, v12, v20
	v_pk_add_f16 v13, v13, v21
	v_pk_fma_f16 v14, v78, v18, v6
	v_pk_fma_f16 v15, v79, v19, v7
	v_pk_fma_f16 v16, v80, v20, v8
	v_pk_fma_f16 v17, v81, v21, v9
	v_pk_add_f16 v6, v46, v74 neg_lo:[0,1] neg_hi:[0,1]
	v_pk_add_f16 v7, v47, v75 neg_lo:[0,1] neg_hi:[0,1]
	v_pk_add_f16 v8, v48, v76 neg_lo:[0,1] neg_hi:[0,1]
	v_pk_add_f16 v9, v49, v77 neg_lo:[0,1] neg_hi:[0,1]
	v_exp_f16_sdwa v18, v6 dst_sel:WORD_0 dst_unused:UNUSED_PAD src0_sel:WORD_0
	v_exp_f16_sdwa v19, v7 dst_sel:WORD_0 dst_unused:UNUSED_PAD src0_sel:WORD_0
	v_exp_f16_sdwa v20, v8 dst_sel:WORD_0 dst_unused:UNUSED_PAD src0_sel:WORD_0
	v_exp_f16_sdwa v21, v9 dst_sel:WORD_0 dst_unused:UNUSED_PAD src0_sel:WORD_0
	v_exp_f16_sdwa v18, v6 dst_sel:WORD_1 dst_unused:UNUSED_PRESERVE src0_sel:WORD_1
	v_exp_f16_sdwa v19, v7 dst_sel:WORD_1 dst_unused:UNUSED_PRESERVE src0_sel:WORD_1
	v_exp_f16_sdwa v20, v8 dst_sel:WORD_1 dst_unused:UNUSED_PRESERVE src0_sel:WORD_1
	v_exp_f16_sdwa v21, v9 dst_sel:WORD_1 dst_unused:UNUSED_PRESERVE src0_sel:WORD_1
	s_nop 0
	v_pk_add_f16 v9, v13, v21
	v_pk_add_f16 v8, v12, v20
	v_pk_add_f16 v7, v11, v19
	v_pk_add_f16 v6, v10, v18
	v_pk_fma_f16 v13, v93, v21, v17
	v_pk_fma_f16 v12, v92, v20, v16
	v_pk_fma_f16 v11, v91, v19, v15
	v_pk_fma_f16 v10, v90, v18, v14
	v_pk_add_f16 v18, v50, v74 neg_lo:[0,1] neg_hi:[0,1]
	v_pk_add_f16 v19, v51, v75 neg_lo:[0,1] neg_hi:[0,1]
	v_pk_add_f16 v20, v52, v76 neg_lo:[0,1] neg_hi:[0,1]
	v_pk_add_f16 v21, v53, v77 neg_lo:[0,1] neg_hi:[0,1]
	v_exp_f16_sdwa v14, v18 dst_sel:WORD_0 dst_unused:UNUSED_PAD src0_sel:WORD_0
	v_exp_f16_sdwa v17, v19 dst_sel:WORD_0 dst_unused:UNUSED_PAD src0_sel:WORD_0
	v_exp_f16_sdwa v15, v20 dst_sel:WORD_0 dst_unused:UNUSED_PAD src0_sel:WORD_0
	v_exp_f16_sdwa v16, v21 dst_sel:WORD_0 dst_unused:UNUSED_PAD src0_sel:WORD_0
	v_exp_f16_sdwa v14, v18 dst_sel:WORD_1 dst_unused:UNUSED_PRESERVE src0_sel:WORD_1
	v_exp_f16_sdwa v17, v19 dst_sel:WORD_1 dst_unused:UNUSED_PRESERVE src0_sel:WORD_1
	v_exp_f16_sdwa v15, v20 dst_sel:WORD_1 dst_unused:UNUSED_PRESERVE src0_sel:WORD_1
	v_exp_f16_sdwa v16, v21 dst_sel:WORD_1 dst_unused:UNUSED_PRESERVE src0_sel:WORD_1
	s_nop 0
.LBB5_42:
	s_and_b64 vcc, exec, s[4:5]
	s_cbranch_vccz .LBB5_3
	s_load_dwordx2 s[0:1], s[22:23], 0x18
	s_waitcnt lgkmcnt(0)
	s_load_dwordx2 s[6:7], s[0:1], 0x0
	s_load_dword s28, s[0:1], 0x8
	v_cmp_lt_u32_e64 s[64:65], 0, v182
	v_cmp_gt_u32_e64 s[66:67], 63, v182
	v_cmp_lt_u32_e64 s[68:69], 0, v162
	v_cmp_gt_u32_e64 s[70:71], 60, v162
	buffer_load_dwordx4 v[184:187], v180, s[16:19], 0 offen
	s_and_b64 s[72:73], s[68:69], s[64:65]
	s_and_b64 s[74:75], s[68:69], s[66:67]
	s_and_b64 s[76:77], s[70:71], s[64:65]
	s_and_b64 s[78:79], s[70:71], s[66:67]
	v_add_u32_e32 v224, 0xfffe7c00, v180
	v_add_u32_e32 v225, 0xfffe8000, v180
	s_mov_b64 exec, s[72:73]
	buffer_load_dwordx4 v[110:113], v224, s[16:19], 0 offen
	buffer_load_dwordx4 v[78:81], v224, s[16:19], 0 offen offset:512
	s_mov_b64 exec, -1
	s_mov_b64 exec, s[68:69]
	buffer_load_dwordx4 v[126:129], v225, s[16:19], 0 offen offset:512
	buffer_load_dwordx4 v[102:105], v225, s[16:19], 0 offen offset:1024
	s_mov_b64 exec, -1
	s_mov_b64 exec, s[74:75]
	buffer_load_dwordx4 v[134:137], v225, s[16:19], 0 offen offset:2048
	buffer_load_dwordx4 v[114:117], v225, s[16:19], 0 offen offset:2560
	s_mov_b64 exec, -1
	v_add_u32_e32 v224, 0xfffffc00, v180
	s_mov_b64 exec, s[64:65]
	buffer_load_dwordx4 v[82:85], v224, s[16:19], 0 offen
	buffer_load_dwordx4 v[42:45], v224, s[16:19], 0 offen offset:512
	s_mov_b64 exec, -1
	buffer_load_dwordx4 v[106:109], v180, s[16:19], 0 offen offset:512
	buffer_load_dwordx4 v[62:65], v180, s[16:19], 0 offen offset:1024
	s_mov_b64 exec, s[66:67]
	buffer_load_dwordx4 v[122:125], v180, s[16:19], 0 offen offset:2048
	buffer_load_dwordx4 v[86:89], v180, s[16:19], 0 offen offset:2560
	s_mov_b64 exec, -1
	v_add_u32_e32 v224, 0x17c00, v180
	v_add_u32_e32 v225, 0x18000, v180
	s_mov_b64 exec, s[64:65]
	buffer_load_dwordx4 v[50:53], v224, s[16:19], 0 offen
	buffer_load_dwordx4 v[22:25], v224, s[16:19], 0 offen offset:512
	s_mov_b64 exec, -1
	buffer_load_dwordx4 v[66:69], v225, s[16:19], 0 offen offset:512
	buffer_load_dwordx4 v[34:37], v225, s[16:19], 0 offen offset:1024
	s_mov_b64 exec, s[66:67]
	buffer_load_dwordx4 v[94:97], v225, s[16:19], 0 offen offset:2048
	buffer_load_dwordx4 v[46:49], v225, s[16:19], 0 offen offset:2560
	s_mov_b64 exec, -1
	v_add_u32_e32 v224, 0x18000, v180
	buffer_load_dwordx4 v[154:157], v224, s[16:19], 0 offen
	v_add_u32_e32 v225, 0x30000, v180
	buffer_load_dwordx4 v[150:153], v225, s[16:19], 0 offen
	v_add_u32_e32 v224, 0x48000, v180
	buffer_load_dwordx4 v[146:149], v224, s[16:19], 0 offen
	v_add_u32_e32 v224, 0x2fc00, v180
	v_add_u32_e32 v225, 0x30000, v180
	v_add_u32_e32 v226, 0x47c00, v180
	v_add_u32_e32 v227, 0x48000, v180
	v_add_u32_e32 v228, 0x5fc00, v180
	v_add_u32_e32 v229, 0x60000, v180
	s_not_b64 exec, s[72:73]
	s_cbranch_execz .Lmyf_D2_0
	v_mov_b32_e32 v110, v172
	v_mov_b32_e32 v111, v174
	v_mov_b32_e32 v112, v176
	v_mov_b32_e32 v113, v178
	v_mov_b32_e32 v78, v173
	v_mov_b32_e32 v79, v175
	v_mov_b32_e32 v80, v177
	v_mov_b32_e32 v81, v179

_Z7k_attn2ILi2EEv8AttnArgs:
	v_readfirstlane_b32 s3, v0
	s_lshl_b32 s12, s3, 1
	v_lshlrev_b32_e32 v3, 3, v0
	s_and_b32 s12, s12, 0x80
	v_and_b32_e32 v3, 0x78, v3
	s_load_dwordx4 s[8:11], s[0:1], 0x0
	s_load_dwordx2 s[4:5], s[0:1], 0x10
	s_load_dwordx2 s[6:7], s[0:1], 0x50
	v_or_b32_e32 v180, s12, v3
	s_lshl_b32 s12, s2, 5
	v_lshrrev_b32_e32 v1, 5, v0
	v_bfe_u32 v2, v0, 4, 2
	s_and_b32 s14, s12, 0xe0
	s_lshr_b32 s12, s2, 3
	v_lshrrev_b32_e32 v0, 6, v0
	v_and_b32_e32 v1, 4, v1
	s_add_i32 s14, s14, s12
	s_and_b32 s2, s2, 56
	v_and_b32_e32 v0, 4, v0
	v_and_or_b32 v181, s14, 56, v0
	v_or3_b32 v182, v2, s2, v1
	s_and_b32 s2, s14, 0x3ffffc0
	v_or_b32_e32 v4, s2, v181
	v_lshlrev_b32_e32 v0, 1, v180
	v_mov_b32_e32 v1, 0
	s_waitcnt lgkmcnt(0)
	v_lshl_add_u64 v[2:3], s[6:7], 0, v[0:1]
	v_lshl_or_b32 v0, v4, 6, v182
	v_lshlrev_b64 v[4:5], 9, v[0:1]
	v_lshl_add_u64 v[8:9], v[2:3], 0, v[4:5]
	v_or_b32_e32 v4, 64, v0
	v_mov_b32_e32 v5, v1
	v_lshlrev_b64 v[4:5], 9, v[4:5]
	v_lshlrev_b32_e32 v20, 2, v180
	v_lshl_add_u64 v[10:11], v[2:3], 0, v[4:5]
	global_load_dwordx4 v[22:25], v20, s[10:11] offset:16
	global_load_dwordx4 v[16:19], v20, s[10:11]
	global_load_dwordx4 v[26:29], v20, s[4:5] offset:16
	global_load_dwordx4 v[30:33], v20, s[4:5]
	global_load_dwordx4 v[12:15], v[8:9], off nt
	global_load_dwordx4 v[4:7], v[10:11], off nt
	v_or_b32_e32 v8, 0x80, v0
	v_mov_b32_e32 v9, v1
	v_lshlrev_b64 v[8:9], 9, v[8:9]
	v_or_b32_e32 v0, 0xc0, v0
	v_lshl_add_u64 v[20:21], v[2:3], 0, v[8:9]
	v_lshlrev_b64 v[0:1], 9, v[0:1]
	v_lshl_add_u64 v[34:35], v[2:3], 0, v[0:1]
	global_load_dwordx4 v[8:11], v[20:21], off nt
	global_load_dwordx4 v[0:3], v[34:35], off nt
	s_bitcmp1_b32 s3, 6
	s_cselect_b64 s[4:5], -1, 0
	s_and_b32 s2, s14, 0x3ffc0
	v_or_b32_e32 v20, s2, v181
	v_lshl_or_b32 v20, v20, 6, v182
	v_add_u32_e32 v184, -1, v182
	v_add_u32_e32 v185, -1, v181
	v_mul_u32_u24_e32 v20, 0x300, v20
	v_or_b32_e32 v34, v185, v184
	v_or_b32_e32 v20, v180, v20
	s_mov_b32 s11, 0x20000
	s_mov_b32 s10, 0x1800000
	s_and_b32 s9, s9, 0xffff
	v_lshlrev_b32_e32 v183, 1, v20
	v_cmp_gt_u32_e64 s[2:3], 64, v34
	s_and_b64 vcc, exec, s[4:5]
	s_waitcnt vmcnt(7)
	v_cvt_pk_f16_f32 v22, v22, v23
	s_waitcnt vmcnt(6)
	v_cvt_pk_f16_f32 v20, v16, v17
	v_cvt_pk_f16_f32 v21, v18, v19
	s_waitcnt vmcnt(4)
	v_cvt_pk_f16_f32 v16, v30, v31
	v_cvt_pk_f16_f32 v17, v32, v33
	v_cvt_pk_f16_f32 v18, v26, v27
	v_cvt_pk_f16_f32 v23, v24, v25
	v_cvt_pk_f16_f32 v19, v28, v29
	s_cbranch_vccz .LBB6_38
	s_load_dwordx2 s[12:13], s[0:1], 0x20
	s_waitcnt lgkmcnt(0)
	s_load_dwordx2 s[4:5], s[12:13], 0x0
	s_load_dword s12, s[12:13], 0x8
	v_cmp_lt_u32_e64 s[64:65], 0, v182
	v_cmp_gt_u32_e64 s[66:67], 63, v182
	v_cmp_lt_u32_e64 s[68:69], 0, v181
	v_cmp_gt_u32_e64 s[70:71], 60, v181
	buffer_load_dwordx4 v[190:193], v183, s[8:11], 0 offen
	s_and_b64 s[72:73], s[68:69], s[64:65]
	s_and_b64 s[74:75], s[68:69], s[66:67]
	s_and_b64 s[76:77], s[70:71], s[64:65]
	s_and_b64 s[78:79], s[70:71], s[66:67]
	v_add_u32_e32 v228, 0xfffe7c00, v183
	v_add_u32_e32 v229, 0xfffe8000, v183
	s_mov_b64 exec, s[72:73]
	buffer_load_dwordx4 v[136:139], v228, s[8:11], 0 offen
	buffer_load_dwordx4 v[96:99], v228, s[8:11], 0 offen offset:512
	s_mov_b64 exec, -1
	s_mov_b64 exec, s[68:69]
	buffer_load_dwordx4 v[152:155], v229, s[8:11], 0 offen offset:512
	buffer_load_dwordx4 v[124:127], v229, s[8:11], 0 offen offset:1024
	s_mov_b64 exec, -1
	s_mov_b64 exec, s[74:75]
	buffer_load_dwordx4 v[160:163], v229, s[8:11], 0 offen offset:2048
	buffer_load_dwordx4 v[140:143], v229, s[8:11], 0 offen offset:2560
	s_mov_b64 exec, -1
	v_add_u32_e32 v228, 0xfffffc00, v183
	s_mov_b64 exec, s[64:65]
	buffer_load_dwordx4 v[112:115], v228, s[8:11], 0 offen
	buffer_load_dwordx4 v[68:71], v228, s[8:11], 0 offen offset:512
	s_mov_b64 exec, -1
	buffer_load_dwordx4 v[132:135], v183, s[8:11], 0 offen offset:512
	buffer_load_dwordx4 v[88:91], v183, s[8:11], 0 offen offset:1024
	s_mov_b64 exec, s[66:67]
	buffer_load_dwordx4 v[148:151], v183, s[8:11], 0 offen offset:2048
	buffer_load_dwordx4 v[108:111], v183, s[8:11], 0 offen offset:2560
	s_mov_b64 exec, -1
	v_add_u32_e32 v228, 0x17c00, v183
	v_add_u32_e32 v229, 0x18000, v183
	s_mov_b64 exec, s[64:65]
	buffer_load_dwordx4 v[76:79], v228, s[8:11], 0 offen
	buffer_load_dwordx4 v[48:51], v228, s[8:11], 0 offen offset:512
	s_mov_b64 exec, -1
	buffer_load_dwordx4 v[92:95], v229, s[8:11], 0 offen offset:512
	buffer_load_dwordx4 v[56:59], v229, s[8:11], 0 offen offset:1024
	s_mov_b64 exec, s[66:67]
	buffer_load_dwordx4 v[116:119], v229, s[8:11], 0 offen offset:2048
	buffer_load_dwordx4 v[72:75], v229, s[8:11], 0 offen offset:2560
	s_mov_b64 exec, -1
	v_add_u32_e32 v228, 0x18000, v183
	buffer_load_dwordx4 v[176:179], v228, s[8:11], 0 offen
	v_add_u32_e32 v229, 0x30000, v183
	buffer_load_dwordx4 v[172:175], v229, s[8:11], 0 offen
	v_add_u32_e32 v228, 0x48000, v183
	buffer_load_dwordx4 v[168:171], v228, s[8:11], 0 offen
	v_add_u32_e32 v228, 0x2fc00, v183
	v_add_u32_e32 v229, 0x30000, v183
	v_add_u32_e32 v230, 0x47c00, v183
	v_add_u32_e32 v231, 0x48000, v183
	v_add_u32_e32 v232, 0x5fc00, v183
	v_add_u32_e32 v233, 0x60000, v183
	s_not_b64 exec, s[72:73]
	s_cbranch_execz .Lmyf_E1_0
	v_mov_b32_e32 v136, v20
	v_mov_b32_e32 v137, v21
	v_mov_b32_e32 v138, v22
	v_mov_b32_e32 v139, v23
	v_mov_b32_e32 v96, v16
	v_mov_b32_e32 v97, v17
	v_mov_b32_e32 v98, v18
	v_mov_b32_e32 v99, v19
.Lmyf_E1_0:
	s_not_b64 exec, s[68:69]
	s_cbranch_execz .Lmyf_E1_1
	v_mov_b32_e32 v152, v20
	v_mov_b32_e32 v153, v21
	v_mov_b32_e32 v154, v22
	v_mov_b32_e32 v155, v23
	v_mov_b32_e32 v124, v16
	v_mov_b32_e32 v125, v17
	v_mov_b32_e32 v126, v18
	v_mov_b32_e32 v127, v19
.Lmyf_E1_1:
	s_not_b64 exec, s[74:75]
	s_cbranch_execz .Lmyf_E1_2
	v_mov_b32_e32 v160, v20
	v_mov_b32_e32 v161, v21
	v_mov_b32_e32 v162, v22
	v_mov_b32_e32 v163, v23
	v_mov_b32_e32 v140, v16
	v_mov_b32_e32 v141, v17
	v_mov_b32_e32 v142, v18
	v_mov_b32_e32 v143, v19
.Lmyf_E1_2:
	s_not_b64 exec, s[64:65]
	s_cbranch_execz .Lmyf_E1_3
	v_mov_b32_e32 v112, v20
	v_mov_b32_e32 v113, v21
	v_mov_b32_e32 v114, v22
	v_mov_b32_e32 v115, v23
	v_mov_b32_e32 v68, v16
	v_mov_b32_e32 v69, v17
	v_mov_b32_e32 v70, v18
	v_mov_b32_e32 v71, v19
	v_mov_b32_e32 v76, v20
	v_mov_b32_e32 v77, v21
	v_mov_b32_e32 v78, v22
	v_mov_b32_e32 v79, v23
	v_mov_b32_e32 v48, v16
	v_mov_b32_e32 v49, v17
	v_mov_b32_e32 v50, v18
	v_mov_b32_e32 v51, v19
	v_mov_b32_e32 v44, v20
	v_mov_b32_e32 v45, v21
	v_mov_b32_e32 v46, v22
	v_mov_b32_e32 v47, v23
	v_mov_b32_e32 v32, v16
	v_mov_b32_e32 v33, v17
	v_mov_b32_e32 v34, v18
	v_mov_b32_e32 v35, v19
	v_mov_b32_e32 v100, v20
	v_mov_b32_e32 v101, v21
	v_mov_b32_e32 v102, v22
	v_mov_b32_e32 v103, v23
	v_mov_b32_e32 v52, v16
	v_mov_b32_e32 v53, v17
	v_mov_b32_e32 v54, v18
	v_mov_b32_e32 v55, v19
.Lmyf_E1_3:
	s_not_b64 exec, s[66:67]
	s_cbranch_execz .Lmyf_E1_4
	v_mov_b32_e32 v148, v20
	v_mov_b32_e32 v149, v21
	v_mov_b32_e32 v150, v22
	v_mov_b32_e32 v151, v23
	v_mov_b32_e32 v108, v16
	v_mov_b32_e32 v109, v17
	v_mov_b32_e32 v110, v18
	v_mov_b32_e32 v111, v19
	v_mov_b32_e32 v116, v20
	v_mov_b32_e32 v117, v21
	v_mov_b32_e32 v118, v22
	v_mov_b32_e32 v119, v23
	v_mov_b32_e32 v72, v16
	v_mov_b32_e32 v73, v17
	v_mov_b32_e32 v74, v18
	v_mov_b32_e32 v75, v19
	v_mov_b32_e32 v80, v20
	v_mov_b32_e32 v81, v21
	v_mov_b32_e32 v82, v22
	v_mov_b32_e32 v83, v23
	v_mov_b32_e32 v40, v16
	v_mov_b32_e32 v41, v17
	v_mov_b32_e32 v42, v18
	v_mov_b32_e32 v43, v19
	v_mov_b32_e32 v144, v20
	v_mov_b32_e32 v145, v21
	v_mov_b32_e32 v146, v22
	v_mov_b32_e32 v147, v23
	v_mov_b32_e32 v84, v16
	v_mov_b32_e32 v85, v17
	v_mov_b32_e32 v86, v18
	v_mov_b32_e32 v87, v19
.Lmyf_E1_4:
	s_not_b64 exec, s[76:77]
	s_cbranch_execz .Lmyf_E1_5
	v_mov_b32_e32 v156, v20
	v_mov_b32_e32 v157, v21
	v_mov_b32_e32 v158, v22
	v_mov_b32_e32 v159, v23
	v_mov_b32_e32 v104, v16
	v_mov_b32_e32 v105, v17
	v_mov_b32_e32 v106, v18
	v_mov_b32_e32 v107, v19
.Lmyf_E1_5:
	s_not_b64 exec, s[70:71]
	s_cbranch_execz .Lmyf_E1_6
	v_mov_b32_e32 v164, v20
	v_mov_b32_e32 v165, v21
	v_mov_b32_e32 v166, v22
	v_mov_b32_e32 v167, v23
	v_mov_b32_e32 v120, v16
	v_mov_b32_e32 v121, v17
	v_mov_b32_e32 v122, v18
	v_mov_b32_e32 v123, v19
.Lmyf_E1_6:
	s_not_b64 exec, s[78:79]
	s_cbranch_execz .Lmyf_E1_7
	v_mov_b32_e32 v28, v20
	v_mov_b32_e32 v29, v21
	v_mov_b32_e32 v30, v22
	v_mov_b32_e32 v31, v23
	v_mov_b32_e32 v24, v16
	v_mov_b32_e32 v25, v17
	v_mov_b32_e32 v26, v18
	v_mov_b32_e32 v27, v19
.Lmyf_E1_7:
	s_mov_b64 exec, -1
	s_waitcnt lgkmcnt(0)
	v_cvt_f16_f32_e32 v186, s5
	v_cvt_f16_f32_e32 v188, s4
	v_cvt_f16_f32_e32 v187, s12
	s_waitcnt vmcnt(3)
	v_pk_mul_f16 v196, v188, v193 op_sel_hi:[0,1]
	v_pk_mul_f16 v200, v186, v193 op_sel_hi:[0,1]
	v_pk_mul_f16 v204, v187, v193 op_sel_hi:[0,1]
	v_pk_mul_f16 v189, v188, v190 op_sel_hi:[0,1]
	v_pk_mul_f16 v194, v188, v191 op_sel_hi:[0,1]
	v_pk_mul_f16 v195, v188, v192 op_sel_hi:[0,1]
	v_pk_mul_f16 v197, v186, v190 op_sel_hi:[0,1]
	s_mov_b64 exec, s[64:65]
	buffer_load_dwordx4 v[44:47], v228, s[8:11], 0 offen
	buffer_load_dwordx4 v[32:35], v228, s[8:11], 0 offen offset:512
	s_mov_b64 exec, -1
	v_pk_mul_f16 v198, v186, v191 op_sel_hi:[0,1]
	v_pk_mul_f16 v199, v186, v192 op_sel_hi:[0,1]
	v_pk_mul_f16 v201, v187, v190 op_sel_hi:[0,1]
	v_pk_mul_f16 v202, v187, v191 op_sel_hi:[0,1]
	v_pk_mul_f16 v203, v187, v192 op_sel_hi:[0,1]
	v_pk_fma_f16 v139, v139, v193, v196
	v_pk_fma_f16 v155, v155, v193, v200
	v_pk_fma_f16 v163, v163, v193, v204
	v_pk_fma_f16 v205, v115, v193, v196
	v_pk_fma_f16 v209, v135, v193, v200
	v_pk_fma_f16 v213, v151, v193, v204
	v_pk_fma_f16 v196, v79, v193, v196
	v_pk_fma_f16 v200, v95, v193, v200
	buffer_load_dwordx4 v[60:63], v229, s[8:11], 0 offen offset:512
	buffer_load_dwordx4 v[36:39], v229, s[8:11], 0 offen offset:1024
	v_pk_fma_f16 v193, v119, v193, v204
	v_pk_maximum3_f16 v204, v139, v155, v163
	v_pk_fma_f16 v138, v138, v192, v195
	v_pk_fma_f16 v137, v137, v191, v194
	v_pk_fma_f16 v136, v136, v190, v189
	v_pk_fma_f16 v154, v154, v192, v199
	v_pk_fma_f16 v153, v153, v191, v198
	v_pk_fma_f16 v152, v152, v190, v197
	v_pk_fma_f16 v162, v162, v192, v203
	v_pk_fma_f16 v161, v161, v191, v202
	v_pk_fma_f16 v160, v160, v190, v201
	v_pk_fma_f16 v206, v114, v192, v195
	v_pk_fma_f16 v207, v113, v191, v194
	v_pk_fma_f16 v208, v112, v190, v189
	v_pk_fma_f16 v210, v134, v192, v199
	v_pk_fma_f16 v211, v133, v191, v198
	s_mov_b64 exec, s[66:67]
	buffer_load_dwordx4 v[80:83], v229, s[8:11], 0 offen offset:2048
	buffer_load_dwordx4 v[40:43], v229, s[8:11], 0 offen offset:2560
	s_mov_b64 exec, -1
	v_pk_fma_f16 v212, v132, v190, v197
	v_pk_fma_f16 v214, v150, v192, v203
	v_pk_fma_f16 v215, v149, v191, v202
	v_pk_fma_f16 v216, v148, v190, v201
	v_pk_fma_f16 v195, v78, v192, v195
	v_pk_fma_f16 v194, v77, v191, v194
	v_pk_fma_f16 v189, v76, v190, v189
	v_pk_fma_f16 v199, v94, v192, v199
	v_pk_fma_f16 v198, v93, v191, v198
	v_pk_fma_f16 v197, v92, v190, v197
	v_pk_fma_f16 v192, v118, v192, v203
	v_pk_fma_f16 v191, v117, v191, v202
	v_pk_fma_f16 v190, v116, v190, v201
	v_pk_maximum3_f16 v201, v136, v152, v160
	v_pk_maximum3_f16 v202, v137, v153, v161
	v_pk_maximum3_f16 v203, v138, v154, v162
	v_pk_maximum3_f16 v220, v205, v209, v213
	v_pk_maximum3_f16 v224, v196, v200, v193
	v_pk_maximum3_f16 v217, v208, v212, v216
	v_pk_maximum3_f16 v218, v207, v211, v215
	v_pk_maximum3_f16 v219, v206, v210, v214
	v_pk_maximum3_f16 v221, v189, v197, v190
	v_pk_maximum3_f16 v222, v194, v198, v191
	v_pk_maximum3_f16 v204, v204, v220, v224
	v_pk_maximum3_f16 v223, v195, v199, v192
	v_pk_maximum3_f16 v201, v201, v217, v221
	v_pk_maximum3_f16 v202, v202, v218, v222
	v_pk_maximum3_f16 v203, v203, v219, v223
	v_pk_add_f16 v139, v139, v204 neg_lo:[0,1] neg_hi:[0,1]
	s_mov_b64 exec, s[64:65]
	buffer_load_dwordx4 v[100:103], v230, s[8:11], 0 offen
	buffer_load_dwordx4 v[52:55], v230, s[8:11], 0 offen offset:512
	s_mov_b64 exec, -1
	v_pk_add_f16 v136, v136, v201 neg_lo:[0,1] neg_hi:[0,1]
	v_pk_add_f16 v137, v137, v202 neg_lo:[0,1] neg_hi:[0,1]
	v_pk_add_f16 v138, v138, v203 neg_lo:[0,1] neg_hi:[0,1]
	v_pk_add_f16 v152, v152, v201 neg_lo:[0,1] neg_hi:[0,1]
	v_exp_f16_sdwa v217, v136 dst_sel:WORD_0 dst_unused:UNUSED_PAD src0_sel:WORD_0
	v_exp_f16_sdwa v218, v137 dst_sel:WORD_0 dst_unused:UNUSED_PAD src0_sel:WORD_0
	v_exp_f16_sdwa v219, v138 dst_sel:WORD_0 dst_unused:UNUSED_PAD src0_sel:WORD_0
	v_exp_f16_sdwa v220, v139 dst_sel:WORD_0 dst_unused:UNUSED_PAD src0_sel:WORD_0
	v_exp_f16_sdwa v217, v136 dst_sel:WORD_1 dst_unused:UNUSED_PRESERVE src0_sel:WORD_1
	v_exp_f16_sdwa v218, v137 dst_sel:WORD_1 dst_unused:UNUSED_PRESERVE src0_sel:WORD_1
	v_exp_f16_sdwa v219, v138 dst_sel:WORD_1 dst_unused:UNUSED_PRESERVE src0_sel:WORD_1
	v_exp_f16_sdwa v220, v139 dst_sel:WORD_1 dst_unused:UNUSED_PRESERVE src0_sel:WORD_1
	v_pk_add_f16 v153, v153, v202 neg_lo:[0,1] neg_hi:[0,1]
	v_pk_add_f16 v139, v217, 0
	v_pk_fma_f16 v99, v99, v220, 0
	v_pk_add_f16 v136, v220, 0
	v_pk_add_f16 v137, v219, 0
	v_pk_add_f16 v138, v218, 0
	v_pk_fma_f16 v98, v98, v219, 0
	v_pk_fma_f16 v97, v97, v218, 0
	v_pk_fma_f16 v96, v96, v217, 0
	v_pk_add_f16 v154, v154, v203 neg_lo:[0,1] neg_hi:[0,1]
	buffer_load_dwordx4 v[128:131], v231, s[8:11], 0 offen offset:512
	buffer_load_dwordx4 v[64:67], v231, s[8:11], 0 offen offset:1024
	v_pk_add_f16 v155, v155, v204 neg_lo:[0,1] neg_hi:[0,1]
	v_exp_f16_sdwa v217, v152 dst_sel:WORD_0 dst_unused:UNUSED_PAD src0_sel:WORD_0
	v_exp_f16_sdwa v218, v153 dst_sel:WORD_0 dst_unused:UNUSED_PAD src0_sel:WORD_0
	v_exp_f16_sdwa v219, v154 dst_sel:WORD_0 dst_unused:UNUSED_PAD src0_sel:WORD_0
	v_exp_f16_sdwa v220, v155 dst_sel:WORD_0 dst_unused:UNUSED_PAD src0_sel:WORD_0
	v_exp_f16_sdwa v217, v152 dst_sel:WORD_1 dst_unused:UNUSED_PRESERVE src0_sel:WORD_1
	v_exp_f16_sdwa v218, v153 dst_sel:WORD_1 dst_unused:UNUSED_PRESERVE src0_sel:WORD_1
	v_exp_f16_sdwa v219, v154 dst_sel:WORD_1 dst_unused:UNUSED_PRESERVE src0_sel:WORD_1
	v_exp_f16_sdwa v220, v155 dst_sel:WORD_1 dst_unused:UNUSED_PRESERVE src0_sel:WORD_1
	v_pk_add_f16 v139, v139, v217
	v_pk_fma_f16 v99, v127, v220, v99
	v_pk_add_f16 v127, v163, v204 neg_lo:[0,1] neg_hi:[0,1]
	v_pk_add_f16 v138, v138, v218
	v_pk_add_f16 v137, v137, v219
	v_pk_add_f16 v136, v136, v220
	v_pk_fma_f16 v96, v124, v217, v96
	v_pk_fma_f16 v97, v125, v218, v97
	v_pk_fma_f16 v98, v126, v219, v98
	v_pk_add_f16 v124, v160, v201 neg_lo:[0,1] neg_hi:[0,1]
	v_pk_add_f16 v125, v161, v202 neg_lo:[0,1] neg_hi:[0,1]
	v_pk_add_f16 v126, v162, v203 neg_lo:[0,1] neg_hi:[0,1]
	v_exp_f16_sdwa v152, v124 dst_sel:WORD_0 dst_unused:UNUSED_PAD src0_sel:WORD_0
	v_exp_f16_sdwa v153, v125 dst_sel:WORD_0 dst_unused:UNUSED_PAD src0_sel:WORD_0
	v_exp_f16_sdwa v154, v126 dst_sel:WORD_0 dst_unused:UNUSED_PAD src0_sel:WORD_0
	v_exp_f16_sdwa v155, v127 dst_sel:WORD_0 dst_unused:UNUSED_PAD src0_sel:WORD_0
	v_exp_f16_sdwa v152, v124 dst_sel:WORD_1 dst_unused:UNUSED_PRESERVE src0_sel:WORD_1
	v_exp_f16_sdwa v153, v125 dst_sel:WORD_1 dst_unused:UNUSED_PRESERVE src0_sel:WORD_1
	v_exp_f16_sdwa v154, v126 dst_sel:WORD_1 dst_unused:UNUSED_PRESERVE src0_sel:WORD_1
	v_exp_f16_sdwa v155, v127 dst_sel:WORD_1 dst_unused:UNUSED_PRESERVE src0_sel:WORD_1
	v_pk_add_f16 v127, v139, v152
	v_pk_add_f16 v124, v136, v155
	s_mov_b64 exec, s[66:67]
	buffer_load_dwordx4 v[144:147], v231, s[8:11], 0 offen offset:2048
	buffer_load_dwordx4 v[84:87], v231, s[8:11], 0 offen offset:2560
	s_mov_b64 exec, -1
	v_pk_add_f16 v125, v137, v154
	v_pk_add_f16 v126, v138, v153
	v_pk_fma_f16 v99, v143, v155, v99
	v_pk_fma_f16 v98, v142, v154, v98
	v_pk_fma_f16 v97, v141, v153, v97
	v_pk_fma_f16 v96, v140, v152, v96
	v_pk_add_f16 v136, v208, v201 neg_lo:[0,1] neg_hi:[0,1]
	v_pk_add_f16 v137, v207, v202 neg_lo:[0,1] neg_hi:[0,1]
	v_pk_add_f16 v138, v206, v203 neg_lo:[0,1] neg_hi:[0,1]
	v_pk_add_f16 v139, v205, v204 neg_lo:[0,1] neg_hi:[0,1]
	v_exp_f16_sdwa v140, v136 dst_sel:WORD_0 dst_unused:UNUSED_PAD src0_sel:WORD_0
	v_exp_f16_sdwa v141, v137 dst_sel:WORD_0 dst_unused:UNUSED_PAD src0_sel:WORD_0
	v_exp_f16_sdwa v142, v138 dst_sel:WORD_0 dst_unused:UNUSED_PAD src0_sel:WORD_0
	v_exp_f16_sdwa v143, v139 dst_sel:WORD_0 dst_unused:UNUSED_PAD src0_sel:WORD_0
	v_exp_f16_sdwa v140, v136 dst_sel:WORD_1 dst_unused:UNUSED_PRESERVE src0_sel:WORD_1
	v_exp_f16_sdwa v141, v137 dst_sel:WORD_1 dst_unused:UNUSED_PRESERVE src0_sel:WORD_1
	v_exp_f16_sdwa v142, v138 dst_sel:WORD_1 dst_unused:UNUSED_PRESERVE src0_sel:WORD_1
	v_exp_f16_sdwa v143, v139 dst_sel:WORD_1 dst_unused:UNUSED_PRESERVE src0_sel:WORD_1
	v_pk_add_f16 v136, v212, v201 neg_lo:[0,1] neg_hi:[0,1]
	v_pk_add_f16 v127, v127, v140
	v_pk_add_f16 v126, v126, v141
	v_pk_add_f16 v125, v125, v142
	s_mov_b64 exec, s[76:77]
	buffer_load_dwordx4 v[156:159], v232, s[8:11], 0 offen
	buffer_load_dwordx4 v[104:107], v232, s[8:11], 0 offen offset:512
	s_mov_b64 exec, -1
	v_pk_add_f16 v124, v124, v143
	v_pk_fma_f16 v96, v68, v140, v96
	v_pk_fma_f16 v97, v69, v141, v97
	v_pk_fma_f16 v98, v70, v142, v98
	v_pk_fma_f16 v99, v71, v143, v99
	v_pk_add_f16 v137, v211, v202 neg_lo:[0,1] neg_hi:[0,1]
	v_pk_add_f16 v138, v210, v203 neg_lo:[0,1] neg_hi:[0,1]
	v_pk_add_f16 v139, v209, v204 neg_lo:[0,1] neg_hi:[0,1]
	v_exp_f16_sdwa v140, v136 dst_sel:WORD_0 dst_unused:UNUSED_PAD src0_sel:WORD_0
	v_exp_f16_sdwa v141, v137 dst_sel:WORD_0 dst_unused:UNUSED_PAD src0_sel:WORD_0
	v_exp_f16_sdwa v142, v138 dst_sel:WORD_0 dst_unused:UNUSED_PAD src0_sel:WORD_0
	v_exp_f16_sdwa v143, v139 dst_sel:WORD_0 dst_unused:UNUSED_PAD src0_sel:WORD_0
	v_exp_f16_sdwa v140, v136 dst_sel:WORD_1 dst_unused:UNUSED_PRESERVE src0_sel:WORD_1
	v_exp_f16_sdwa v141, v137 dst_sel:WORD_1 dst_unused:UNUSED_PRESERVE src0_sel:WORD_1
	v_exp_f16_sdwa v142, v138 dst_sel:WORD_1 dst_unused:UNUSED_PRESERVE src0_sel:WORD_1
	v_exp_f16_sdwa v143, v139 dst_sel:WORD_1 dst_unused:UNUSED_PRESERVE src0_sel:WORD_1
	v_pk_add_f16 v136, v216, v201 neg_lo:[0,1] neg_hi:[0,1]
	v_pk_add_f16 v127, v127, v140
	v_pk_add_f16 v124, v124, v143
	v_pk_add_f16 v125, v125, v142
	v_pk_add_f16 v126, v126, v141
	v_pk_fma_f16 v99, v91, v143, v99
	v_pk_fma_f16 v98, v90, v142, v98
	s_mov_b64 exec, s[70:71]
	buffer_load_dwordx4 v[164:167], v233, s[8:11], 0 offen offset:512
	buffer_load_dwordx4 v[120:123], v233, s[8:11], 0 offen offset:1024
	s_mov_b64 exec, -1
	v_pk_fma_f16 v97, v89, v141, v97
	v_pk_fma_f16 v96, v88, v140, v96
	v_pk_add_f16 v137, v215, v202 neg_lo:[0,1] neg_hi:[0,1]
	v_pk_add_f16 v138, v214, v203 neg_lo:[0,1] neg_hi:[0,1]
	v_pk_add_f16 v139, v213, v204 neg_lo:[0,1] neg_hi:[0,1]
	v_exp_f16_sdwa v140, v136 dst_sel:WORD_0 dst_unused:UNUSED_PAD src0_sel:WORD_0
	v_exp_f16_sdwa v141, v137 dst_sel:WORD_0 dst_unused:UNUSED_PAD src0_sel:WORD_0
	v_exp_f16_sdwa v142, v138 dst_sel:WORD_0 dst_unused:UNUSED_PAD src0_sel:WORD_0
	v_exp_f16_sdwa v143, v139 dst_sel:WORD_0 dst_unused:UNUSED_PAD src0_sel:WORD_0
	v_exp_f16_sdwa v140, v136 dst_sel:WORD_1 dst_unused:UNUSED_PRESERVE src0_sel:WORD_1
	v_exp_f16_sdwa v141, v137 dst_sel:WORD_1 dst_unused:UNUSED_PRESERVE src0_sel:WORD_1
	v_exp_f16_sdwa v142, v138 dst_sel:WORD_1 dst_unused:UNUSED_PRESERVE src0_sel:WORD_1
	v_exp_f16_sdwa v143, v139 dst_sel:WORD_1 dst_unused:UNUSED_PRESERVE src0_sel:WORD_1
	v_pk_add_f16 v136, v189, v201 neg_lo:[0,1] neg_hi:[0,1]
	v_pk_add_f16 v127, v127, v140
	v_pk_add_f16 v126, v126, v141
	v_pk_add_f16 v125, v125, v142
	v_pk_add_f16 v124, v124, v143
	v_pk_fma_f16 v96, v108, v140, v96
	v_pk_fma_f16 v97, v109, v141, v97
	v_pk_fma_f16 v98, v110, v142, v98
	v_pk_fma_f16 v99, v111, v143, v99
	s_mov_b64 exec, s[78:79]
	buffer_load_dwordx4 v[28:31], v233, s[8:11], 0 offen offset:2048
	buffer_load_dwordx4 v[24:27], v233, s[8:11], 0 offen offset:2560
	s_mov_b64 exec, -1
	v_pk_add_f16 v137, v194, v202 neg_lo:[0,1] neg_hi:[0,1]
	v_pk_add_f16 v138, v195, v203 neg_lo:[0,1] neg_hi:[0,1]
	v_pk_add_f16 v139, v196, v204 neg_lo:[0,1] neg_hi:[0,1]
	v_exp_f16_sdwa v140, v136 dst_sel:WORD_0 dst_unused:UNUSED_PAD src0_sel:WORD_0
	v_exp_f16_sdwa v141, v137 dst_sel:WORD_0 dst_unused:UNUSED_PAD src0_sel:WORD_0
	v_exp_f16_sdwa v142, v138 dst_sel:WORD_0 dst_unused:UNUSED_PAD src0_sel:WORD_0
	v_exp_f16_sdwa v143, v139 dst_sel:WORD_0 dst_unused:UNUSED_PAD src0_sel:WORD_0
	v_exp_f16_sdwa v140, v136 dst_sel:WORD_1 dst_unused:UNUSED_PRESERVE src0_sel:WORD_1
	v_exp_f16_sdwa v141, v137 dst_sel:WORD_1 dst_unused:UNUSED_PRESERVE src0_sel:WORD_1
	v_exp_f16_sdwa v142, v138 dst_sel:WORD_1 dst_unused:UNUSED_PRESERVE src0_sel:WORD_1
	v_exp_f16_sdwa v143, v139 dst_sel:WORD_1 dst_unused:UNUSED_PRESERVE src0_sel:WORD_1
	v_pk_add_f16 v136, v197, v201 neg_lo:[0,1] neg_hi:[0,1]
	v_pk_add_f16 v127, v127, v140
	v_pk_add_f16 v124, v124, v143
	v_pk_add_f16 v125, v125, v142
	v_pk_add_f16 v126, v126, v141
	v_pk_fma_f16 v99, v51, v143, v99
	v_pk_fma_f16 v98, v50, v142, v98
	v_pk_fma_f16 v97, v49, v141, v97
	v_pk_fma_f16 v96, v48, v140, v96
	v_pk_add_f16 v137, v198, v202 neg_lo:[0,1] neg_hi:[0,1]
	v_pk_add_f16 v138, v199, v203 neg_lo:[0,1] neg_hi:[0,1]
	v_pk_add_f16 v139, v200, v204 neg_lo:[0,1] neg_hi:[0,1]
	v_exp_f16_sdwa v140, v136 dst_sel:WORD_0 dst_unused:UNUSED_PAD src0_sel:WORD_0
	v_exp_f16_sdwa v141, v137 dst_sel:WORD_0 dst_unused:UNUSED_PAD src0_sel:WORD_0
	v_exp_f16_sdwa v142, v138 dst_sel:WORD_0 dst_unused:UNUSED_PAD src0_sel:WORD_0
	v_exp_f16_sdwa v143, v139 dst_sel:WORD_0 dst_unused:UNUSED_PAD src0_sel:WORD_0
	v_exp_f16_sdwa v140, v136 dst_sel:WORD_1 dst_unused:UNUSED_PRESERVE src0_sel:WORD_1
	v_exp_f16_sdwa v141, v137 dst_sel:WORD_1 dst_unused:UNUSED_PRESERVE src0_sel:WORD_1
	v_exp_f16_sdwa v142, v138 dst_sel:WORD_1 dst_unused:UNUSED_PRESERVE src0_sel:WORD_1
	v_exp_f16_sdwa v143, v139 dst_sel:WORD_1 dst_unused:UNUSED_PRESERVE src0_sel:WORD_1
	v_pk_add_f16 v136, v190, v201 neg_lo:[0,1] neg_hi:[0,1]
	v_pk_add_f16 v127, v127, v140
	v_pk_add_f16 v126, v126, v141
	v_pk_add_f16 v125, v125, v142
	v_pk_add_f16 v124, v124, v143
	v_pk_fma_f16 v96, v56, v140, v96
	v_pk_fma_f16 v97, v57, v141, v97
	v_pk_fma_f16 v98, v58, v142, v98
	v_pk_fma_f16 v99, v59, v143, v99
	v_pk_add_f16 v137, v191, v202 neg_lo:[0,1] neg_hi:[0,1]
	v_pk_add_f16 v138, v192, v203 neg_lo:[0,1] neg_hi:[0,1]
	v_pk_add_f16 v139, v193, v204 neg_lo:[0,1] neg_hi:[0,1]
	v_exp_f16_sdwa v140, v136 dst_sel:WORD_0 dst_unused:UNUSED_PAD src0_sel:WORD_0
	v_exp_f16_sdwa v141, v137 dst_sel:WORD_0 dst_unused:UNUSED_PAD src0_sel:WORD_0
	v_exp_f16_sdwa v142, v138 dst_sel:WORD_0 dst_unused:UNUSED_PAD src0_sel:WORD_0
	v_exp_f16_sdwa v143, v139 dst_sel:WORD_0 dst_unused:UNUSED_PAD src0_sel:WORD_0
	v_exp_f16_sdwa v140, v136 dst_sel:WORD_1 dst_unused:UNUSED_PRESERVE src0_sel:WORD_1
	v_exp_f16_sdwa v141, v137 dst_sel:WORD_1 dst_unused:UNUSED_PRESERVE src0_sel:WORD_1
	v_exp_f16_sdwa v142, v138 dst_sel:WORD_1 dst_unused:UNUSED_PRESERVE src0_sel:WORD_1
	v_exp_f16_sdwa v143, v139 dst_sel:WORD_1 dst_unused:UNUSED_PRESERVE src0_sel:WORD_1
	v_pk_add_f16 v127, v127, v140
	v_pk_add_f16 v126, v126, v141
	v_rcp_f16_e32 v136, v127
	v_rcp_f16_sdwa v127, v127 dst_sel:DWORD dst_unused:UNUSED_PAD src0_sel:WORD_1
	v_pk_add_f16 v125, v125, v142
	v_rcp_f16_e32 v137, v126
	v_rcp_f16_sdwa v126, v126 dst_sel:DWORD dst_unused:UNUSED_PAD src0_sel:WORD_1
	v_pk_add_f16 v124, v124, v143
	v_rcp_f16_e32 v138, v125
	v_rcp_f16_sdwa v139, v125 dst_sel:DWORD dst_unused:UNUSED_PAD src0_sel:WORD_1
	v_pk_fma_f16 v97, v73, v141, v97
	v_pk_fma_f16 v96, v72, v140, v96
	v_rcp_f16_e32 v140, v124
	v_rcp_f16_sdwa v141, v124 dst_sel:DWORD dst_unused:UNUSED_PAD src0_sel:WORD_1
	v_pack_b32_f16 v124, v136, v127
	v_pk_mul_f16 v124, v96, v124
	v_pack_b32_f16 v96, v137, v126
	v_pk_fma_f16 v98, v74, v142, v98
	v_pk_mul_f16 v125, v97, v96
	v_pack_b32_f16 v96, v138, v139
	v_pk_fma_f16 v99, v75, v143, v99
	v_pk_mul_f16 v126, v98, v96
	v_pack_b32_f16 v96, v140, v141
	v_pk_mul_f16 v127, v99, v96
	s_waitcnt vmcnt(12)
	v_pk_mul_f16 v99, v188, v179 op_sel_hi:[0,1]
	v_pk_mul_f16 v139, v186, v179 op_sel_hi:[0,1]
	v_pk_mul_f16 v143, v187, v179 op_sel_hi:[0,1]
	v_pk_mul_f16 v96, v188, v176 op_sel_hi:[0,1]
	v_pk_mul_f16 v97, v188, v177 op_sel_hi:[0,1]
	v_pk_mul_f16 v98, v188, v178 op_sel_hi:[0,1]
	v_pk_mul_f16 v136, v186, v176 op_sel_hi:[0,1]
	v_pk_mul_f16 v137, v186, v177 op_sel_hi:[0,1]
	v_pk_mul_f16 v138, v186, v178 op_sel_hi:[0,1]
	v_pk_mul_f16 v140, v187, v176 op_sel_hi:[0,1]
	v_pk_mul_f16 v141, v187, v177 op_sel_hi:[0,1]
	v_pk_mul_f16 v142, v187, v178 op_sel_hi:[0,1]
	v_pk_fma_f16 v115, v115, v179, v99
	v_pk_fma_f16 v135, v135, v179, v139
	v_pk_fma_f16 v151, v151, v179, v143
	v_pk_fma_f16 v152, v79, v179, v99
	v_pk_fma_f16 v160, v95, v179, v139
	v_pk_fma_f16 v189, v119, v179, v143
	v_pk_fma_f16 v99, v47, v179, v99
	v_pk_fma_f16 v139, v63, v179, v139
	v_pk_fma_f16 v143, v83, v179, v143
	v_pk_maximum3_f16 v179, v115, v135, v151
	v_pk_fma_f16 v114, v114, v178, v98
	v_pk_fma_f16 v113, v113, v177, v97
	v_pk_fma_f16 v112, v112, v176, v96
	v_pk_fma_f16 v134, v134, v178, v138
	v_pk_fma_f16 v133, v133, v177, v137
	v_pk_fma_f16 v132, v132, v176, v136
	v_pk_fma_f16 v150, v150, v178, v142
	v_pk_fma_f16 v149, v149, v177, v141
	v_pk_fma_f16 v148, v148, v176, v140
	v_pk_fma_f16 v153, v78, v178, v98
	v_pk_fma_f16 v154, v77, v177, v97
	v_pk_fma_f16 v155, v76, v176, v96
	v_pk_fma_f16 v161, v94, v178, v138
	v_pk_fma_f16 v162, v93, v177, v137
	v_pk_fma_f16 v163, v92, v176, v136
	v_pk_fma_f16 v190, v118, v178, v142
	v_pk_fma_f16 v191, v117, v177, v141
	v_pk_fma_f16 v192, v116, v176, v140
	v_pk_fma_f16 v98, v46, v178, v98
	v_pk_fma_f16 v97, v45, v177, v97
	v_pk_fma_f16 v96, v44, v176, v96
	v_pk_fma_f16 v138, v62, v178, v138
	v_pk_fma_f16 v137, v61, v177, v137
	v_pk_fma_f16 v136, v60, v176, v136
	v_pk_fma_f16 v142, v82, v178, v142
	v_pk_fma_f16 v141, v81, v177, v141
	v_pk_fma_f16 v140, v80, v176, v140
	v_pk_maximum3_f16 v176, v112, v132, v148
	v_pk_maximum3_f16 v177, v113, v133, v149
	v_pk_maximum3_f16 v178, v114, v134, v150
	v_pk_maximum3_f16 v196, v152, v160, v189
	v_pk_maximum3_f16 v200, v99, v139, v143
	v_pk_maximum3_f16 v193, v155, v163, v192
	v_pk_maximum3_f16 v194, v154, v162, v191
	v_pk_maximum3_f16 v195, v153, v161, v190
	v_pk_maximum3_f16 v197, v96, v136, v140
	v_pk_maximum3_f16 v198, v97, v137, v141
	v_pk_maximum3_f16 v179, v179, v196, v200
	v_pk_maximum3_f16 v199, v98, v138, v142
	v_pk_maximum3_f16 v176, v176, v193, v197
	v_pk_maximum3_f16 v177, v177, v194, v198
	v_pk_maximum3_f16 v178, v178, v195, v199
	v_pk_add_f16 v115, v115, v179 neg_lo:[0,1] neg_hi:[0,1]
	v_pk_add_f16 v112, v112, v176 neg_lo:[0,1] neg_hi:[0,1]
	v_pk_add_f16 v113, v113, v177 neg_lo:[0,1] neg_hi:[0,1]
	v_pk_add_f16 v114, v114, v178 neg_lo:[0,1] neg_hi:[0,1]
	v_pk_add_f16 v132, v132, v176 neg_lo:[0,1] neg_hi:[0,1]
	v_exp_f16_sdwa v193, v112 dst_sel:WORD_0 dst_unused:UNUSED_PAD src0_sel:WORD_0
	v_exp_f16_sdwa v194, v113 dst_sel:WORD_0 dst_unused:UNUSED_PAD src0_sel:WORD_0
	v_exp_f16_sdwa v195, v114 dst_sel:WORD_0 dst_unused:UNUSED_PAD src0_sel:WORD_0
	v_exp_f16_sdwa v196, v115 dst_sel:WORD_0 dst_unused:UNUSED_PAD src0_sel:WORD_0
	v_exp_f16_sdwa v193, v112 dst_sel:WORD_1 dst_unused:UNUSED_PRESERVE src0_sel:WORD_1
	v_exp_f16_sdwa v194, v113 dst_sel:WORD_1 dst_unused:UNUSED_PRESERVE src0_sel:WORD_1
	v_exp_f16_sdwa v195, v114 dst_sel:WORD_1 dst_unused:UNUSED_PRESERVE src0_sel:WORD_1
	v_exp_f16_sdwa v196, v115 dst_sel:WORD_1 dst_unused:UNUSED_PRESERVE src0_sel:WORD_1
	v_pk_add_f16 v133, v133, v177 neg_lo:[0,1] neg_hi:[0,1]
	v_pk_add_f16 v115, v193, 0
	v_pk_fma_f16 v71, v71, v196, 0
	v_pk_add_f16 v112, v196, 0
	v_pk_add_f16 v113, v195, 0
	v_pk_add_f16 v114, v194, 0
	v_pk_fma_f16 v70, v70, v195, 0
	v_pk_fma_f16 v69, v69, v194, 0
	v_pk_fma_f16 v68, v68, v193, 0
	v_pk_add_f16 v134, v134, v178 neg_lo:[0,1] neg_hi:[0,1]
	v_pk_add_f16 v135, v135, v179 neg_lo:[0,1] neg_hi:[0,1]
	v_pk_add_f16 v96, v96, v176 neg_lo:[0,1] neg_hi:[0,1]
	v_exp_f16_sdwa v193, v132 dst_sel:WORD_0 dst_unused:UNUSED_PAD src0_sel:WORD_0
	v_exp_f16_sdwa v194, v133 dst_sel:WORD_0 dst_unused:UNUSED_PAD src0_sel:WORD_0
	v_exp_f16_sdwa v195, v134 dst_sel:WORD_0 dst_unused:UNUSED_PAD src0_sel:WORD_0
	v_exp_f16_sdwa v196, v135 dst_sel:WORD_0 dst_unused:UNUSED_PAD src0_sel:WORD_0
	v_exp_f16_sdwa v193, v132 dst_sel:WORD_1 dst_unused:UNUSED_PRESERVE src0_sel:WORD_1
	v_exp_f16_sdwa v194, v133 dst_sel:WORD_1 dst_unused:UNUSED_PRESERVE src0_sel:WORD_1
	v_exp_f16_sdwa v195, v134 dst_sel:WORD_1 dst_unused:UNUSED_PRESERVE src0_sel:WORD_1
	v_exp_f16_sdwa v196, v135 dst_sel:WORD_1 dst_unused:UNUSED_PRESERVE src0_sel:WORD_1
	v_pk_add_f16 v97, v97, v177 neg_lo:[0,1] neg_hi:[0,1]
	v_pk_add_f16 v115, v115, v193
	v_pk_fma_f16 v71, v91, v196, v71
	v_pk_add_f16 v91, v151, v179 neg_lo:[0,1] neg_hi:[0,1]
	v_pk_add_f16 v114, v114, v194
	v_pk_add_f16 v113, v113, v195
	v_pk_add_f16 v112, v112, v196
	v_pk_fma_f16 v68, v88, v193, v68
	v_pk_fma_f16 v69, v89, v194, v69
	v_pk_fma_f16 v70, v90, v195, v70
	v_pk_add_f16 v88, v148, v176 neg_lo:[0,1] neg_hi:[0,1]
	v_pk_add_f16 v89, v149, v177 neg_lo:[0,1] neg_hi:[0,1]
	v_pk_add_f16 v90, v150, v178 neg_lo:[0,1] neg_hi:[0,1]
	v_pk_add_f16 v98, v98, v178 neg_lo:[0,1] neg_hi:[0,1]
	v_exp_f16_sdwa v132, v88 dst_sel:WORD_0 dst_unused:UNUSED_PAD src0_sel:WORD_0
	v_exp_f16_sdwa v133, v89 dst_sel:WORD_0 dst_unused:UNUSED_PAD src0_sel:WORD_0
	v_exp_f16_sdwa v134, v90 dst_sel:WORD_0 dst_unused:UNUSED_PAD src0_sel:WORD_0
	v_exp_f16_sdwa v135, v91 dst_sel:WORD_0 dst_unused:UNUSED_PAD src0_sel:WORD_0
	v_exp_f16_sdwa v132, v88 dst_sel:WORD_1 dst_unused:UNUSED_PRESERVE src0_sel:WORD_1
	v_exp_f16_sdwa v133, v89 dst_sel:WORD_1 dst_unused:UNUSED_PRESERVE src0_sel:WORD_1
	v_exp_f16_sdwa v134, v90 dst_sel:WORD_1 dst_unused:UNUSED_PRESERVE src0_sel:WORD_1
	v_exp_f16_sdwa v135, v91 dst_sel:WORD_1 dst_unused:UNUSED_PRESERVE src0_sel:WORD_1
	v_pk_add_f16 v99, v99, v179 neg_lo:[0,1] neg_hi:[0,1]
	v_pk_add_f16 v91, v115, v132
	v_pk_add_f16 v88, v112, v135
	v_pk_add_f16 v89, v113, v134
	v_pk_add_f16 v90, v114, v133
	v_pk_fma_f16 v71, v111, v135, v71
	v_pk_fma_f16 v70, v110, v134, v70
	v_pk_fma_f16 v69, v109, v133, v69
	v_pk_fma_f16 v68, v108, v132, v68
	v_pk_add_f16 v108, v155, v176 neg_lo:[0,1] neg_hi:[0,1]
	v_pk_add_f16 v109, v154, v177 neg_lo:[0,1] neg_hi:[0,1]
	v_pk_add_f16 v110, v153, v178 neg_lo:[0,1] neg_hi:[0,1]
	v_pk_add_f16 v111, v152, v179 neg_lo:[0,1] neg_hi:[0,1]
	v_exp_f16_sdwa v112, v108 dst_sel:WORD_0 dst_unused:UNUSED_PAD src0_sel:WORD_0
	v_exp_f16_sdwa v113, v109 dst_sel:WORD_0 dst_unused:UNUSED_PAD src0_sel:WORD_0
	v_exp_f16_sdwa v114, v110 dst_sel:WORD_0 dst_unused:UNUSED_PAD src0_sel:WORD_0
	v_exp_f16_sdwa v115, v111 dst_sel:WORD_0 dst_unused:UNUSED_PAD src0_sel:WORD_0
	v_exp_f16_sdwa v112, v108 dst_sel:WORD_1 dst_unused:UNUSED_PRESERVE src0_sel:WORD_1
	v_exp_f16_sdwa v113, v109 dst_sel:WORD_1 dst_unused:UNUSED_PRESERVE src0_sel:WORD_1
	v_exp_f16_sdwa v114, v110 dst_sel:WORD_1 dst_unused:UNUSED_PRESERVE src0_sel:WORD_1
	v_exp_f16_sdwa v115, v111 dst_sel:WORD_1 dst_unused:UNUSED_PRESERVE src0_sel:WORD_1
	v_pk_add_f16 v108, v163, v176 neg_lo:[0,1] neg_hi:[0,1]
	v_pk_add_f16 v91, v91, v112
	v_pk_add_f16 v90, v90, v113
	v_pk_add_f16 v89, v89, v114
	v_pk_add_f16 v88, v88, v115
	v_pk_fma_f16 v68, v48, v112, v68
	v_pk_fma_f16 v69, v49, v113, v69
	v_pk_fma_f16 v70, v50, v114, v70
	v_pk_fma_f16 v71, v51, v115, v71
	v_pk_add_f16 v109, v162, v177 neg_lo:[0,1] neg_hi:[0,1]
	v_pk_add_f16 v110, v161, v178 neg_lo:[0,1] neg_hi:[0,1]
	v_pk_add_f16 v111, v160, v179 neg_lo:[0,1] neg_hi:[0,1]
	v_exp_f16_sdwa v112, v108 dst_sel:WORD_0 dst_unused:UNUSED_PAD src0_sel:WORD_0
	v_exp_f16_sdwa v113, v109 dst_sel:WORD_0 dst_unused:UNUSED_PAD src0_sel:WORD_0
	v_exp_f16_sdwa v114, v110 dst_sel:WORD_0 dst_unused:UNUSED_PAD src0_sel:WORD_0
	v_exp_f16_sdwa v115, v111 dst_sel:WORD_0 dst_unused:UNUSED_PAD src0_sel:WORD_0
	v_exp_f16_sdwa v112, v108 dst_sel:WORD_1 dst_unused:UNUSED_PRESERVE src0_sel:WORD_1
	v_exp_f16_sdwa v113, v109 dst_sel:WORD_1 dst_unused:UNUSED_PRESERVE src0_sel:WORD_1
	v_exp_f16_sdwa v114, v110 dst_sel:WORD_1 dst_unused:UNUSED_PRESERVE src0_sel:WORD_1
	v_exp_f16_sdwa v115, v111 dst_sel:WORD_1 dst_unused:UNUSED_PRESERVE src0_sel:WORD_1
	v_pk_add_f16 v108, v192, v176 neg_lo:[0,1] neg_hi:[0,1]
	v_pk_add_f16 v91, v91, v112
	v_pk_add_f16 v88, v88, v115
	v_pk_add_f16 v89, v89, v114
	v_pk_add_f16 v90, v90, v113
	v_pk_fma_f16 v71, v59, v115, v71
	v_pk_fma_f16 v70, v58, v114, v70
	v_pk_fma_f16 v69, v57, v113, v69
	v_pk_fma_f16 v68, v56, v112, v68
	v_pk_add_f16 v109, v191, v177 neg_lo:[0,1] neg_hi:[0,1]
	v_pk_add_f16 v110, v190, v178 neg_lo:[0,1] neg_hi:[0,1]
	v_pk_add_f16 v111, v189, v179 neg_lo:[0,1] neg_hi:[0,1]
	v_exp_f16_sdwa v112, v108 dst_sel:WORD_0 dst_unused:UNUSED_PAD src0_sel:WORD_0
	v_exp_f16_sdwa v113, v109 dst_sel:WORD_0 dst_unused:UNUSED_PAD src0_sel:WORD_0
	v_exp_f16_sdwa v114, v110 dst_sel:WORD_0 dst_unused:UNUSED_PAD src0_sel:WORD_0
	v_exp_f16_sdwa v115, v111 dst_sel:WORD_0 dst_unused:UNUSED_PAD src0_sel:WORD_0
	v_exp_f16_sdwa v112, v108 dst_sel:WORD_1 dst_unused:UNUSED_PRESERVE src0_sel:WORD_1
	v_exp_f16_sdwa v113, v109 dst_sel:WORD_1 dst_unused:UNUSED_PRESERVE src0_sel:WORD_1
	v_exp_f16_sdwa v114, v110 dst_sel:WORD_1 dst_unused:UNUSED_PRESERVE src0_sel:WORD_1
	v_exp_f16_sdwa v115, v111 dst_sel:WORD_1 dst_unused:UNUSED_PRESERVE src0_sel:WORD_1
	v_exp_f16_sdwa v108, v96 dst_sel:WORD_0 dst_unused:UNUSED_PAD src0_sel:WORD_0
	v_exp_f16_sdwa v109, v97 dst_sel:WORD_0 dst_unused:UNUSED_PAD src0_sel:WORD_0
	v_exp_f16_sdwa v110, v98 dst_sel:WORD_0 dst_unused:UNUSED_PAD src0_sel:WORD_0
	v_exp_f16_sdwa v111, v99 dst_sel:WORD_0 dst_unused:UNUSED_PAD src0_sel:WORD_0
	v_exp_f16_sdwa v108, v96 dst_sel:WORD_1 dst_unused:UNUSED_PRESERVE src0_sel:WORD_1
	v_exp_f16_sdwa v109, v97 dst_sel:WORD_1 dst_unused:UNUSED_PRESERVE src0_sel:WORD_1
	v_exp_f16_sdwa v110, v98 dst_sel:WORD_1 dst_unused:UNUSED_PRESERVE src0_sel:WORD_1
	v_exp_f16_sdwa v111, v99 dst_sel:WORD_1 dst_unused:UNUSED_PRESERVE src0_sel:WORD_1
	v_pk_add_f16 v96, v136, v176 neg_lo:[0,1] neg_hi:[0,1]
	v_pk_add_f16 v91, v91, v112
	v_pk_add_f16 v90, v90, v113
	v_pk_add_f16 v89, v89, v114
	v_pk_add_f16 v88, v88, v115
	v_pk_fma_f16 v68, v72, v112, v68
	v_pk_fma_f16 v69, v73, v113, v69
	v_pk_fma_f16 v70, v74, v114, v70
	v_pk_fma_f16 v71, v75, v115, v71
	v_pk_add_f16 v91, v91, v108
	v_pk_add_f16 v88, v88, v111
	v_pk_add_f16 v89, v89, v110
	v_pk_add_f16 v90, v90, v109
	v_pk_fma_f16 v71, v35, v111, v71
	v_pk_fma_f16 v70, v34, v110, v70
	v_pk_fma_f16 v69, v33, v109, v69
	v_pk_fma_f16 v68, v32, v108, v68
	v_pk_add_f16 v97, v137, v177 neg_lo:[0,1] neg_hi:[0,1]
	v_pk_add_f16 v98, v138, v178 neg_lo:[0,1] neg_hi:[0,1]
	v_pk_add_f16 v99, v139, v179 neg_lo:[0,1] neg_hi:[0,1]
	v_exp_f16_sdwa v108, v96 dst_sel:WORD_0 dst_unused:UNUSED_PAD src0_sel:WORD_0
	v_exp_f16_sdwa v109, v97 dst_sel:WORD_0 dst_unused:UNUSED_PAD src0_sel:WORD_0
	v_exp_f16_sdwa v110, v98 dst_sel:WORD_0 dst_unused:UNUSED_PAD src0_sel:WORD_0
	v_exp_f16_sdwa v111, v99 dst_sel:WORD_0 dst_unused:UNUSED_PAD src0_sel:WORD_0
	v_exp_f16_sdwa v108, v96 dst_sel:WORD_1 dst_unused:UNUSED_PRESERVE src0_sel:WORD_1
	v_exp_f16_sdwa v109, v97 dst_sel:WORD_1 dst_unused:UNUSED_PRESERVE src0_sel:WORD_1
	v_exp_f16_sdwa v110, v98 dst_sel:WORD_1 dst_unused:UNUSED_PRESERVE src0_sel:WORD_1
	v_exp_f16_sdwa v111, v99 dst_sel:WORD_1 dst_unused:UNUSED_PRESERVE src0_sel:WORD_1
	v_pk_add_f16 v96, v140, v176 neg_lo:[0,1] neg_hi:[0,1]
	v_pk_add_f16 v91, v91, v108
	v_pk_add_f16 v90, v90, v109
	v_pk_add_f16 v89, v89, v110
	v_pk_add_f16 v88, v88, v111
	v_pk_fma_f16 v68, v36, v108, v68
	v_pk_fma_f16 v69, v37, v109, v69
	v_pk_fma_f16 v70, v38, v110, v70
	v_pk_fma_f16 v71, v39, v111, v71
	v_pk_add_f16 v97, v141, v177 neg_lo:[0,1] neg_hi:[0,1]
	v_pk_add_f16 v98, v142, v178 neg_lo:[0,1] neg_hi:[0,1]
	v_pk_add_f16 v99, v143, v179 neg_lo:[0,1] neg_hi:[0,1]
	v_exp_f16_sdwa v108, v96 dst_sel:WORD_0 dst_unused:UNUSED_PAD src0_sel:WORD_0
	v_exp_f16_sdwa v109, v97 dst_sel:WORD_0 dst_unused:UNUSED_PAD src0_sel:WORD_0
	v_exp_f16_sdwa v110, v98 dst_sel:WORD_0 dst_unused:UNUSED_PAD src0_sel:WORD_0
	v_exp_f16_sdwa v111, v99 dst_sel:WORD_0 dst_unused:UNUSED_PAD src0_sel:WORD_0
	v_exp_f16_sdwa v108, v96 dst_sel:WORD_1 dst_unused:UNUSED_PRESERVE src0_sel:WORD_1
	v_exp_f16_sdwa v109, v97 dst_sel:WORD_1 dst_unused:UNUSED_PRESERVE src0_sel:WORD_1
	v_exp_f16_sdwa v110, v98 dst_sel:WORD_1 dst_unused:UNUSED_PRESERVE src0_sel:WORD_1
	v_exp_f16_sdwa v111, v99 dst_sel:WORD_1 dst_unused:UNUSED_PRESERVE src0_sel:WORD_1
	v_pk_add_f16 v91, v91, v108
	v_pk_add_f16 v90, v90, v109
	v_rcp_f16_e32 v96, v91
	v_rcp_f16_sdwa v91, v91 dst_sel:DWORD dst_unused:UNUSED_PAD src0_sel:WORD_1
	v_pk_add_f16 v89, v89, v110
	v_rcp_f16_e32 v97, v90
	v_rcp_f16_sdwa v90, v90 dst_sel:DWORD dst_unused:UNUSED_PAD src0_sel:WORD_1
	v_pk_add_f16 v88, v88, v111
	v_rcp_f16_e32 v98, v89
	v_rcp_f16_sdwa v99, v89 dst_sel:DWORD dst_unused:UNUSED_PAD src0_sel:WORD_1
	v_pk_fma_f16 v69, v41, v109, v69
	v_pk_fma_f16 v68, v40, v108, v68
	v_rcp_f16_e32 v108, v88
	v_rcp_f16_sdwa v109, v88 dst_sel:DWORD dst_unused:UNUSED_PAD src0_sel:WORD_1
	v_pack_b32_f16 v88, v96, v91
	v_pk_mul_f16 v88, v68, v88
	v_pack_b32_f16 v68, v97, v90
	v_pk_fma_f16 v70, v42, v110, v70
	v_pk_mul_f16 v89, v69, v68
	v_pack_b32_f16 v68, v98, v99
	v_pk_fma_f16 v71, v43, v111, v71
	v_pk_mul_f16 v90, v70, v68
	v_pack_b32_f16 v68, v108, v109
	v_pk_mul_f16 v91, v71, v68
	s_waitcnt vmcnt(6)
	v_pk_mul_f16 v68, v188, v172 op_sel_hi:[0,1]
	v_pk_mul_f16 v96, v186, v172 op_sel_hi:[0,1]
	v_pk_mul_f16 v108, v187, v172 op_sel_hi:[0,1]
	v_pk_mul_f16 v69, v188, v173 op_sel_hi:[0,1]
	v_pk_mul_f16 v70, v188, v174 op_sel_hi:[0,1]
	v_pk_mul_f16 v71, v188, v175 op_sel_hi:[0,1]
	v_pk_mul_f16 v97, v186, v173 op_sel_hi:[0,1]
	v_pk_mul_f16 v98, v186, v174 op_sel_hi:[0,1]
	v_pk_mul_f16 v99, v186, v175 op_sel_hi:[0,1]
	v_pk_mul_f16 v109, v187, v173 op_sel_hi:[0,1]
	v_pk_mul_f16 v110, v187, v174 op_sel_hi:[0,1]
	v_pk_mul_f16 v111, v187, v175 op_sel_hi:[0,1]
	v_pk_fma_f16 v76, v76, v172, v68
	v_pk_fma_f16 v92, v92, v172, v96
	v_pk_fma_f16 v115, v116, v172, v108
	v_pk_fma_f16 v79, v79, v175, v71
	v_pk_maximum3_f16 v140, v76, v92, v115
	v_pk_fma_f16 v78, v78, v174, v70
	v_pk_fma_f16 v77, v77, v173, v69
	v_pk_fma_f16 v95, v95, v175, v99
	v_pk_fma_f16 v94, v94, v174, v98
	v_pk_fma_f16 v93, v93, v173, v97
	v_pk_fma_f16 v112, v119, v175, v111
	v_pk_fma_f16 v113, v118, v174, v110
	v_pk_fma_f16 v114, v117, v173, v109
	v_pk_fma_f16 v119, v44, v172, v68
	v_pk_fma_f16 v135, v60, v172, v96
	v_pk_fma_f16 v139, v80, v172, v108
	v_pk_fma_f16 v68, v100, v172, v68
	v_pk_fma_f16 v96, v128, v172, v96
	v_pk_fma_f16 v108, v144, v172, v108
	v_pk_maximum3_f16 v141, v77, v93, v114
	v_pk_maximum3_f16 v142, v78, v94, v113
	v_pk_maximum3_f16 v143, v79, v95, v112
	v_pk_maximum3_f16 v148, v119, v135, v139
	v_pk_fma_f16 v116, v47, v175, v71
	v_pk_maximum3_f16 v152, v68, v96, v108
	v_pk_fma_f16 v117, v46, v174, v70
	v_pk_maximum3_f16 v140, v140, v148, v152
	v_pk_fma_f16 v118, v45, v173, v69
	v_pk_fma_f16 v132, v63, v175, v99
	v_pk_fma_f16 v133, v62, v174, v98
	v_pk_fma_f16 v134, v61, v173, v97
	v_pk_fma_f16 v136, v83, v175, v111
	v_pk_fma_f16 v137, v82, v174, v110
	v_pk_fma_f16 v138, v81, v173, v109
	v_pk_fma_f16 v71, v103, v175, v71
	v_pk_fma_f16 v70, v102, v174, v70
	v_pk_fma_f16 v69, v101, v173, v69
	v_pk_fma_f16 v99, v131, v175, v99
	v_pk_fma_f16 v98, v130, v174, v98
	v_pk_fma_f16 v97, v129, v173, v97
	v_pk_fma_f16 v111, v147, v175, v111
	v_pk_fma_f16 v110, v146, v174, v110
	v_pk_fma_f16 v109, v145, v173, v109
	v_pk_maximum3_f16 v149, v118, v134, v138
	v_pk_maximum3_f16 v150, v117, v133, v137
	v_pk_maximum3_f16 v151, v116, v132, v136
	v_pk_maximum3_f16 v154, v70, v98, v110
	v_pk_maximum3_f16 v155, v71, v99, v111
	v_pk_maximum3_f16 v153, v69, v97, v109
	v_pk_maximum3_f16 v141, v141, v149, v153
	v_pk_maximum3_f16 v142, v142, v150, v154
	v_pk_maximum3_f16 v143, v143, v151, v155
	v_pk_add_f16 v76, v76, v140 neg_lo:[0,1] neg_hi:[0,1]
	v_pk_add_f16 v77, v77, v141 neg_lo:[0,1] neg_hi:[0,1]
	v_pk_add_f16 v78, v78, v142 neg_lo:[0,1] neg_hi:[0,1]
	v_pk_add_f16 v79, v79, v143 neg_lo:[0,1] neg_hi:[0,1]
	v_pk_add_f16 v92, v92, v140 neg_lo:[0,1] neg_hi:[0,1]
	v_exp_f16_sdwa v148, v76 dst_sel:WORD_0 dst_unused:UNUSED_PAD src0_sel:WORD_0
	v_exp_f16_sdwa v149, v77 dst_sel:WORD_0 dst_unused:UNUSED_PAD src0_sel:WORD_0
	v_exp_f16_sdwa v150, v78 dst_sel:WORD_0 dst_unused:UNUSED_PAD src0_sel:WORD_0
	v_exp_f16_sdwa v151, v79 dst_sel:WORD_0 dst_unused:UNUSED_PAD src0_sel:WORD_0
	v_exp_f16_sdwa v148, v76 dst_sel:WORD_1 dst_unused:UNUSED_PRESERVE src0_sel:WORD_1
	v_exp_f16_sdwa v149, v77 dst_sel:WORD_1 dst_unused:UNUSED_PRESERVE src0_sel:WORD_1
	v_exp_f16_sdwa v150, v78 dst_sel:WORD_1 dst_unused:UNUSED_PRESERVE src0_sel:WORD_1
	v_exp_f16_sdwa v151, v79 dst_sel:WORD_1 dst_unused:UNUSED_PRESERVE src0_sel:WORD_1
	v_pk_add_f16 v93, v93, v141 neg_lo:[0,1] neg_hi:[0,1]
	v_pk_add_f16 v76, v151, 0
	v_pk_fma_f16 v48, v48, v148, 0
	v_pk_add_f16 v77, v150, 0
	v_pk_add_f16 v78, v149, 0
	v_pk_add_f16 v79, v148, 0
	v_pk_fma_f16 v49, v49, v149, 0
	v_pk_fma_f16 v50, v50, v150, 0
	v_pk_fma_f16 v51, v51, v151, 0
	v_pk_add_f16 v94, v94, v142 neg_lo:[0,1] neg_hi:[0,1]
	v_pk_add_f16 v95, v95, v143 neg_lo:[0,1] neg_hi:[0,1]
	v_pk_add_f16 v68, v68, v140 neg_lo:[0,1] neg_hi:[0,1]
	v_exp_f16_sdwa v148, v92 dst_sel:WORD_0 dst_unused:UNUSED_PAD src0_sel:WORD_0
	v_exp_f16_sdwa v149, v93 dst_sel:WORD_0 dst_unused:UNUSED_PAD src0_sel:WORD_0
	v_exp_f16_sdwa v150, v94 dst_sel:WORD_0 dst_unused:UNUSED_PAD src0_sel:WORD_0
	v_exp_f16_sdwa v151, v95 dst_sel:WORD_0 dst_unused:UNUSED_PAD src0_sel:WORD_0
	v_exp_f16_sdwa v148, v92 dst_sel:WORD_1 dst_unused:UNUSED_PRESERVE src0_sel:WORD_1
	v_exp_f16_sdwa v149, v93 dst_sel:WORD_1 dst_unused:UNUSED_PRESERVE src0_sel:WORD_1
	v_exp_f16_sdwa v150, v94 dst_sel:WORD_1 dst_unused:UNUSED_PRESERVE src0_sel:WORD_1
	v_exp_f16_sdwa v151, v95 dst_sel:WORD_1 dst_unused:UNUSED_PRESERVE src0_sel:WORD_1
	v_pk_add_f16 v69, v69, v141 neg_lo:[0,1] neg_hi:[0,1]
	v_pk_add_f16 v76, v76, v151
	v_pk_fma_f16 v48, v56, v148, v48
	v_pk_add_f16 v56, v115, v140 neg_lo:[0,1] neg_hi:[0,1]
	v_pk_add_f16 v79, v79, v148
	v_pk_add_f16 v78, v78, v149
	v_pk_add_f16 v77, v77, v150
	v_pk_fma_f16 v51, v59, v151, v51
	v_pk_fma_f16 v50, v58, v150, v50
	v_pk_fma_f16 v49, v57, v149, v49
	v_pk_add_f16 v57, v114, v141 neg_lo:[0,1] neg_hi:[0,1]
	v_pk_add_f16 v58, v113, v142 neg_lo:[0,1] neg_hi:[0,1]
	v_pk_add_f16 v59, v112, v143 neg_lo:[0,1] neg_hi:[0,1]
	v_pk_add_f16 v70, v70, v142 neg_lo:[0,1] neg_hi:[0,1]
	v_exp_f16_sdwa v92, v56 dst_sel:WORD_0 dst_unused:UNUSED_PAD src0_sel:WORD_0
	v_exp_f16_sdwa v93, v57 dst_sel:WORD_0 dst_unused:UNUSED_PAD src0_sel:WORD_0
	v_exp_f16_sdwa v94, v58 dst_sel:WORD_0 dst_unused:UNUSED_PAD src0_sel:WORD_0
	v_exp_f16_sdwa v95, v59 dst_sel:WORD_0 dst_unused:UNUSED_PAD src0_sel:WORD_0
	v_exp_f16_sdwa v92, v56 dst_sel:WORD_1 dst_unused:UNUSED_PRESERVE src0_sel:WORD_1
	v_exp_f16_sdwa v93, v57 dst_sel:WORD_1 dst_unused:UNUSED_PRESERVE src0_sel:WORD_1
	v_exp_f16_sdwa v94, v58 dst_sel:WORD_1 dst_unused:UNUSED_PRESERVE src0_sel:WORD_1
	v_exp_f16_sdwa v95, v59 dst_sel:WORD_1 dst_unused:UNUSED_PRESERVE src0_sel:WORD_1
	v_pk_add_f16 v71, v71, v143 neg_lo:[0,1] neg_hi:[0,1]
	v_pk_add_f16 v56, v76, v95
	v_pk_add_f16 v57, v77, v94
	v_pk_add_f16 v58, v78, v93
	v_pk_add_f16 v59, v79, v92
	v_pk_fma_f16 v48, v72, v92, v48
	v_pk_fma_f16 v49, v73, v93, v49
	v_pk_fma_f16 v50, v74, v94, v50
	v_pk_fma_f16 v51, v75, v95, v51
	v_pk_add_f16 v72, v119, v140 neg_lo:[0,1] neg_hi:[0,1]
	v_pk_add_f16 v73, v118, v141 neg_lo:[0,1] neg_hi:[0,1]
	v_pk_add_f16 v74, v117, v142 neg_lo:[0,1] neg_hi:[0,1]
	v_pk_add_f16 v75, v116, v143 neg_lo:[0,1] neg_hi:[0,1]
	v_exp_f16_sdwa v76, v72 dst_sel:WORD_0 dst_unused:UNUSED_PAD src0_sel:WORD_0
	v_exp_f16_sdwa v77, v73 dst_sel:WORD_0 dst_unused:UNUSED_PAD src0_sel:WORD_0
	v_exp_f16_sdwa v78, v74 dst_sel:WORD_0 dst_unused:UNUSED_PAD src0_sel:WORD_0
	v_exp_f16_sdwa v79, v75 dst_sel:WORD_0 dst_unused:UNUSED_PAD src0_sel:WORD_0
	v_exp_f16_sdwa v76, v72 dst_sel:WORD_1 dst_unused:UNUSED_PRESERVE src0_sel:WORD_1
	v_exp_f16_sdwa v77, v73 dst_sel:WORD_1 dst_unused:UNUSED_PRESERVE src0_sel:WORD_1
	v_exp_f16_sdwa v78, v74 dst_sel:WORD_1 dst_unused:UNUSED_PRESERVE src0_sel:WORD_1
	v_exp_f16_sdwa v79, v75 dst_sel:WORD_1 dst_unused:UNUSED_PRESERVE src0_sel:WORD_1
	v_pk_add_f16 v72, v135, v140 neg_lo:[0,1] neg_hi:[0,1]
	v_pk_add_f16 v56, v56, v79
	v_pk_add_f16 v59, v59, v76
	v_pk_add_f16 v58, v58, v77
	v_pk_add_f16 v57, v57, v78
	v_pk_fma_f16 v51, v35, v79, v51
	v_pk_fma_f16 v50, v34, v78, v50
	v_pk_fma_f16 v49, v33, v77, v49
	v_pk_fma_f16 v48, v32, v76, v48
	v_pk_add_f16 v73, v134, v141 neg_lo:[0,1] neg_hi:[0,1]
	v_pk_add_f16 v74, v133, v142 neg_lo:[0,1] neg_hi:[0,1]
	v_pk_add_f16 v75, v132, v143 neg_lo:[0,1] neg_hi:[0,1]
	v_exp_f16_sdwa v76, v72 dst_sel:WORD_0 dst_unused:UNUSED_PAD src0_sel:WORD_0
	v_exp_f16_sdwa v77, v73 dst_sel:WORD_0 dst_unused:UNUSED_PAD src0_sel:WORD_0
	v_exp_f16_sdwa v78, v74 dst_sel:WORD_0 dst_unused:UNUSED_PAD src0_sel:WORD_0
	v_exp_f16_sdwa v79, v75 dst_sel:WORD_0 dst_unused:UNUSED_PAD src0_sel:WORD_0
	v_exp_f16_sdwa v76, v72 dst_sel:WORD_1 dst_unused:UNUSED_PRESERVE src0_sel:WORD_1
	v_exp_f16_sdwa v77, v73 dst_sel:WORD_1 dst_unused:UNUSED_PRESERVE src0_sel:WORD_1
	v_exp_f16_sdwa v78, v74 dst_sel:WORD_1 dst_unused:UNUSED_PRESERVE src0_sel:WORD_1
	v_exp_f16_sdwa v79, v75 dst_sel:WORD_1 dst_unused:UNUSED_PRESERVE src0_sel:WORD_1
	v_pk_add_f16 v72, v139, v140 neg_lo:[0,1] neg_hi:[0,1]
	v_pk_add_f16 v56, v56, v79
	v_pk_add_f16 v57, v57, v78
	v_pk_add_f16 v58, v58, v77
	v_pk_add_f16 v59, v59, v76
	v_pk_fma_f16 v48, v36, v76, v48
	v_pk_fma_f16 v49, v37, v77, v49
	v_pk_fma_f16 v50, v38, v78, v50
	v_pk_fma_f16 v51, v39, v79, v51
	v_pk_add_f16 v73, v138, v141 neg_lo:[0,1] neg_hi:[0,1]
	v_pk_add_f16 v74, v137, v142 neg_lo:[0,1] neg_hi:[0,1]
	v_pk_add_f16 v75, v136, v143 neg_lo:[0,1] neg_hi:[0,1]
	v_exp_f16_sdwa v76, v72 dst_sel:WORD_0 dst_unused:UNUSED_PAD src0_sel:WORD_0
	v_exp_f16_sdwa v77, v73 dst_sel:WORD_0 dst_unused:UNUSED_PAD src0_sel:WORD_0
	v_exp_f16_sdwa v78, v74 dst_sel:WORD_0 dst_unused:UNUSED_PAD src0_sel:WORD_0
	v_exp_f16_sdwa v79, v75 dst_sel:WORD_0 dst_unused:UNUSED_PAD src0_sel:WORD_0
	v_exp_f16_sdwa v76, v72 dst_sel:WORD_1 dst_unused:UNUSED_PRESERVE src0_sel:WORD_1
	v_exp_f16_sdwa v77, v73 dst_sel:WORD_1 dst_unused:UNUSED_PRESERVE src0_sel:WORD_1
	v_exp_f16_sdwa v78, v74 dst_sel:WORD_1 dst_unused:UNUSED_PRESERVE src0_sel:WORD_1
	v_exp_f16_sdwa v79, v75 dst_sel:WORD_1 dst_unused:UNUSED_PRESERVE src0_sel:WORD_1
	v_exp_f16_sdwa v72, v68 dst_sel:WORD_0 dst_unused:UNUSED_PAD src0_sel:WORD_0
	v_exp_f16_sdwa v73, v69 dst_sel:WORD_0 dst_unused:UNUSED_PAD src0_sel:WORD_0
	v_exp_f16_sdwa v74, v70 dst_sel:WORD_0 dst_unused:UNUSED_PAD src0_sel:WORD_0
	v_exp_f16_sdwa v75, v71 dst_sel:WORD_0 dst_unused:UNUSED_PAD src0_sel:WORD_0
	v_exp_f16_sdwa v72, v68 dst_sel:WORD_1 dst_unused:UNUSED_PRESERVE src0_sel:WORD_1
	v_exp_f16_sdwa v73, v69 dst_sel:WORD_1 dst_unused:UNUSED_PRESERVE src0_sel:WORD_1
	v_exp_f16_sdwa v74, v70 dst_sel:WORD_1 dst_unused:UNUSED_PRESERVE src0_sel:WORD_1
	v_exp_f16_sdwa v75, v71 dst_sel:WORD_1 dst_unused:UNUSED_PRESERVE src0_sel:WORD_1
	v_pk_add_f16 v68, v96, v140 neg_lo:[0,1] neg_hi:[0,1]
	v_pk_add_f16 v56, v56, v79
	v_pk_add_f16 v59, v59, v76
	v_pk_add_f16 v58, v58, v77
	v_pk_add_f16 v57, v57, v78
	v_pk_fma_f16 v51, v43, v79, v51
	v_pk_fma_f16 v50, v42, v78, v50
	v_pk_fma_f16 v49, v41, v77, v49
	v_pk_fma_f16 v48, v40, v76, v48
	v_pk_add_f16 v56, v56, v75
	v_pk_add_f16 v57, v57, v74
	v_pk_add_f16 v58, v58, v73
	v_pk_add_f16 v59, v59, v72
	v_pk_fma_f16 v48, v52, v72, v48
	v_pk_fma_f16 v49, v53, v73, v49
	v_pk_fma_f16 v50, v54, v74, v50
	v_pk_fma_f16 v51, v55, v75, v51
	v_pk_add_f16 v69, v97, v141 neg_lo:[0,1] neg_hi:[0,1]
	v_pk_add_f16 v70, v98, v142 neg_lo:[0,1] neg_hi:[0,1]
	v_pk_add_f16 v71, v99, v143 neg_lo:[0,1] neg_hi:[0,1]
	v_exp_f16_sdwa v72, v68 dst_sel:WORD_0 dst_unused:UNUSED_PAD src0_sel:WORD_0
	v_exp_f16_sdwa v73, v69 dst_sel:WORD_0 dst_unused:UNUSED_PAD src0_sel:WORD_0
	v_exp_f16_sdwa v74, v70 dst_sel:WORD_0 dst_unused:UNUSED_PAD src0_sel:WORD_0
	v_exp_f16_sdwa v75, v71 dst_sel:WORD_0 dst_unused:UNUSED_PAD src0_sel:WORD_0
	v_exp_f16_sdwa v72, v68 dst_sel:WORD_1 dst_unused:UNUSED_PRESERVE src0_sel:WORD_1
	v_exp_f16_sdwa v73, v69 dst_sel:WORD_1 dst_unused:UNUSED_PRESERVE src0_sel:WORD_1
	v_exp_f16_sdwa v74, v70 dst_sel:WORD_1 dst_unused:UNUSED_PRESERVE src0_sel:WORD_1
	v_exp_f16_sdwa v75, v71 dst_sel:WORD_1 dst_unused:UNUSED_PRESERVE src0_sel:WORD_1
	v_pk_add_f16 v68, v108, v140 neg_lo:[0,1] neg_hi:[0,1]
	v_pk_add_f16 v56, v56, v75
	v_pk_add_f16 v59, v59, v72
	v_pk_add_f16 v58, v58, v73
	v_pk_add_f16 v57, v57, v74
	v_pk_fma_f16 v51, v67, v75, v51
	v_pk_fma_f16 v50, v66, v74, v50
	v_pk_fma_f16 v49, v65, v73, v49
	v_pk_fma_f16 v48, v64, v72, v48
	v_pk_add_f16 v69, v109, v141 neg_lo:[0,1] neg_hi:[0,1]
	v_pk_add_f16 v70, v110, v142 neg_lo:[0,1] neg_hi:[0,1]
	v_pk_add_f16 v71, v111, v143 neg_lo:[0,1] neg_hi:[0,1]
	v_exp_f16_sdwa v72, v68 dst_sel:WORD_0 dst_unused:UNUSED_PAD src0_sel:WORD_0
	v_exp_f16_sdwa v73, v69 dst_sel:WORD_0 dst_unused:UNUSED_PAD src0_sel:WORD_0
	v_exp_f16_sdwa v74, v70 dst_sel:WORD_0 dst_unused:UNUSED_PAD src0_sel:WORD_0
	v_exp_f16_sdwa v75, v71 dst_sel:WORD_0 dst_unused:UNUSED_PAD src0_sel:WORD_0
	v_exp_f16_sdwa v72, v68 dst_sel:WORD_1 dst_unused:UNUSED_PRESERVE src0_sel:WORD_1
	v_exp_f16_sdwa v73, v69 dst_sel:WORD_1 dst_unused:UNUSED_PRESERVE src0_sel:WORD_1
	v_exp_f16_sdwa v74, v70 dst_sel:WORD_1 dst_unused:UNUSED_PRESERVE src0_sel:WORD_1
	v_exp_f16_sdwa v75, v71 dst_sel:WORD_1 dst_unused:UNUSED_PRESERVE src0_sel:WORD_1
	s_nop 0
	v_pk_add_f16 v56, v56, v75
	v_pk_add_f16 v57, v57, v74
	v_rcp_f16_e32 v70, v56
	v_rcp_f16_sdwa v56, v56 dst_sel:DWORD dst_unused:UNUSED_PAD src0_sel:WORD_1
	v_pk_add_f16 v58, v58, v73
	v_rcp_f16_e32 v71, v57
	v_rcp_f16_sdwa v57, v57 dst_sel:DWORD dst_unused:UNUSED_PAD src0_sel:WORD_1
	v_pk_add_f16 v59, v59, v72
	v_rcp_f16_e32 v69, v58
	v_rcp_f16_sdwa v58, v58 dst_sel:DWORD dst_unused:UNUSED_PAD src0_sel:WORD_1
	v_rcp_f16_e32 v68, v59
	v_rcp_f16_sdwa v59, v59 dst_sel:DWORD dst_unused:UNUSED_PAD src0_sel:WORD_1
	v_pk_fma_f16 v51, v87, v75, v51
	v_pack_b32_f16 v56, v70, v56
	v_pk_fma_f16 v50, v86, v74, v50
	v_pk_mul_f16 v51, v51, v56
	v_pack_b32_f16 v56, v71, v57
	v_pk_fma_f16 v49, v85, v73, v49
	v_pk_mul_f16 v50, v50, v56
	v_pack_b32_f16 v56, v69, v58
	v_pk_fma_f16 v48, v84, v72, v48
	v_pk_mul_f16 v49, v49, v56
	v_pack_b32_f16 v56, v68, v59
	v_pk_mul_f16 v48, v48, v56
	s_waitcnt vmcnt(0)
	v_pk_mul_f16 v56, v188, v168 op_sel_hi:[0,1]
	v_pk_mul_f16 v57, v188, v169 op_sel_hi:[0,1]
	v_pk_mul_f16 v58, v188, v170 op_sel_hi:[0,1]
	v_pk_mul_f16 v59, v188, v171 op_sel_hi:[0,1]
	v_pk_mul_f16 v68, v186, v168 op_sel_hi:[0,1]
	v_pk_mul_f16 v69, v186, v169 op_sel_hi:[0,1]
	v_pk_mul_f16 v70, v186, v170 op_sel_hi:[0,1]
	v_pk_mul_f16 v71, v186, v171 op_sel_hi:[0,1]
	v_pk_mul_f16 v72, v187, v168 op_sel_hi:[0,1]
	v_pk_mul_f16 v73, v187, v169 op_sel_hi:[0,1]
	v_pk_mul_f16 v74, v187, v170 op_sel_hi:[0,1]
	v_pk_mul_f16 v75, v187, v171 op_sel_hi:[0,1]
	v_pk_fma_f16 v47, v47, v171, v59
	v_pk_fma_f16 v46, v46, v170, v58
	v_pk_fma_f16 v45, v45, v169, v57
	v_pk_fma_f16 v44, v44, v168, v56
	v_pk_fma_f16 v63, v63, v171, v71
	v_pk_fma_f16 v62, v62, v170, v70
	v_pk_fma_f16 v61, v61, v169, v69
	v_pk_fma_f16 v60, v60, v168, v68
	v_pk_fma_f16 v76, v83, v171, v75
	v_pk_fma_f16 v77, v82, v170, v74
	v_pk_fma_f16 v78, v81, v169, v73
	v_pk_fma_f16 v79, v80, v168, v72
	v_pk_fma_f16 v80, v103, v171, v59
	v_pk_fma_f16 v81, v102, v170, v58
	v_pk_fma_f16 v82, v101, v169, v57
	v_pk_fma_f16 v83, v100, v168, v56
	v_pk_fma_f16 v92, v131, v171, v71
	v_pk_fma_f16 v93, v130, v170, v70
	v_pk_fma_f16 v94, v129, v169, v69
	v_pk_fma_f16 v95, v128, v168, v68
	v_pk_fma_f16 v96, v147, v171, v75
	v_pk_fma_f16 v97, v146, v170, v74
	v_pk_fma_f16 v98, v145, v169, v73
	v_pk_fma_f16 v99, v144, v168, v72
	v_pk_fma_f16 v75, v31, v171, v75
	v_pk_fma_f16 v74, v30, v170, v74
	v_pk_fma_f16 v73, v29, v169, v73
	v_pk_fma_f16 v72, v28, v168, v72
	v_pk_maximum3_f16 v28, v44, v60, v79
	v_pk_maximum3_f16 v29, v45, v61, v78
	v_pk_maximum3_f16 v30, v46, v62, v77
	v_pk_maximum3_f16 v31, v47, v63, v76
	v_pk_maximum3_f16 v100, v83, v95, v99
	v_pk_maximum3_f16 v101, v82, v94, v98
	v_pk_maximum3_f16 v102, v81, v93, v97
	v_pk_maximum3_f16 v103, v80, v92, v96
	v_pk_fma_f16 v59, v159, v171, v59
	v_pk_fma_f16 v58, v158, v170, v58
	v_pk_fma_f16 v57, v157, v169, v57
	v_pk_fma_f16 v56, v156, v168, v56
	v_pk_fma_f16 v71, v167, v171, v71
	v_pk_fma_f16 v70, v166, v170, v70
	v_pk_fma_f16 v69, v165, v169, v69
	v_pk_fma_f16 v68, v164, v168, v68
	v_pk_maximum3_f16 v109, v57, v69, v73
	v_pk_maximum3_f16 v110, v58, v70, v74
	v_pk_maximum3_f16 v111, v59, v71, v75
	v_pk_maximum3_f16 v108, v56, v68, v72
	v_pk_maximum3_f16 v29, v29, v101, v109
	v_pk_maximum3_f16 v30, v30, v102, v110
	v_pk_maximum3_f16 v31, v31, v103, v111
	v_pk_maximum3_f16 v28, v28, v100, v108
	v_xor_b32_e32 v100, 0x80008000, v31
	v_xor_b32_e32 v101, 0x80008000, v30
	v_xor_b32_e32 v102, 0x80008000, v29
	v_xor_b32_e32 v103, 0x80008000, v28
	v_pk_add_f16 v28, v44, v103
	v_pk_add_f16 v29, v45, v102
	v_pk_add_f16 v30, v46, v101
	v_pk_add_f16 v31, v47, v100
	v_exp_f16_sdwa v44, v28 dst_sel:WORD_0 dst_unused:UNUSED_PAD src0_sel:WORD_0
	v_exp_f16_sdwa v45, v29 dst_sel:WORD_0 dst_unused:UNUSED_PAD src0_sel:WORD_0
	v_exp_f16_sdwa v46, v30 dst_sel:WORD_0 dst_unused:UNUSED_PAD src0_sel:WORD_0
	v_exp_f16_sdwa v47, v31 dst_sel:WORD_0 dst_unused:UNUSED_PAD src0_sel:WORD_0
	v_exp_f16_sdwa v44, v28 dst_sel:WORD_1 dst_unused:UNUSED_PRESERVE src0_sel:WORD_1
	v_exp_f16_sdwa v45, v29 dst_sel:WORD_1 dst_unused:UNUSED_PRESERVE src0_sel:WORD_1
	v_exp_f16_sdwa v46, v30 dst_sel:WORD_1 dst_unused:UNUSED_PRESERVE src0_sel:WORD_1
	v_exp_f16_sdwa v47, v31 dst_sel:WORD_1 dst_unused:UNUSED_PRESERVE src0_sel:WORD_1
	v_pk_add_f16 v28, v44, 0
	v_pk_add_f16 v29, v45, 0
	v_pk_add_f16 v30, v46, 0
	v_pk_add_f16 v31, v47, 0
	v_pk_fma_f16 v32, v32, v44, 0
	v_pk_fma_f16 v33, v33, v45, 0
	v_pk_fma_f16 v34, v34, v46, 0
	v_pk_fma_f16 v35, v35, v47, 0
	v_pk_add_f16 v44, v60, v103
	v_pk_add_f16 v45, v61, v102
	v_pk_add_f16 v46, v62, v101
	v_pk_add_f16 v47, v63, v100
	v_exp_f16_sdwa v60, v44 dst_sel:WORD_0 dst_unused:UNUSED_PAD src0_sel:WORD_0
	v_exp_f16_sdwa v61, v45 dst_sel:WORD_0 dst_unused:UNUSED_PAD src0_sel:WORD_0
	v_exp_f16_sdwa v62, v46 dst_sel:WORD_0 dst_unused:UNUSED_PAD src0_sel:WORD_0
	v_exp_f16_sdwa v63, v47 dst_sel:WORD_0 dst_unused:UNUSED_PAD src0_sel:WORD_0
	v_exp_f16_sdwa v60, v44 dst_sel:WORD_1 dst_unused:UNUSED_PRESERVE src0_sel:WORD_1
	v_exp_f16_sdwa v61, v45 dst_sel:WORD_1 dst_unused:UNUSED_PRESERVE src0_sel:WORD_1
	v_exp_f16_sdwa v62, v46 dst_sel:WORD_1 dst_unused:UNUSED_PRESERVE src0_sel:WORD_1
	v_exp_f16_sdwa v63, v47 dst_sel:WORD_1 dst_unused:UNUSED_PRESERVE src0_sel:WORD_1
	s_nop 0
	v_pk_add_f16 v31, v31, v63
	v_pk_add_f16 v30, v30, v62
	v_pk_add_f16 v29, v29, v61
	v_pk_add_f16 v28, v28, v60
	v_pk_fma_f16 v35, v39, v63, v35
	v_pk_fma_f16 v34, v38, v62, v34
	v_pk_fma_f16 v33, v37, v61, v33
	v_pk_fma_f16 v32, v36, v60, v32
	v_pk_add_f16 v36, v79, v103
	v_pk_add_f16 v37, v78, v102
	v_pk_add_f16 v38, v77, v101
	v_pk_add_f16 v39, v76, v100
	v_exp_f16_sdwa v44, v36 dst_sel:WORD_0 dst_unused:UNUSED_PAD src0_sel:WORD_0
	v_exp_f16_sdwa v45, v37 dst_sel:WORD_0 dst_unused:UNUSED_PAD src0_sel:WORD_0
	v_exp_f16_sdwa v46, v38 dst_sel:WORD_0 dst_unused:UNUSED_PAD src0_sel:WORD_0
	v_exp_f16_sdwa v47, v39 dst_sel:WORD_0 dst_unused:UNUSED_PAD src0_sel:WORD_0
	v_exp_f16_sdwa v44, v36 dst_sel:WORD_1 dst_unused:UNUSED_PRESERVE src0_sel:WORD_1
	v_exp_f16_sdwa v45, v37 dst_sel:WORD_1 dst_unused:UNUSED_PRESERVE src0_sel:WORD_1
	v_exp_f16_sdwa v46, v38 dst_sel:WORD_1 dst_unused:UNUSED_PRESERVE src0_sel:WORD_1
	v_exp_f16_sdwa v47, v39 dst_sel:WORD_1 dst_unused:UNUSED_PRESERVE src0_sel:WORD_1
	v_pk_add_f16 v36, v83, v103
	v_pk_add_f16 v28, v28, v44
	v_pk_add_f16 v29, v29, v45
	v_pk_add_f16 v30, v30, v46
	v_pk_add_f16 v31, v31, v47
	v_pk_fma_f16 v32, v40, v44, v32
	v_pk_fma_f16 v33, v41, v45, v33
	v_pk_fma_f16 v34, v42, v46, v34
	v_pk_fma_f16 v35, v43, v47, v35
	v_pk_add_f16 v37, v82, v102
	v_pk_add_f16 v38, v81, v101
	v_pk_add_f16 v39, v80, v100
	v_exp_f16_sdwa v40, v36 dst_sel:WORD_0 dst_unused:UNUSED_PAD src0_sel:WORD_0
	v_exp_f16_sdwa v41, v37 dst_sel:WORD_0 dst_unused:UNUSED_PAD src0_sel:WORD_0
	v_exp_f16_sdwa v42, v38 dst_sel:WORD_0 dst_unused:UNUSED_PAD src0_sel:WORD_0
	v_exp_f16_sdwa v43, v39 dst_sel:WORD_0 dst_unused:UNUSED_PAD src0_sel:WORD_0
	v_exp_f16_sdwa v40, v36 dst_sel:WORD_1 dst_unused:UNUSED_PRESERVE src0_sel:WORD_1
	v_exp_f16_sdwa v41, v37 dst_sel:WORD_1 dst_unused:UNUSED_PRESERVE src0_sel:WORD_1
	v_exp_f16_sdwa v42, v38 dst_sel:WORD_1 dst_unused:UNUSED_PRESERVE src0_sel:WORD_1
	v_exp_f16_sdwa v43, v39 dst_sel:WORD_1 dst_unused:UNUSED_PRESERVE src0_sel:WORD_1
	v_pk_add_f16 v36, v95, v103
	v_pk_add_f16 v31, v31, v43
	v_pk_add_f16 v30, v30, v42
	v_pk_add_f16 v29, v29, v41
	v_pk_add_f16 v28, v28, v40
	v_pk_fma_f16 v35, v55, v43, v35
	v_pk_fma_f16 v34, v54, v42, v34
	v_pk_fma_f16 v33, v53, v41, v33
	v_pk_fma_f16 v32, v52, v40, v32
	v_pk_add_f16 v37, v94, v102
	v_pk_add_f16 v38, v93, v101
	v_pk_add_f16 v39, v92, v100
	v_exp_f16_sdwa v40, v36 dst_sel:WORD_0 dst_unused:UNUSED_PAD src0_sel:WORD_0
	v_exp_f16_sdwa v41, v37 dst_sel:WORD_0 dst_unused:UNUSED_PAD src0_sel:WORD_0
	v_exp_f16_sdwa v42, v38 dst_sel:WORD_0 dst_unused:UNUSED_PAD src0_sel:WORD_0
	v_exp_f16_sdwa v43, v39 dst_sel:WORD_0 dst_unused:UNUSED_PAD src0_sel:WORD_0
	v_exp_f16_sdwa v40, v36 dst_sel:WORD_1 dst_unused:UNUSED_PRESERVE src0_sel:WORD_1
	v_exp_f16_sdwa v41, v37 dst_sel:WORD_1 dst_unused:UNUSED_PRESERVE src0_sel:WORD_1
	v_exp_f16_sdwa v42, v38 dst_sel:WORD_1 dst_unused:UNUSED_PRESERVE src0_sel:WORD_1
	v_exp_f16_sdwa v43, v39 dst_sel:WORD_1 dst_unused:UNUSED_PRESERVE src0_sel:WORD_1
	v_pk_add_f16 v36, v99, v103
	v_pk_add_f16 v28, v28, v40
	v_pk_add_f16 v29, v29, v41
	v_pk_add_f16 v30, v30, v42
	v_pk_add_f16 v31, v31, v43
	v_pk_fma_f16 v32, v64, v40, v32
	v_pk_fma_f16 v33, v65, v41, v33
	v_pk_fma_f16 v34, v66, v42, v34
	v_pk_fma_f16 v35, v67, v43, v35
	v_pk_add_f16 v37, v98, v102
	v_pk_add_f16 v38, v97, v101
	v_pk_add_f16 v39, v96, v100
	v_exp_f16_sdwa v40, v36 dst_sel:WORD_0 dst_unused:UNUSED_PAD src0_sel:WORD_0
	v_exp_f16_sdwa v41, v37 dst_sel:WORD_0 dst_unused:UNUSED_PAD src0_sel:WORD_0
	v_exp_f16_sdwa v42, v38 dst_sel:WORD_0 dst_unused:UNUSED_PAD src0_sel:WORD_0
	v_exp_f16_sdwa v43, v39 dst_sel:WORD_0 dst_unused:UNUSED_PAD src0_sel:WORD_0
	v_exp_f16_sdwa v40, v36 dst_sel:WORD_1 dst_unused:UNUSED_PRESERVE src0_sel:WORD_1
	v_exp_f16_sdwa v41, v37 dst_sel:WORD_1 dst_unused:UNUSED_PRESERVE src0_sel:WORD_1
	v_exp_f16_sdwa v42, v38 dst_sel:WORD_1 dst_unused:UNUSED_PRESERVE src0_sel:WORD_1
	v_exp_f16_sdwa v43, v39 dst_sel:WORD_1 dst_unused:UNUSED_PRESERVE src0_sel:WORD_1
	v_pk_add_f16 v36, v56, v103
	v_pk_add_f16 v31, v31, v43
	v_pk_add_f16 v30, v30, v42
	v_pk_add_f16 v29, v29, v41
	v_pk_add_f16 v28, v28, v40
	v_pk_fma_f16 v35, v87, v43, v35
	v_pk_fma_f16 v34, v86, v42, v34
	v_pk_fma_f16 v33, v85, v41, v33
	v_pk_fma_f16 v32, v84, v40, v32
	v_pk_add_f16 v37, v57, v102
	v_pk_add_f16 v38, v58, v101
	v_pk_add_f16 v39, v59, v100
	v_exp_f16_sdwa v40, v36 dst_sel:WORD_0 dst_unused:UNUSED_PAD src0_sel:WORD_0
	v_exp_f16_sdwa v41, v37 dst_sel:WORD_0 dst_unused:UNUSED_PAD src0_sel:WORD_0
	v_exp_f16_sdwa v42, v38 dst_sel:WORD_0 dst_unused:UNUSED_PAD src0_sel:WORD_0
	v_exp_f16_sdwa v43, v39 dst_sel:WORD_0 dst_unused:UNUSED_PAD src0_sel:WORD_0
	v_exp_f16_sdwa v40, v36 dst_sel:WORD_1 dst_unused:UNUSED_PRESERVE src0_sel:WORD_1
	v_exp_f16_sdwa v41, v37 dst_sel:WORD_1 dst_unused:UNUSED_PRESERVE src0_sel:WORD_1
	v_exp_f16_sdwa v42, v38 dst_sel:WORD_1 dst_unused:UNUSED_PRESERVE src0_sel:WORD_1
	v_exp_f16_sdwa v43, v39 dst_sel:WORD_1 dst_unused:UNUSED_PRESERVE src0_sel:WORD_1
	v_pk_add_f16 v36, v68, v103
	v_pk_add_f16 v28, v28, v40
	v_pk_add_f16 v29, v29, v41
	v_pk_add_f16 v30, v30, v42
	v_pk_add_f16 v31, v31, v43
	v_pk_fma_f16 v32, v104, v40, v32
	v_pk_fma_f16 v33, v105, v41, v33
	v_pk_fma_f16 v34, v106, v42, v34
	v_pk_fma_f16 v35, v107, v43, v35
	v_pk_add_f16 v37, v69, v102
	v_pk_add_f16 v38, v70, v101
	v_pk_add_f16 v39, v71, v100
	v_exp_f16_sdwa v40, v36 dst_sel:WORD_0 dst_unused:UNUSED_PAD src0_sel:WORD_0
	v_exp_f16_sdwa v41, v37 dst_sel:WORD_0 dst_unused:UNUSED_PAD src0_sel:WORD_0
	v_exp_f16_sdwa v42, v38 dst_sel:WORD_0 dst_unused:UNUSED_PAD src0_sel:WORD_0
	v_exp_f16_sdwa v43, v39 dst_sel:WORD_0 dst_unused:UNUSED_PAD src0_sel:WORD_0
	v_exp_f16_sdwa v40, v36 dst_sel:WORD_1 dst_unused:UNUSED_PRESERVE src0_sel:WORD_1
	v_exp_f16_sdwa v41, v37 dst_sel:WORD_1 dst_unused:UNUSED_PRESERVE src0_sel:WORD_1
	v_exp_f16_sdwa v42, v38 dst_sel:WORD_1 dst_unused:UNUSED_PRESERVE src0_sel:WORD_1
	v_exp_f16_sdwa v43, v39 dst_sel:WORD_1 dst_unused:UNUSED_PRESERVE src0_sel:WORD_1
	s_nop 0
	v_pk_add_f16 v31, v31, v43
	v_pk_add_f16 v30, v30, v42
	v_pk_add_f16 v29, v29, v41
	v_pk_add_f16 v28, v28, v40
	v_pk_fma_f16 v35, v123, v43, v35
	v_pk_fma_f16 v34, v122, v42, v34
	v_pk_fma_f16 v33, v121, v41, v33
	v_pk_fma_f16 v32, v120, v40, v32
	v_pk_add_f16 v40, v72, v103
	v_pk_add_f16 v41, v73, v102
	v_pk_add_f16 v42, v74, v101
	v_pk_add_f16 v43, v75, v100
	v_exp_f16_sdwa v36, v40 dst_sel:WORD_0 dst_unused:UNUSED_PAD src0_sel:WORD_0
	v_exp_f16_sdwa v37, v41 dst_sel:WORD_0 dst_unused:UNUSED_PAD src0_sel:WORD_0
	v_exp_f16_sdwa v38, v42 dst_sel:WORD_0 dst_unused:UNUSED_PAD src0_sel:WORD_0
	v_exp_f16_sdwa v39, v43 dst_sel:WORD_0 dst_unused:UNUSED_PAD src0_sel:WORD_0
	v_exp_f16_sdwa v36, v40 dst_sel:WORD_1 dst_unused:UNUSED_PRESERVE src0_sel:WORD_1
	v_exp_f16_sdwa v37, v41 dst_sel:WORD_1 dst_unused:UNUSED_PRESERVE src0_sel:WORD_1
	v_exp_f16_sdwa v38, v42 dst_sel:WORD_1 dst_unused:UNUSED_PRESERVE src0_sel:WORD_1
	v_exp_f16_sdwa v39, v43 dst_sel:WORD_1 dst_unused:UNUSED_PRESERVE src0_sel:WORD_1
	s_nop 0
	s_load_dwordx2 s[12:13], s[0:1], 0x60
	s_branch .LBB6_76
.LBB6_38:
	s_load_dwordx2 s[12:13], s[0:1], 0x60
	s_cbranch_execz .LBB6_76
	s_load_dwordx2 s[2:3], s[0:1], 0x18
	s_waitcnt lgkmcnt(0)
	s_load_dwordx2 s[0:1], s[2:3], 0x0
	s_load_dword s4, s[2:3], 0x8
	v_cmp_lt_u32_e64 s[64:65], 0, v182
	v_cmp_gt_u32_e64 s[66:67], 63, v182
	v_cmp_lt_u32_e64 s[68:69], 0, v181
	v_cmp_gt_u32_e64 s[70:71], 60, v181
	buffer_load_dwordx4 v[168:171], v183, s[8:11], 0 offen
	s_and_b64 s[72:73], s[68:69], s[64:65]
	s_and_b64 s[74:75], s[68:69], s[66:67]
	s_and_b64 s[76:77], s[70:71], s[64:65]
	s_and_b64 s[78:79], s[70:71], s[66:67]
	v_add_u32_e32 v228, 0xfffe7c00, v183
	v_add_u32_e32 v229, 0xfffe8000, v183
	s_mov_b64 exec, s[72:73]
	buffer_load_dwordx4 v[140:143], v228, s[8:11], 0 offen
	buffer_load_dwordx4 v[120:123], v228, s[8:11], 0 offen offset:512
	s_mov_b64 exec, -1
	s_mov_b64 exec, s[68:69]
	buffer_load_dwordx4 v[152:155], v229, s[8:11], 0 offen offset:512
	buffer_load_dwordx4 v[132:135], v229, s[8:11], 0 offen offset:1024
	s_mov_b64 exec, -1
	s_mov_b64 exec, s[74:75]
	buffer_load_dwordx4 v[156:159], v229, s[8:11], 0 offen offset:2048
	buffer_load_dwordx4 v[144:147], v229, s[8:11], 0 offen offset:2560
	s_mov_b64 exec, -1
	v_add_u32_e32 v228, 0xfffffc00, v183
	s_mov_b64 exec, s[64:65]
	buffer_load_dwordx4 v[124:127], v228, s[8:11], 0 offen
	buffer_load_dwordx4 v[104:107], v228, s[8:11], 0 offen offset:512
	s_mov_b64 exec, -1
	buffer_load_dwordx4 v[136:139], v183, s[8:11], 0 offen offset:512
	buffer_load_dwordx4 v[108:111], v183, s[8:11], 0 offen offset:1024
	s_mov_b64 exec, s[66:67]
	buffer_load_dwordx4 v[148:151], v183, s[8:11], 0 offen offset:2048
	buffer_load_dwordx4 v[88:91], v183, s[8:11], 0 offen offset:2560
	s_mov_b64 exec, -1
	v_add_u32_e32 v228, 0x17c00, v183
	v_add_u32_e32 v229, 0x18000, v183
	s_mov_b64 exec, s[64:65]
	buffer_load_dwordx4 v[64:67], v228, s[8:11], 0 offen
	buffer_load_dwordx4 v[40:43], v228, s[8:11], 0 offen offset:512
	s_mov_b64 exec, -1
	buffer_load_dwordx4 v[76:79], v229, s[8:11], 0 offen offset:512
	buffer_load_dwordx4 v[48:51], v229, s[8:11], 0 offen offset:1024
	s_mov_b64 exec, s[66:67]
	buffer_load_dwordx4 v[92:95], v229, s[8:11], 0 offen offset:2048
	buffer_load_dwordx4 v[60:63], v229, s[8:11], 0 offen offset:2560
	s_mov_b64 exec, -1
	v_add_u32_e32 v228, 0x2fc00, v183
	v_add_u32_e32 v229, 0x30000, v183
	s_mov_b64 exec, s[64:65]
	buffer_load_dwordx4 v[36:39], v228, s[8:11], 0 offen
	buffer_load_dwordx4 v[24:27], v228, s[8:11], 0 offen offset:512
	s_mov_b64 exec, -1
	buffer_load_dwordx4 v[52:55], v229, s[8:11], 0 offen offset:512
	buffer_load_dwordx4 v[28:31], v229, s[8:11], 0 offen offset:1024
	s_mov_b64 exec, s[66:67]
	buffer_load_dwordx4 v[68:71], v229, s[8:11], 0 offen offset:2048
	buffer_load_dwordx4 v[32:35], v229, s[8:11], 0 offen offset:2560
	s_mov_b64 exec, -1
	v_add_u32_e32 v228, 0x18000, v183
	buffer_load_dwordx4 v[160:163], v228, s[8:11], 0 offen
	v_add_u32_e32 v228, 0x47c00, v183
	v_add_u32_e32 v229, 0x48000, v183
	v_add_u32_e32 v230, 0x5fc00, v183
	v_add_u32_e32 v231, 0x60000, v183
	s_not_b64 exec, s[72:73]
	s_cbranch_execz .Lmyf_E2_0
	v_mov_b32_e32 v140, v20
	v_mov_b32_e32 v141, v21
	v_mov_b32_e32 v142, v22
	v_mov_b32_e32 v143, v23
	v_mov_b32_e32 v120, v16
	v_mov_b32_e32 v121, v17
	v_mov_b32_e32 v122, v18
	v_mov_b32_e32 v123, v19
.Lmyf_E2_0:
	s_not_b64 exec, s[68:69]
	s_cbranch_execz .Lmyf_E2_1
	v_mov_b32_e32 v152, v20
	v_mov_b32_e32 v153, v21
	v_mov_b32_e32 v154, v22
	v_mov_b32_e32 v155, v23
	v_mov_b32_e32 v132, v16
	v_mov_b32_e32 v133, v17
	v_mov_b32_e32 v134, v18
	v_mov_b32_e32 v135, v19
.Lmyf_E2_1:
	s_not_b64 exec, s[74:75]
	s_cbranch_execz .Lmyf_E2_2
	v_mov_b32_e32 v156, v20
	v_mov_b32_e32 v157, v21
	v_mov_b32_e32 v158, v22
	v_mov_b32_e32 v159, v23
	v_mov_b32_e32 v144, v16
	v_mov_b32_e32 v145, v17
	v_mov_b32_e32 v146, v18
	v_mov_b32_e32 v147, v19
.Lmyf_E2_2:
	s_not_b64 exec, s[64:65]
	s_cbranch_execz .Lmyf_E2_3
	v_mov_b32_e32 v124, v20
	v_mov_b32_e32 v125, v21
	v_mov_b32_e32 v126, v22
	v_mov_b32_e32 v127, v23
	v_mov_b32_e32 v104, v16
	v_mov_b32_e32 v105, v17
	v_mov_b32_e32 v106, v18
	v_mov_b32_e32 v107, v19
	v_mov_b32_e32 v64, v20
	v_mov_b32_e32 v65, v21
	v_mov_b32_e32 v66, v22
	v_mov_b32_e32 v67, v23
	v_mov_b32_e32 v40, v16
	v_mov_b32_e32 v41, v17
	v_mov_b32_e32 v42, v18
	v_mov_b32_e32 v43, v19
	v_mov_b32_e32 v36, v20
	v_mov_b32_e32 v37, v21
	v_mov_b32_e32 v38, v22
	v_mov_b32_e32 v39, v23
	v_mov_b32_e32 v24, v16
	v_mov_b32_e32 v25, v17
	v_mov_b32_e32 v26, v18
	v_mov_b32_e32 v27, v19
	v_mov_b32_e32 v80, v20
	v_mov_b32_e32 v81, v21
	v_mov_b32_e32 v82, v22
	v_mov_b32_e32 v83, v23
	v_mov_b32_e32 v44, v16
	v_mov_b32_e32 v45, v17
	v_mov_b32_e32 v46, v18
	v_mov_b32_e32 v47, v19
.Lmyf_E2_3:
	s_not_b64 exec, s[66:67]
	s_cbranch_execz .Lmyf_E2_4
	v_mov_b32_e32 v148, v20
	v_mov_b32_e32 v149, v21
	v_mov_b32_e32 v150, v22
	v_mov_b32_e32 v151, v23
	v_mov_b32_e32 v88, v16
	v_mov_b32_e32 v89, v17
	v_mov_b32_e32 v90, v18
	v_mov_b32_e32 v91, v19
	v_mov_b32_e32 v92, v20
	v_mov_b32_e32 v93, v21
	v_mov_b32_e32 v94, v22
	v_mov_b32_e32 v95, v23
	v_mov_b32_e32 v60, v16
	v_mov_b32_e32 v61, v17
	v_mov_b32_e32 v62, v18
	v_mov_b32_e32 v63, v19
	v_mov_b32_e32 v68, v20
	v_mov_b32_e32 v69, v21
	v_mov_b32_e32 v70, v22
	v_mov_b32_e32 v71, v23
	v_mov_b32_e32 v32, v16
	v_mov_b32_e32 v33, v17
	v_mov_b32_e32 v34, v18
	v_mov_b32_e32 v35, v19
	v_mov_b32_e32 v112, v20
	v_mov_b32_e32 v113, v21
	v_mov_b32_e32 v114, v22
	v_mov_b32_e32 v115, v23
	v_mov_b32_e32 v72, v16
	v_mov_b32_e32 v73, v17
	v_mov_b32_e32 v74, v18
	v_mov_b32_e32 v75, v19
.Lmyf_E2_4:
	s_not_b64 exec, s[76:77]
	s_cbranch_execz .Lmyf_E2_5
	v_mov_b32_e32 v116, v20
	v_mov_b32_e32 v117, v21
	v_mov_b32_e32 v118, v22
	v_mov_b32_e32 v119, v23
	v_mov_b32_e32 v84, v16
	v_mov_b32_e32 v85, v17
	v_mov_b32_e32 v86, v18
	v_mov_b32_e32 v87, v19
.Lmyf_E2_5:
	s_not_b64 exec, s[70:71]
	s_cbranch_execz .Lmyf_E2_6
	v_mov_b32_e32 v128, v20
	v_mov_b32_e32 v129, v21
	v_mov_b32_e32 v130, v22
	v_mov_b32_e32 v131, v23
	v_mov_b32_e32 v96, v16
	v_mov_b32_e32 v97, v17
	v_mov_b32_e32 v98, v18
	v_mov_b32_e32 v99, v19

.Lmyf_E2_7:
	s_mov_b64 exec, -1
	s_waitcnt lgkmcnt(0)
	v_cvt_f16_f32_e32 v164, s0
	v_cvt_f16_f32_e32 v165, s1
	v_cvt_f16_f32_e32 v166, s4
	s_waitcnt vmcnt(7)
	v_pk_mul_f16 v167, v164, v168 op_sel_hi:[0,1]
	v_pk_mul_f16 v172, v164, v169 op_sel_hi:[0,1]
	v_pk_mul_f16 v173, v164, v170 op_sel_hi:[0,1]
	v_pk_mul_f16 v174, v164, v171 op_sel_hi:[0,1]
	v_pk_mul_f16 v175, v165, v170 op_sel_hi:[0,1]
	v_pk_mul_f16 v176, v165, v171 op_sel_hi:[0,1]
	v_pk_mul_f16 v177, v165, v169 op_sel_hi:[0,1]
	v_pk_mul_f16 v178, v165, v168 op_sel_hi:[0,1]
	v_pk_mul_f16 v179, v166, v171 op_sel_hi:[0,1]
	v_pk_mul_f16 v184, v166, v170 op_sel_hi:[0,1]
	v_pk_mul_f16 v185, v166, v169 op_sel_hi:[0,1]
	v_pk_mul_f16 v186, v166, v168 op_sel_hi:[0,1]
	v_pk_fma_f16 v143, v143, v171, v174
	v_pk_fma_f16 v142, v142, v170, v173
	v_pk_fma_f16 v141, v141, v169, v172
	v_pk_fma_f16 v140, v140, v168, v167
	v_pk_fma_f16 v155, v155, v171, v174
	v_pk_fma_f16 v154, v154, v170, v173
	v_pk_fma_f16 v153, v153, v169, v172
	v_pk_fma_f16 v152, v152, v168, v167
	v_pk_fma_f16 v159, v159, v171, v174
	v_pk_fma_f16 v158, v158, v170, v173
	v_pk_fma_f16 v157, v157, v169, v172
	v_pk_fma_f16 v156, v156, v168, v167
	v_pk_fma_f16 v167, v127, v171, v176
	v_pk_fma_f16 v172, v126, v170, v175
	v_pk_fma_f16 v173, v139, v171, v176
	v_pk_fma_f16 v174, v138, v170, v175
	v_pk_fma_f16 v176, v151, v171, v176
	v_pk_fma_f16 v175, v150, v170, v175
	v_pk_fma_f16 v187, v125, v169, v177
	v_pk_fma_f16 v188, v137, v169, v177
	v_pk_fma_f16 v177, v149, v169, v177
	v_pk_fma_f16 v189, v124, v168, v178
	v_pk_fma_f16 v190, v136, v168, v178
	v_pk_fma_f16 v178, v148, v168, v178
	v_pk_fma_f16 v191, v67, v171, v179
	v_pk_fma_f16 v192, v79, v171, v179
	v_pk_fma_f16 v171, v95, v171, v179
	v_pk_fma_f16 v179, v66, v170, v184
	v_pk_fma_f16 v193, v78, v170, v184
	v_pk_fma_f16 v170, v94, v170, v184
	v_pk_fma_f16 v184, v65, v169, v185
	v_pk_fma_f16 v194, v77, v169, v185
	v_pk_fma_f16 v169, v93, v169, v185
	v_pk_fma_f16 v185, v64, v168, v186
	v_pk_fma_f16 v195, v76, v168, v186
	v_pk_fma_f16 v168, v92, v168, v186
	v_pk_maximum3_f16 v186, v140, v152, v156
	v_pk_maximum3_f16 v196, v189, v190, v178
	v_pk_maximum3_f16 v198, v141, v153, v157
	v_pk_maximum3_f16 v199, v187, v188, v177
	v_pk_maximum3_f16 v200, v184, v194, v169
	v_pk_maximum3_f16 v197, v185, v195, v168
	v_pk_maximum3_f16 v201, v142, v154, v158
	v_pk_maximum3_f16 v202, v172, v174, v175
	v_pk_maximum3_f16 v203, v179, v193, v170
	v_pk_maximum3_f16 v204, v143, v155, v159
	v_pk_maximum3_f16 v205, v167, v173, v176
	v_pk_maximum3_f16 v206, v191, v192, v171
	v_pk_maximum3_f16 v186, v186, v196, v197
	v_pk_maximum3_f16 v196, v198, v199, v200
	v_pk_maximum3_f16 v197, v201, v202, v203
	s_waitcnt vmcnt(0)
	v_pk_mul_f16 v203, v166, v163 op_sel_hi:[0,1]
	v_pk_maximum3_f16 v198, v204, v205, v206
	v_pk_add_f16 v140, v140, v186 neg_lo:[0,1] neg_hi:[0,1]
	v_pk_add_f16 v141, v141, v196 neg_lo:[0,1] neg_hi:[0,1]
	v_pk_add_f16 v142, v142, v197 neg_lo:[0,1] neg_hi:[0,1]
	v_pk_add_f16 v143, v143, v198 neg_lo:[0,1] neg_hi:[0,1]
	v_pk_add_f16 v152, v152, v186 neg_lo:[0,1] neg_hi:[0,1]
	v_exp_f16_sdwa v199, v140 dst_sel:WORD_0 dst_unused:UNUSED_PAD src0_sel:WORD_0
	v_exp_f16_sdwa v200, v141 dst_sel:WORD_0 dst_unused:UNUSED_PAD src0_sel:WORD_0
	v_exp_f16_sdwa v201, v142 dst_sel:WORD_0 dst_unused:UNUSED_PAD src0_sel:WORD_0
	v_exp_f16_sdwa v202, v143 dst_sel:WORD_0 dst_unused:UNUSED_PAD src0_sel:WORD_0
	v_exp_f16_sdwa v199, v140 dst_sel:WORD_1 dst_unused:UNUSED_PRESERVE src0_sel:WORD_1
	v_exp_f16_sdwa v200, v141 dst_sel:WORD_1 dst_unused:UNUSED_PRESERVE src0_sel:WORD_1
	v_exp_f16_sdwa v201, v142 dst_sel:WORD_1 dst_unused:UNUSED_PRESERVE src0_sel:WORD_1
	v_exp_f16_sdwa v202, v143 dst_sel:WORD_1 dst_unused:UNUSED_PRESERVE src0_sel:WORD_1
	v_pk_add_f16 v153, v153, v196 neg_lo:[0,1] neg_hi:[0,1]
	v_pk_fma_f16 v123, v123, v202, 0
	v_pk_fma_f16 v120, v120, v199, 0
	v_pk_add_f16 v154, v154, v197 neg_lo:[0,1] neg_hi:[0,1]
	v_pk_add_f16 v155, v155, v198 neg_lo:[0,1] neg_hi:[0,1]
	v_pk_fma_f16 v122, v122, v201, 0
	v_exp_f16_sdwa v140, v152 dst_sel:WORD_0 dst_unused:UNUSED_PAD src0_sel:WORD_0
	v_exp_f16_sdwa v141, v153 dst_sel:WORD_0 dst_unused:UNUSED_PAD src0_sel:WORD_0
	v_exp_f16_sdwa v142, v154 dst_sel:WORD_0 dst_unused:UNUSED_PAD src0_sel:WORD_0
	v_exp_f16_sdwa v143, v155 dst_sel:WORD_0 dst_unused:UNUSED_PAD src0_sel:WORD_0
	v_exp_f16_sdwa v140, v152 dst_sel:WORD_1 dst_unused:UNUSED_PRESERVE src0_sel:WORD_1
	v_exp_f16_sdwa v141, v153 dst_sel:WORD_1 dst_unused:UNUSED_PRESERVE src0_sel:WORD_1
	v_exp_f16_sdwa v142, v154 dst_sel:WORD_1 dst_unused:UNUSED_PRESERVE src0_sel:WORD_1
	v_exp_f16_sdwa v143, v155 dst_sel:WORD_1 dst_unused:UNUSED_PRESERVE src0_sel:WORD_1
	v_pk_fma_f16 v121, v121, v200, 0
	v_pk_fma_f16 v120, v132, v140, v120
	v_pk_fma_f16 v123, v135, v143, v123
	s_mov_b64 exec, s[64:65]
	buffer_load_dwordx4 v[80:83], v228, s[8:11], 0 offen
	buffer_load_dwordx4 v[44:47], v228, s[8:11], 0 offen offset:512
	s_mov_b64 exec, -1
	v_pk_add_f16 v135, v159, v198 neg_lo:[0,1] neg_hi:[0,1]
	v_pk_fma_f16 v121, v133, v141, v121
	v_pk_fma_f16 v122, v134, v142, v122
	v_pk_add_f16 v132, v156, v186 neg_lo:[0,1] neg_hi:[0,1]
	v_pk_add_f16 v133, v157, v196 neg_lo:[0,1] neg_hi:[0,1]
	v_pk_add_f16 v134, v158, v197 neg_lo:[0,1] neg_hi:[0,1]
	v_pk_fma_f16 v204, v39, v163, v203
	v_exp_f16_sdwa v152, v132 dst_sel:WORD_0 dst_unused:UNUSED_PAD src0_sel:WORD_0
	v_exp_f16_sdwa v153, v133 dst_sel:WORD_0 dst_unused:UNUSED_PAD src0_sel:WORD_0
	v_exp_f16_sdwa v154, v134 dst_sel:WORD_0 dst_unused:UNUSED_PAD src0_sel:WORD_0
	v_exp_f16_sdwa v155, v135 dst_sel:WORD_0 dst_unused:UNUSED_PAD src0_sel:WORD_0
	v_exp_f16_sdwa v152, v132 dst_sel:WORD_1 dst_unused:UNUSED_PRESERVE src0_sel:WORD_1
	v_exp_f16_sdwa v153, v133 dst_sel:WORD_1 dst_unused:UNUSED_PRESERVE src0_sel:WORD_1
	v_exp_f16_sdwa v154, v134 dst_sel:WORD_1 dst_unused:UNUSED_PRESERVE src0_sel:WORD_1
	v_exp_f16_sdwa v155, v135 dst_sel:WORD_1 dst_unused:UNUSED_PRESERVE src0_sel:WORD_1
	v_pk_mul_f16 v135, v164, v163 op_sel_hi:[0,1]
	v_pk_fma_f16 v120, v144, v152, v120
	v_pk_mul_f16 v144, v165, v163 op_sel_hi:[0,1]
	v_pk_fma_f16 v123, v147, v155, v123
	v_pk_fma_f16 v122, v146, v154, v122
	v_pk_fma_f16 v121, v145, v153, v121
	v_pk_mul_f16 v132, v164, v160 op_sel_hi:[0,1]
	v_pk_mul_f16 v133, v164, v161 op_sel_hi:[0,1]
	v_pk_mul_f16 v134, v164, v162 op_sel_hi:[0,1]
	v_pk_fma_f16 v127, v127, v163, v135
	v_pk_fma_f16 v139, v139, v163, v135
	v_pk_fma_f16 v135, v151, v163, v135
	v_pk_fma_f16 v145, v67, v163, v144
	v_pk_fma_f16 v146, v79, v163, v144
	v_pk_fma_f16 v144, v95, v163, v144
	v_pk_mul_f16 v147, v165, v162 op_sel_hi:[0,1]
	v_pk_fma_f16 v205, v55, v163, v203
	buffer_load_dwordx4 v[100:103], v229, s[8:11], 0 offen offset:512
	buffer_load_dwordx4 v[56:59], v229, s[8:11], 0 offen offset:1024
	v_pk_fma_f16 v163, v71, v163, v203
	v_pk_mul_f16 v203, v166, v162 op_sel_hi:[0,1]
	v_pk_fma_f16 v126, v126, v162, v134
	v_pk_fma_f16 v125, v125, v161, v133
	v_pk_fma_f16 v124, v124, v160, v132
	v_pk_fma_f16 v138, v138, v162, v134
	v_pk_fma_f16 v137, v137, v161, v133
	v_pk_fma_f16 v136, v136, v160, v132
	v_pk_fma_f16 v134, v150, v162, v134
	v_pk_fma_f16 v133, v149, v161, v133
	v_pk_fma_f16 v132, v148, v160, v132
	v_pk_fma_f16 v148, v66, v162, v147
	v_pk_fma_f16 v149, v78, v162, v147
	v_pk_fma_f16 v147, v94, v162, v147
	v_pk_mul_f16 v150, v165, v161 op_sel_hi:[0,1]
	v_pk_fma_f16 v206, v38, v162, v203
	v_pk_fma_f16 v207, v54, v162, v203
	v_pk_fma_f16 v162, v70, v162, v203
	v_pk_mul_f16 v203, v166, v161 op_sel_hi:[0,1]
	v_pk_fma_f16 v151, v65, v161, v150
	v_pk_fma_f16 v156, v77, v161, v150
	v_pk_fma_f16 v150, v93, v161, v150
	v_pk_mul_f16 v157, v165, v160 op_sel_hi:[0,1]
	s_mov_b64 exec, s[66:67]
	buffer_load_dwordx4 v[112:115], v229, s[8:11], 0 offen offset:2048
	buffer_load_dwordx4 v[72:75], v229, s[8:11], 0 offen offset:2560
	s_mov_b64 exec, -1
	v_pk_fma_f16 v208, v37, v161, v203
	v_pk_fma_f16 v209, v53, v161, v203
	v_pk_fma_f16 v161, v69, v161, v203
	v_pk_mul_f16 v203, v166, v160 op_sel_hi:[0,1]
	v_pk_fma_f16 v158, v64, v160, v157
	v_pk_fma_f16 v159, v76, v160, v157
	v_pk_fma_f16 v157, v92, v160, v157
	v_pk_fma_f16 v210, v36, v160, v203
	v_pk_fma_f16 v211, v52, v160, v203
	v_pk_fma_f16 v160, v68, v160, v203
	v_pk_maximum3_f16 v203, v124, v136, v132
	v_pk_maximum3_f16 v212, v158, v159, v157
	v_pk_maximum3_f16 v214, v208, v209, v161
	v_pk_maximum3_f16 v215, v206, v207, v162
	v_pk_maximum3_f16 v216, v204, v205, v163
	v_pk_maximum3_f16 v213, v210, v211, v160
	v_pk_add_f16 v189, v189, v186 neg_lo:[0,1] neg_hi:[0,1]
	v_pk_maximum3_f16 v203, v203, v212, v213
	v_pk_maximum3_f16 v212, v125, v137, v133
	v_pk_maximum3_f16 v213, v151, v156, v150
	v_pk_add_f16 v187, v187, v196 neg_lo:[0,1] neg_hi:[0,1]
	v_pk_maximum3_f16 v212, v212, v213, v214
	v_pk_maximum3_f16 v213, v126, v138, v134
	v_pk_maximum3_f16 v214, v148, v149, v147
	v_pk_add_f16 v172, v172, v197 neg_lo:[0,1] neg_hi:[0,1]
	v_pk_maximum3_f16 v213, v213, v214, v215
	v_pk_maximum3_f16 v214, v127, v139, v135
	v_pk_maximum3_f16 v215, v145, v146, v144
	v_pk_add_f16 v167, v167, v198 neg_lo:[0,1] neg_hi:[0,1]
	v_pk_maximum3_f16 v214, v214, v215, v216
	v_exp_f16_sdwa v215, v189 dst_sel:WORD_0 dst_unused:UNUSED_PAD src0_sel:WORD_0
	v_exp_f16_sdwa v216, v187 dst_sel:WORD_0 dst_unused:UNUSED_PAD src0_sel:WORD_0
	v_exp_f16_sdwa v217, v172 dst_sel:WORD_0 dst_unused:UNUSED_PAD src0_sel:WORD_0
	v_exp_f16_sdwa v218, v167 dst_sel:WORD_0 dst_unused:UNUSED_PAD src0_sel:WORD_0
	v_exp_f16_sdwa v215, v189 dst_sel:WORD_1 dst_unused:UNUSED_PRESERVE src0_sel:WORD_1
	v_exp_f16_sdwa v216, v187 dst_sel:WORD_1 dst_unused:UNUSED_PRESERVE src0_sel:WORD_1
	v_exp_f16_sdwa v217, v172 dst_sel:WORD_1 dst_unused:UNUSED_PRESERVE src0_sel:WORD_1
	v_exp_f16_sdwa v218, v167 dst_sel:WORD_1 dst_unused:UNUSED_PRESERVE src0_sel:WORD_1
	v_xor_b32_e32 v167, 0x80008000, v214
	v_xor_b32_e32 v172, 0x80008000, v213
	v_xor_b32_e32 v187, 0x80008000, v212
	v_xor_b32_e32 v189, 0x80008000, v203
	v_pk_add_f16 v124, v124, v189
	v_pk_add_f16 v125, v125, v187
	v_pk_add_f16 v126, v126, v172
	v_pk_add_f16 v127, v127, v167
	v_pk_fma_f16 v120, v104, v215, v120
	v_pk_fma_f16 v121, v105, v216, v121
	v_exp_f16_sdwa v203, v124 dst_sel:WORD_0 dst_unused:UNUSED_PAD src0_sel:WORD_0
	v_exp_f16_sdwa v212, v125 dst_sel:WORD_0 dst_unused:UNUSED_PAD src0_sel:WORD_0
	v_exp_f16_sdwa v213, v126 dst_sel:WORD_0 dst_unused:UNUSED_PAD src0_sel:WORD_0
	v_exp_f16_sdwa v214, v127 dst_sel:WORD_0 dst_unused:UNUSED_PAD src0_sel:WORD_0
	v_exp_f16_sdwa v203, v124 dst_sel:WORD_1 dst_unused:UNUSED_PRESERVE src0_sel:WORD_1
	v_exp_f16_sdwa v212, v125 dst_sel:WORD_1 dst_unused:UNUSED_PRESERVE src0_sel:WORD_1
	v_exp_f16_sdwa v213, v126 dst_sel:WORD_1 dst_unused:UNUSED_PRESERVE src0_sel:WORD_1
	v_exp_f16_sdwa v214, v127 dst_sel:WORD_1 dst_unused:UNUSED_PRESERVE src0_sel:WORD_1
	v_pk_add_f16 v124, v190, v186 neg_lo:[0,1] neg_hi:[0,1]
	v_pk_fma_f16 v105, v105, v212, 0
	v_pk_fma_f16 v104, v104, v203, 0
	v_pk_add_f16 v125, v188, v196 neg_lo:[0,1] neg_hi:[0,1]
	v_pk_add_f16 v126, v174, v197 neg_lo:[0,1] neg_hi:[0,1]
	v_pk_add_f16 v127, v173, v198 neg_lo:[0,1] neg_hi:[0,1]
	v_pk_fma_f16 v122, v106, v217, v122
	v_pk_fma_f16 v123, v107, v218, v123
	s_mov_b64 exec, s[76:77]
	buffer_load_dwordx4 v[116:119], v230, s[8:11], 0 offen
	buffer_load_dwordx4 v[84:87], v230, s[8:11], 0 offen offset:512
	s_mov_b64 exec, -1
	v_pk_fma_f16 v107, v107, v214, 0
	v_pk_fma_f16 v106, v106, v213, 0
	v_exp_f16_sdwa v173, v124 dst_sel:WORD_0 dst_unused:UNUSED_PAD src0_sel:WORD_0
	v_exp_f16_sdwa v174, v125 dst_sel:WORD_0 dst_unused:UNUSED_PAD src0_sel:WORD_0
	v_exp_f16_sdwa v188, v126 dst_sel:WORD_0 dst_unused:UNUSED_PAD src0_sel:WORD_0
	v_exp_f16_sdwa v190, v127 dst_sel:WORD_0 dst_unused:UNUSED_PAD src0_sel:WORD_0
	v_exp_f16_sdwa v173, v124 dst_sel:WORD_1 dst_unused:UNUSED_PRESERVE src0_sel:WORD_1
	v_exp_f16_sdwa v174, v125 dst_sel:WORD_1 dst_unused:UNUSED_PRESERVE src0_sel:WORD_1
	v_exp_f16_sdwa v188, v126 dst_sel:WORD_1 dst_unused:UNUSED_PRESERVE src0_sel:WORD_1
	v_exp_f16_sdwa v190, v127 dst_sel:WORD_1 dst_unused:UNUSED_PRESERVE src0_sel:WORD_1
	v_pk_add_f16 v124, v136, v189
	v_pk_add_f16 v125, v137, v187
	v_pk_add_f16 v126, v138, v172
	v_pk_add_f16 v127, v139, v167
	v_pk_fma_f16 v123, v111, v190, v123
	v_exp_f16_sdwa v136, v124 dst_sel:WORD_0 dst_unused:UNUSED_PAD src0_sel:WORD_0
	v_exp_f16_sdwa v137, v125 dst_sel:WORD_0 dst_unused:UNUSED_PAD src0_sel:WORD_0
	v_exp_f16_sdwa v138, v126 dst_sel:WORD_0 dst_unused:UNUSED_PAD src0_sel:WORD_0
	v_exp_f16_sdwa v139, v127 dst_sel:WORD_0 dst_unused:UNUSED_PAD src0_sel:WORD_0
	v_exp_f16_sdwa v136, v124 dst_sel:WORD_1 dst_unused:UNUSED_PRESERVE src0_sel:WORD_1
	v_exp_f16_sdwa v137, v125 dst_sel:WORD_1 dst_unused:UNUSED_PRESERVE src0_sel:WORD_1
	v_exp_f16_sdwa v138, v126 dst_sel:WORD_1 dst_unused:UNUSED_PRESERVE src0_sel:WORD_1
	v_exp_f16_sdwa v139, v127 dst_sel:WORD_1 dst_unused:UNUSED_PRESERVE src0_sel:WORD_1
	v_pk_fma_f16 v122, v110, v188, v122
	v_pk_fma_f16 v219, v108, v136, v104
	v_pk_fma_f16 v220, v109, v137, v105
	v_pk_add_f16 v104, v199, 0
	v_pk_add_f16 v105, v200, 0
	v_pk_fma_f16 v221, v110, v138, v106
	v_pk_fma_f16 v222, v111, v139, v107
	v_pk_add_f16 v104, v104, v140
	v_pk_add_f16 v105, v105, v141
	v_pk_add_f16 v106, v201, 0
	v_pk_add_f16 v107, v202, 0
	v_pk_add_f16 v106, v106, v142
	v_pk_add_f16 v107, v107, v143
	v_pk_add_f16 v105, v105, v153
	v_pk_add_f16 v104, v104, v152
	v_pk_add_f16 v107, v107, v155
	v_pk_add_f16 v106, v106, v154
	v_pk_add_f16 v104, v104, v215
	s_mov_b64 exec, s[70:71]
	buffer_load_dwordx4 v[128:131], v231, s[8:11], 0 offen offset:512
	buffer_load_dwordx4 v[96:99], v231, s[8:11], 0 offen offset:1024
	s_mov_b64 exec, -1
	v_pk_add_f16 v105, v105, v216
	v_pk_add_f16 v106, v106, v217
	v_pk_add_f16 v107, v107, v218
	v_pk_add_f16 v105, v105, v174
	v_pk_add_f16 v104, v104, v173
	v_pk_fma_f16 v121, v109, v174, v121
	v_pk_fma_f16 v120, v108, v173, v120
	v_pk_add_f16 v107, v107, v190
	v_pk_add_f16 v106, v106, v188
	v_pk_add_f16 v108, v178, v186 neg_lo:[0,1] neg_hi:[0,1]
	v_pk_add_f16 v109, v177, v196 neg_lo:[0,1] neg_hi:[0,1]
	v_pk_add_f16 v110, v175, v197 neg_lo:[0,1] neg_hi:[0,1]
	v_pk_add_f16 v111, v176, v198 neg_lo:[0,1] neg_hi:[0,1]
	v_pk_add_f16 v132, v132, v189
	v_exp_f16_sdwa v124, v108 dst_sel:WORD_0 dst_unused:UNUSED_PAD src0_sel:WORD_0
	v_exp_f16_sdwa v125, v109 dst_sel:WORD_0 dst_unused:UNUSED_PAD src0_sel:WORD_0
	v_exp_f16_sdwa v126, v110 dst_sel:WORD_0 dst_unused:UNUSED_PAD src0_sel:WORD_0
	v_exp_f16_sdwa v127, v111 dst_sel:WORD_0 dst_unused:UNUSED_PAD src0_sel:WORD_0
	v_exp_f16_sdwa v124, v108 dst_sel:WORD_1 dst_unused:UNUSED_PRESERVE src0_sel:WORD_1
	v_exp_f16_sdwa v125, v109 dst_sel:WORD_1 dst_unused:UNUSED_PRESERVE src0_sel:WORD_1
	v_exp_f16_sdwa v126, v110 dst_sel:WORD_1 dst_unused:UNUSED_PRESERVE src0_sel:WORD_1
	v_exp_f16_sdwa v127, v111 dst_sel:WORD_1 dst_unused:UNUSED_PRESERVE src0_sel:WORD_1
	v_pk_add_f16 v133, v133, v187
	v_pk_add_f16 v104, v104, v124
	v_pk_add_f16 v105, v105, v125
	v_pk_fma_f16 v108, v88, v124, v120
	v_pk_fma_f16 v109, v89, v125, v121
	v_pk_add_f16 v106, v106, v126
	v_pk_fma_f16 v110, v90, v126, v122
	v_pk_add_f16 v107, v107, v127
	v_pk_fma_f16 v111, v91, v127, v123
	v_pk_add_f16 v120, v185, v186 neg_lo:[0,1] neg_hi:[0,1]
	s_mov_b64 exec, s[78:79]
	buffer_load_dwordx4 v[20:23], v231, s[8:11], 0 offen offset:2048
	buffer_load_dwordx4 v[16:19], v231, s[8:11], 0 offen offset:2560
	s_mov_b64 exec, -1
	v_pk_add_f16 v121, v184, v196 neg_lo:[0,1] neg_hi:[0,1]
	v_pk_add_f16 v122, v179, v197 neg_lo:[0,1] neg_hi:[0,1]
	v_pk_add_f16 v123, v191, v198 neg_lo:[0,1] neg_hi:[0,1]
	v_pk_add_f16 v134, v134, v172
	v_exp_f16_sdwa v124, v120 dst_sel:WORD_0 dst_unused:UNUSED_PAD src0_sel:WORD_0
	v_exp_f16_sdwa v125, v121 dst_sel:WORD_0 dst_unused:UNUSED_PAD src0_sel:WORD_0
	v_exp_f16_sdwa v126, v122 dst_sel:WORD_0 dst_unused:UNUSED_PAD src0_sel:WORD_0
	v_exp_f16_sdwa v127, v123 dst_sel:WORD_0 dst_unused:UNUSED_PAD src0_sel:WORD_0
	v_exp_f16_sdwa v124, v120 dst_sel:WORD_1 dst_unused:UNUSED_PRESERVE src0_sel:WORD_1
	v_exp_f16_sdwa v125, v121 dst_sel:WORD_1 dst_unused:UNUSED_PRESERVE src0_sel:WORD_1
	v_exp_f16_sdwa v126, v122 dst_sel:WORD_1 dst_unused:UNUSED_PRESERVE src0_sel:WORD_1
	v_exp_f16_sdwa v127, v123 dst_sel:WORD_1 dst_unused:UNUSED_PRESERVE src0_sel:WORD_1
	v_pk_add_f16 v120, v195, v186 neg_lo:[0,1] neg_hi:[0,1]
	v_pk_add_f16 v105, v105, v125
	v_pk_add_f16 v104, v104, v124
	v_pk_add_f16 v107, v107, v127
	v_pk_fma_f16 v111, v43, v127, v111
	v_pk_add_f16 v106, v106, v126
	v_pk_fma_f16 v110, v42, v126, v110
	v_pk_fma_f16 v109, v41, v125, v109
	v_pk_fma_f16 v108, v40, v124, v108
	v_pk_add_f16 v121, v194, v196 neg_lo:[0,1] neg_hi:[0,1]
	v_pk_add_f16 v122, v193, v197 neg_lo:[0,1] neg_hi:[0,1]
	v_pk_add_f16 v123, v192, v198 neg_lo:[0,1] neg_hi:[0,1]
	v_pk_add_f16 v135, v135, v167
	v_exp_f16_sdwa v124, v120 dst_sel:WORD_0 dst_unused:UNUSED_PAD src0_sel:WORD_0
	v_exp_f16_sdwa v125, v121 dst_sel:WORD_0 dst_unused:UNUSED_PAD src0_sel:WORD_0
	v_exp_f16_sdwa v126, v122 dst_sel:WORD_0 dst_unused:UNUSED_PAD src0_sel:WORD_0
	v_exp_f16_sdwa v127, v123 dst_sel:WORD_0 dst_unused:UNUSED_PAD src0_sel:WORD_0
	v_exp_f16_sdwa v124, v120 dst_sel:WORD_1 dst_unused:UNUSED_PRESERVE src0_sel:WORD_1
	v_exp_f16_sdwa v125, v121 dst_sel:WORD_1 dst_unused:UNUSED_PRESERVE src0_sel:WORD_1
	v_exp_f16_sdwa v126, v122 dst_sel:WORD_1 dst_unused:UNUSED_PRESERVE src0_sel:WORD_1
	v_exp_f16_sdwa v127, v123 dst_sel:WORD_1 dst_unused:UNUSED_PRESERVE src0_sel:WORD_1
	v_pk_add_f16 v120, v168, v186 neg_lo:[0,1] neg_hi:[0,1]
	v_pk_add_f16 v104, v104, v124
	v_pk_add_f16 v105, v105, v125
	v_pk_fma_f16 v108, v48, v124, v108
	v_pk_fma_f16 v109, v49, v125, v109
	v_pk_add_f16 v106, v106, v126
	v_pk_fma_f16 v110, v50, v126, v110
	v_pk_add_f16 v107, v107, v127
	v_pk_fma_f16 v111, v51, v127, v111
	v_pk_add_f16 v121, v169, v196 neg_lo:[0,1] neg_hi:[0,1]
	v_pk_add_f16 v122, v170, v197 neg_lo:[0,1] neg_hi:[0,1]
	v_pk_add_f16 v123, v171, v198 neg_lo:[0,1] neg_hi:[0,1]
	v_exp_f16_sdwa v124, v120 dst_sel:WORD_0 dst_unused:UNUSED_PAD src0_sel:WORD_0
	v_exp_f16_sdwa v125, v121 dst_sel:WORD_0 dst_unused:UNUSED_PAD src0_sel:WORD_0
	v_exp_f16_sdwa v126, v122 dst_sel:WORD_0 dst_unused:UNUSED_PAD src0_sel:WORD_0
	v_exp_f16_sdwa v127, v123 dst_sel:WORD_0 dst_unused:UNUSED_PAD src0_sel:WORD_0
	v_exp_f16_sdwa v124, v120 dst_sel:WORD_1 dst_unused:UNUSED_PRESERVE src0_sel:WORD_1
	v_exp_f16_sdwa v125, v121 dst_sel:WORD_1 dst_unused:UNUSED_PRESERVE src0_sel:WORD_1
	v_exp_f16_sdwa v126, v122 dst_sel:WORD_1 dst_unused:UNUSED_PRESERVE src0_sel:WORD_1
	v_exp_f16_sdwa v127, v123 dst_sel:WORD_1 dst_unused:UNUSED_PRESERVE src0_sel:WORD_1
	v_pk_add_f16 v123, v213, 0
	v_pk_add_f16 v105, v105, v125
	v_pk_add_f16 v104, v104, v124
	v_rcp_f16_e32 v121, v105
	v_rcp_f16_e32 v120, v104
	v_rcp_f16_sdwa v104, v104 dst_sel:DWORD dst_unused:UNUSED_PAD src0_sel:WORD_1
	v_rcp_f16_sdwa v105, v105 dst_sel:DWORD dst_unused:UNUSED_PAD src0_sel:WORD_1
	v_pk_add_f16 v107, v107, v127
	v_pk_add_f16 v106, v106, v126
	v_pk_fma_f16 v109, v61, v125, v109
	v_pk_fma_f16 v108, v60, v124, v108
	v_pack_b32_f16 v104, v120, v104
	v_pack_b32_f16 v105, v121, v105
	v_pk_mul_f16 v124, v108, v104
	v_rcp_f16_e32 v108, v106
	v_rcp_f16_sdwa v106, v106 dst_sel:DWORD dst_unused:UNUSED_PAD src0_sel:WORD_1
	v_pk_mul_f16 v125, v109, v105
	v_rcp_f16_e32 v105, v107
	v_rcp_f16_sdwa v107, v107 dst_sel:DWORD dst_unused:UNUSED_PAD src0_sel:WORD_1
	v_pk_fma_f16 v111, v63, v127, v111
	v_pk_fma_f16 v110, v62, v126, v110
	v_pack_b32_f16 v106, v108, v106
	v_pack_b32_f16 v105, v105, v107
	v_add_u32_e32 v104, 0x30000, v183
	v_pk_mul_f16 v126, v110, v106
	v_pk_mul_f16 v127, v111, v105
	v_pk_add_f16 v105, v212, 0
	v_pk_add_f16 v106, v203, 0
	v_add_u32_e32 v120, 0x48000, v183
	v_pk_add_f16 v121, v106, v136
	v_pk_add_f16 v122, v105, v137
	buffer_load_dwordx4 v[108:111], v104, s[8:11], 0 offen
	s_nop 0
	buffer_load_dwordx4 v[104:107], v120, s[8:11], 0 offen
	v_pk_add_f16 v120, v214, 0
	v_pk_add_f16 v123, v123, v138
	v_pk_add_f16 v120, v120, v139
	v_exp_f16_sdwa v136, v132 dst_sel:WORD_0 dst_unused:UNUSED_PAD src0_sel:WORD_0
	v_exp_f16_sdwa v137, v133 dst_sel:WORD_0 dst_unused:UNUSED_PAD src0_sel:WORD_0
	v_exp_f16_sdwa v138, v134 dst_sel:WORD_0 dst_unused:UNUSED_PAD src0_sel:WORD_0
	v_exp_f16_sdwa v139, v135 dst_sel:WORD_0 dst_unused:UNUSED_PAD src0_sel:WORD_0
	v_exp_f16_sdwa v136, v132 dst_sel:WORD_1 dst_unused:UNUSED_PRESERVE src0_sel:WORD_1
	v_exp_f16_sdwa v137, v133 dst_sel:WORD_1 dst_unused:UNUSED_PRESERVE src0_sel:WORD_1
	v_exp_f16_sdwa v138, v134 dst_sel:WORD_1 dst_unused:UNUSED_PRESERVE src0_sel:WORD_1
	v_exp_f16_sdwa v139, v135 dst_sel:WORD_1 dst_unused:UNUSED_PRESERVE src0_sel:WORD_1
	v_pk_add_f16 v132, v158, v189
	v_pk_add_f16 v121, v121, v136
	v_pk_add_f16 v120, v120, v139
	v_pk_add_f16 v123, v123, v138
	v_pk_add_f16 v122, v122, v137
	v_pk_fma_f16 v91, v91, v139, v222
	v_pk_fma_f16 v90, v90, v138, v221
	v_pk_fma_f16 v89, v89, v137, v220
	v_pk_fma_f16 v88, v88, v136, v219
	v_pk_add_f16 v133, v151, v187
	v_pk_add_f16 v134, v148, v172
	v_pk_add_f16 v135, v145, v167
	v_exp_f16_sdwa v136, v132 dst_sel:WORD_0 dst_unused:UNUSED_PAD src0_sel:WORD_0
	v_exp_f16_sdwa v137, v133 dst_sel:WORD_0 dst_unused:UNUSED_PAD src0_sel:WORD_0
	v_exp_f16_sdwa v138, v134 dst_sel:WORD_0 dst_unused:UNUSED_PAD src0_sel:WORD_0
	v_exp_f16_sdwa v139, v135 dst_sel:WORD_0 dst_unused:UNUSED_PAD src0_sel:WORD_0
	v_exp_f16_sdwa v136, v132 dst_sel:WORD_1 dst_unused:UNUSED_PRESERVE src0_sel:WORD_1
	v_exp_f16_sdwa v137, v133 dst_sel:WORD_1 dst_unused:UNUSED_PRESERVE src0_sel:WORD_1
	v_exp_f16_sdwa v138, v134 dst_sel:WORD_1 dst_unused:UNUSED_PRESERVE src0_sel:WORD_1
	v_exp_f16_sdwa v139, v135 dst_sel:WORD_1 dst_unused:UNUSED_PRESERVE src0_sel:WORD_1
	v_pk_add_f16 v132, v159, v189
	v_pk_add_f16 v121, v121, v136
	v_pk_add_f16 v122, v122, v137
	v_pk_add_f16 v123, v123, v138
	v_pk_add_f16 v120, v120, v139
	v_pk_fma_f16 v88, v40, v136, v88
	v_pk_fma_f16 v89, v41, v137, v89
	v_pk_fma_f16 v90, v42, v138, v90
	v_pk_fma_f16 v91, v43, v139, v91
	v_pk_add_f16 v133, v156, v187
	v_pk_add_f16 v134, v149, v172
	v_pk_add_f16 v135, v146, v167
	v_exp_f16_sdwa v136, v132 dst_sel:WORD_0 dst_unused:UNUSED_PAD src0_sel:WORD_0
	v_exp_f16_sdwa v137, v133 dst_sel:WORD_0 dst_unused:UNUSED_PAD src0_sel:WORD_0
	v_exp_f16_sdwa v138, v134 dst_sel:WORD_0 dst_unused:UNUSED_PAD src0_sel:WORD_0
	v_exp_f16_sdwa v139, v135 dst_sel:WORD_0 dst_unused:UNUSED_PAD src0_sel:WORD_0
	v_exp_f16_sdwa v136, v132 dst_sel:WORD_1 dst_unused:UNUSED_PRESERVE src0_sel:WORD_1
	v_exp_f16_sdwa v137, v133 dst_sel:WORD_1 dst_unused:UNUSED_PRESERVE src0_sel:WORD_1
	v_exp_f16_sdwa v138, v134 dst_sel:WORD_1 dst_unused:UNUSED_PRESERVE src0_sel:WORD_1
	v_exp_f16_sdwa v139, v135 dst_sel:WORD_1 dst_unused:UNUSED_PRESERVE src0_sel:WORD_1
	v_pk_add_f16 v132, v157, v189
	v_pk_add_f16 v121, v121, v136
	v_pk_add_f16 v120, v120, v139
	v_pk_add_f16 v123, v123, v138
	v_pk_add_f16 v122, v122, v137
	v_pk_fma_f16 v91, v51, v139, v91
	v_pk_fma_f16 v90, v50, v138, v90
	v_pk_fma_f16 v89, v49, v137, v89
	v_pk_fma_f16 v88, v48, v136, v88
	v_pk_add_f16 v133, v150, v187
	v_pk_add_f16 v134, v147, v172
	v_pk_add_f16 v135, v144, v167
	v_exp_f16_sdwa v136, v132 dst_sel:WORD_0 dst_unused:UNUSED_PAD src0_sel:WORD_0
	v_exp_f16_sdwa v137, v133 dst_sel:WORD_0 dst_unused:UNUSED_PAD src0_sel:WORD_0
	v_exp_f16_sdwa v138, v134 dst_sel:WORD_0 dst_unused:UNUSED_PAD src0_sel:WORD_0
	v_exp_f16_sdwa v139, v135 dst_sel:WORD_0 dst_unused:UNUSED_PAD src0_sel:WORD_0
	v_exp_f16_sdwa v136, v132 dst_sel:WORD_1 dst_unused:UNUSED_PRESERVE src0_sel:WORD_1
	v_exp_f16_sdwa v137, v133 dst_sel:WORD_1 dst_unused:UNUSED_PRESERVE src0_sel:WORD_1
	v_exp_f16_sdwa v138, v134 dst_sel:WORD_1 dst_unused:UNUSED_PRESERVE src0_sel:WORD_1
	v_exp_f16_sdwa v139, v135 dst_sel:WORD_1 dst_unused:UNUSED_PRESERVE src0_sel:WORD_1
	v_pk_add_f16 v132, v210, v189
	v_pk_add_f16 v121, v121, v136
	v_pk_add_f16 v122, v122, v137
	v_pk_add_f16 v123, v123, v138
	v_pk_add_f16 v120, v120, v139
	v_pk_fma_f16 v88, v60, v136, v88
	v_pk_fma_f16 v89, v61, v137, v89
	v_pk_fma_f16 v90, v62, v138, v90
	v_pk_fma_f16 v91, v63, v139, v91
	v_pk_add_f16 v133, v208, v187
	v_pk_add_f16 v134, v206, v172
	v_pk_add_f16 v135, v204, v167
	v_exp_f16_sdwa v136, v132 dst_sel:WORD_0 dst_unused:UNUSED_PAD src0_sel:WORD_0
	v_exp_f16_sdwa v137, v133 dst_sel:WORD_0 dst_unused:UNUSED_PAD src0_sel:WORD_0
	v_exp_f16_sdwa v138, v134 dst_sel:WORD_0 dst_unused:UNUSED_PAD src0_sel:WORD_0
	v_exp_f16_sdwa v139, v135 dst_sel:WORD_0 dst_unused:UNUSED_PAD src0_sel:WORD_0
	v_exp_f16_sdwa v136, v132 dst_sel:WORD_1 dst_unused:UNUSED_PRESERVE src0_sel:WORD_1
	v_exp_f16_sdwa v137, v133 dst_sel:WORD_1 dst_unused:UNUSED_PRESERVE src0_sel:WORD_1
	v_exp_f16_sdwa v138, v134 dst_sel:WORD_1 dst_unused:UNUSED_PRESERVE src0_sel:WORD_1
	v_exp_f16_sdwa v139, v135 dst_sel:WORD_1 dst_unused:UNUSED_PRESERVE src0_sel:WORD_1
	v_pk_add_f16 v132, v211, v189
	v_pk_add_f16 v121, v121, v136
	v_pk_add_f16 v120, v120, v139
	v_pk_add_f16 v123, v123, v138
	v_pk_add_f16 v122, v122, v137
	v_pk_fma_f16 v91, v27, v139, v91
	v_pk_fma_f16 v90, v26, v138, v90
	v_pk_fma_f16 v89, v25, v137, v89
	v_pk_fma_f16 v88, v24, v136, v88
	v_pk_add_f16 v133, v209, v187
	v_pk_add_f16 v134, v207, v172
	v_pk_add_f16 v135, v205, v167
	v_exp_f16_sdwa v136, v132 dst_sel:WORD_0 dst_unused:UNUSED_PAD src0_sel:WORD_0
	v_exp_f16_sdwa v137, v133 dst_sel:WORD_0 dst_unused:UNUSED_PAD src0_sel:WORD_0
	v_exp_f16_sdwa v138, v134 dst_sel:WORD_0 dst_unused:UNUSED_PAD src0_sel:WORD_0
	v_exp_f16_sdwa v139, v135 dst_sel:WORD_0 dst_unused:UNUSED_PAD src0_sel:WORD_0
	v_exp_f16_sdwa v136, v132 dst_sel:WORD_1 dst_unused:UNUSED_PRESERVE src0_sel:WORD_1
	v_exp_f16_sdwa v137, v133 dst_sel:WORD_1 dst_unused:UNUSED_PRESERVE src0_sel:WORD_1
	v_exp_f16_sdwa v138, v134 dst_sel:WORD_1 dst_unused:UNUSED_PRESERVE src0_sel:WORD_1
	v_exp_f16_sdwa v139, v135 dst_sel:WORD_1 dst_unused:UNUSED_PRESERVE src0_sel:WORD_1
	v_pk_add_f16 v132, v160, v189
	v_pk_add_f16 v121, v121, v136
	v_pk_add_f16 v122, v122, v137
	v_pk_add_f16 v123, v123, v138
	v_pk_add_f16 v120, v120, v139
	v_pk_fma_f16 v88, v28, v136, v88
	v_pk_fma_f16 v89, v29, v137, v89
	v_pk_fma_f16 v90, v30, v138, v90
	v_pk_fma_f16 v91, v31, v139, v91
	v_pk_add_f16 v133, v161, v187
	v_pk_add_f16 v134, v162, v172
	v_pk_add_f16 v135, v163, v167
	v_exp_f16_sdwa v136, v132 dst_sel:WORD_0 dst_unused:UNUSED_PAD src0_sel:WORD_0
	v_exp_f16_sdwa v137, v133 dst_sel:WORD_0 dst_unused:UNUSED_PAD src0_sel:WORD_0
	v_exp_f16_sdwa v138, v134 dst_sel:WORD_0 dst_unused:UNUSED_PAD src0_sel:WORD_0
	v_exp_f16_sdwa v139, v135 dst_sel:WORD_0 dst_unused:UNUSED_PAD src0_sel:WORD_0
	v_exp_f16_sdwa v136, v132 dst_sel:WORD_1 dst_unused:UNUSED_PRESERVE src0_sel:WORD_1
	v_exp_f16_sdwa v137, v133 dst_sel:WORD_1 dst_unused:UNUSED_PRESERVE src0_sel:WORD_1
	v_exp_f16_sdwa v138, v134 dst_sel:WORD_1 dst_unused:UNUSED_PRESERVE src0_sel:WORD_1
	v_exp_f16_sdwa v139, v135 dst_sel:WORD_1 dst_unused:UNUSED_PRESERVE src0_sel:WORD_1
	v_pk_add_f16 v121, v121, v136
	v_pk_add_f16 v120, v120, v139
	v_pk_add_f16 v122, v122, v137
	v_rcp_f16_e32 v132, v121
	v_rcp_f16_sdwa v121, v121 dst_sel:DWORD dst_unused:UNUSED_PAD src0_sel:WORD_1
	v_pk_add_f16 v123, v123, v138
	v_rcp_f16_e32 v133, v122
	v_rcp_f16_sdwa v122, v122 dst_sel:DWORD dst_unused:UNUSED_PAD src0_sel:WORD_1
	v_rcp_f16_e32 v135, v120
	v_rcp_f16_sdwa v120, v120 dst_sel:DWORD dst_unused:UNUSED_PAD src0_sel:WORD_1
	v_rcp_f16_e32 v134, v123
	v_rcp_f16_sdwa v123, v123 dst_sel:DWORD dst_unused:UNUSED_PAD src0_sel:WORD_1
	v_pk_fma_f16 v88, v32, v136, v88
	v_pack_b32_f16 v121, v132, v121
	v_pk_fma_f16 v91, v35, v139, v91
	v_pk_fma_f16 v89, v33, v137, v89
	v_pk_mul_f16 v88, v88, v121
	v_pack_b32_f16 v121, v133, v122
	v_pack_b32_f16 v120, v135, v120
	v_pk_fma_f16 v90, v34, v138, v90
	v_pk_mul_f16 v89, v89, v121
	v_pack_b32_f16 v121, v134, v123
	v_pk_mul_f16 v91, v91, v120
	s_waitcnt vmcnt(1)
	v_pk_mul_f16 v120, v164, v108 op_sel_hi:[0,1]
	v_pk_mul_f16 v123, v164, v111 op_sel_hi:[0,1]
	v_pk_mul_f16 v132, v165, v108 op_sel_hi:[0,1]
	v_pk_mul_f16 v135, v165, v111 op_sel_hi:[0,1]
	v_pk_mul_f16 v136, v166, v108 op_sel_hi:[0,1]
	v_pk_mul_f16 v139, v166, v111 op_sel_hi:[0,1]
	v_pk_mul_f16 v90, v90, v121
	v_pk_mul_f16 v121, v164, v109 op_sel_hi:[0,1]
	v_pk_mul_f16 v122, v164, v110 op_sel_hi:[0,1]
	v_pk_mul_f16 v133, v165, v109 op_sel_hi:[0,1]
	v_pk_mul_f16 v134, v165, v110 op_sel_hi:[0,1]
	v_pk_mul_f16 v137, v166, v109 op_sel_hi:[0,1]
	v_pk_mul_f16 v138, v166, v110 op_sel_hi:[0,1]
	v_pk_fma_f16 v67, v67, v111, v123
	v_pk_fma_f16 v64, v64, v108, v120
	v_pk_fma_f16 v79, v79, v111, v123
	v_pk_fma_f16 v76, v76, v108, v120
	v_pk_fma_f16 v95, v95, v111, v123
	v_pk_fma_f16 v92, v92, v108, v120
	v_pk_fma_f16 v120, v39, v111, v135
	v_pk_fma_f16 v123, v36, v108, v132
	v_pk_fma_f16 v140, v55, v111, v135
	v_pk_fma_f16 v143, v52, v108, v132
	v_pk_fma_f16 v135, v71, v111, v135
	v_pk_fma_f16 v132, v68, v108, v132
	v_pk_fma_f16 v144, v83, v111, v139
	v_pk_fma_f16 v147, v80, v108, v136
	v_pk_fma_f16 v148, v103, v111, v139
	v_pk_fma_f16 v151, v100, v108, v136
	v_pk_fma_f16 v111, v115, v111, v139
	v_pk_fma_f16 v108, v112, v108, v136
	v_pk_maximum3_f16 v136, v64, v76, v92
	v_pk_maximum3_f16 v139, v67, v79, v95
	v_pk_fma_f16 v66, v66, v110, v122
	v_pk_fma_f16 v65, v65, v109, v121
	v_pk_fma_f16 v78, v78, v110, v122
	v_pk_fma_f16 v77, v77, v109, v121
	v_pk_fma_f16 v94, v94, v110, v122
	v_pk_fma_f16 v93, v93, v109, v121
	v_pk_fma_f16 v121, v38, v110, v134
	v_pk_fma_f16 v122, v37, v109, v133
	v_pk_fma_f16 v141, v54, v110, v134
	v_pk_fma_f16 v142, v53, v109, v133
	v_pk_fma_f16 v134, v70, v110, v134
	v_pk_fma_f16 v133, v69, v109, v133
	v_pk_fma_f16 v145, v82, v110, v138
	v_pk_fma_f16 v146, v81, v109, v137
	v_pk_fma_f16 v149, v102, v110, v138
	v_pk_fma_f16 v150, v101, v109, v137
	v_pk_fma_f16 v110, v114, v110, v138
	v_pk_fma_f16 v109, v113, v109, v137
	v_pk_maximum3_f16 v137, v65, v77, v93
	v_pk_maximum3_f16 v138, v66, v78, v94
	v_pk_maximum3_f16 v152, v123, v143, v132
	v_pk_maximum3_f16 v155, v120, v140, v135
	v_pk_maximum3_f16 v156, v147, v151, v108
	v_pk_maximum3_f16 v159, v144, v148, v111
	v_pk_maximum3_f16 v153, v122, v142, v133
	v_pk_maximum3_f16 v154, v121, v141, v134
	v_pk_maximum3_f16 v157, v146, v150, v109
	v_pk_maximum3_f16 v158, v145, v149, v110
	v_pk_maximum3_f16 v136, v136, v152, v156
	v_pk_maximum3_f16 v139, v139, v155, v159
	v_pk_maximum3_f16 v137, v137, v153, v157
	v_pk_maximum3_f16 v138, v138, v154, v158
	v_pk_add_f16 v64, v64, v136 neg_lo:[0,1] neg_hi:[0,1]
	v_pk_add_f16 v67, v67, v139 neg_lo:[0,1] neg_hi:[0,1]
	v_pk_add_f16 v65, v65, v137 neg_lo:[0,1] neg_hi:[0,1]
	v_pk_add_f16 v66, v66, v138 neg_lo:[0,1] neg_hi:[0,1]
	v_pk_add_f16 v76, v76, v136 neg_lo:[0,1] neg_hi:[0,1]
	v_exp_f16_sdwa v152, v64 dst_sel:WORD_0 dst_unused:UNUSED_PAD src0_sel:WORD_0
	v_exp_f16_sdwa v153, v65 dst_sel:WORD_0 dst_unused:UNUSED_PAD src0_sel:WORD_0
	v_exp_f16_sdwa v154, v66 dst_sel:WORD_0 dst_unused:UNUSED_PAD src0_sel:WORD_0
	v_exp_f16_sdwa v155, v67 dst_sel:WORD_0 dst_unused:UNUSED_PAD src0_sel:WORD_0
	v_exp_f16_sdwa v152, v64 dst_sel:WORD_1 dst_unused:UNUSED_PRESERVE src0_sel:WORD_1
	v_exp_f16_sdwa v153, v65 dst_sel:WORD_1 dst_unused:UNUSED_PRESERVE src0_sel:WORD_1
	v_exp_f16_sdwa v154, v66 dst_sel:WORD_1 dst_unused:UNUSED_PRESERVE src0_sel:WORD_1
	v_exp_f16_sdwa v155, v67 dst_sel:WORD_1 dst_unused:UNUSED_PRESERVE src0_sel:WORD_1
	v_pk_add_f16 v77, v77, v137 neg_lo:[0,1] neg_hi:[0,1]
	v_pk_add_f16 v64, v155, 0
	v_pk_add_f16 v67, v152, 0
	v_pk_fma_f16 v40, v40, v152, 0
	v_pk_fma_f16 v43, v43, v155, 0
	v_pk_add_f16 v65, v154, 0
	v_pk_add_f16 v66, v153, 0
	v_pk_fma_f16 v41, v41, v153, 0
	v_pk_fma_f16 v42, v42, v154, 0
	v_pk_add_f16 v78, v78, v138 neg_lo:[0,1] neg_hi:[0,1]
	v_pk_add_f16 v79, v79, v139 neg_lo:[0,1] neg_hi:[0,1]
	v_exp_f16_sdwa v152, v76 dst_sel:WORD_0 dst_unused:UNUSED_PAD src0_sel:WORD_0
	v_exp_f16_sdwa v153, v77 dst_sel:WORD_0 dst_unused:UNUSED_PAD src0_sel:WORD_0
	v_exp_f16_sdwa v154, v78 dst_sel:WORD_0 dst_unused:UNUSED_PAD src0_sel:WORD_0
	v_exp_f16_sdwa v155, v79 dst_sel:WORD_0 dst_unused:UNUSED_PAD src0_sel:WORD_0
	v_exp_f16_sdwa v152, v76 dst_sel:WORD_1 dst_unused:UNUSED_PRESERVE src0_sel:WORD_1
	v_exp_f16_sdwa v153, v77 dst_sel:WORD_1 dst_unused:UNUSED_PRESERVE src0_sel:WORD_1
	v_exp_f16_sdwa v154, v78 dst_sel:WORD_1 dst_unused:UNUSED_PRESERVE src0_sel:WORD_1
	v_exp_f16_sdwa v155, v79 dst_sel:WORD_1 dst_unused:UNUSED_PRESERVE src0_sel:WORD_1
	v_pk_add_f16 v67, v67, v152
	v_pk_add_f16 v64, v64, v155
	v_pk_fma_f16 v43, v51, v155, v43
	v_pk_fma_f16 v40, v48, v152, v40
	v_pk_add_f16 v48, v92, v136 neg_lo:[0,1] neg_hi:[0,1]
	v_pk_add_f16 v51, v95, v139 neg_lo:[0,1] neg_hi:[0,1]
	v_pk_add_f16 v66, v66, v153
	v_pk_add_f16 v65, v65, v154
	v_pk_fma_f16 v42, v50, v154, v42
	v_pk_fma_f16 v41, v49, v153, v41
	v_pk_add_f16 v49, v93, v137 neg_lo:[0,1] neg_hi:[0,1]
	v_pk_add_f16 v50, v94, v138 neg_lo:[0,1] neg_hi:[0,1]
	v_exp_f16_sdwa v76, v48 dst_sel:WORD_0 dst_unused:UNUSED_PAD src0_sel:WORD_0
	v_exp_f16_sdwa v77, v49 dst_sel:WORD_0 dst_unused:UNUSED_PAD src0_sel:WORD_0
	v_exp_f16_sdwa v78, v50 dst_sel:WORD_0 dst_unused:UNUSED_PAD src0_sel:WORD_0
	v_exp_f16_sdwa v79, v51 dst_sel:WORD_0 dst_unused:UNUSED_PAD src0_sel:WORD_0
	v_exp_f16_sdwa v76, v48 dst_sel:WORD_1 dst_unused:UNUSED_PRESERVE src0_sel:WORD_1
	v_exp_f16_sdwa v77, v49 dst_sel:WORD_1 dst_unused:UNUSED_PRESERVE src0_sel:WORD_1
	v_exp_f16_sdwa v78, v50 dst_sel:WORD_1 dst_unused:UNUSED_PRESERVE src0_sel:WORD_1
	v_exp_f16_sdwa v79, v51 dst_sel:WORD_1 dst_unused:UNUSED_PRESERVE src0_sel:WORD_1
	s_nop 0
	v_pk_add_f16 v48, v64, v79
	v_pk_add_f16 v51, v67, v76
	v_pk_add_f16 v49, v65, v78
	v_pk_add_f16 v50, v66, v77
	v_pk_fma_f16 v40, v60, v76, v40
	v_pk_fma_f16 v41, v61, v77, v41
	v_pk_fma_f16 v42, v62, v78, v42
	v_pk_fma_f16 v43, v63, v79, v43
	v_pk_add_f16 v60, v123, v136 neg_lo:[0,1] neg_hi:[0,1]
	v_pk_add_f16 v61, v122, v137 neg_lo:[0,1] neg_hi:[0,1]
	v_pk_add_f16 v62, v121, v138 neg_lo:[0,1] neg_hi:[0,1]
	v_pk_add_f16 v63, v120, v139 neg_lo:[0,1] neg_hi:[0,1]
	v_exp_f16_sdwa v64, v60 dst_sel:WORD_0 dst_unused:UNUSED_PAD src0_sel:WORD_0
	v_exp_f16_sdwa v65, v61 dst_sel:WORD_0 dst_unused:UNUSED_PAD src0_sel:WORD_0
	v_exp_f16_sdwa v66, v62 dst_sel:WORD_0 dst_unused:UNUSED_PAD src0_sel:WORD_0
	v_exp_f16_sdwa v67, v63 dst_sel:WORD_0 dst_unused:UNUSED_PAD src0_sel:WORD_0
	v_exp_f16_sdwa v64, v60 dst_sel:WORD_1 dst_unused:UNUSED_PRESERVE src0_sel:WORD_1
	v_exp_f16_sdwa v65, v61 dst_sel:WORD_1 dst_unused:UNUSED_PRESERVE src0_sel:WORD_1
	v_exp_f16_sdwa v66, v62 dst_sel:WORD_1 dst_unused:UNUSED_PRESERVE src0_sel:WORD_1
	v_exp_f16_sdwa v67, v63 dst_sel:WORD_1 dst_unused:UNUSED_PRESERVE src0_sel:WORD_1
	v_pk_add_f16 v60, v143, v136 neg_lo:[0,1] neg_hi:[0,1]
	v_pk_add_f16 v51, v51, v64
	v_pk_add_f16 v48, v48, v67
	v_pk_add_f16 v50, v50, v65
	v_pk_add_f16 v49, v49, v66
	v_pk_fma_f16 v43, v27, v67, v43
	v_pk_fma_f16 v42, v26, v66, v42
	v_pk_fma_f16 v41, v25, v65, v41
	v_pk_fma_f16 v40, v24, v64, v40
	v_pk_add_f16 v61, v142, v137 neg_lo:[0,1] neg_hi:[0,1]
	v_pk_add_f16 v62, v141, v138 neg_lo:[0,1] neg_hi:[0,1]
	v_pk_add_f16 v63, v140, v139 neg_lo:[0,1] neg_hi:[0,1]
	v_exp_f16_sdwa v64, v60 dst_sel:WORD_0 dst_unused:UNUSED_PAD src0_sel:WORD_0
	v_exp_f16_sdwa v65, v61 dst_sel:WORD_0 dst_unused:UNUSED_PAD src0_sel:WORD_0
	v_exp_f16_sdwa v66, v62 dst_sel:WORD_0 dst_unused:UNUSED_PAD src0_sel:WORD_0
	v_exp_f16_sdwa v67, v63 dst_sel:WORD_0 dst_unused:UNUSED_PAD src0_sel:WORD_0
	v_exp_f16_sdwa v64, v60 dst_sel:WORD_1 dst_unused:UNUSED_PRESERVE src0_sel:WORD_1
	v_exp_f16_sdwa v65, v61 dst_sel:WORD_1 dst_unused:UNUSED_PRESERVE src0_sel:WORD_1
	v_exp_f16_sdwa v66, v62 dst_sel:WORD_1 dst_unused:UNUSED_PRESERVE src0_sel:WORD_1
	v_exp_f16_sdwa v67, v63 dst_sel:WORD_1 dst_unused:UNUSED_PRESERVE src0_sel:WORD_1
	v_pk_add_f16 v60, v132, v136 neg_lo:[0,1] neg_hi:[0,1]
	v_pk_add_f16 v48, v48, v67
	v_pk_add_f16 v51, v51, v64
	v_pk_add_f16 v49, v49, v66
	v_pk_add_f16 v50, v50, v65
	v_pk_fma_f16 v40, v28, v64, v40
	v_pk_fma_f16 v41, v29, v65, v41
	v_pk_fma_f16 v42, v30, v66, v42
	v_pk_fma_f16 v43, v31, v67, v43
	v_pk_add_f16 v61, v133, v137 neg_lo:[0,1] neg_hi:[0,1]
	v_pk_add_f16 v62, v134, v138 neg_lo:[0,1] neg_hi:[0,1]
	v_pk_add_f16 v63, v135, v139 neg_lo:[0,1] neg_hi:[0,1]
	v_exp_f16_sdwa v64, v60 dst_sel:WORD_0 dst_unused:UNUSED_PAD src0_sel:WORD_0
	v_exp_f16_sdwa v65, v61 dst_sel:WORD_0 dst_unused:UNUSED_PAD src0_sel:WORD_0
	v_exp_f16_sdwa v66, v62 dst_sel:WORD_0 dst_unused:UNUSED_PAD src0_sel:WORD_0
	v_exp_f16_sdwa v67, v63 dst_sel:WORD_0 dst_unused:UNUSED_PAD src0_sel:WORD_0
	v_exp_f16_sdwa v64, v60 dst_sel:WORD_1 dst_unused:UNUSED_PRESERVE src0_sel:WORD_1
	v_exp_f16_sdwa v65, v61 dst_sel:WORD_1 dst_unused:UNUSED_PRESERVE src0_sel:WORD_1
	v_exp_f16_sdwa v66, v62 dst_sel:WORD_1 dst_unused:UNUSED_PRESERVE src0_sel:WORD_1
	v_exp_f16_sdwa v67, v63 dst_sel:WORD_1 dst_unused:UNUSED_PRESERVE src0_sel:WORD_1
	v_pk_add_f16 v60, v147, v136 neg_lo:[0,1] neg_hi:[0,1]
	v_pk_add_f16 v51, v51, v64
	v_pk_add_f16 v48, v48, v67
	v_pk_add_f16 v50, v50, v65
	v_pk_add_f16 v49, v49, v66
	v_pk_fma_f16 v43, v35, v67, v43
	v_pk_fma_f16 v42, v34, v66, v42
	v_pk_fma_f16 v41, v33, v65, v41
	v_pk_fma_f16 v40, v32, v64, v40
	v_pk_add_f16 v61, v146, v137 neg_lo:[0,1] neg_hi:[0,1]
	v_pk_add_f16 v62, v145, v138 neg_lo:[0,1] neg_hi:[0,1]
	v_pk_add_f16 v63, v144, v139 neg_lo:[0,1] neg_hi:[0,1]
	v_exp_f16_sdwa v64, v60 dst_sel:WORD_0 dst_unused:UNUSED_PAD src0_sel:WORD_0
	v_exp_f16_sdwa v65, v61 dst_sel:WORD_0 dst_unused:UNUSED_PAD src0_sel:WORD_0
	v_exp_f16_sdwa v66, v62 dst_sel:WORD_0 dst_unused:UNUSED_PAD src0_sel:WORD_0
	v_exp_f16_sdwa v67, v63 dst_sel:WORD_0 dst_unused:UNUSED_PAD src0_sel:WORD_0
	v_exp_f16_sdwa v64, v60 dst_sel:WORD_1 dst_unused:UNUSED_PRESERVE src0_sel:WORD_1
	v_exp_f16_sdwa v65, v61 dst_sel:WORD_1 dst_unused:UNUSED_PRESERVE src0_sel:WORD_1
	v_exp_f16_sdwa v66, v62 dst_sel:WORD_1 dst_unused:UNUSED_PRESERVE src0_sel:WORD_1
	v_exp_f16_sdwa v67, v63 dst_sel:WORD_1 dst_unused:UNUSED_PRESERVE src0_sel:WORD_1
	v_pk_add_f16 v60, v151, v136 neg_lo:[0,1] neg_hi:[0,1]
	v_pk_add_f16 v48, v48, v67
	v_pk_add_f16 v51, v51, v64
	v_pk_add_f16 v49, v49, v66
	v_pk_add_f16 v50, v50, v65
	v_pk_fma_f16 v40, v44, v64, v40
	v_pk_fma_f16 v41, v45, v65, v41
	v_pk_fma_f16 v42, v46, v66, v42
	v_pk_fma_f16 v43, v47, v67, v43
	v_pk_add_f16 v61, v150, v137 neg_lo:[0,1] neg_hi:[0,1]
	v_pk_add_f16 v62, v149, v138 neg_lo:[0,1] neg_hi:[0,1]
	v_pk_add_f16 v63, v148, v139 neg_lo:[0,1] neg_hi:[0,1]
	v_exp_f16_sdwa v64, v60 dst_sel:WORD_0 dst_unused:UNUSED_PAD src0_sel:WORD_0
	v_exp_f16_sdwa v65, v61 dst_sel:WORD_0 dst_unused:UNUSED_PAD src0_sel:WORD_0
	v_exp_f16_sdwa v66, v62 dst_sel:WORD_0 dst_unused:UNUSED_PAD src0_sel:WORD_0
	v_exp_f16_sdwa v67, v63 dst_sel:WORD_0 dst_unused:UNUSED_PAD src0_sel:WORD_0
	v_exp_f16_sdwa v64, v60 dst_sel:WORD_1 dst_unused:UNUSED_PRESERVE src0_sel:WORD_1
	v_exp_f16_sdwa v65, v61 dst_sel:WORD_1 dst_unused:UNUSED_PRESERVE src0_sel:WORD_1
	v_exp_f16_sdwa v66, v62 dst_sel:WORD_1 dst_unused:UNUSED_PRESERVE src0_sel:WORD_1
	v_exp_f16_sdwa v67, v63 dst_sel:WORD_1 dst_unused:UNUSED_PRESERVE src0_sel:WORD_1
	v_pk_add_f16 v60, v108, v136 neg_lo:[0,1] neg_hi:[0,1]
	v_pk_add_f16 v51, v51, v64
	v_pk_add_f16 v48, v48, v67
	v_pk_add_f16 v50, v50, v65
	v_pk_add_f16 v49, v49, v66
	v_pk_fma_f16 v43, v59, v67, v43
	v_pk_fma_f16 v42, v58, v66, v42
	v_pk_fma_f16 v41, v57, v65, v41
	v_pk_fma_f16 v40, v56, v64, v40
	v_pk_add_f16 v61, v109, v137 neg_lo:[0,1] neg_hi:[0,1]
	v_pk_add_f16 v62, v110, v138 neg_lo:[0,1] neg_hi:[0,1]
	v_pk_add_f16 v63, v111, v139 neg_lo:[0,1] neg_hi:[0,1]
	v_exp_f16_sdwa v64, v60 dst_sel:WORD_0 dst_unused:UNUSED_PAD src0_sel:WORD_0
	v_exp_f16_sdwa v65, v61 dst_sel:WORD_0 dst_unused:UNUSED_PAD src0_sel:WORD_0
	v_exp_f16_sdwa v66, v62 dst_sel:WORD_0 dst_unused:UNUSED_PAD src0_sel:WORD_0
	v_exp_f16_sdwa v67, v63 dst_sel:WORD_0 dst_unused:UNUSED_PAD src0_sel:WORD_0
	v_exp_f16_sdwa v64, v60 dst_sel:WORD_1 dst_unused:UNUSED_PRESERVE src0_sel:WORD_1
	v_exp_f16_sdwa v65, v61 dst_sel:WORD_1 dst_unused:UNUSED_PRESERVE src0_sel:WORD_1
	v_exp_f16_sdwa v66, v62 dst_sel:WORD_1 dst_unused:UNUSED_PRESERVE src0_sel:WORD_1
	v_exp_f16_sdwa v67, v63 dst_sel:WORD_1 dst_unused:UNUSED_PRESERVE src0_sel:WORD_1
	s_nop 0
	v_pk_add_f16 v48, v48, v67
	v_pk_add_f16 v51, v51, v64
	v_pk_add_f16 v49, v49, v66
	v_rcp_f16_e32 v60, v51
	v_rcp_f16_sdwa v61, v51 dst_sel:DWORD dst_unused:UNUSED_PAD src0_sel:WORD_1
	v_rcp_f16_e32 v51, v48
	v_rcp_f16_sdwa v48, v48 dst_sel:DWORD dst_unused:UNUSED_PAD src0_sel:WORD_1
	v_pk_add_f16 v50, v50, v65
	v_rcp_f16_e32 v63, v49
	v_rcp_f16_sdwa v49, v49 dst_sel:DWORD dst_unused:UNUSED_PAD src0_sel:WORD_1
	v_pk_fma_f16 v40, v72, v64, v40
	v_rcp_f16_e32 v62, v50
	v_rcp_f16_sdwa v64, v50 dst_sel:DWORD dst_unused:UNUSED_PAD src0_sel:WORD_1
	v_pk_fma_f16 v43, v75, v67, v43
	v_pack_b32_f16 v48, v51, v48
	v_pk_fma_f16 v42, v74, v66, v42
	v_pk_mul_f16 v51, v43, v48
	v_pack_b32_f16 v43, v63, v49
	v_pk_fma_f16 v41, v73, v65, v41
	v_pk_mul_f16 v50, v42, v43
	v_pack_b32_f16 v42, v62, v64
	v_pk_mul_f16 v49, v41, v42
	v_pack_b32_f16 v41, v60, v61
	v_pk_mul_f16 v48, v40, v41
	s_waitcnt vmcnt(0)
	v_pk_mul_f16 v40, v164, v104 op_sel_hi:[0,1]
	v_pk_mul_f16 v41, v164, v105 op_sel_hi:[0,1]
	v_pk_mul_f16 v42, v164, v106 op_sel_hi:[0,1]
	v_pk_mul_f16 v43, v164, v107 op_sel_hi:[0,1]
	v_pk_mul_f16 v60, v165, v104 op_sel_hi:[0,1]
	v_pk_mul_f16 v61, v165, v105 op_sel_hi:[0,1]
	v_pk_mul_f16 v62, v165, v106 op_sel_hi:[0,1]
	v_pk_mul_f16 v63, v165, v107 op_sel_hi:[0,1]
	v_pk_mul_f16 v64, v166, v104 op_sel_hi:[0,1]
	v_pk_mul_f16 v65, v166, v105 op_sel_hi:[0,1]
	v_pk_mul_f16 v66, v166, v106 op_sel_hi:[0,1]
	v_pk_mul_f16 v67, v166, v107 op_sel_hi:[0,1]
	v_pk_fma_f16 v39, v39, v107, v43
	v_pk_fma_f16 v38, v38, v106, v42
	v_pk_fma_f16 v37, v37, v105, v41
	v_pk_fma_f16 v36, v36, v104, v40
	v_pk_fma_f16 v55, v55, v107, v43
	v_pk_fma_f16 v54, v54, v106, v42
	v_pk_fma_f16 v53, v53, v105, v41
	v_pk_fma_f16 v52, v52, v104, v40
	v_pk_fma_f16 v43, v71, v107, v43
	v_pk_fma_f16 v42, v70, v106, v42
	v_pk_fma_f16 v41, v69, v105, v41
	v_pk_fma_f16 v40, v68, v104, v40
	v_pk_fma_f16 v68, v83, v107, v63
	v_pk_fma_f16 v69, v82, v106, v62
	v_pk_fma_f16 v70, v81, v105, v61
	v_pk_fma_f16 v71, v80, v104, v60
	v_pk_fma_f16 v80, v119, v107, v67
	v_pk_fma_f16 v81, v118, v106, v66
	v_pk_fma_f16 v82, v117, v105, v65
	v_pk_fma_f16 v83, v116, v104, v64
	v_pk_fma_f16 v92, v131, v107, v67
	v_pk_fma_f16 v93, v130, v106, v66
	v_pk_fma_f16 v94, v129, v105, v65
	v_pk_fma_f16 v95, v128, v104, v64
	v_pk_fma_f16 v23, v23, v107, v67
	v_pk_fma_f16 v22, v22, v106, v66
	v_pk_fma_f16 v21, v21, v105, v65
	v_pk_fma_f16 v20, v20, v104, v64
	v_pk_maximum3_f16 v64, v36, v52, v40
	v_pk_maximum3_f16 v65, v37, v53, v41
	v_pk_maximum3_f16 v66, v38, v54, v42
	v_pk_maximum3_f16 v67, v39, v55, v43
	v_pk_fma_f16 v76, v103, v107, v63
	v_pk_fma_f16 v77, v102, v106, v62
	v_pk_fma_f16 v78, v101, v105, v61
	v_pk_fma_f16 v79, v100, v104, v60
	v_pk_fma_f16 v63, v115, v107, v63
	v_pk_fma_f16 v62, v114, v106, v62
	v_pk_fma_f16 v61, v113, v105, v61
	v_pk_fma_f16 v60, v112, v104, v60
	v_pk_maximum3_f16 v101, v70, v78, v61
	v_pk_maximum3_f16 v102, v69, v77, v62
	v_pk_maximum3_f16 v103, v68, v76, v63
	v_pk_maximum3_f16 v104, v83, v95, v20
	v_pk_maximum3_f16 v105, v82, v94, v21
	v_pk_maximum3_f16 v100, v71, v79, v60
	v_pk_maximum3_f16 v106, v81, v93, v22
	v_pk_maximum3_f16 v107, v80, v92, v23
	v_pk_maximum3_f16 v64, v64, v100, v104
	v_pk_maximum3_f16 v65, v65, v101, v105
	v_pk_maximum3_f16 v66, v66, v102, v106
	v_pk_maximum3_f16 v67, v67, v103, v107
	s_nop 0
	v_pk_add_f16 v36, v36, v64 neg_lo:[0,1] neg_hi:[0,1]
	v_pk_add_f16 v37, v37, v65 neg_lo:[0,1] neg_hi:[0,1]
	v_pk_add_f16 v38, v38, v66 neg_lo:[0,1] neg_hi:[0,1]
	v_pk_add_f16 v39, v39, v67 neg_lo:[0,1] neg_hi:[0,1]
	v_pk_add_f16 v52, v52, v64 neg_lo:[0,1] neg_hi:[0,1]
	v_exp_f16_sdwa v100, v36 dst_sel:WORD_0 dst_unused:UNUSED_PAD src0_sel:WORD_0
	v_exp_f16_sdwa v101, v37 dst_sel:WORD_0 dst_unused:UNUSED_PAD src0_sel:WORD_0
	v_exp_f16_sdwa v102, v38 dst_sel:WORD_0 dst_unused:UNUSED_PAD src0_sel:WORD_0
	v_exp_f16_sdwa v103, v39 dst_sel:WORD_0 dst_unused:UNUSED_PAD src0_sel:WORD_0
	v_exp_f16_sdwa v100, v36 dst_sel:WORD_1 dst_unused:UNUSED_PRESERVE src0_sel:WORD_1
	v_exp_f16_sdwa v101, v37 dst_sel:WORD_1 dst_unused:UNUSED_PRESERVE src0_sel:WORD_1
	v_exp_f16_sdwa v102, v38 dst_sel:WORD_1 dst_unused:UNUSED_PRESERVE src0_sel:WORD_1
	v_exp_f16_sdwa v103, v39 dst_sel:WORD_1 dst_unused:UNUSED_PRESERVE src0_sel:WORD_1
	v_pk_add_f16 v53, v53, v65 neg_lo:[0,1] neg_hi:[0,1]
	v_pk_add_f16 v36, v100, 0
	v_pk_add_f16 v37, v101, 0
	v_pk_add_f16 v38, v102, 0
	v_pk_add_f16 v39, v103, 0
	v_pk_fma_f16 v24, v24, v100, 0
	v_pk_fma_f16 v25, v25, v101, 0
	v_pk_fma_f16 v26, v26, v102, 0
	v_pk_fma_f16 v27, v27, v103, 0
	v_pk_add_f16 v54, v54, v66 neg_lo:[0,1] neg_hi:[0,1]
	v_pk_add_f16 v55, v55, v67 neg_lo:[0,1] neg_hi:[0,1]
	v_pk_add_f16 v20, v20, v64 neg_lo:[0,1] neg_hi:[0,1]
	v_exp_f16_sdwa v100, v52 dst_sel:WORD_0 dst_unused:UNUSED_PAD src0_sel:WORD_0
	v_exp_f16_sdwa v101, v53 dst_sel:WORD_0 dst_unused:UNUSED_PAD src0_sel:WORD_0
	v_exp_f16_sdwa v102, v54 dst_sel:WORD_0 dst_unused:UNUSED_PAD src0_sel:WORD_0
	v_exp_f16_sdwa v103, v55 dst_sel:WORD_0 dst_unused:UNUSED_PAD src0_sel:WORD_0
	v_exp_f16_sdwa v100, v52 dst_sel:WORD_1 dst_unused:UNUSED_PRESERVE src0_sel:WORD_1
	v_exp_f16_sdwa v101, v53 dst_sel:WORD_1 dst_unused:UNUSED_PRESERVE src0_sel:WORD_1
	v_exp_f16_sdwa v102, v54 dst_sel:WORD_1 dst_unused:UNUSED_PRESERVE src0_sel:WORD_1
	v_exp_f16_sdwa v103, v55 dst_sel:WORD_1 dst_unused:UNUSED_PRESERVE src0_sel:WORD_1
	v_pk_add_f16 v21, v21, v65 neg_lo:[0,1] neg_hi:[0,1]
	v_pk_add_f16 v39, v39, v103
	v_pk_add_f16 v38, v38, v102
	v_pk_add_f16 v37, v37, v101
	v_pk_add_f16 v36, v36, v100
	v_pk_fma_f16 v27, v31, v103, v27
	v_pk_fma_f16 v26, v30, v102, v26
	v_pk_fma_f16 v25, v29, v101, v25
	v_pk_fma_f16 v24, v28, v100, v24
	v_pk_add_f16 v28, v40, v64 neg_lo:[0,1] neg_hi:[0,1]
	v_pk_add_f16 v29, v41, v65 neg_lo:[0,1] neg_hi:[0,1]
	v_pk_add_f16 v30, v42, v66 neg_lo:[0,1] neg_hi:[0,1]
	v_pk_add_f16 v31, v43, v67 neg_lo:[0,1] neg_hi:[0,1]
	v_pk_add_f16 v22, v22, v66 neg_lo:[0,1] neg_hi:[0,1]
	v_exp_f16_sdwa v40, v28 dst_sel:WORD_0 dst_unused:UNUSED_PAD src0_sel:WORD_0
	v_exp_f16_sdwa v41, v29 dst_sel:WORD_0 dst_unused:UNUSED_PAD src0_sel:WORD_0
	v_exp_f16_sdwa v42, v30 dst_sel:WORD_0 dst_unused:UNUSED_PAD src0_sel:WORD_0
	v_exp_f16_sdwa v43, v31 dst_sel:WORD_0 dst_unused:UNUSED_PAD src0_sel:WORD_0
	v_exp_f16_sdwa v40, v28 dst_sel:WORD_1 dst_unused:UNUSED_PRESERVE src0_sel:WORD_1
	v_exp_f16_sdwa v41, v29 dst_sel:WORD_1 dst_unused:UNUSED_PRESERVE src0_sel:WORD_1
	v_exp_f16_sdwa v42, v30 dst_sel:WORD_1 dst_unused:UNUSED_PRESERVE src0_sel:WORD_1
	v_exp_f16_sdwa v43, v31 dst_sel:WORD_1 dst_unused:UNUSED_PRESERVE src0_sel:WORD_1
	v_pk_add_f16 v23, v23, v67 neg_lo:[0,1] neg_hi:[0,1]
	v_pk_add_f16 v28, v36, v40
	v_pk_add_f16 v29, v37, v41
	v_pk_add_f16 v30, v38, v42
	v_pk_add_f16 v31, v39, v43
	v_pk_fma_f16 v24, v32, v40, v24
	v_pk_fma_f16 v25, v33, v41, v25
	v_pk_fma_f16 v26, v34, v42, v26
	v_pk_fma_f16 v27, v35, v43, v27
	v_pk_add_f16 v32, v71, v64 neg_lo:[0,1] neg_hi:[0,1]
	v_pk_add_f16 v33, v70, v65 neg_lo:[0,1] neg_hi:[0,1]
	v_pk_add_f16 v34, v69, v66 neg_lo:[0,1] neg_hi:[0,1]
	v_pk_add_f16 v35, v68, v67 neg_lo:[0,1] neg_hi:[0,1]
	v_exp_f16_sdwa v36, v32 dst_sel:WORD_0 dst_unused:UNUSED_PAD src0_sel:WORD_0
	v_exp_f16_sdwa v37, v33 dst_sel:WORD_0 dst_unused:UNUSED_PAD src0_sel:WORD_0
	v_exp_f16_sdwa v38, v34 dst_sel:WORD_0 dst_unused:UNUSED_PAD src0_sel:WORD_0
	v_exp_f16_sdwa v39, v35 dst_sel:WORD_0 dst_unused:UNUSED_PAD src0_sel:WORD_0
	v_exp_f16_sdwa v36, v32 dst_sel:WORD_1 dst_unused:UNUSED_PRESERVE src0_sel:WORD_1
	v_exp_f16_sdwa v37, v33 dst_sel:WORD_1 dst_unused:UNUSED_PRESERVE src0_sel:WORD_1
	v_exp_f16_sdwa v38, v34 dst_sel:WORD_1 dst_unused:UNUSED_PRESERVE src0_sel:WORD_1
	v_exp_f16_sdwa v39, v35 dst_sel:WORD_1 dst_unused:UNUSED_PRESERVE src0_sel:WORD_1
	v_pk_add_f16 v32, v79, v64 neg_lo:[0,1] neg_hi:[0,1]
	v_pk_add_f16 v31, v31, v39
	v_pk_add_f16 v30, v30, v38
	v_pk_add_f16 v29, v29, v37
	v_pk_add_f16 v28, v28, v36
	v_pk_fma_f16 v27, v47, v39, v27
	v_pk_fma_f16 v26, v46, v38, v26
	v_pk_fma_f16 v25, v45, v37, v25
	v_pk_fma_f16 v24, v44, v36, v24
	v_pk_add_f16 v33, v78, v65 neg_lo:[0,1] neg_hi:[0,1]
	v_pk_add_f16 v34, v77, v66 neg_lo:[0,1] neg_hi:[0,1]
	v_pk_add_f16 v35, v76, v67 neg_lo:[0,1] neg_hi:[0,1]
	v_exp_f16_sdwa v36, v32 dst_sel:WORD_0 dst_unused:UNUSED_PAD src0_sel:WORD_0
	v_exp_f16_sdwa v37, v33 dst_sel:WORD_0 dst_unused:UNUSED_PAD src0_sel:WORD_0
	v_exp_f16_sdwa v38, v34 dst_sel:WORD_0 dst_unused:UNUSED_PAD src0_sel:WORD_0
	v_exp_f16_sdwa v39, v35 dst_sel:WORD_0 dst_unused:UNUSED_PAD src0_sel:WORD_0
	v_exp_f16_sdwa v36, v32 dst_sel:WORD_1 dst_unused:UNUSED_PRESERVE src0_sel:WORD_1
	v_exp_f16_sdwa v37, v33 dst_sel:WORD_1 dst_unused:UNUSED_PRESERVE src0_sel:WORD_1
	v_exp_f16_sdwa v38, v34 dst_sel:WORD_1 dst_unused:UNUSED_PRESERVE src0_sel:WORD_1
	v_exp_f16_sdwa v39, v35 dst_sel:WORD_1 dst_unused:UNUSED_PRESERVE src0_sel:WORD_1
	v_pk_add_f16 v32, v60, v64 neg_lo:[0,1] neg_hi:[0,1]
	v_pk_add_f16 v28, v28, v36
	v_pk_add_f16 v29, v29, v37
	v_pk_add_f16 v30, v30, v38
	v_pk_add_f16 v31, v31, v39
	v_pk_fma_f16 v24, v56, v36, v24
	v_pk_fma_f16 v25, v57, v37, v25
	v_pk_fma_f16 v26, v58, v38, v26
	v_pk_fma_f16 v27, v59, v39, v27
	v_pk_add_f16 v33, v61, v65 neg_lo:[0,1] neg_hi:[0,1]
	v_pk_add_f16 v34, v62, v66 neg_lo:[0,1] neg_hi:[0,1]
	v_pk_add_f16 v35, v63, v67 neg_lo:[0,1] neg_hi:[0,1]
	v_exp_f16_sdwa v36, v32 dst_sel:WORD_0 dst_unused:UNUSED_PAD src0_sel:WORD_0
	v_exp_f16_sdwa v37, v33 dst_sel:WORD_0 dst_unused:UNUSED_PAD src0_sel:WORD_0
	v_exp_f16_sdwa v38, v34 dst_sel:WORD_0 dst_unused:UNUSED_PAD src0_sel:WORD_0
	v_exp_f16_sdwa v39, v35 dst_sel:WORD_0 dst_unused:UNUSED_PAD src0_sel:WORD_0
	v_exp_f16_sdwa v36, v32 dst_sel:WORD_1 dst_unused:UNUSED_PRESERVE src0_sel:WORD_1
	v_exp_f16_sdwa v37, v33 dst_sel:WORD_1 dst_unused:UNUSED_PRESERVE src0_sel:WORD_1
	v_exp_f16_sdwa v38, v34 dst_sel:WORD_1 dst_unused:UNUSED_PRESERVE src0_sel:WORD_1
	v_exp_f16_sdwa v39, v35 dst_sel:WORD_1 dst_unused:UNUSED_PRESERVE src0_sel:WORD_1
	v_pk_add_f16 v32, v83, v64 neg_lo:[0,1] neg_hi:[0,1]
	v_pk_add_f16 v31, v31, v39
	v_pk_add_f16 v30, v30, v38
	v_pk_add_f16 v29, v29, v37
	v_pk_add_f16 v28, v28, v36
	v_pk_fma_f16 v27, v75, v39, v27
	v_pk_fma_f16 v26, v74, v38, v26
	v_pk_fma_f16 v25, v73, v37, v25
	v_pk_fma_f16 v24, v72, v36, v24
	v_pk_add_f16 v33, v82, v65 neg_lo:[0,1] neg_hi:[0,1]
	v_pk_add_f16 v34, v81, v66 neg_lo:[0,1] neg_hi:[0,1]
	v_pk_add_f16 v35, v80, v67 neg_lo:[0,1] neg_hi:[0,1]
	v_exp_f16_sdwa v36, v32 dst_sel:WORD_0 dst_unused:UNUSED_PAD src0_sel:WORD_0
	v_exp_f16_sdwa v37, v33 dst_sel:WORD_0 dst_unused:UNUSED_PAD src0_sel:WORD_0
	v_exp_f16_sdwa v38, v34 dst_sel:WORD_0 dst_unused:UNUSED_PAD src0_sel:WORD_0
	v_exp_f16_sdwa v39, v35 dst_sel:WORD_0 dst_unused:UNUSED_PAD src0_sel:WORD_0
	v_exp_f16_sdwa v36, v32 dst_sel:WORD_1 dst_unused:UNUSED_PRESERVE src0_sel:WORD_1
	v_exp_f16_sdwa v37, v33 dst_sel:WORD_1 dst_unused:UNUSED_PRESERVE src0_sel:WORD_1
	v_exp_f16_sdwa v38, v34 dst_sel:WORD_1 dst_unused:UNUSED_PRESERVE src0_sel:WORD_1
	v_exp_f16_sdwa v39, v35 dst_sel:WORD_1 dst_unused:UNUSED_PRESERVE src0_sel:WORD_1
	v_pk_add_f16 v32, v95, v64 neg_lo:[0,1] neg_hi:[0,1]
	v_pk_add_f16 v28, v28, v36
	v_pk_add_f16 v29, v29, v37
	v_pk_add_f16 v30, v30, v38
	v_pk_add_f16 v31, v31, v39
	v_pk_fma_f16 v24, v84, v36, v24
	v_pk_fma_f16 v25, v85, v37, v25
	v_pk_fma_f16 v26, v86, v38, v26
	v_pk_fma_f16 v27, v87, v39, v27
	v_pk_add_f16 v33, v94, v65 neg_lo:[0,1] neg_hi:[0,1]
	v_pk_add_f16 v34, v93, v66 neg_lo:[0,1] neg_hi:[0,1]
	v_pk_add_f16 v35, v92, v67 neg_lo:[0,1] neg_hi:[0,1]
	v_exp_f16_sdwa v36, v32 dst_sel:WORD_0 dst_unused:UNUSED_PAD src0_sel:WORD_0
	v_exp_f16_sdwa v37, v33 dst_sel:WORD_0 dst_unused:UNUSED_PAD src0_sel:WORD_0
	v_exp_f16_sdwa v38, v34 dst_sel:WORD_0 dst_unused:UNUSED_PAD src0_sel:WORD_0
	v_exp_f16_sdwa v39, v35 dst_sel:WORD_0 dst_unused:UNUSED_PAD src0_sel:WORD_0
	v_exp_f16_sdwa v36, v32 dst_sel:WORD_1 dst_unused:UNUSED_PRESERVE src0_sel:WORD_1
	v_exp_f16_sdwa v37, v33 dst_sel:WORD_1 dst_unused:UNUSED_PRESERVE src0_sel:WORD_1
	v_exp_f16_sdwa v38, v34 dst_sel:WORD_1 dst_unused:UNUSED_PRESERVE src0_sel:WORD_1
	v_exp_f16_sdwa v39, v35 dst_sel:WORD_1 dst_unused:UNUSED_PRESERVE src0_sel:WORD_1
	s_nop 0
	v_pk_add_f16 v31, v31, v39
	v_pk_add_f16 v30, v30, v38
	v_pk_add_f16 v29, v29, v37
	v_pk_add_f16 v28, v28, v36
	v_pk_fma_f16 v35, v99, v39, v27
	v_pk_fma_f16 v34, v98, v38, v26
	v_pk_fma_f16 v33, v97, v37, v25
	v_pk_fma_f16 v32, v96, v36, v24
	v_exp_f16_sdwa v36, v20 dst_sel:WORD_0 dst_unused:UNUSED_PAD src0_sel:WORD_0
	v_exp_f16_sdwa v37, v21 dst_sel:WORD_0 dst_unused:UNUSED_PAD src0_sel:WORD_0
	v_exp_f16_sdwa v38, v22 dst_sel:WORD_0 dst_unused:UNUSED_PAD src0_sel:WORD_0
	v_exp_f16_sdwa v39, v23 dst_sel:WORD_0 dst_unused:UNUSED_PAD src0_sel:WORD_0
	v_exp_f16_sdwa v36, v20 dst_sel:WORD_1 dst_unused:UNUSED_PRESERVE src0_sel:WORD_1
	v_exp_f16_sdwa v37, v21 dst_sel:WORD_1 dst_unused:UNUSED_PRESERVE src0_sel:WORD_1
	v_exp_f16_sdwa v38, v22 dst_sel:WORD_1 dst_unused:UNUSED_PRESERVE src0_sel:WORD_1
	v_exp_f16_sdwa v39, v23 dst_sel:WORD_1 dst_unused:UNUSED_PRESERVE src0_sel:WORD_1
	v_mov_b32_e32 v27, v19
	v_mov_b32_e32 v26, v18
	v_mov_b32_e32 v25, v17
	v_mov_b32_e32 v24, v16
